# v100: v96 + mid-block s_setprio 0/3 toggles removed (one priority window per 32-MFMA block, load phases now nearly VALU-free)
# speedup vs baseline: 1.0049x; 1.0049x over previous
; #define PG8_STAGE_A(b, h, ptr, NX) do { if constexpr (Sched::GATHER) { unsigned gs_[2]; gs_[0] = ((NX) && last_) ? gN[h][0] : gA[h][0]; gs_[1] = ((NX) && last_) ? gN[h][1] : gA[h][1]; PG8_STAGE(PG8_SA(b, h), ptr, gs_); } \
;         else PG8_STAGE(PG8_SA(b, h), (ptr) + ((h) ? hstep : (size_t)0), voffA); } while (0)
; #define PG8_STAGE(bufoff, gbase, voff) do { _Pragma("unroll") for (int _i = 0; _i < 2; ++_i) \
;         __builtin_amdgcn_global_load_lds((const unsigned*)((const char*)(gbase) + (voff)[_i]), (PG8_LAS unsigned*)(lds + (bufoff) + ldsw + _i * 8192), 16, 0, 0); } while (0)
; #define PG8_LDA(dst, b, h) do { _Pragma("unroll") for (int m = 0; m < 4; ++m) _Pragma("unroll") for (int k = 0; k < 2; ++k) dst[m][k] = *(const PG8_LAS bf16x8*)(lds + PG8_SA(b, h) + aoff + m * 2048 + k * 1024); } while (0)
; #define PG8_WAIT_V(n) asm volatile("s_waitcnt vmcnt(" #n ")" ::: "memory")
; #define PG8_WAIT_L(n) asm volatile("s_waitcnt lgkmcnt(" #n ")" ::: "memory")
; #define PG8_BAR __builtin_amdgcn_s_barrier()
; template <class Epi, class Sched, bool ALIGN_EPI = false, bool SP2 = false>
; __device__ __forceinline__ void gemm_phase(PG8_LAS unsigned char* lds, const Gemm g, const Sched& S, const Epi& E, const bool skip_epi = false) {
;     ...
;         const char* nA = has_next ? (const char*)g.A + (size_t)nxt.pm * pmstepA + nxt.ko : cA; const char* nB = has_next ? (const char*)g.Bt + (size_t)nxt.pn * tstep + nxt.ko : cB;
;         for (int t = 0; t < nt; t += 2) {
;             const bool last = (t == nt - 2); last_ = last && has_next;
;             const char* a1 = cA + (size_t)(t + 1) * kstep;
;             const char* a2 = last ? nA : cA + (size_t)(t + 2) * kstep; const char* b2 = last ? nB : cB + (size_t)(t + 2) * kstep;
;             const char* a3 = a2 + kstep; const char* b3 = b2 + kstep;
;             if (last && has_next) S.a_ready(nxt);
;             if constexpr (SP2) {
;             PG8_LDB(B0, 0, 0); PG8_LDB(B1, 0, 1); PG8_SCHED; PG8_LDA(At, 0, 0); PG8_STAGE_A(1, 1, a1, false);
;             PG8_WAIT_V(8); PG8_WAIT_L(0); PG8_BAR; PG8_MMA(0, 0, At, B0); PG8_MMA(0, 1, At, B1); PG8_BAR; PG8_SCHED;
;             PG8_LDA(At, 0, 1); PG8_STAGE(PG8_SB(0, 0), b2, voffB); PG8_STAGE(PG8_SB(0, 1), b2 + hstep, voffB); PG8_STAGE_A(0, 0, a2, true);
;             PG8_WAIT_V(8); PG8_WAIT_L(0); PG8_BAR; PG8_MMA(1, 0, At, B0); PG8_MMA(1, 1, At, B1); PG8_BAR; PG8_SCHED;
.LBB0_252:
	s_ashr_i32 s17, s16, 31
	s_lshl_b64 s[18:19], s[16:17], 19
	s_add_u32 s18, s86, s18
	s_addc_u32 s19, s87, s19
	s_and_b64 s[20:21], s[4:5], exec
	s_cselect_b32 s17, s19, s25
	s_cselect_b32 s56, s18, s24
	s_ashr_i32 s15, s14, 31
	s_lshl_b64 s[20:21], s[14:15], 19
	v_readlane_b32 s28, v254, 36
	v_readlane_b32 s29, v254, 37
	s_add_u32 s20, s28, s20
	s_addc_u32 s21, s29, s21
	s_and_b64 s[28:29], s[4:5], exec
	s_cselect_b32 s15, s21, s27
	s_cselect_b32 s57, s20, s26
	s_add_u32 s24, s24, 0x40080
	s_addc_u32 s25, s25, 0
	s_add_u32 s58, s26, 0x100
	s_addc_u32 s59, s27, 0
	s_mov_b32 s60, -2
	s_waitcnt vmcnt(0)
	ds_read_b128 v[148:151], v170
	ds_read_b128 v[152:155], v170 offset:1024
	ds_read_b128 v[156:159], v170 offset:2048
	ds_read_b128 v[160:163], v170 offset:3072
	ds_read_b128 v[176:179], v171
	ds_read_b128 v[180:183], v171 offset:1024
	ds_read_b128 v[184:187], v171 offset:2048
	ds_read_b128 v[188:191], v171 offset:3072
	s_add_u32 s26, s24, 0xfffc0080
	s_addc_u32 s27, s25, -1
	s_cmp_eq_u32 s60, 12
	s_cselect_b32 s29, s17, s27
	s_cselect_b32 s28, s56, s26
	s_cselect_b32 s27, s15, s59
	s_cselect_b32 s26, s57, s58
	s_add_i32 m0, s23, 0xc000
	ds_read_b128 v[192:195], v172
	ds_read_b128 v[196:199], v172 offset:1024
	ds_read_b128 v[200:203], v172 offset:2048
	ds_read_b128 v[204:207], v172 offset:3072
	ds_read_b128 v[208:211], v172 offset:4096
	ds_read_b128 v[212:215], v172 offset:5120
	ds_read_b128 v[216:219], v172 offset:6144
	ds_read_b128 v[220:223], v172 offset:7168
	global_load_lds_dwordx4 v140, s[24:25]
	s_add_i32 m0, s23, 0xe000
	s_nop 0
	global_load_lds_dwordx4 v142, s[24:25]
	s_waitcnt vmcnt(8)
	s_waitcnt lgkmcnt(0)
	s_barrier
	s_setprio 3
	s_waitcnt lgkmcnt(0)
	v_mfma_f32_16x16x32_bf16 v[126:129], v[148:151], v[192:195], 0
	v_mfma_f32_16x16x32_bf16 v[122:125], v[156:159], v[192:195], 0
	v_mfma_f32_16x16x32_bf16 v[114:117], v[148:151], v[200:203], 0
	v_mfma_f32_16x16x32_bf16 v[106:109], v[156:159], v[200:203], 0
	v_mfma_f32_16x16x32_bf16 v[98:101], v[148:151], v[208:211], 0
	v_mfma_f32_16x16x32_bf16 v[90:93], v[156:159], v[208:211], 0
	v_mfma_f32_16x16x32_bf16 v[82:85], v[148:151], v[216:219], 0
	v_mfma_f32_16x16x32_bf16 v[74:77], v[156:159], v[216:219], 0
	v_mfma_f32_16x16x32_bf16 v[126:129], v[152:155], v[196:199], v[126:129]
	v_mfma_f32_16x16x32_bf16 v[122:125], v[160:163], v[196:199], v[122:125]
	v_mfma_f32_16x16x32_bf16 v[114:117], v[152:155], v[204:207], v[114:117]
	v_mfma_f32_16x16x32_bf16 v[106:109], v[160:163], v[204:207], v[106:109]
	v_mfma_f32_16x16x32_bf16 v[98:101], v[152:155], v[212:215], v[98:101]
	v_mfma_f32_16x16x32_bf16 v[90:93], v[160:163], v[212:215], v[90:93]
	v_mfma_f32_16x16x32_bf16 v[82:85], v[152:155], v[220:223], v[82:85]
	v_mfma_f32_16x16x32_bf16 v[74:77], v[160:163], v[220:223], v[74:77]
	v_mfma_f32_16x16x32_bf16 v[118:121], v[176:179], v[192:195], 0
	v_mfma_f32_16x16x32_bf16 v[110:113], v[184:187], v[192:195], 0
	v_mfma_f32_16x16x32_bf16 v[102:105], v[176:179], v[200:203], 0
	v_mfma_f32_16x16x32_bf16 v[94:97], v[184:187], v[200:203], 0
	v_mfma_f32_16x16x32_bf16 v[86:89], v[176:179], v[208:211], 0
	v_mfma_f32_16x16x32_bf16 v[78:81], v[184:187], v[208:211], 0
	v_mfma_f32_16x16x32_bf16 v[70:73], v[176:179], v[216:219], 0
	v_mfma_f32_16x16x32_bf16 v[66:69], v[184:187], v[216:219], 0
	v_mfma_f32_16x16x32_bf16 v[118:121], v[180:183], v[196:199], v[118:121]
	v_mfma_f32_16x16x32_bf16 v[110:113], v[188:191], v[196:199], v[110:113]
	v_mfma_f32_16x16x32_bf16 v[102:105], v[180:183], v[204:207], v[102:105]
	v_mfma_f32_16x16x32_bf16 v[94:97], v[188:191], v[204:207], v[94:97]
	v_mfma_f32_16x16x32_bf16 v[86:89], v[180:183], v[212:215], v[86:89]
	v_mfma_f32_16x16x32_bf16 v[78:81], v[188:191], v[212:215], v[78:81]
	v_mfma_f32_16x16x32_bf16 v[70:73], v[180:183], v[220:223], v[70:73]
	v_mfma_f32_16x16x32_bf16 v[66:69], v[188:191], v[220:223], v[66:69]
	s_setprio 0
	s_barrier
	s_add_i32 s61, s46, s2
	v_lshl_add_u64 v[164:165], s[26:27], 0, v[134:135]
	s_mov_b32 m0, s61
	ds_read_b128 v[192:195], v172 offset:16384
	ds_read_b128 v[196:199], v172 offset:17408
	ds_read_b128 v[200:203], v172 offset:18432
	ds_read_b128 v[204:207], v172 offset:19456
	ds_read_b128 v[208:211], v172 offset:20480
	ds_read_b128 v[212:215], v172 offset:21504
	ds_read_b128 v[216:219], v172 offset:22528
	ds_read_b128 v[220:223], v172 offset:23552
	global_load_lds_dwordx4 v[164:165], off
	s_add_i32 m0, s61, 0x2000
	s_add_u32 s62, s26, 0x40000
	v_lshl_add_u64 v[224:225], s[26:27], 0, v[130:131]
	s_addc_u32 s63, s27, 0
	s_add_i32 s61, s47, s2
	global_load_lds_dwordx4 v[224:225], off
	s_mov_b32 m0, s61
	v_lshl_add_u64 v[230:231], s[28:29], 0, v[132:133]
	global_load_lds_dwordx4 v134, s[62:63]
	s_add_i32 m0, s61, 0x2000
	s_nop 0
	global_load_lds_dwordx4 v130, s[62:63]
	v_lshl_add_u64 v[226:227], s[28:29], 0, v[136:137]
	s_mov_b32 m0, s23
	s_nop 0
	global_load_lds_dwordx4 v[226:227], off
	s_mov_b32 m0, s31
	s_nop 0
	global_load_lds_dwordx4 v[230:231], off
	s_waitcnt vmcnt(8)
	s_waitcnt lgkmcnt(0)
	s_barrier
; #define PG8_STAGE_A(b, h, ptr, NX) do { if constexpr (Sched::GATHER) { unsigned gs_[2]; gs_[0] = ((NX) && last_) ? gN[h][0] : gA[h][0]; gs_[1] = ((NX) && last_) ? gN[h][1] : gA[h][1]; PG8_STAGE(PG8_SA(b, h), ptr, gs_); } \
;         else PG8_STAGE(PG8_SA(b, h), (ptr) + ((h) ? hstep : (size_t)0), voffA); } while (0)
; #define PG8_STAGE(bufoff, gbase, voff) do { _Pragma("unroll") for (int _i = 0; _i < 2; ++_i) \
;         __builtin_amdgcn_global_load_lds((const unsigned*)((const char*)(gbase) + (voff)[_i]), (PG8_LAS unsigned*)(lds + (bufoff) + ldsw + _i * 8192), 16, 0, 0); } while (0)
; #define PG8_LDA(dst, b, h) do { _Pragma("unroll") for (int m = 0; m < 4; ++m) _Pragma("unroll") for (int k = 0; k < 2; ++k) dst[m][k] = *(const PG8_LAS bf16x8*)(lds + PG8_SA(b, h) + aoff + m * 2048 + k * 1024); } while (0)
; #define PG8_LDB(dst, b, h) do { _Pragma("unroll") for (int n = 0; n < 2; ++n) _Pragma("unroll") for (int k = 0; k < 2; ++k) dst[n][k] = *(const PG8_LAS bf16x8*)(lds + PG8_SB(b, h) + boff + n * 2048 + k * 1024); } while (0)
; #define PG8_MMA(ai, bj, At, Bt) do { __builtin_amdgcn_s_setprio(1); _Pragma("unroll") for (int m = 0; m < 4; ++m) _Pragma("unroll") for (int n = 0; n < 2; ++n) _Pragma("unroll") for (int k = 0; k < 2; ++k) \
;         acc[ai][bj][m][n] = __builtin_amdgcn_mfma_f32_16x16x32_bf16(Bt[n][k], At[m][k], acc[ai][bj][m][n], 0, 0, 0); __builtin_amdgcn_s_setprio(0); } while (0)
; #define PG8_WAIT_V(n) asm volatile("s_waitcnt vmcnt(" #n ")" ::: "memory")
; #define PG8_BAR __builtin_amdgcn_s_barrier()
; template <class Epi, class Sched, bool ALIGN_EPI = false, bool SP2 = false>
; __device__ __forceinline__ void gemm_phase(PG8_LAS unsigned char* lds, const Gemm g, const Sched& S, const Epi& E, const bool skip_epi = false) {
;     ...
;             PG8_WAIT_V(8); PG8_WAIT_L(0); PG8_BAR; PG8_MMA(0, 0, At, B0); PG8_MMA(0, 1, At, B1); PG8_BAR; PG8_SCHED;
;             PG8_LDA(At, 0, 1); PG8_STAGE(PG8_SB(0, 0), b2, voffB); PG8_STAGE(PG8_SB(0, 1), b2 + hstep, voffB); PG8_STAGE_A(0, 0, a2, true);
;             PG8_WAIT_V(8); PG8_WAIT_L(0); PG8_BAR; PG8_MMA(1, 0, At, B0); PG8_MMA(1, 1, At, B1); PG8_BAR; PG8_SCHED;
;             PG8_LDB(B0, 1, 0); PG8_LDB(B1, 1, 1); PG8_SCHED; PG8_LDA(At, 1, 0); PG8_STAGE_A(0, 1, a2, true);
;             PG8_WAIT_V(8); PG8_WAIT_L(0); PG8_BAR; PG8_MMA(0, 0, At, B0); PG8_MMA(0, 1, At, B1); PG8_BAR; PG8_SCHED;
	s_setprio 3
	s_waitcnt lgkmcnt(0)
	v_mfma_f32_16x16x32_bf16 v[62:65], v[148:151], v[192:195], 0
	v_mfma_f32_16x16x32_bf16 v[58:61], v[156:159], v[192:195], 0
	v_mfma_f32_16x16x32_bf16 v[50:53], v[148:151], v[200:203], 0
	v_mfma_f32_16x16x32_bf16 v[42:45], v[156:159], v[200:203], 0
	v_mfma_f32_16x16x32_bf16 v[34:37], v[148:151], v[208:211], 0
	v_mfma_f32_16x16x32_bf16 v[26:29], v[156:159], v[208:211], 0
	v_mfma_f32_16x16x32_bf16 v[18:21], v[148:151], v[216:219], 0
	v_mfma_f32_16x16x32_bf16 v[10:13], v[156:159], v[216:219], 0
	v_mfma_f32_16x16x32_bf16 v[62:65], v[152:155], v[196:199], v[62:65]
	v_mfma_f32_16x16x32_bf16 v[58:61], v[160:163], v[196:199], v[58:61]
	v_mfma_f32_16x16x32_bf16 v[50:53], v[152:155], v[204:207], v[50:53]
	v_mfma_f32_16x16x32_bf16 v[42:45], v[160:163], v[204:207], v[42:45]
	v_mfma_f32_16x16x32_bf16 v[34:37], v[152:155], v[212:215], v[34:37]
	v_mfma_f32_16x16x32_bf16 v[26:29], v[160:163], v[212:215], v[26:29]
	v_mfma_f32_16x16x32_bf16 v[18:21], v[152:155], v[220:223], v[18:21]
	v_mfma_f32_16x16x32_bf16 v[10:13], v[160:163], v[220:223], v[10:13]
	v_mfma_f32_16x16x32_bf16 v[54:57], v[176:179], v[192:195], 0
	v_mfma_f32_16x16x32_bf16 v[46:49], v[184:187], v[192:195], 0
	v_mfma_f32_16x16x32_bf16 v[38:41], v[176:179], v[200:203], 0
	v_mfma_f32_16x16x32_bf16 v[30:33], v[184:187], v[200:203], 0
	v_mfma_f32_16x16x32_bf16 v[22:25], v[176:179], v[208:211], 0
	v_mfma_f32_16x16x32_bf16 v[14:17], v[184:187], v[208:211], 0
	v_mfma_f32_16x16x32_bf16 v[6:9], v[176:179], v[216:219], 0
	v_mfma_f32_16x16x32_bf16 v[2:5], v[184:187], v[216:219], 0
	v_mfma_f32_16x16x32_bf16 v[54:57], v[180:183], v[196:199], v[54:57]
	v_mfma_f32_16x16x32_bf16 v[46:49], v[188:191], v[196:199], v[46:49]
	v_mfma_f32_16x16x32_bf16 v[38:41], v[180:183], v[204:207], v[38:41]
	v_mfma_f32_16x16x32_bf16 v[30:33], v[188:191], v[204:207], v[30:33]
	v_mfma_f32_16x16x32_bf16 v[22:25], v[180:183], v[212:215], v[22:25]
	v_mfma_f32_16x16x32_bf16 v[14:17], v[188:191], v[212:215], v[14:17]
	v_mfma_f32_16x16x32_bf16 v[6:9], v[180:183], v[220:223], v[6:9]
	v_mfma_f32_16x16x32_bf16 v[2:5], v[188:191], v[220:223], v[2:5]
	s_setprio 0
	s_barrier
	s_add_i32 s61, 0, 0x18000
	s_add_i32 s62, 0, 0x1c000
	v_add_u32_e32 v160, s61, v1
	v_add_u32_e32 v188, s62, v1
	ds_read_b128 v[148:151], v160
	ds_read_b128 v[152:155], v160 offset:1024
	ds_read_b128 v[156:159], v160 offset:2048
	ds_read_b128 v[160:163], v160 offset:3072
	ds_read_b128 v[176:179], v188
	ds_read_b128 v[180:183], v188 offset:1024
	ds_read_b128 v[184:187], v188 offset:2048
	ds_read_b128 v[188:191], v188 offset:3072
	s_add_u32 s28, s28, 0x40000
	s_addc_u32 s29, s29, 0
	s_mov_b32 m0, s34
	ds_read_b128 v[192:195], v172 offset:32768
	ds_read_b128 v[196:199], v172 offset:33792
	ds_read_b128 v[200:203], v172 offset:34816
	ds_read_b128 v[204:207], v172 offset:35840
	ds_read_b128 v[208:211], v172 offset:36864
	ds_read_b128 v[212:215], v172 offset:37888
	ds_read_b128 v[216:219], v172 offset:38912
	ds_read_b128 v[220:223], v172 offset:39936
	global_load_lds_dwordx4 v136, s[28:29]
	s_mov_b32 m0, s35
	s_nop 0
	global_load_lds_dwordx4 v132, s[28:29]
	s_waitcnt vmcnt(8)
	s_waitcnt lgkmcnt(0)
	s_barrier
	s_setprio 3
	s_waitcnt lgkmcnt(0)
	v_mfma_f32_16x16x32_bf16 v[126:129], v[148:151], v[192:195], v[126:129]
	v_mfma_f32_16x16x32_bf16 v[122:125], v[156:159], v[192:195], v[122:125]
	v_mfma_f32_16x16x32_bf16 v[114:117], v[148:151], v[200:203], v[114:117]
	v_mfma_f32_16x16x32_bf16 v[106:109], v[156:159], v[200:203], v[106:109]
	v_mfma_f32_16x16x32_bf16 v[98:101], v[148:151], v[208:211], v[98:101]
	v_mfma_f32_16x16x32_bf16 v[90:93], v[156:159], v[208:211], v[90:93]
	v_mfma_f32_16x16x32_bf16 v[82:85], v[148:151], v[216:219], v[82:85]
	v_mfma_f32_16x16x32_bf16 v[74:77], v[156:159], v[216:219], v[74:77]
	v_mfma_f32_16x16x32_bf16 v[126:129], v[152:155], v[196:199], v[126:129]
	v_mfma_f32_16x16x32_bf16 v[122:125], v[160:163], v[196:199], v[122:125]
	v_mfma_f32_16x16x32_bf16 v[114:117], v[152:155], v[204:207], v[114:117]
	v_mfma_f32_16x16x32_bf16 v[106:109], v[160:163], v[204:207], v[106:109]
	v_mfma_f32_16x16x32_bf16 v[98:101], v[152:155], v[212:215], v[98:101]
	v_mfma_f32_16x16x32_bf16 v[90:93], v[160:163], v[212:215], v[90:93]
	v_mfma_f32_16x16x32_bf16 v[82:85], v[152:155], v[220:223], v[82:85]
	v_mfma_f32_16x16x32_bf16 v[74:77], v[160:163], v[220:223], v[74:77]
	v_mfma_f32_16x16x32_bf16 v[118:121], v[176:179], v[192:195], v[118:121]
	v_mfma_f32_16x16x32_bf16 v[110:113], v[184:187], v[192:195], v[110:113]
	v_mfma_f32_16x16x32_bf16 v[102:105], v[176:179], v[200:203], v[102:105]
	v_mfma_f32_16x16x32_bf16 v[94:97], v[184:187], v[200:203], v[94:97]
	v_mfma_f32_16x16x32_bf16 v[86:89], v[176:179], v[208:211], v[86:89]
	v_mfma_f32_16x16x32_bf16 v[78:81], v[184:187], v[208:211], v[78:81]
	v_mfma_f32_16x16x32_bf16 v[70:73], v[176:179], v[216:219], v[70:73]
	v_mfma_f32_16x16x32_bf16 v[66:69], v[184:187], v[216:219], v[66:69]
	v_mfma_f32_16x16x32_bf16 v[118:121], v[180:183], v[196:199], v[118:121]
	v_mfma_f32_16x16x32_bf16 v[110:113], v[188:191], v[196:199], v[110:113]
	v_mfma_f32_16x16x32_bf16 v[102:105], v[180:183], v[204:207], v[102:105]
	v_mfma_f32_16x16x32_bf16 v[94:97], v[188:191], v[204:207], v[94:97]
	v_mfma_f32_16x16x32_bf16 v[86:89], v[180:183], v[212:215], v[86:89]
	v_mfma_f32_16x16x32_bf16 v[78:81], v[188:191], v[212:215], v[78:81]
	v_mfma_f32_16x16x32_bf16 v[70:73], v[180:183], v[220:223], v[70:73]
	v_mfma_f32_16x16x32_bf16 v[66:69], v[188:191], v[220:223], v[66:69]
	s_setprio 0
	s_barrier
; #define PG8_STAGE_A(b, h, ptr, NX) do { if constexpr (Sched::GATHER) { unsigned gs_[2]; gs_[0] = ((NX) && last_) ? gN[h][0] : gA[h][0]; gs_[1] = ((NX) && last_) ? gN[h][1] : gA[h][1]; PG8_STAGE(PG8_SA(b, h), ptr, gs_); } \
;         else PG8_STAGE(PG8_SA(b, h), (ptr) + ((h) ? hstep : (size_t)0), voffA); } while (0)
; #define PG8_STAGE(bufoff, gbase, voff) do { _Pragma("unroll") for (int _i = 0; _i < 2; ++_i) \
;         __builtin_amdgcn_global_load_lds((const unsigned*)((const char*)(gbase) + (voff)[_i]), (PG8_LAS unsigned*)(lds + (bufoff) + ldsw + _i * 8192), 16, 0, 0); } while (0)
; #define PG8_WAIT_V(n) asm volatile("s_waitcnt vmcnt(" #n ")" ::: "memory")
; #define PG8_BAR __builtin_amdgcn_s_barrier()
; template <class Epi, class Sched, bool ALIGN_EPI = false, bool SP2 = false>
; __device__ __forceinline__ void gemm_phase(PG8_LAS unsigned char* lds, const Gemm g, const Sched& S, const Epi& E, const bool skip_epi = false) {
;     ...
;         for (int t = 0; t < nt; t += 2) {
;             const bool last = (t == nt - 2); last_ = last && has_next;
;             const char* a1 = cA + (size_t)(t + 1) * kstep;
;             const char* a2 = last ? nA : cA + (size_t)(t + 2) * kstep; const char* b2 = last ? nB : cB + (size_t)(t + 2) * kstep;
;             const char* a3 = a2 + kstep; const char* b3 = b2 + kstep;
;             if (last && has_next) S.a_ready(nxt);
;             if constexpr (SP2) {
;             PG8_LDB(B0, 0, 0); PG8_LDB(B1, 0, 1); PG8_SCHED; PG8_LDA(At, 0, 0); PG8_STAGE_A(1, 1, a1, false);
;             PG8_WAIT_V(8); PG8_WAIT_L(0); PG8_BAR; PG8_MMA(0, 0, At, B0); PG8_MMA(0, 1, At, B1); PG8_BAR; PG8_SCHED;
;             PG8_LDA(At, 0, 1); PG8_STAGE(PG8_SB(0, 0), b2, voffB); PG8_STAGE(PG8_SB(0, 1), b2 + hstep, voffB); PG8_STAGE_A(0, 0, a2, true);
;             PG8_WAIT_V(8); PG8_WAIT_L(0); PG8_BAR; PG8_MMA(1, 0, At, B0); PG8_MMA(1, 1, At, B1); PG8_BAR; PG8_SCHED;
;             PG8_LDB(B0, 1, 0); PG8_LDB(B1, 1, 1); PG8_SCHED; PG8_LDA(At, 1, 0); PG8_STAGE_A(0, 1, a2, true);
;             PG8_WAIT_V(8); PG8_WAIT_L(0); PG8_BAR; PG8_MMA(0, 0, At, B0); PG8_MMA(0, 1, At, B1); PG8_BAR; PG8_SCHED;
;             PG8_LDA(At, 1, 1); PG8_STAGE(PG8_SB(1, 0), b3, voffB); PG8_STAGE(PG8_SB(1, 1), b3 + hstep, voffB); PG8_STAGE_A(1, 0, a3, true);
;             PG8_WAIT_V(8); PG8_WAIT_L(0); PG8_BAR; PG8_MMA(1, 0, At, B0); PG8_MMA(1, 1, At, B1); PG8_BAR; PG8_SCHED;
	s_add_i32 s28, s61, s2
	s_add_i32 m0, s28, 0xffffff80
	ds_read_b128 v[192:195], v172 offset:49152
	ds_read_b128 v[196:199], v172 offset:50176
	ds_read_b128 v[200:203], v172 offset:51200
	ds_read_b128 v[204:207], v172 offset:52224
	ds_read_b128 v[208:211], v172 offset:53248
	ds_read_b128 v[212:215], v172 offset:54272
	ds_read_b128 v[216:219], v172 offset:55296
	ds_read_b128 v[220:223], v172 offset:56320
	global_load_lds_dwordx4 v[164:165], off offset:128
	s_add_i32 m0, s28, 0x1f80
	s_add_u32 s26, s26, 0x40080
	s_addc_u32 s27, s27, 0
	s_add_i32 s28, s62, s2
	global_load_lds_dwordx4 v[224:225], off offset:128
	s_mov_b32 m0, s28
	s_nop 0
	global_load_lds_dwordx4 v134, s[26:27]
	s_add_i32 m0, s28, 0x2000
	s_nop 0
	global_load_lds_dwordx4 v130, s[26:27]
	s_add_i32 m0, s37, 0xffffff80
	s_nop 0
	global_load_lds_dwordx4 v[226:227], off offset:128
	s_add_i32 m0, s38, 0xffffff80
	s_nop 0
	global_load_lds_dwordx4 v[230:231], off offset:128
	s_waitcnt vmcnt(8)
	s_waitcnt lgkmcnt(0)
	s_barrier
	s_setprio 3
	s_waitcnt lgkmcnt(0)
	v_mfma_f32_16x16x32_bf16 v[62:65], v[148:151], v[192:195], v[62:65]
	v_mfma_f32_16x16x32_bf16 v[58:61], v[156:159], v[192:195], v[58:61]
	v_mfma_f32_16x16x32_bf16 v[50:53], v[148:151], v[200:203], v[50:53]
	v_mfma_f32_16x16x32_bf16 v[42:45], v[156:159], v[200:203], v[42:45]
	v_mfma_f32_16x16x32_bf16 v[34:37], v[148:151], v[208:211], v[34:37]
	v_mfma_f32_16x16x32_bf16 v[26:29], v[156:159], v[208:211], v[26:29]
	v_mfma_f32_16x16x32_bf16 v[18:21], v[148:151], v[216:219], v[18:21]
	v_mfma_f32_16x16x32_bf16 v[10:13], v[156:159], v[216:219], v[10:13]
	v_mfma_f32_16x16x32_bf16 v[62:65], v[152:155], v[196:199], v[62:65]
	v_mfma_f32_16x16x32_bf16 v[58:61], v[160:163], v[196:199], v[58:61]
	v_mfma_f32_16x16x32_bf16 v[50:53], v[152:155], v[204:207], v[50:53]
	v_mfma_f32_16x16x32_bf16 v[42:45], v[160:163], v[204:207], v[42:45]
	v_mfma_f32_16x16x32_bf16 v[34:37], v[152:155], v[212:215], v[34:37]
	v_mfma_f32_16x16x32_bf16 v[26:29], v[160:163], v[212:215], v[26:29]
	v_mfma_f32_16x16x32_bf16 v[18:21], v[152:155], v[220:223], v[18:21]
	v_mfma_f32_16x16x32_bf16 v[10:13], v[160:163], v[220:223], v[10:13]
	v_mfma_f32_16x16x32_bf16 v[54:57], v[176:179], v[192:195], v[54:57]
	v_mfma_f32_16x16x32_bf16 v[46:49], v[184:187], v[192:195], v[46:49]
	v_mfma_f32_16x16x32_bf16 v[38:41], v[176:179], v[200:203], v[38:41]
	v_mfma_f32_16x16x32_bf16 v[30:33], v[184:187], v[200:203], v[30:33]
	v_mfma_f32_16x16x32_bf16 v[22:25], v[176:179], v[208:211], v[22:25]
	v_mfma_f32_16x16x32_bf16 v[14:17], v[184:187], v[208:211], v[14:17]
	v_mfma_f32_16x16x32_bf16 v[6:9], v[176:179], v[216:219], v[6:9]
	v_mfma_f32_16x16x32_bf16 v[2:5], v[184:187], v[216:219], v[2:5]
	v_mfma_f32_16x16x32_bf16 v[54:57], v[180:183], v[196:199], v[54:57]
	v_mfma_f32_16x16x32_bf16 v[46:49], v[188:191], v[196:199], v[46:49]
	v_mfma_f32_16x16x32_bf16 v[38:41], v[180:183], v[204:207], v[38:41]
	v_mfma_f32_16x16x32_bf16 v[30:33], v[188:191], v[204:207], v[30:33]
	v_mfma_f32_16x16x32_bf16 v[22:25], v[180:183], v[212:215], v[22:25]
	v_mfma_f32_16x16x32_bf16 v[14:17], v[188:191], v[212:215], v[14:17]
	v_mfma_f32_16x16x32_bf16 v[6:9], v[180:183], v[220:223], v[6:9]
	v_mfma_f32_16x16x32_bf16 v[2:5], v[188:191], v[220:223], v[2:5]
	s_setprio 0
	s_barrier
	s_add_i32 s60, s60, 2
	s_add_u32 s24, s24, 0x100
	s_addc_u32 s25, s25, 0
	s_add_u32 s58, s58, 0x100
	s_addc_u32 s59, s59, 0
	s_cmp_gt_u32 s60, 13
.LBB0_253:
	ds_read_b128 v[148:151], v170
	ds_read_b128 v[152:155], v170 offset:1024
	ds_read_b128 v[156:159], v170 offset:2048
	ds_read_b128 v[160:163], v170 offset:3072
	ds_read_b128 v[176:179], v171
	ds_read_b128 v[180:183], v171 offset:1024
	ds_read_b128 v[184:187], v171 offset:2048
	ds_read_b128 v[188:191], v171 offset:3072
	s_add_u32 s26, s24, 0xfffc0080
	s_addc_u32 s27, s25, -1
	s_cmp_eq_u32 s60, 12
	s_cselect_b32 s29, s17, s27
	s_cselect_b32 s28, s56, s26
	s_cselect_b32 s27, s15, s59
	s_cselect_b32 s26, s57, s58
	s_add_i32 m0, s23, 0xc000
	ds_read_b128 v[192:195], v172
	ds_read_b128 v[196:199], v172 offset:1024
	ds_read_b128 v[200:203], v172 offset:2048
	ds_read_b128 v[204:207], v172 offset:3072
	ds_read_b128 v[208:211], v172 offset:4096
	ds_read_b128 v[212:215], v172 offset:5120
	ds_read_b128 v[216:219], v172 offset:6144
	ds_read_b128 v[220:223], v172 offset:7168
	global_load_lds_dwordx4 v140, s[24:25]
	s_add_i32 m0, s23, 0xe000
	s_nop 0
	global_load_lds_dwordx4 v142, s[24:25]
	s_waitcnt vmcnt(8)
	s_waitcnt lgkmcnt(0)
	s_barrier
	s_setprio 3
	s_waitcnt lgkmcnt(0)
	v_mfma_f32_16x16x32_bf16 v[126:129], v[148:151], v[192:195], v[126:129]
	v_mfma_f32_16x16x32_bf16 v[122:125], v[156:159], v[192:195], v[122:125]
	v_mfma_f32_16x16x32_bf16 v[114:117], v[148:151], v[200:203], v[114:117]
	v_mfma_f32_16x16x32_bf16 v[106:109], v[156:159], v[200:203], v[106:109]
	v_mfma_f32_16x16x32_bf16 v[98:101], v[148:151], v[208:211], v[98:101]
	v_mfma_f32_16x16x32_bf16 v[90:93], v[156:159], v[208:211], v[90:93]
	v_mfma_f32_16x16x32_bf16 v[82:85], v[148:151], v[216:219], v[82:85]
	v_mfma_f32_16x16x32_bf16 v[74:77], v[156:159], v[216:219], v[74:77]
	v_mfma_f32_16x16x32_bf16 v[126:129], v[152:155], v[196:199], v[126:129]
	v_mfma_f32_16x16x32_bf16 v[122:125], v[160:163], v[196:199], v[122:125]
	v_mfma_f32_16x16x32_bf16 v[114:117], v[152:155], v[204:207], v[114:117]
	v_mfma_f32_16x16x32_bf16 v[106:109], v[160:163], v[204:207], v[106:109]
	v_mfma_f32_16x16x32_bf16 v[98:101], v[152:155], v[212:215], v[98:101]
	v_mfma_f32_16x16x32_bf16 v[90:93], v[160:163], v[212:215], v[90:93]
	v_mfma_f32_16x16x32_bf16 v[82:85], v[152:155], v[220:223], v[82:85]
	v_mfma_f32_16x16x32_bf16 v[74:77], v[160:163], v[220:223], v[74:77]
	v_mfma_f32_16x16x32_bf16 v[118:121], v[176:179], v[192:195], v[118:121]
	v_mfma_f32_16x16x32_bf16 v[110:113], v[184:187], v[192:195], v[110:113]
	v_mfma_f32_16x16x32_bf16 v[102:105], v[176:179], v[200:203], v[102:105]
	v_mfma_f32_16x16x32_bf16 v[94:97], v[184:187], v[200:203], v[94:97]
	v_mfma_f32_16x16x32_bf16 v[86:89], v[176:179], v[208:211], v[86:89]
	v_mfma_f32_16x16x32_bf16 v[78:81], v[184:187], v[208:211], v[78:81]
	v_mfma_f32_16x16x32_bf16 v[70:73], v[176:179], v[216:219], v[70:73]
	v_mfma_f32_16x16x32_bf16 v[66:69], v[184:187], v[216:219], v[66:69]
	v_mfma_f32_16x16x32_bf16 v[118:121], v[180:183], v[196:199], v[118:121]
	v_mfma_f32_16x16x32_bf16 v[110:113], v[188:191], v[196:199], v[110:113]
	v_mfma_f32_16x16x32_bf16 v[102:105], v[180:183], v[204:207], v[102:105]
	v_mfma_f32_16x16x32_bf16 v[94:97], v[188:191], v[204:207], v[94:97]
	v_mfma_f32_16x16x32_bf16 v[86:89], v[180:183], v[212:215], v[86:89]
	v_mfma_f32_16x16x32_bf16 v[78:81], v[188:191], v[212:215], v[78:81]
	v_mfma_f32_16x16x32_bf16 v[70:73], v[180:183], v[220:223], v[70:73]
	v_mfma_f32_16x16x32_bf16 v[66:69], v[188:191], v[220:223], v[66:69]
	s_setprio 0
	s_barrier
; #define PG8_STAGE_A(b, h, ptr, NX) do { if constexpr (Sched::GATHER) { unsigned gs_[2]; gs_[0] = ((NX) && last_) ? gN[h][0] : gA[h][0]; gs_[1] = ((NX) && last_) ? gN[h][1] : gA[h][1]; PG8_STAGE(PG8_SA(b, h), ptr, gs_); } \
;         else PG8_STAGE(PG8_SA(b, h), (ptr) + ((h) ? hstep : (size_t)0), voffA); } while (0)
; #define PG8_STAGE(bufoff, gbase, voff) do { _Pragma("unroll") for (int _i = 0; _i < 2; ++_i) \
;         __builtin_amdgcn_global_load_lds((const unsigned*)((const char*)(gbase) + (voff)[_i]), (PG8_LAS unsigned*)(lds + (bufoff) + ldsw + _i * 8192), 16, 0, 0); } while (0)
; #define PG8_LDA(dst, b, h) do { _Pragma("unroll") for (int m = 0; m < 4; ++m) _Pragma("unroll") for (int k = 0; k < 2; ++k) dst[m][k] = *(const PG8_LAS bf16x8*)(lds + PG8_SA(b, h) + aoff + m * 2048 + k * 1024); } while (0)
; #define PG8_LDB(dst, b, h) do { _Pragma("unroll") for (int n = 0; n < 2; ++n) _Pragma("unroll") for (int k = 0; k < 2; ++k) dst[n][k] = *(const PG8_LAS bf16x8*)(lds + PG8_SB(b, h) + boff + n * 2048 + k * 1024); } while (0)
; #define PG8_MMA(ai, bj, At, Bt) do { __builtin_amdgcn_s_setprio(1); _Pragma("unroll") for (int m = 0; m < 4; ++m) _Pragma("unroll") for (int n = 0; n < 2; ++n) _Pragma("unroll") for (int k = 0; k < 2; ++k) \
;         acc[ai][bj][m][n] = __builtin_amdgcn_mfma_f32_16x16x32_bf16(Bt[n][k], At[m][k], acc[ai][bj][m][n], 0, 0, 0); __builtin_amdgcn_s_setprio(0); } while (0)
; #define PG8_WAIT_V(n) asm volatile("s_waitcnt vmcnt(" #n ")" ::: "memory")
; #define PG8_WAIT_L(n) asm volatile("s_waitcnt lgkmcnt(" #n ")" ::: "memory")
; #define PG8_BAR __builtin_amdgcn_s_barrier()
; #define PG8_SCHED __builtin_amdgcn_sched_barrier(0)
; template <class Epi, class Sched, bool ALIGN_EPI = false, bool SP2 = false>
; __device__ __forceinline__ void gemm_phase(PG8_LAS unsigned char* lds, const Gemm g, const Sched& S, const Epi& E, const bool skip_epi = false) {
;     ...
;             PG8_LDA(At, 0, 1); PG8_STAGE(PG8_SB(0, 0), b2, voffB); PG8_STAGE(PG8_SB(0, 1), b2 + hstep, voffB); PG8_STAGE_A(0, 0, a2, true);
;             PG8_WAIT_V(8); PG8_WAIT_L(0); PG8_BAR; PG8_MMA(1, 0, At, B0); PG8_MMA(1, 1, At, B1); PG8_BAR; PG8_SCHED;
;             PG8_LDB(B0, 1, 0); PG8_LDB(B1, 1, 1); PG8_SCHED; PG8_LDA(At, 1, 0); PG8_STAGE_A(0, 1, a2, true);
;             PG8_WAIT_V(8); PG8_WAIT_L(0); PG8_BAR; PG8_MMA(0, 0, At, B0); PG8_MMA(0, 1, At, B1); PG8_BAR; PG8_SCHED;
	s_add_i32 s61, s46, s2
	v_lshl_add_u64 v[164:165], s[26:27], 0, v[134:135]
	s_mov_b32 m0, s61
	ds_read_b128 v[192:195], v172 offset:16384
	ds_read_b128 v[196:199], v172 offset:17408
	ds_read_b128 v[200:203], v172 offset:18432
	ds_read_b128 v[204:207], v172 offset:19456
	ds_read_b128 v[208:211], v172 offset:20480
	ds_read_b128 v[212:215], v172 offset:21504
	ds_read_b128 v[216:219], v172 offset:22528
	ds_read_b128 v[220:223], v172 offset:23552
	global_load_lds_dwordx4 v[164:165], off
	s_add_i32 m0, s61, 0x2000
	s_add_u32 s62, s26, 0x40000
	v_lshl_add_u64 v[224:225], s[26:27], 0, v[130:131]
	s_addc_u32 s63, s27, 0
	s_add_i32 s61, s47, s2
	global_load_lds_dwordx4 v[224:225], off
	s_mov_b32 m0, s61
	v_lshl_add_u64 v[230:231], s[28:29], 0, v[132:133]
	global_load_lds_dwordx4 v134, s[62:63]
	s_add_i32 m0, s61, 0x2000
	s_nop 0
	global_load_lds_dwordx4 v130, s[62:63]
	v_lshl_add_u64 v[226:227], s[28:29], 0, v[136:137]
	s_mov_b32 m0, s23
	s_nop 0
	global_load_lds_dwordx4 v[226:227], off
	s_mov_b32 m0, s31
	s_nop 0
	global_load_lds_dwordx4 v[230:231], off
	s_waitcnt vmcnt(8)
	s_waitcnt lgkmcnt(0)
	s_barrier
	s_setprio 3
	s_waitcnt lgkmcnt(0)
	v_mfma_f32_16x16x32_bf16 v[62:65], v[148:151], v[192:195], v[62:65]
	v_mfma_f32_16x16x32_bf16 v[58:61], v[156:159], v[192:195], v[58:61]
	v_mfma_f32_16x16x32_bf16 v[50:53], v[148:151], v[200:203], v[50:53]
	v_mfma_f32_16x16x32_bf16 v[42:45], v[156:159], v[200:203], v[42:45]
	v_mfma_f32_16x16x32_bf16 v[34:37], v[148:151], v[208:211], v[34:37]
	v_mfma_f32_16x16x32_bf16 v[26:29], v[156:159], v[208:211], v[26:29]
	v_mfma_f32_16x16x32_bf16 v[18:21], v[148:151], v[216:219], v[18:21]
	v_mfma_f32_16x16x32_bf16 v[10:13], v[156:159], v[216:219], v[10:13]
	v_mfma_f32_16x16x32_bf16 v[62:65], v[152:155], v[196:199], v[62:65]
	v_mfma_f32_16x16x32_bf16 v[58:61], v[160:163], v[196:199], v[58:61]
	v_mfma_f32_16x16x32_bf16 v[50:53], v[152:155], v[204:207], v[50:53]
	v_mfma_f32_16x16x32_bf16 v[42:45], v[160:163], v[204:207], v[42:45]
	v_mfma_f32_16x16x32_bf16 v[34:37], v[152:155], v[212:215], v[34:37]
	v_mfma_f32_16x16x32_bf16 v[26:29], v[160:163], v[212:215], v[26:29]
	v_mfma_f32_16x16x32_bf16 v[18:21], v[152:155], v[220:223], v[18:21]
	v_mfma_f32_16x16x32_bf16 v[10:13], v[160:163], v[220:223], v[10:13]
	v_mfma_f32_16x16x32_bf16 v[54:57], v[176:179], v[192:195], v[54:57]
	v_mfma_f32_16x16x32_bf16 v[46:49], v[184:187], v[192:195], v[46:49]
	v_mfma_f32_16x16x32_bf16 v[38:41], v[176:179], v[200:203], v[38:41]
	v_mfma_f32_16x16x32_bf16 v[30:33], v[184:187], v[200:203], v[30:33]
	v_mfma_f32_16x16x32_bf16 v[22:25], v[176:179], v[208:211], v[22:25]
	v_mfma_f32_16x16x32_bf16 v[14:17], v[184:187], v[208:211], v[14:17]
	v_mfma_f32_16x16x32_bf16 v[6:9], v[176:179], v[216:219], v[6:9]
	v_mfma_f32_16x16x32_bf16 v[2:5], v[184:187], v[216:219], v[2:5]
	v_mfma_f32_16x16x32_bf16 v[54:57], v[180:183], v[196:199], v[54:57]
	v_mfma_f32_16x16x32_bf16 v[46:49], v[188:191], v[196:199], v[46:49]
	v_mfma_f32_16x16x32_bf16 v[38:41], v[180:183], v[204:207], v[38:41]
	v_mfma_f32_16x16x32_bf16 v[30:33], v[188:191], v[204:207], v[30:33]
	v_mfma_f32_16x16x32_bf16 v[22:25], v[180:183], v[212:215], v[22:25]
	v_mfma_f32_16x16x32_bf16 v[14:17], v[188:191], v[212:215], v[14:17]
	v_mfma_f32_16x16x32_bf16 v[6:9], v[180:183], v[220:223], v[6:9]
	v_mfma_f32_16x16x32_bf16 v[2:5], v[188:191], v[220:223], v[2:5]
	s_setprio 0
	s_barrier
	s_add_i32 s61, 0, 0x18000
	s_add_i32 s62, 0, 0x1c000
	v_add_u32_e32 v160, s61, v1
	v_add_u32_e32 v188, s62, v1
	ds_read_b128 v[148:151], v160
	ds_read_b128 v[152:155], v160 offset:1024
	ds_read_b128 v[156:159], v160 offset:2048
	ds_read_b128 v[160:163], v160 offset:3072
	ds_read_b128 v[176:179], v188
	ds_read_b128 v[180:183], v188 offset:1024
	ds_read_b128 v[184:187], v188 offset:2048
	ds_read_b128 v[188:191], v188 offset:3072
	s_add_u32 s28, s28, 0x40000
	s_addc_u32 s29, s29, 0
	s_mov_b32 m0, s34
	ds_read_b128 v[192:195], v172 offset:32768
	ds_read_b128 v[196:199], v172 offset:33792
	ds_read_b128 v[200:203], v172 offset:34816
	ds_read_b128 v[204:207], v172 offset:35840
	ds_read_b128 v[208:211], v172 offset:36864
	ds_read_b128 v[212:215], v172 offset:37888
	ds_read_b128 v[216:219], v172 offset:38912
	ds_read_b128 v[220:223], v172 offset:39936
	global_load_lds_dwordx4 v136, s[28:29]
	s_mov_b32 m0, s35
	s_nop 0
	global_load_lds_dwordx4 v132, s[28:29]
	s_waitcnt vmcnt(8)
	s_waitcnt lgkmcnt(0)
	s_barrier
; #define PG8_STAGE_A(b, h, ptr, NX) do { if constexpr (Sched::GATHER) { unsigned gs_[2]; gs_[0] = ((NX) && last_) ? gN[h][0] : gA[h][0]; gs_[1] = ((NX) && last_) ? gN[h][1] : gA[h][1]; PG8_STAGE(PG8_SA(b, h), ptr, gs_); } \
;         else PG8_STAGE(PG8_SA(b, h), (ptr) + ((h) ? hstep : (size_t)0), voffA); } while (0)
; #define PG8_STAGE(bufoff, gbase, voff) do { _Pragma("unroll") for (int _i = 0; _i < 2; ++_i) \
;         __builtin_amdgcn_global_load_lds((const unsigned*)((const char*)(gbase) + (voff)[_i]), (PG8_LAS unsigned*)(lds + (bufoff) + ldsw + _i * 8192), 16, 0, 0); } while (0)
; #define PG8_LDA(dst, b, h) do { _Pragma("unroll") for (int m = 0; m < 4; ++m) _Pragma("unroll") for (int k = 0; k < 2; ++k) dst[m][k] = *(const PG8_LAS bf16x8*)(lds + PG8_SA(b, h) + aoff + m * 2048 + k * 1024); } while (0)
; #define PG8_MMA(ai, bj, At, Bt) do { __builtin_amdgcn_s_setprio(1); _Pragma("unroll") for (int m = 0; m < 4; ++m) _Pragma("unroll") for (int n = 0; n < 2; ++n) _Pragma("unroll") for (int k = 0; k < 2; ++k) \
;         acc[ai][bj][m][n] = __builtin_amdgcn_mfma_f32_16x16x32_bf16(Bt[n][k], At[m][k], acc[ai][bj][m][n], 0, 0, 0); __builtin_amdgcn_s_setprio(0); } while (0)
; #define PG8_WAIT_V(n) asm volatile("s_waitcnt vmcnt(" #n ")" ::: "memory")
; #define PG8_WAIT_L(n) asm volatile("s_waitcnt lgkmcnt(" #n ")" ::: "memory")
; #define PG8_BAR __builtin_amdgcn_s_barrier()
; #define PG8_SCHED __builtin_amdgcn_sched_barrier(0)
; __device__ __forceinline__ void rstd8(const float* SS, int rowb, int lane, float (&rs)[2][4]) {
;     f32x4 p[2][4];
; #pragma unroll
;     for (int ai = 0; ai < 2; ++ai)
; #pragma unroll
;         for (int m = 0; m < 4; ++m) p[ai][m] = *(const f32x4*)(SS + (size_t)(rowb + HALF * ai + 16 * m + (lane >> 2)) * 16 + 4 * (lane & 3));
; template <class Epi, class Sched, bool ALIGN_EPI = false, bool SP2 = false>
; __device__ __forceinline__ void gemm_phase(PG8_LAS unsigned char* lds, const Gemm g, const Sched& S, const Epi& E, const bool skip_epi = false) {
;     ...
;             PG8_WAIT_V(8); PG8_WAIT_L(0); PG8_BAR; PG8_MMA(0, 0, At, B0); PG8_MMA(0, 1, At, B1); PG8_BAR; PG8_SCHED;
;             PG8_LDA(At, 1, 1); PG8_STAGE(PG8_SB(1, 0), b3, voffB); PG8_STAGE(PG8_SB(1, 1), b3 + hstep, voffB); PG8_STAGE_A(1, 0, a3, true);
;             PG8_WAIT_V(8); PG8_WAIT_L(0); PG8_BAR; PG8_MMA(1, 0, At, B0); PG8_MMA(1, 1, At, B1); PG8_BAR; PG8_SCHED;
	s_setprio 3
	s_waitcnt lgkmcnt(0)
	v_mfma_f32_16x16x32_bf16 v[126:129], v[148:151], v[192:195], v[126:129]
	v_mfma_f32_16x16x32_bf16 v[122:125], v[156:159], v[192:195], v[122:125]
	v_mfma_f32_16x16x32_bf16 v[114:117], v[148:151], v[200:203], v[114:117]
	v_mfma_f32_16x16x32_bf16 v[106:109], v[156:159], v[200:203], v[106:109]
	v_mfma_f32_16x16x32_bf16 v[98:101], v[148:151], v[208:211], v[98:101]
	v_mfma_f32_16x16x32_bf16 v[90:93], v[156:159], v[208:211], v[90:93]
	v_mfma_f32_16x16x32_bf16 v[82:85], v[148:151], v[216:219], v[82:85]
	v_mfma_f32_16x16x32_bf16 v[74:77], v[156:159], v[216:219], v[74:77]
	v_mfma_f32_16x16x32_bf16 v[126:129], v[152:155], v[196:199], v[126:129]
	v_mfma_f32_16x16x32_bf16 v[122:125], v[160:163], v[196:199], v[122:125]
	v_mfma_f32_16x16x32_bf16 v[114:117], v[152:155], v[204:207], v[114:117]
	v_mfma_f32_16x16x32_bf16 v[106:109], v[160:163], v[204:207], v[106:109]
	v_mfma_f32_16x16x32_bf16 v[98:101], v[152:155], v[212:215], v[98:101]
	v_mfma_f32_16x16x32_bf16 v[90:93], v[160:163], v[212:215], v[90:93]
	v_mfma_f32_16x16x32_bf16 v[82:85], v[152:155], v[220:223], v[82:85]
	v_mfma_f32_16x16x32_bf16 v[74:77], v[160:163], v[220:223], v[74:77]
	v_mfma_f32_16x16x32_bf16 v[118:121], v[176:179], v[192:195], v[118:121]
	v_mfma_f32_16x16x32_bf16 v[110:113], v[184:187], v[192:195], v[110:113]
	v_mfma_f32_16x16x32_bf16 v[102:105], v[176:179], v[200:203], v[102:105]
	v_mfma_f32_16x16x32_bf16 v[94:97], v[184:187], v[200:203], v[94:97]
	v_mfma_f32_16x16x32_bf16 v[86:89], v[176:179], v[208:211], v[86:89]
	v_mfma_f32_16x16x32_bf16 v[78:81], v[184:187], v[208:211], v[78:81]
	v_mfma_f32_16x16x32_bf16 v[70:73], v[176:179], v[216:219], v[70:73]
	v_mfma_f32_16x16x32_bf16 v[66:69], v[184:187], v[216:219], v[66:69]
	v_mfma_f32_16x16x32_bf16 v[118:121], v[180:183], v[196:199], v[118:121]
	v_mfma_f32_16x16x32_bf16 v[110:113], v[188:191], v[196:199], v[110:113]
	v_mfma_f32_16x16x32_bf16 v[102:105], v[180:183], v[204:207], v[102:105]
	v_mfma_f32_16x16x32_bf16 v[94:97], v[188:191], v[204:207], v[94:97]
	v_mfma_f32_16x16x32_bf16 v[86:89], v[180:183], v[212:215], v[86:89]
	v_mfma_f32_16x16x32_bf16 v[78:81], v[188:191], v[212:215], v[78:81]
	v_mfma_f32_16x16x32_bf16 v[70:73], v[180:183], v[220:223], v[70:73]
	v_mfma_f32_16x16x32_bf16 v[66:69], v[188:191], v[220:223], v[66:69]
	s_setprio 0
	s_barrier
	s_add_i32 s28, s61, s2
	s_add_i32 m0, s28, 0xffffff80
	ds_read_b128 v[192:195], v172 offset:49152
	ds_read_b128 v[196:199], v172 offset:50176
	ds_read_b128 v[200:203], v172 offset:51200
	ds_read_b128 v[204:207], v172 offset:52224
	ds_read_b128 v[208:211], v172 offset:53248
	ds_read_b128 v[212:215], v172 offset:54272
	ds_read_b128 v[216:219], v172 offset:55296
	ds_read_b128 v[220:223], v172 offset:56320
	global_load_lds_dwordx4 v[164:165], off offset:128
	s_add_i32 m0, s28, 0x1f80
	s_add_u32 s26, s26, 0x40080
	s_addc_u32 s27, s27, 0
	s_add_i32 s28, s62, s2
	global_load_lds_dwordx4 v[224:225], off offset:128
	s_mov_b32 m0, s28
	s_nop 0
	global_load_lds_dwordx4 v134, s[26:27]
	s_add_i32 m0, s28, 0x2000
	s_nop 0
	global_load_lds_dwordx4 v130, s[26:27]
	s_add_i32 m0, s37, 0xffffff80
	s_nop 0
	global_load_lds_dwordx4 v[226:227], off offset:128
	s_add_i32 m0, s38, 0xffffff80
	s_nop 0
	global_load_lds_dwordx4 v[230:231], off offset:128
	s_waitcnt vmcnt(8)
	s_waitcnt lgkmcnt(0)
	s_barrier
	s_setprio 3
	s_waitcnt lgkmcnt(0)
	v_mfma_f32_16x16x32_bf16 v[62:65], v[148:151], v[192:195], v[62:65]
	v_mfma_f32_16x16x32_bf16 v[58:61], v[156:159], v[192:195], v[58:61]
	v_mfma_f32_16x16x32_bf16 v[50:53], v[148:151], v[200:203], v[50:53]
	v_mfma_f32_16x16x32_bf16 v[42:45], v[156:159], v[200:203], v[42:45]
	v_mfma_f32_16x16x32_bf16 v[34:37], v[148:151], v[208:211], v[34:37]
	v_mfma_f32_16x16x32_bf16 v[26:29], v[156:159], v[208:211], v[26:29]
	v_mfma_f32_16x16x32_bf16 v[18:21], v[148:151], v[216:219], v[18:21]
	v_mfma_f32_16x16x32_bf16 v[10:13], v[156:159], v[216:219], v[10:13]
	v_mfma_f32_16x16x32_bf16 v[62:65], v[152:155], v[196:199], v[62:65]
	v_mfma_f32_16x16x32_bf16 v[58:61], v[160:163], v[196:199], v[58:61]
	v_mfma_f32_16x16x32_bf16 v[50:53], v[152:155], v[204:207], v[50:53]
	v_mfma_f32_16x16x32_bf16 v[42:45], v[160:163], v[204:207], v[42:45]
	v_mfma_f32_16x16x32_bf16 v[34:37], v[152:155], v[212:215], v[34:37]
	v_mfma_f32_16x16x32_bf16 v[26:29], v[160:163], v[212:215], v[26:29]
	v_mfma_f32_16x16x32_bf16 v[18:21], v[152:155], v[220:223], v[18:21]
	v_mfma_f32_16x16x32_bf16 v[10:13], v[160:163], v[220:223], v[10:13]
	v_mfma_f32_16x16x32_bf16 v[54:57], v[176:179], v[192:195], v[54:57]
	v_mfma_f32_16x16x32_bf16 v[46:49], v[184:187], v[192:195], v[46:49]
	v_mfma_f32_16x16x32_bf16 v[38:41], v[176:179], v[200:203], v[38:41]
	v_mfma_f32_16x16x32_bf16 v[30:33], v[184:187], v[200:203], v[30:33]
	v_mfma_f32_16x16x32_bf16 v[22:25], v[176:179], v[208:211], v[22:25]
	v_mfma_f32_16x16x32_bf16 v[14:17], v[184:187], v[208:211], v[14:17]
	v_mfma_f32_16x16x32_bf16 v[6:9], v[176:179], v[216:219], v[6:9]
	v_mfma_f32_16x16x32_bf16 v[2:5], v[184:187], v[216:219], v[2:5]
	v_mfma_f32_16x16x32_bf16 v[54:57], v[180:183], v[196:199], v[54:57]
	v_mfma_f32_16x16x32_bf16 v[46:49], v[188:191], v[196:199], v[46:49]
	v_mfma_f32_16x16x32_bf16 v[38:41], v[180:183], v[204:207], v[38:41]
	v_mfma_f32_16x16x32_bf16 v[30:33], v[188:191], v[204:207], v[30:33]
	v_mfma_f32_16x16x32_bf16 v[22:25], v[180:183], v[212:215], v[22:25]
	v_mfma_f32_16x16x32_bf16 v[14:17], v[188:191], v[212:215], v[14:17]
	v_mfma_f32_16x16x32_bf16 v[6:9], v[180:183], v[220:223], v[6:9]
	v_mfma_f32_16x16x32_bf16 v[2:5], v[188:191], v[220:223], v[2:5]
	s_setprio 0
	s_barrier
	s_add_i32 s60, s60, 2
	s_add_u32 s24, s24, 0x100
	s_addc_u32 s25, s25, 0
	s_add_u32 s58, s58, 0x100
	s_addc_u32 s59, s59, 0
	s_cmp_gt_u32 s60, 13
	s_cbranch_scc0 .LBB0_253
	v_lshl_add_u32 v164, s22, 8, v167
	v_ashrrev_i32_e32 v165, 31, v164
	v_lshlrev_b64 v[148:149], 6, v[164:165]
	v_lshl_add_u64 v[148:149], v[138:139], 0, v[148:149]
	v_add_co_u32_e32 v150, vcc, 0x2000, v148
	v_addc_co_u32_e32 v151, vcc, 0, v149, vcc
	global_load_dwordx4 v[176:179], v[148:149], off
	global_load_dwordx4 v[180:183], v[148:149], off offset:1024
	global_load_dwordx4 v[184:187], v[148:149], off offset:2048
	global_load_dwordx4 v[188:191], v[148:149], off offset:3072
	global_load_dwordx4 v[192:195], v[150:151], off
	global_load_dwordx4 v[196:199], v[150:151], off offset:1024
	global_load_dwordx4 v[200:203], v[150:151], off offset:2048
	global_load_dwordx4 v[204:207], v[150:151], off offset:3072
	s_and_b64 vcc, exec, s[12:13]
	s_cbranch_vccz .LBB0_256
	s_barrier

; #define PG8_STAGE_A(b, h, ptr, NX) do { if constexpr (Sched::GATHER) { unsigned gs_[2]; gs_[0] = ((NX) && last_) ? gN[h][0] : gA[h][0]; gs_[1] = ((NX) && last_) ? gN[h][1] : gA[h][1]; PG8_STAGE(PG8_SA(b, h), ptr, gs_); } \
;         else PG8_STAGE(PG8_SA(b, h), (ptr) + ((h) ? hstep : (size_t)0), voffA); } while (0)
; #define PG8_STAGE(bufoff, gbase, voff) do { _Pragma("unroll") for (int _i = 0; _i < 2; ++_i) \
;         __builtin_amdgcn_global_load_lds((const unsigned*)((const char*)(gbase) + (voff)[_i]), (PG8_LAS unsigned*)(lds + (bufoff) + ldsw + _i * 8192), 16, 0, 0); } while (0)
; #define PG8_LDA(dst, b, h) do { _Pragma("unroll") for (int m = 0; m < 4; ++m) _Pragma("unroll") for (int k = 0; k < 2; ++k) dst[m][k] = *(const PG8_LAS bf16x8*)(lds + PG8_SA(b, h) + aoff + m * 2048 + k * 1024); } while (0)
; #define PG8_WAIT_V(n) asm volatile("s_waitcnt vmcnt(" #n ")" ::: "memory")
; #define PG8_WAIT_L(n) asm volatile("s_waitcnt lgkmcnt(" #n ")" ::: "memory")
; #define PG8_BAR __builtin_amdgcn_s_barrier()
; template <class Epi, class Sched, bool ALIGN_EPI = false, bool SP2 = false>
; __device__ __forceinline__ void gemm_phase(PG8_LAS unsigned char* lds, const Gemm g, const Sched& S, const Epi& E, const bool skip_epi = false) {
;     ...
;         const char* nA = has_next ? (const char*)g.A + (size_t)nxt.pm * pmstepA + nxt.ko : cA; const char* nB = has_next ? (const char*)g.Bt + (size_t)nxt.pn * tstep + nxt.ko : cB;
;         for (int t = 0; t < nt; t += 2) {
;             const bool last = (t == nt - 2); last_ = last && has_next;
;             const char* a1 = cA + (size_t)(t + 1) * kstep;
;             const char* a2 = last ? nA : cA + (size_t)(t + 2) * kstep; const char* b2 = last ? nB : cB + (size_t)(t + 2) * kstep;
;             const char* a3 = a2 + kstep; const char* b3 = b2 + kstep;
;             if (last && has_next) S.a_ready(nxt);
;             if constexpr (SP2) {
;             PG8_LDB(B0, 0, 0); PG8_LDB(B1, 0, 1); PG8_SCHED; PG8_LDA(At, 0, 0); PG8_STAGE_A(1, 1, a1, false);
;             PG8_WAIT_V(8); PG8_WAIT_L(0); PG8_BAR; PG8_MMA(0, 0, At, B0); PG8_MMA(0, 1, At, B1); PG8_BAR; PG8_SCHED;
;             PG8_LDA(At, 0, 1); PG8_STAGE(PG8_SB(0, 0), b2, voffB); PG8_STAGE(PG8_SB(0, 1), b2 + hstep, voffB); PG8_STAGE_A(0, 0, a2, true);
;             PG8_WAIT_V(8); PG8_WAIT_L(0); PG8_BAR; PG8_MMA(1, 0, At, B0); PG8_MMA(1, 1, At, B1); PG8_BAR; PG8_SCHED;
.LBB0_633:
	s_ashr_i32 s19, s18, 31
	s_lshl_b64 s[20:21], s[18:19], 19
	s_add_u32 s20, s46, s20
	s_addc_u32 s21, s47, s21
	s_and_b64 s[22:23], s[6:7], exec
	s_cselect_b32 s19, s21, s27
	s_cselect_b32 s25, s20, s26
	s_ashr_i32 s17, s16, 31
	s_lshl_b64 s[22:23], s[16:17], 19
	v_readlane_b32 s17, v254, 40
	s_add_u32 s22, s17, s22
	v_readlane_b32 s17, v254, 41
	s_addc_u32 s23, s17, s23
	s_and_b64 s[30:31], s[6:7], exec
	s_cselect_b32 s17, s23, s29
	s_cselect_b32 s60, s22, s28
	s_add_u32 s26, s26, 0x40080
	s_addc_u32 s27, s27, 0
	s_add_u32 s61, s28, 0x100
	s_addc_u32 s62, s29, 0
	s_mov_b32 s63, -2
	s_waitcnt lgkmcnt(0)
	ds_read_b128 v[98:101], v234
	ds_read_b128 v[110:113], v234 offset:1024
	ds_read_b128 v[122:125], v234 offset:2048
	ds_read_b128 v[126:129], v234 offset:3072
	ds_read_b128 v[138:141], v235
	ds_read_b128 v[142:145], v235 offset:1024
	ds_read_b128 v[146:149], v235 offset:2048
	ds_read_b128 v[150:153], v235 offset:3072
	s_add_u32 s28, s26, 0xfffc0080
	s_addc_u32 s29, s27, -1
	s_cmp_eq_u32 s63, 12
	s_cselect_b32 s31, s19, s29
	s_cselect_b32 s30, s25, s28
	s_cselect_b32 s29, s17, s62
	s_cselect_b32 s28, s60, s61
	s_add_i32 m0, s3, 0xc000
	ds_read_b128 v[154:157], v236
	ds_read_b128 v[166:169], v236 offset:1024
	ds_read_b128 v[170:173], v236 offset:2048
	ds_read_b128 v[174:177], v236 offset:3072
	ds_read_b128 v[178:181], v236 offset:4096
	ds_read_b128 v[182:185], v236 offset:5120
	ds_read_b128 v[186:189], v236 offset:6144
	ds_read_b128 v[206:209], v236 offset:7168
	global_load_lds_dwordx4 v198, s[26:27]
	s_add_i32 m0, s3, 0xe000
	s_nop 0
	global_load_lds_dwordx4 v200, s[26:27]
	s_waitcnt vmcnt(8)
	s_waitcnt lgkmcnt(0)
	s_barrier
	s_setprio 3
	s_waitcnt lgkmcnt(0)
	v_mfma_f32_16x16x32_bf16 v[162:165], v[98:101], v[154:157], 0
	v_mfma_f32_16x16x32_bf16 v[158:161], v[122:125], v[154:157], 0
	v_mfma_f32_16x16x32_bf16 v[118:121], v[98:101], v[170:173], 0
	v_mfma_f32_16x16x32_bf16 v[114:117], v[122:125], v[170:173], 0
	v_mfma_f32_16x16x32_bf16 v[94:97], v[98:101], v[178:181], 0
	v_mfma_f32_16x16x32_bf16 v[90:93], v[122:125], v[178:181], 0
	v_mfma_f32_16x16x32_bf16 v[78:81], v[98:101], v[186:189], 0
	v_mfma_f32_16x16x32_bf16 v[74:77], v[122:125], v[186:189], 0
	v_mfma_f32_16x16x32_bf16 v[162:165], v[110:113], v[166:169], v[162:165]
	v_mfma_f32_16x16x32_bf16 v[158:161], v[126:129], v[166:169], v[158:161]
	v_mfma_f32_16x16x32_bf16 v[118:121], v[110:113], v[174:177], v[118:121]
	v_mfma_f32_16x16x32_bf16 v[114:117], v[126:129], v[174:177], v[114:117]
	v_mfma_f32_16x16x32_bf16 v[94:97], v[110:113], v[182:185], v[94:97]
	v_mfma_f32_16x16x32_bf16 v[90:93], v[126:129], v[182:185], v[90:93]
	v_mfma_f32_16x16x32_bf16 v[78:81], v[110:113], v[206:209], v[78:81]
	v_mfma_f32_16x16x32_bf16 v[74:77], v[126:129], v[206:209], v[74:77]
	v_mfma_f32_16x16x32_bf16 v[134:137], v[138:141], v[154:157], 0
	v_mfma_f32_16x16x32_bf16 v[130:133], v[146:149], v[154:157], 0
	v_mfma_f32_16x16x32_bf16 v[106:109], v[138:141], v[170:173], 0
	v_mfma_f32_16x16x32_bf16 v[102:105], v[146:149], v[170:173], 0
	v_mfma_f32_16x16x32_bf16 v[86:89], v[138:141], v[178:181], 0
	v_mfma_f32_16x16x32_bf16 v[82:85], v[146:149], v[178:181], 0
	v_mfma_f32_16x16x32_bf16 v[70:73], v[138:141], v[186:189], 0
	v_mfma_f32_16x16x32_bf16 v[66:69], v[146:149], v[186:189], 0
	v_mfma_f32_16x16x32_bf16 v[134:137], v[142:145], v[166:169], v[134:137]
	v_mfma_f32_16x16x32_bf16 v[130:133], v[150:153], v[166:169], v[130:133]
	v_mfma_f32_16x16x32_bf16 v[106:109], v[142:145], v[174:177], v[106:109]
	v_mfma_f32_16x16x32_bf16 v[102:105], v[150:153], v[174:177], v[102:105]
	v_mfma_f32_16x16x32_bf16 v[86:89], v[142:145], v[182:185], v[86:89]
	v_mfma_f32_16x16x32_bf16 v[82:85], v[150:153], v[182:185], v[82:85]
	v_mfma_f32_16x16x32_bf16 v[70:73], v[142:145], v[206:209], v[70:73]
	v_mfma_f32_16x16x32_bf16 v[66:69], v[150:153], v[206:209], v[66:69]
	s_setprio 0
	s_barrier
	s_add_i32 s64, s57, s2
	v_lshl_add_u64 v[210:211], s[28:29], 0, v[192:193]
	s_mov_b32 m0, s64
	ds_read_b128 v[154:157], v236 offset:16384
	ds_read_b128 v[166:169], v236 offset:17408
	ds_read_b128 v[170:173], v236 offset:18432
	ds_read_b128 v[174:177], v236 offset:19456
	ds_read_b128 v[178:181], v236 offset:20480
	ds_read_b128 v[182:185], v236 offset:21504
	ds_read_b128 v[186:189], v236 offset:22528
	ds_read_b128 v[206:209], v236 offset:23552
	global_load_lds_dwordx4 v[210:211], off
	s_add_i32 m0, s64, 0x2000
	s_add_u32 s64, s28, 0x40000
	v_lshl_add_u64 v[212:213], s[28:29], 0, v[196:197]
	s_addc_u32 s65, s29, 0
	s_add_i32 s66, s58, s2
	global_load_lds_dwordx4 v[212:213], off
	s_mov_b32 m0, s66
	v_lshl_add_u64 v[216:217], s[30:31], 0, v[194:195]
	global_load_lds_dwordx4 v192, s[64:65]
	s_add_i32 m0, s66, 0x2000
	s_nop 0
	global_load_lds_dwordx4 v196, s[64:65]
	v_lshl_add_u64 v[214:215], s[30:31], 0, v[190:191]
	s_mov_b32 m0, s3
	s_nop 0
	global_load_lds_dwordx4 v[214:215], off
	s_mov_b32 m0, s34
	s_nop 0
	global_load_lds_dwordx4 v[216:217], off
	s_waitcnt vmcnt(8)
	s_waitcnt lgkmcnt(0)
	s_barrier
; #define PG8_STAGE_A(b, h, ptr, NX) do { if constexpr (Sched::GATHER) { unsigned gs_[2]; gs_[0] = ((NX) && last_) ? gN[h][0] : gA[h][0]; gs_[1] = ((NX) && last_) ? gN[h][1] : gA[h][1]; PG8_STAGE(PG8_SA(b, h), ptr, gs_); } \
;         else PG8_STAGE(PG8_SA(b, h), (ptr) + ((h) ? hstep : (size_t)0), voffA); } while (0)
; #define PG8_LDA(dst, b, h) do { _Pragma("unroll") for (int m = 0; m < 4; ++m) _Pragma("unroll") for (int k = 0; k < 2; ++k) dst[m][k] = *(const PG8_LAS bf16x8*)(lds + PG8_SA(b, h) + aoff + m * 2048 + k * 1024); } while (0)
; #define PG8_LDB(dst, b, h) do { _Pragma("unroll") for (int n = 0; n < 2; ++n) _Pragma("unroll") for (int k = 0; k < 2; ++k) dst[n][k] = *(const PG8_LAS bf16x8*)(lds + PG8_SB(b, h) + boff + n * 2048 + k * 1024); } while (0)
; #define PG8_MMA(ai, bj, At, Bt) do { __builtin_amdgcn_s_setprio(1); _Pragma("unroll") for (int m = 0; m < 4; ++m) _Pragma("unroll") for (int n = 0; n < 2; ++n) _Pragma("unroll") for (int k = 0; k < 2; ++k) \
;         acc[ai][bj][m][n] = __builtin_amdgcn_mfma_f32_16x16x32_bf16(Bt[n][k], At[m][k], acc[ai][bj][m][n], 0, 0, 0); __builtin_amdgcn_s_setprio(0); } while (0)
; #define PG8_WAIT_V(n) asm volatile("s_waitcnt vmcnt(" #n ")" ::: "memory")
; #define PG8_WAIT_L(n) asm volatile("s_waitcnt lgkmcnt(" #n ")" ::: "memory")
; #define PG8_BAR __builtin_amdgcn_s_barrier()
; #define PG8_SCHED __builtin_amdgcn_sched_barrier(0)
; template <class Epi, class Sched, bool ALIGN_EPI = false, bool SP2 = false>
; __device__ __forceinline__ void gemm_phase(PG8_LAS unsigned char* lds, const Gemm g, const Sched& S, const Epi& E, const bool skip_epi = false) {
;     ...
;             PG8_WAIT_V(8); PG8_WAIT_L(0); PG8_BAR; PG8_MMA(1, 0, At, B0); PG8_MMA(1, 1, At, B1); PG8_BAR; PG8_SCHED;
;             PG8_LDB(B0, 1, 0); PG8_LDB(B1, 1, 1); PG8_SCHED; PG8_LDA(At, 1, 0); PG8_STAGE_A(0, 1, a2, true);
;             PG8_WAIT_V(8); PG8_WAIT_L(0); PG8_BAR; PG8_MMA(0, 0, At, B0); PG8_MMA(0, 1, At, B1); PG8_BAR; PG8_SCHED;
	s_setprio 3
	s_waitcnt lgkmcnt(0)
	v_mfma_f32_16x16x32_bf16 v[62:65], v[98:101], v[154:157], 0
	v_mfma_f32_16x16x32_bf16 v[58:61], v[122:125], v[154:157], 0
	v_mfma_f32_16x16x32_bf16 v[46:49], v[98:101], v[170:173], 0
	v_mfma_f32_16x16x32_bf16 v[42:45], v[122:125], v[170:173], 0
	v_mfma_f32_16x16x32_bf16 v[30:33], v[98:101], v[178:181], 0
	v_mfma_f32_16x16x32_bf16 v[26:29], v[122:125], v[178:181], 0
	v_mfma_f32_16x16x32_bf16 v[14:17], v[98:101], v[186:189], 0
	v_mfma_f32_16x16x32_bf16 v[10:13], v[122:125], v[186:189], 0
	v_mfma_f32_16x16x32_bf16 v[62:65], v[110:113], v[166:169], v[62:65]
	v_mfma_f32_16x16x32_bf16 v[58:61], v[126:129], v[166:169], v[58:61]
	v_mfma_f32_16x16x32_bf16 v[46:49], v[110:113], v[174:177], v[46:49]
	v_mfma_f32_16x16x32_bf16 v[42:45], v[126:129], v[174:177], v[42:45]
	v_mfma_f32_16x16x32_bf16 v[30:33], v[110:113], v[182:185], v[30:33]
	v_mfma_f32_16x16x32_bf16 v[26:29], v[126:129], v[182:185], v[26:29]
	v_mfma_f32_16x16x32_bf16 v[14:17], v[110:113], v[206:209], v[14:17]
	v_mfma_f32_16x16x32_bf16 v[10:13], v[126:129], v[206:209], v[10:13]
	v_mfma_f32_16x16x32_bf16 v[54:57], v[138:141], v[154:157], 0
	v_mfma_f32_16x16x32_bf16 v[50:53], v[146:149], v[154:157], 0
	v_mfma_f32_16x16x32_bf16 v[38:41], v[138:141], v[170:173], 0
	v_mfma_f32_16x16x32_bf16 v[34:37], v[146:149], v[170:173], 0
	v_mfma_f32_16x16x32_bf16 v[22:25], v[138:141], v[178:181], 0
	v_mfma_f32_16x16x32_bf16 v[18:21], v[146:149], v[178:181], 0
	v_mfma_f32_16x16x32_bf16 v[6:9], v[138:141], v[186:189], 0
	v_mfma_f32_16x16x32_bf16 v[2:5], v[146:149], v[186:189], 0
	v_mfma_f32_16x16x32_bf16 v[54:57], v[142:145], v[166:169], v[54:57]
	v_mfma_f32_16x16x32_bf16 v[50:53], v[150:153], v[166:169], v[50:53]
	v_mfma_f32_16x16x32_bf16 v[38:41], v[142:145], v[174:177], v[38:41]
	v_mfma_f32_16x16x32_bf16 v[34:37], v[150:153], v[174:177], v[34:37]
	v_mfma_f32_16x16x32_bf16 v[22:25], v[142:145], v[182:185], v[22:25]
	v_mfma_f32_16x16x32_bf16 v[18:21], v[150:153], v[182:185], v[18:21]
	v_mfma_f32_16x16x32_bf16 v[6:9], v[142:145], v[206:209], v[6:9]
	v_mfma_f32_16x16x32_bf16 v[2:5], v[150:153], v[206:209], v[2:5]
	s_setprio 0
	s_barrier
	s_add_i32 s64, 0, 0x18000
	s_add_i32 s65, 0, 0x1c000
	v_add_u32_e32 v126, s64, v229
	v_add_u32_e32 v150, s65, v229
	ds_read_b128 v[98:101], v126
	ds_read_b128 v[110:113], v126 offset:1024
	ds_read_b128 v[122:125], v126 offset:2048
	ds_read_b128 v[126:129], v126 offset:3072
	ds_read_b128 v[138:141], v150
	ds_read_b128 v[142:145], v150 offset:1024
	ds_read_b128 v[146:149], v150 offset:2048
	ds_read_b128 v[150:153], v150 offset:3072
	s_add_u32 s30, s30, 0x40000
	s_addc_u32 s31, s31, 0
	s_mov_b32 m0, s35
	ds_read_b128 v[154:157], v236 offset:32768
	ds_read_b128 v[166:169], v236 offset:33792
	ds_read_b128 v[170:173], v236 offset:34816
	ds_read_b128 v[174:177], v236 offset:35840
	ds_read_b128 v[178:181], v236 offset:36864
	ds_read_b128 v[182:185], v236 offset:37888
	ds_read_b128 v[186:189], v236 offset:38912
	ds_read_b128 v[206:209], v236 offset:39936
	global_load_lds_dwordx4 v190, s[30:31]
	s_mov_b32 m0, s36
	s_nop 0
	global_load_lds_dwordx4 v194, s[30:31]
	s_waitcnt vmcnt(8)
	s_waitcnt lgkmcnt(0)
	s_barrier
	s_setprio 3
	s_waitcnt lgkmcnt(0)
	v_mfma_f32_16x16x32_bf16 v[162:165], v[98:101], v[154:157], v[162:165]
	v_mfma_f32_16x16x32_bf16 v[158:161], v[122:125], v[154:157], v[158:161]
	v_mfma_f32_16x16x32_bf16 v[118:121], v[98:101], v[170:173], v[118:121]
	v_mfma_f32_16x16x32_bf16 v[114:117], v[122:125], v[170:173], v[114:117]
	v_mfma_f32_16x16x32_bf16 v[94:97], v[98:101], v[178:181], v[94:97]
	v_mfma_f32_16x16x32_bf16 v[90:93], v[122:125], v[178:181], v[90:93]
	v_mfma_f32_16x16x32_bf16 v[78:81], v[98:101], v[186:189], v[78:81]
	v_mfma_f32_16x16x32_bf16 v[74:77], v[122:125], v[186:189], v[74:77]
	v_mfma_f32_16x16x32_bf16 v[162:165], v[110:113], v[166:169], v[162:165]
	v_mfma_f32_16x16x32_bf16 v[158:161], v[126:129], v[166:169], v[158:161]
	v_mfma_f32_16x16x32_bf16 v[118:121], v[110:113], v[174:177], v[118:121]
	v_mfma_f32_16x16x32_bf16 v[114:117], v[126:129], v[174:177], v[114:117]
	v_mfma_f32_16x16x32_bf16 v[94:97], v[110:113], v[182:185], v[94:97]
	v_mfma_f32_16x16x32_bf16 v[90:93], v[126:129], v[182:185], v[90:93]
	v_mfma_f32_16x16x32_bf16 v[78:81], v[110:113], v[206:209], v[78:81]
	v_mfma_f32_16x16x32_bf16 v[74:77], v[126:129], v[206:209], v[74:77]
	v_mfma_f32_16x16x32_bf16 v[134:137], v[138:141], v[154:157], v[134:137]
	v_mfma_f32_16x16x32_bf16 v[130:133], v[146:149], v[154:157], v[130:133]
	v_mfma_f32_16x16x32_bf16 v[106:109], v[138:141], v[170:173], v[106:109]
	v_mfma_f32_16x16x32_bf16 v[102:105], v[146:149], v[170:173], v[102:105]
	v_mfma_f32_16x16x32_bf16 v[86:89], v[138:141], v[178:181], v[86:89]
	v_mfma_f32_16x16x32_bf16 v[82:85], v[146:149], v[178:181], v[82:85]
	v_mfma_f32_16x16x32_bf16 v[70:73], v[138:141], v[186:189], v[70:73]
	v_mfma_f32_16x16x32_bf16 v[66:69], v[146:149], v[186:189], v[66:69]
	v_mfma_f32_16x16x32_bf16 v[134:137], v[142:145], v[166:169], v[134:137]
	v_mfma_f32_16x16x32_bf16 v[130:133], v[150:153], v[166:169], v[130:133]
	v_mfma_f32_16x16x32_bf16 v[106:109], v[142:145], v[174:177], v[106:109]
	v_mfma_f32_16x16x32_bf16 v[102:105], v[150:153], v[174:177], v[102:105]
	v_mfma_f32_16x16x32_bf16 v[86:89], v[142:145], v[182:185], v[86:89]
	v_mfma_f32_16x16x32_bf16 v[82:85], v[150:153], v[182:185], v[82:85]
	v_mfma_f32_16x16x32_bf16 v[70:73], v[142:145], v[206:209], v[70:73]
	v_mfma_f32_16x16x32_bf16 v[66:69], v[150:153], v[206:209], v[66:69]
	s_setprio 0
	s_barrier
; #define PG8_STAGE_A(b, h, ptr, NX) do { if constexpr (Sched::GATHER) { unsigned gs_[2]; gs_[0] = ((NX) && last_) ? gN[h][0] : gA[h][0]; gs_[1] = ((NX) && last_) ? gN[h][1] : gA[h][1]; PG8_STAGE(PG8_SA(b, h), ptr, gs_); } \
;         else PG8_STAGE(PG8_SA(b, h), (ptr) + ((h) ? hstep : (size_t)0), voffA); } while (0)
; #define PG8_STAGE(bufoff, gbase, voff) do { _Pragma("unroll") for (int _i = 0; _i < 2; ++_i) \
;         __builtin_amdgcn_global_load_lds((const unsigned*)((const char*)(gbase) + (voff)[_i]), (PG8_LAS unsigned*)(lds + (bufoff) + ldsw + _i * 8192), 16, 0, 0); } while (0)
; #define PG8_LDA(dst, b, h) do { _Pragma("unroll") for (int m = 0; m < 4; ++m) _Pragma("unroll") for (int k = 0; k < 2; ++k) dst[m][k] = *(const PG8_LAS bf16x8*)(lds + PG8_SA(b, h) + aoff + m * 2048 + k * 1024); } while (0)
; #define PG8_LDB(dst, b, h) do { _Pragma("unroll") for (int n = 0; n < 2; ++n) _Pragma("unroll") for (int k = 0; k < 2; ++k) dst[n][k] = *(const PG8_LAS bf16x8*)(lds + PG8_SB(b, h) + boff + n * 2048 + k * 1024); } while (0)
; #define PG8_WAIT_V(n) asm volatile("s_waitcnt vmcnt(" #n ")" ::: "memory")
; #define PG8_BAR __builtin_amdgcn_s_barrier()
; template <class Epi, class Sched, bool ALIGN_EPI = false, bool SP2 = false>
; __device__ __forceinline__ void gemm_phase(PG8_LAS unsigned char* lds, const Gemm g, const Sched& S, const Epi& E, const bool skip_epi = false) {
;     ...
;             PG8_LDB(B0, 0, 0); PG8_LDB(B1, 0, 1); PG8_SCHED; PG8_LDA(At, 0, 0); PG8_STAGE_A(1, 1, a1, false);
;             PG8_WAIT_V(8); PG8_WAIT_L(0); PG8_BAR; PG8_MMA(0, 0, At, B0); PG8_MMA(0, 1, At, B1); PG8_BAR; PG8_SCHED;
;             PG8_LDA(At, 0, 1); PG8_STAGE(PG8_SB(0, 0), b2, voffB); PG8_STAGE(PG8_SB(0, 1), b2 + hstep, voffB); PG8_STAGE_A(0, 0, a2, true);
;             PG8_WAIT_V(8); PG8_WAIT_L(0); PG8_BAR; PG8_MMA(1, 0, At, B0); PG8_MMA(1, 1, At, B1); PG8_BAR; PG8_SCHED;
;             PG8_LDB(B0, 1, 0); PG8_LDB(B1, 1, 1); PG8_SCHED; PG8_LDA(At, 1, 0); PG8_STAGE_A(0, 1, a2, true);
;             PG8_WAIT_V(8); PG8_WAIT_L(0); PG8_BAR; PG8_MMA(0, 0, At, B0); PG8_MMA(0, 1, At, B1); PG8_BAR; PG8_SCHED;
;             PG8_LDA(At, 1, 1); PG8_STAGE(PG8_SB(1, 0), b3, voffB); PG8_STAGE(PG8_SB(1, 1), b3 + hstep, voffB); PG8_STAGE_A(1, 0, a3, true);
;             PG8_WAIT_V(8); PG8_WAIT_L(0); PG8_BAR; PG8_MMA(1, 0, At, B0); PG8_MMA(1, 1, At, B1); PG8_BAR; PG8_SCHED;
	s_add_i32 s30, s64, s2
	s_add_i32 m0, s30, 0xffffff80
	ds_read_b128 v[154:157], v236 offset:49152
	ds_read_b128 v[166:169], v236 offset:50176
	ds_read_b128 v[170:173], v236 offset:51200
	ds_read_b128 v[174:177], v236 offset:52224
	ds_read_b128 v[178:181], v236 offset:53248
	ds_read_b128 v[182:185], v236 offset:54272
	ds_read_b128 v[186:189], v236 offset:55296
	ds_read_b128 v[206:209], v236 offset:56320
	global_load_lds_dwordx4 v[210:211], off offset:128
	s_add_i32 m0, s30, 0x1f80
	s_add_u32 s28, s28, 0x40080
	s_addc_u32 s29, s29, 0
	s_add_i32 s30, s65, s2
	global_load_lds_dwordx4 v[212:213], off offset:128
	s_mov_b32 m0, s30
	s_nop 0
	global_load_lds_dwordx4 v192, s[28:29]
	s_add_i32 m0, s30, 0x2000
	s_nop 0
	global_load_lds_dwordx4 v196, s[28:29]
	s_add_i32 m0, s39, 0xffffff80
	s_nop 0
	global_load_lds_dwordx4 v[214:215], off offset:128
	s_add_i32 m0, s48, 0xffffff80
	s_nop 0
	global_load_lds_dwordx4 v[216:217], off offset:128
	s_waitcnt vmcnt(8)
	s_waitcnt lgkmcnt(0)
	s_barrier
	s_setprio 3
	s_waitcnt lgkmcnt(0)
	v_mfma_f32_16x16x32_bf16 v[62:65], v[98:101], v[154:157], v[62:65]
	v_mfma_f32_16x16x32_bf16 v[58:61], v[122:125], v[154:157], v[58:61]
	v_mfma_f32_16x16x32_bf16 v[46:49], v[98:101], v[170:173], v[46:49]
	v_mfma_f32_16x16x32_bf16 v[42:45], v[122:125], v[170:173], v[42:45]
	v_mfma_f32_16x16x32_bf16 v[30:33], v[98:101], v[178:181], v[30:33]
	v_mfma_f32_16x16x32_bf16 v[26:29], v[122:125], v[178:181], v[26:29]
	v_mfma_f32_16x16x32_bf16 v[14:17], v[98:101], v[186:189], v[14:17]
	v_mfma_f32_16x16x32_bf16 v[10:13], v[122:125], v[186:189], v[10:13]
	v_mfma_f32_16x16x32_bf16 v[62:65], v[110:113], v[166:169], v[62:65]
	v_mfma_f32_16x16x32_bf16 v[58:61], v[126:129], v[166:169], v[58:61]
	v_mfma_f32_16x16x32_bf16 v[46:49], v[110:113], v[174:177], v[46:49]
	v_mfma_f32_16x16x32_bf16 v[42:45], v[126:129], v[174:177], v[42:45]
	v_mfma_f32_16x16x32_bf16 v[30:33], v[110:113], v[182:185], v[30:33]
	v_mfma_f32_16x16x32_bf16 v[26:29], v[126:129], v[182:185], v[26:29]
	v_mfma_f32_16x16x32_bf16 v[14:17], v[110:113], v[206:209], v[14:17]
	v_mfma_f32_16x16x32_bf16 v[10:13], v[126:129], v[206:209], v[10:13]
	v_mfma_f32_16x16x32_bf16 v[54:57], v[138:141], v[154:157], v[54:57]
	v_mfma_f32_16x16x32_bf16 v[50:53], v[146:149], v[154:157], v[50:53]
	v_mfma_f32_16x16x32_bf16 v[38:41], v[138:141], v[170:173], v[38:41]
	v_mfma_f32_16x16x32_bf16 v[34:37], v[146:149], v[170:173], v[34:37]
	v_mfma_f32_16x16x32_bf16 v[22:25], v[138:141], v[178:181], v[22:25]
	v_mfma_f32_16x16x32_bf16 v[18:21], v[146:149], v[178:181], v[18:21]
	v_mfma_f32_16x16x32_bf16 v[6:9], v[138:141], v[186:189], v[6:9]
	v_mfma_f32_16x16x32_bf16 v[2:5], v[146:149], v[186:189], v[2:5]
	v_mfma_f32_16x16x32_bf16 v[54:57], v[142:145], v[166:169], v[54:57]
	v_mfma_f32_16x16x32_bf16 v[50:53], v[150:153], v[166:169], v[50:53]
	v_mfma_f32_16x16x32_bf16 v[38:41], v[142:145], v[174:177], v[38:41]
	v_mfma_f32_16x16x32_bf16 v[34:37], v[150:153], v[174:177], v[34:37]
	v_mfma_f32_16x16x32_bf16 v[22:25], v[142:145], v[182:185], v[22:25]
	v_mfma_f32_16x16x32_bf16 v[18:21], v[150:153], v[182:185], v[18:21]
	v_mfma_f32_16x16x32_bf16 v[6:9], v[142:145], v[206:209], v[6:9]
	v_mfma_f32_16x16x32_bf16 v[2:5], v[150:153], v[206:209], v[2:5]
	s_setprio 0
	s_barrier
	s_add_i32 s63, s63, 2
	s_add_u32 s26, s26, 0x100
	s_addc_u32 s27, s27, 0
	s_add_u32 s61, s61, 0x100
	s_addc_u32 s62, s62, 0
	s_cmp_gt_u32 s63, 13
.LBB0_634:
	ds_read_b128 v[98:101], v234
	ds_read_b128 v[110:113], v234 offset:1024
	ds_read_b128 v[122:125], v234 offset:2048
	ds_read_b128 v[126:129], v234 offset:3072
	ds_read_b128 v[138:141], v235
	ds_read_b128 v[142:145], v235 offset:1024
	ds_read_b128 v[146:149], v235 offset:2048
	ds_read_b128 v[150:153], v235 offset:3072
	s_add_u32 s28, s26, 0xfffc0080
	s_addc_u32 s29, s27, -1
	s_cmp_eq_u32 s63, 12
	s_cselect_b32 s31, s19, s29
	s_cselect_b32 s30, s25, s28
	s_cselect_b32 s29, s17, s62
	s_cselect_b32 s28, s60, s61
	s_add_i32 m0, s3, 0xc000
	ds_read_b128 v[154:157], v236
	ds_read_b128 v[166:169], v236 offset:1024
	ds_read_b128 v[170:173], v236 offset:2048
	ds_read_b128 v[174:177], v236 offset:3072
	ds_read_b128 v[178:181], v236 offset:4096
	ds_read_b128 v[182:185], v236 offset:5120
	ds_read_b128 v[186:189], v236 offset:6144
	ds_read_b128 v[206:209], v236 offset:7168
	global_load_lds_dwordx4 v198, s[26:27]
	s_add_i32 m0, s3, 0xe000
	s_nop 0
	global_load_lds_dwordx4 v200, s[26:27]
	s_waitcnt vmcnt(8)
	s_waitcnt lgkmcnt(0)
	s_barrier
	s_setprio 3
	s_waitcnt lgkmcnt(0)
	v_mfma_f32_16x16x32_bf16 v[162:165], v[98:101], v[154:157], v[162:165]
	v_mfma_f32_16x16x32_bf16 v[158:161], v[122:125], v[154:157], v[158:161]
	v_mfma_f32_16x16x32_bf16 v[118:121], v[98:101], v[170:173], v[118:121]
	v_mfma_f32_16x16x32_bf16 v[114:117], v[122:125], v[170:173], v[114:117]
	v_mfma_f32_16x16x32_bf16 v[94:97], v[98:101], v[178:181], v[94:97]
	v_mfma_f32_16x16x32_bf16 v[90:93], v[122:125], v[178:181], v[90:93]
	v_mfma_f32_16x16x32_bf16 v[78:81], v[98:101], v[186:189], v[78:81]
	v_mfma_f32_16x16x32_bf16 v[74:77], v[122:125], v[186:189], v[74:77]
	v_mfma_f32_16x16x32_bf16 v[162:165], v[110:113], v[166:169], v[162:165]
	v_mfma_f32_16x16x32_bf16 v[158:161], v[126:129], v[166:169], v[158:161]
	v_mfma_f32_16x16x32_bf16 v[118:121], v[110:113], v[174:177], v[118:121]
	v_mfma_f32_16x16x32_bf16 v[114:117], v[126:129], v[174:177], v[114:117]
	v_mfma_f32_16x16x32_bf16 v[94:97], v[110:113], v[182:185], v[94:97]
	v_mfma_f32_16x16x32_bf16 v[90:93], v[126:129], v[182:185], v[90:93]
	v_mfma_f32_16x16x32_bf16 v[78:81], v[110:113], v[206:209], v[78:81]
	v_mfma_f32_16x16x32_bf16 v[74:77], v[126:129], v[206:209], v[74:77]
	v_mfma_f32_16x16x32_bf16 v[134:137], v[138:141], v[154:157], v[134:137]
	v_mfma_f32_16x16x32_bf16 v[130:133], v[146:149], v[154:157], v[130:133]
	v_mfma_f32_16x16x32_bf16 v[106:109], v[138:141], v[170:173], v[106:109]
	v_mfma_f32_16x16x32_bf16 v[102:105], v[146:149], v[170:173], v[102:105]
	v_mfma_f32_16x16x32_bf16 v[86:89], v[138:141], v[178:181], v[86:89]
	v_mfma_f32_16x16x32_bf16 v[82:85], v[146:149], v[178:181], v[82:85]
	v_mfma_f32_16x16x32_bf16 v[70:73], v[138:141], v[186:189], v[70:73]
	v_mfma_f32_16x16x32_bf16 v[66:69], v[146:149], v[186:189], v[66:69]
	v_mfma_f32_16x16x32_bf16 v[134:137], v[142:145], v[166:169], v[134:137]
	v_mfma_f32_16x16x32_bf16 v[130:133], v[150:153], v[166:169], v[130:133]
	v_mfma_f32_16x16x32_bf16 v[106:109], v[142:145], v[174:177], v[106:109]
	v_mfma_f32_16x16x32_bf16 v[102:105], v[150:153], v[174:177], v[102:105]
	v_mfma_f32_16x16x32_bf16 v[86:89], v[142:145], v[182:185], v[86:89]
	v_mfma_f32_16x16x32_bf16 v[82:85], v[150:153], v[182:185], v[82:85]
	v_mfma_f32_16x16x32_bf16 v[70:73], v[142:145], v[206:209], v[70:73]
	v_mfma_f32_16x16x32_bf16 v[66:69], v[150:153], v[206:209], v[66:69]
	s_setprio 0
	s_barrier
; #define PG8_STAGE_A(b, h, ptr, NX) do { if constexpr (Sched::GATHER) { unsigned gs_[2]; gs_[0] = ((NX) && last_) ? gN[h][0] : gA[h][0]; gs_[1] = ((NX) && last_) ? gN[h][1] : gA[h][1]; PG8_STAGE(PG8_SA(b, h), ptr, gs_); } \
;         else PG8_STAGE(PG8_SA(b, h), (ptr) + ((h) ? hstep : (size_t)0), voffA); } while (0)
; #define PG8_STAGE(bufoff, gbase, voff) do { _Pragma("unroll") for (int _i = 0; _i < 2; ++_i) \
;         __builtin_amdgcn_global_load_lds((const unsigned*)((const char*)(gbase) + (voff)[_i]), (PG8_LAS unsigned*)(lds + (bufoff) + ldsw + _i * 8192), 16, 0, 0); } while (0)
; #define PG8_LDA(dst, b, h) do { _Pragma("unroll") for (int m = 0; m < 4; ++m) _Pragma("unroll") for (int k = 0; k < 2; ++k) dst[m][k] = *(const PG8_LAS bf16x8*)(lds + PG8_SA(b, h) + aoff + m * 2048 + k * 1024); } while (0)
; #define PG8_LDB(dst, b, h) do { _Pragma("unroll") for (int n = 0; n < 2; ++n) _Pragma("unroll") for (int k = 0; k < 2; ++k) dst[n][k] = *(const PG8_LAS bf16x8*)(lds + PG8_SB(b, h) + boff + n * 2048 + k * 1024); } while (0)
; #define PG8_MMA(ai, bj, At, Bt) do { __builtin_amdgcn_s_setprio(1); _Pragma("unroll") for (int m = 0; m < 4; ++m) _Pragma("unroll") for (int n = 0; n < 2; ++n) _Pragma("unroll") for (int k = 0; k < 2; ++k) \
;         acc[ai][bj][m][n] = __builtin_amdgcn_mfma_f32_16x16x32_bf16(Bt[n][k], At[m][k], acc[ai][bj][m][n], 0, 0, 0); __builtin_amdgcn_s_setprio(0); } while (0)
; #define PG8_WAIT_V(n) asm volatile("s_waitcnt vmcnt(" #n ")" ::: "memory")
; #define PG8_WAIT_L(n) asm volatile("s_waitcnt lgkmcnt(" #n ")" ::: "memory")
; #define PG8_BAR __builtin_amdgcn_s_barrier()
; #define PG8_SCHED __builtin_amdgcn_sched_barrier(0)
; template <class Epi, class Sched, bool ALIGN_EPI = false, bool SP2 = false>
; __device__ __forceinline__ void gemm_phase(PG8_LAS unsigned char* lds, const Gemm g, const Sched& S, const Epi& E, const bool skip_epi = false) {
;     ...
;             PG8_LDA(At, 0, 1); PG8_STAGE(PG8_SB(0, 0), b2, voffB); PG8_STAGE(PG8_SB(0, 1), b2 + hstep, voffB); PG8_STAGE_A(0, 0, a2, true);
;             PG8_WAIT_V(8); PG8_WAIT_L(0); PG8_BAR; PG8_MMA(1, 0, At, B0); PG8_MMA(1, 1, At, B1); PG8_BAR; PG8_SCHED;
;             PG8_LDB(B0, 1, 0); PG8_LDB(B1, 1, 1); PG8_SCHED; PG8_LDA(At, 1, 0); PG8_STAGE_A(0, 1, a2, true);
;             PG8_WAIT_V(8); PG8_WAIT_L(0); PG8_BAR; PG8_MMA(0, 0, At, B0); PG8_MMA(0, 1, At, B1); PG8_BAR; PG8_SCHED;
	s_add_i32 s64, s57, s2
	v_lshl_add_u64 v[210:211], s[28:29], 0, v[192:193]
	s_mov_b32 m0, s64
	ds_read_b128 v[154:157], v236 offset:16384
	ds_read_b128 v[166:169], v236 offset:17408
	ds_read_b128 v[170:173], v236 offset:18432
	ds_read_b128 v[174:177], v236 offset:19456
	ds_read_b128 v[178:181], v236 offset:20480
	ds_read_b128 v[182:185], v236 offset:21504
	ds_read_b128 v[186:189], v236 offset:22528
	ds_read_b128 v[206:209], v236 offset:23552
	global_load_lds_dwordx4 v[210:211], off
	s_add_i32 m0, s64, 0x2000
	s_add_u32 s64, s28, 0x40000
	v_lshl_add_u64 v[212:213], s[28:29], 0, v[196:197]
	s_addc_u32 s65, s29, 0
	s_add_i32 s66, s58, s2
	global_load_lds_dwordx4 v[212:213], off
	s_mov_b32 m0, s66
	v_lshl_add_u64 v[216:217], s[30:31], 0, v[194:195]
	global_load_lds_dwordx4 v192, s[64:65]
	s_add_i32 m0, s66, 0x2000
	s_nop 0
	global_load_lds_dwordx4 v196, s[64:65]
	v_lshl_add_u64 v[214:215], s[30:31], 0, v[190:191]
	s_mov_b32 m0, s3
	s_nop 0
	global_load_lds_dwordx4 v[214:215], off
	s_mov_b32 m0, s34
	s_nop 0
	global_load_lds_dwordx4 v[216:217], off
	s_waitcnt vmcnt(8)
	s_waitcnt lgkmcnt(0)
	s_barrier
	s_setprio 3
	s_waitcnt lgkmcnt(0)
	v_mfma_f32_16x16x32_bf16 v[62:65], v[98:101], v[154:157], v[62:65]
	v_mfma_f32_16x16x32_bf16 v[58:61], v[122:125], v[154:157], v[58:61]
	v_mfma_f32_16x16x32_bf16 v[46:49], v[98:101], v[170:173], v[46:49]
	v_mfma_f32_16x16x32_bf16 v[42:45], v[122:125], v[170:173], v[42:45]
	v_mfma_f32_16x16x32_bf16 v[30:33], v[98:101], v[178:181], v[30:33]
	v_mfma_f32_16x16x32_bf16 v[26:29], v[122:125], v[178:181], v[26:29]
	v_mfma_f32_16x16x32_bf16 v[14:17], v[98:101], v[186:189], v[14:17]
	v_mfma_f32_16x16x32_bf16 v[10:13], v[122:125], v[186:189], v[10:13]
	v_mfma_f32_16x16x32_bf16 v[62:65], v[110:113], v[166:169], v[62:65]
	v_mfma_f32_16x16x32_bf16 v[58:61], v[126:129], v[166:169], v[58:61]
	v_mfma_f32_16x16x32_bf16 v[46:49], v[110:113], v[174:177], v[46:49]
	v_mfma_f32_16x16x32_bf16 v[42:45], v[126:129], v[174:177], v[42:45]
	v_mfma_f32_16x16x32_bf16 v[30:33], v[110:113], v[182:185], v[30:33]
	v_mfma_f32_16x16x32_bf16 v[26:29], v[126:129], v[182:185], v[26:29]
	v_mfma_f32_16x16x32_bf16 v[14:17], v[110:113], v[206:209], v[14:17]
	v_mfma_f32_16x16x32_bf16 v[10:13], v[126:129], v[206:209], v[10:13]
	v_mfma_f32_16x16x32_bf16 v[54:57], v[138:141], v[154:157], v[54:57]
	v_mfma_f32_16x16x32_bf16 v[50:53], v[146:149], v[154:157], v[50:53]
	v_mfma_f32_16x16x32_bf16 v[38:41], v[138:141], v[170:173], v[38:41]
	v_mfma_f32_16x16x32_bf16 v[34:37], v[146:149], v[170:173], v[34:37]
	v_mfma_f32_16x16x32_bf16 v[22:25], v[138:141], v[178:181], v[22:25]
	v_mfma_f32_16x16x32_bf16 v[18:21], v[146:149], v[178:181], v[18:21]
	v_mfma_f32_16x16x32_bf16 v[6:9], v[138:141], v[186:189], v[6:9]
	v_mfma_f32_16x16x32_bf16 v[2:5], v[146:149], v[186:189], v[2:5]
	v_mfma_f32_16x16x32_bf16 v[54:57], v[142:145], v[166:169], v[54:57]
	v_mfma_f32_16x16x32_bf16 v[50:53], v[150:153], v[166:169], v[50:53]
	v_mfma_f32_16x16x32_bf16 v[38:41], v[142:145], v[174:177], v[38:41]
	v_mfma_f32_16x16x32_bf16 v[34:37], v[150:153], v[174:177], v[34:37]
	v_mfma_f32_16x16x32_bf16 v[22:25], v[142:145], v[182:185], v[22:25]
	v_mfma_f32_16x16x32_bf16 v[18:21], v[150:153], v[182:185], v[18:21]
	v_mfma_f32_16x16x32_bf16 v[6:9], v[142:145], v[206:209], v[6:9]
	v_mfma_f32_16x16x32_bf16 v[2:5], v[150:153], v[206:209], v[2:5]
	s_setprio 0
	s_barrier
	s_add_i32 s64, 0, 0x18000
	s_add_i32 s65, 0, 0x1c000
	v_add_u32_e32 v126, s64, v229
	v_add_u32_e32 v150, s65, v229
	ds_read_b128 v[98:101], v126
	ds_read_b128 v[110:113], v126 offset:1024
	ds_read_b128 v[122:125], v126 offset:2048
	ds_read_b128 v[126:129], v126 offset:3072
	ds_read_b128 v[138:141], v150
	ds_read_b128 v[142:145], v150 offset:1024
	ds_read_b128 v[146:149], v150 offset:2048
	ds_read_b128 v[150:153], v150 offset:3072
	s_add_u32 s30, s30, 0x40000
	s_addc_u32 s31, s31, 0
	s_mov_b32 m0, s35
	ds_read_b128 v[154:157], v236 offset:32768
	ds_read_b128 v[166:169], v236 offset:33792
	ds_read_b128 v[170:173], v236 offset:34816
	ds_read_b128 v[174:177], v236 offset:35840
	ds_read_b128 v[178:181], v236 offset:36864
	ds_read_b128 v[182:185], v236 offset:37888
	ds_read_b128 v[186:189], v236 offset:38912
	ds_read_b128 v[206:209], v236 offset:39936
	global_load_lds_dwordx4 v190, s[30:31]
	s_mov_b32 m0, s36
	s_nop 0
	global_load_lds_dwordx4 v194, s[30:31]
	s_waitcnt vmcnt(8)
	s_waitcnt lgkmcnt(0)
	s_barrier
; #define PG8_STAGE_A(b, h, ptr, NX) do { if constexpr (Sched::GATHER) { unsigned gs_[2]; gs_[0] = ((NX) && last_) ? gN[h][0] : gA[h][0]; gs_[1] = ((NX) && last_) ? gN[h][1] : gA[h][1]; PG8_STAGE(PG8_SA(b, h), ptr, gs_); } \
;         else PG8_STAGE(PG8_SA(b, h), (ptr) + ((h) ? hstep : (size_t)0), voffA); } while (0)
; #define PG8_STAGE(bufoff, gbase, voff) do { _Pragma("unroll") for (int _i = 0; _i < 2; ++_i) \
;         __builtin_amdgcn_global_load_lds((const unsigned*)((const char*)(gbase) + (voff)[_i]), (PG8_LAS unsigned*)(lds + (bufoff) + ldsw + _i * 8192), 16, 0, 0); } while (0)
; #define PG8_LDA(dst, b, h) do { _Pragma("unroll") for (int m = 0; m < 4; ++m) _Pragma("unroll") for (int k = 0; k < 2; ++k) dst[m][k] = *(const PG8_LAS bf16x8*)(lds + PG8_SA(b, h) + aoff + m * 2048 + k * 1024); } while (0)
; #define PG8_MMA(ai, bj, At, Bt) do { __builtin_amdgcn_s_setprio(1); _Pragma("unroll") for (int m = 0; m < 4; ++m) _Pragma("unroll") for (int n = 0; n < 2; ++n) _Pragma("unroll") for (int k = 0; k < 2; ++k) \
;         acc[ai][bj][m][n] = __builtin_amdgcn_mfma_f32_16x16x32_bf16(Bt[n][k], At[m][k], acc[ai][bj][m][n], 0, 0, 0); __builtin_amdgcn_s_setprio(0); } while (0)
; #define PG8_WAIT_V(n) asm volatile("s_waitcnt vmcnt(" #n ")" ::: "memory")
; #define PG8_WAIT_L(n) asm volatile("s_waitcnt lgkmcnt(" #n ")" ::: "memory")
; #define PG8_BAR __builtin_amdgcn_s_barrier()
; #define PG8_SCHED __builtin_amdgcn_sched_barrier(0)
; template <class Epi, class Sched, bool ALIGN_EPI = false, bool SP2 = false>
; __device__ __forceinline__ void gemm_phase(PG8_LAS unsigned char* lds, const Gemm g, const Sched& S, const Epi& E, const bool skip_epi = false) {
;     ...
;             PG8_WAIT_V(8); PG8_WAIT_L(0); PG8_BAR; PG8_MMA(0, 0, At, B0); PG8_MMA(0, 1, At, B1); PG8_BAR; PG8_SCHED;
;             PG8_LDA(At, 1, 1); PG8_STAGE(PG8_SB(1, 0), b3, voffB); PG8_STAGE(PG8_SB(1, 1), b3 + hstep, voffB); PG8_STAGE_A(1, 0, a3, true);
;             PG8_WAIT_V(8); PG8_WAIT_L(0); PG8_BAR; PG8_MMA(1, 0, At, B0); PG8_MMA(1, 1, At, B1); PG8_BAR; PG8_SCHED;
;     ...
;         if constexpr (ALIGN_EPI) { if (wr == 0) PG8_BAR; }
	s_setprio 3
	s_waitcnt lgkmcnt(0)
	v_mfma_f32_16x16x32_bf16 v[162:165], v[98:101], v[154:157], v[162:165]
	v_mfma_f32_16x16x32_bf16 v[158:161], v[122:125], v[154:157], v[158:161]
	v_mfma_f32_16x16x32_bf16 v[118:121], v[98:101], v[170:173], v[118:121]
	v_mfma_f32_16x16x32_bf16 v[114:117], v[122:125], v[170:173], v[114:117]
	v_mfma_f32_16x16x32_bf16 v[94:97], v[98:101], v[178:181], v[94:97]
	v_mfma_f32_16x16x32_bf16 v[90:93], v[122:125], v[178:181], v[90:93]
	v_mfma_f32_16x16x32_bf16 v[78:81], v[98:101], v[186:189], v[78:81]
	v_mfma_f32_16x16x32_bf16 v[74:77], v[122:125], v[186:189], v[74:77]
	v_mfma_f32_16x16x32_bf16 v[162:165], v[110:113], v[166:169], v[162:165]
	v_mfma_f32_16x16x32_bf16 v[158:161], v[126:129], v[166:169], v[158:161]
	v_mfma_f32_16x16x32_bf16 v[118:121], v[110:113], v[174:177], v[118:121]
	v_mfma_f32_16x16x32_bf16 v[114:117], v[126:129], v[174:177], v[114:117]
	v_mfma_f32_16x16x32_bf16 v[94:97], v[110:113], v[182:185], v[94:97]
	v_mfma_f32_16x16x32_bf16 v[90:93], v[126:129], v[182:185], v[90:93]
	v_mfma_f32_16x16x32_bf16 v[78:81], v[110:113], v[206:209], v[78:81]
	v_mfma_f32_16x16x32_bf16 v[74:77], v[126:129], v[206:209], v[74:77]
	v_mfma_f32_16x16x32_bf16 v[134:137], v[138:141], v[154:157], v[134:137]
	v_mfma_f32_16x16x32_bf16 v[130:133], v[146:149], v[154:157], v[130:133]
	v_mfma_f32_16x16x32_bf16 v[106:109], v[138:141], v[170:173], v[106:109]
	v_mfma_f32_16x16x32_bf16 v[102:105], v[146:149], v[170:173], v[102:105]
	v_mfma_f32_16x16x32_bf16 v[86:89], v[138:141], v[178:181], v[86:89]
	v_mfma_f32_16x16x32_bf16 v[82:85], v[146:149], v[178:181], v[82:85]
	v_mfma_f32_16x16x32_bf16 v[70:73], v[138:141], v[186:189], v[70:73]
	v_mfma_f32_16x16x32_bf16 v[66:69], v[146:149], v[186:189], v[66:69]
	v_mfma_f32_16x16x32_bf16 v[134:137], v[142:145], v[166:169], v[134:137]
	v_mfma_f32_16x16x32_bf16 v[130:133], v[150:153], v[166:169], v[130:133]
	v_mfma_f32_16x16x32_bf16 v[106:109], v[142:145], v[174:177], v[106:109]
	v_mfma_f32_16x16x32_bf16 v[102:105], v[150:153], v[174:177], v[102:105]
	v_mfma_f32_16x16x32_bf16 v[86:89], v[142:145], v[182:185], v[86:89]
	v_mfma_f32_16x16x32_bf16 v[82:85], v[150:153], v[182:185], v[82:85]
	v_mfma_f32_16x16x32_bf16 v[70:73], v[142:145], v[206:209], v[70:73]
	v_mfma_f32_16x16x32_bf16 v[66:69], v[150:153], v[206:209], v[66:69]
	s_setprio 0
	s_barrier
	s_add_i32 s30, s64, s2
	s_add_i32 m0, s30, 0xffffff80
	ds_read_b128 v[154:157], v236 offset:49152
	ds_read_b128 v[166:169], v236 offset:50176
	ds_read_b128 v[170:173], v236 offset:51200
	ds_read_b128 v[174:177], v236 offset:52224
	ds_read_b128 v[178:181], v236 offset:53248
	ds_read_b128 v[182:185], v236 offset:54272
	ds_read_b128 v[186:189], v236 offset:55296
	ds_read_b128 v[206:209], v236 offset:56320
	global_load_lds_dwordx4 v[210:211], off offset:128
	s_add_i32 m0, s30, 0x1f80
	s_add_u32 s28, s28, 0x40080
	s_addc_u32 s29, s29, 0
	s_add_i32 s30, s65, s2
	global_load_lds_dwordx4 v[212:213], off offset:128
	s_mov_b32 m0, s30
	s_nop 0
	global_load_lds_dwordx4 v192, s[28:29]
	s_add_i32 m0, s30, 0x2000
	s_nop 0
	global_load_lds_dwordx4 v196, s[28:29]
	s_add_i32 m0, s39, 0xffffff80
	s_nop 0
	global_load_lds_dwordx4 v[214:215], off offset:128
	s_add_i32 m0, s48, 0xffffff80
	s_nop 0
	global_load_lds_dwordx4 v[216:217], off offset:128
	s_waitcnt vmcnt(8)
	s_waitcnt lgkmcnt(0)
	s_barrier
	s_setprio 3
	s_waitcnt lgkmcnt(0)
	v_mfma_f32_16x16x32_bf16 v[62:65], v[98:101], v[154:157], v[62:65]
	v_mfma_f32_16x16x32_bf16 v[58:61], v[122:125], v[154:157], v[58:61]
	v_mfma_f32_16x16x32_bf16 v[46:49], v[98:101], v[170:173], v[46:49]
	v_mfma_f32_16x16x32_bf16 v[42:45], v[122:125], v[170:173], v[42:45]
	v_mfma_f32_16x16x32_bf16 v[30:33], v[98:101], v[178:181], v[30:33]
	v_mfma_f32_16x16x32_bf16 v[26:29], v[122:125], v[178:181], v[26:29]
	v_mfma_f32_16x16x32_bf16 v[14:17], v[98:101], v[186:189], v[14:17]
	v_mfma_f32_16x16x32_bf16 v[10:13], v[122:125], v[186:189], v[10:13]
	v_mfma_f32_16x16x32_bf16 v[62:65], v[110:113], v[166:169], v[62:65]
	v_mfma_f32_16x16x32_bf16 v[58:61], v[126:129], v[166:169], v[58:61]
	v_mfma_f32_16x16x32_bf16 v[46:49], v[110:113], v[174:177], v[46:49]
	v_mfma_f32_16x16x32_bf16 v[42:45], v[126:129], v[174:177], v[42:45]
	v_mfma_f32_16x16x32_bf16 v[30:33], v[110:113], v[182:185], v[30:33]
	v_mfma_f32_16x16x32_bf16 v[26:29], v[126:129], v[182:185], v[26:29]
	v_mfma_f32_16x16x32_bf16 v[14:17], v[110:113], v[206:209], v[14:17]
	v_mfma_f32_16x16x32_bf16 v[10:13], v[126:129], v[206:209], v[10:13]
	v_mfma_f32_16x16x32_bf16 v[54:57], v[138:141], v[154:157], v[54:57]
	v_mfma_f32_16x16x32_bf16 v[50:53], v[146:149], v[154:157], v[50:53]
	v_mfma_f32_16x16x32_bf16 v[38:41], v[138:141], v[170:173], v[38:41]
	v_mfma_f32_16x16x32_bf16 v[34:37], v[146:149], v[170:173], v[34:37]
	v_mfma_f32_16x16x32_bf16 v[22:25], v[138:141], v[178:181], v[22:25]
	v_mfma_f32_16x16x32_bf16 v[18:21], v[146:149], v[178:181], v[18:21]
	v_mfma_f32_16x16x32_bf16 v[6:9], v[138:141], v[186:189], v[6:9]
	v_mfma_f32_16x16x32_bf16 v[2:5], v[146:149], v[186:189], v[2:5]
	v_mfma_f32_16x16x32_bf16 v[54:57], v[142:145], v[166:169], v[54:57]
	v_mfma_f32_16x16x32_bf16 v[50:53], v[150:153], v[166:169], v[50:53]
	v_mfma_f32_16x16x32_bf16 v[38:41], v[142:145], v[174:177], v[38:41]
	v_mfma_f32_16x16x32_bf16 v[34:37], v[150:153], v[174:177], v[34:37]
	v_mfma_f32_16x16x32_bf16 v[22:25], v[142:145], v[182:185], v[22:25]
	v_mfma_f32_16x16x32_bf16 v[18:21], v[150:153], v[182:185], v[18:21]
	v_mfma_f32_16x16x32_bf16 v[6:9], v[142:145], v[206:209], v[6:9]
	v_mfma_f32_16x16x32_bf16 v[2:5], v[150:153], v[206:209], v[2:5]
	s_setprio 0
	s_barrier
	s_add_i32 s63, s63, 2
	s_add_u32 s26, s26, 0x100
	s_addc_u32 s27, s27, 0
	s_add_u32 s61, s61, 0x100
	s_addc_u32 s62, s62, 0
	s_cmp_gt_u32 s63, 13
	s_cbranch_scc0 .LBB0_634
	s_and_b64 vcc, exec, s[14:15]
	s_cbranch_vccz .LBB0_637
	s_barrier

; #define PG8_STAGE_A(b, h, ptr, NX) do { if constexpr (Sched::GATHER) { unsigned gs_[2]; gs_[0] = ((NX) && last_) ? gN[h][0] : gA[h][0]; gs_[1] = ((NX) && last_) ? gN[h][1] : gA[h][1]; PG8_STAGE(PG8_SA(b, h), ptr, gs_); } \
;         else PG8_STAGE(PG8_SA(b, h), (ptr) + ((h) ? hstep : (size_t)0), voffA); } while (0)
; #define PG8_STAGE(bufoff, gbase, voff) do { _Pragma("unroll") for (int _i = 0; _i < 2; ++_i) \
;         __builtin_amdgcn_global_load_lds((const unsigned*)((const char*)(gbase) + (voff)[_i]), (PG8_LAS unsigned*)(lds + (bufoff) + ldsw + _i * 8192), 16, 0, 0); } while (0)
; #define PG8_LDA(dst, b, h) do { _Pragma("unroll") for (int m = 0; m < 4; ++m) _Pragma("unroll") for (int k = 0; k < 2; ++k) dst[m][k] = *(const PG8_LAS bf16x8*)(lds + PG8_SA(b, h) + aoff + m * 2048 + k * 1024); } while (0)
; #define PG8_WAIT_V(n) asm volatile("s_waitcnt vmcnt(" #n ")" ::: "memory")
; #define PG8_WAIT_L(n) asm volatile("s_waitcnt lgkmcnt(" #n ")" ::: "memory")
; #define PG8_BAR __builtin_amdgcn_s_barrier()
; template <class Epi, class Sched, bool ALIGN_EPI = false, bool SP2 = false>
; __device__ __forceinline__ void gemm_phase(PG8_LAS unsigned char* lds, const Gemm g, const Sched& S, const Epi& E, const bool skip_epi = false) {
;     ...
;         const char* nA = has_next ? (const char*)g.A + (size_t)nxt.pm * pmstepA + nxt.ko : cA; const char* nB = has_next ? (const char*)g.Bt + (size_t)nxt.pn * tstep + nxt.ko : cB;
;         for (int t = 0; t < nt; t += 2) {
;             const bool last = (t == nt - 2); last_ = last && has_next;
;             const char* a1 = cA + (size_t)(t + 1) * kstep;
;             const char* a2 = last ? nA : cA + (size_t)(t + 2) * kstep; const char* b2 = last ? nB : cB + (size_t)(t + 2) * kstep;
;             const char* a3 = a2 + kstep; const char* b3 = b2 + kstep;
;             if (last && has_next) S.a_ready(nxt);
;             if constexpr (SP2) {
;             PG8_LDB(B0, 0, 0); PG8_LDB(B1, 0, 1); PG8_SCHED; PG8_LDA(At, 0, 0); PG8_STAGE_A(1, 1, a1, false);
;             PG8_WAIT_V(8); PG8_WAIT_L(0); PG8_BAR; PG8_MMA(0, 0, At, B0); PG8_MMA(0, 1, At, B1); PG8_BAR; PG8_SCHED;
;             PG8_LDA(At, 0, 1); PG8_STAGE(PG8_SB(0, 0), b2, voffB); PG8_STAGE(PG8_SB(0, 1), b2 + hstep, voffB); PG8_STAGE_A(0, 0, a2, true);
;             PG8_WAIT_V(8); PG8_WAIT_L(0); PG8_BAR; PG8_MMA(1, 0, At, B0); PG8_MMA(1, 1, At, B1); PG8_BAR; PG8_SCHED;
.LBB0_720:
	s_ashr_i32 s15, s14, 31
	s_lshl_b64 s[16:17], s[14:15], 19
	s_add_u32 s16, s86, s16
	s_addc_u32 s17, s87, s17
	s_and_b64 s[18:19], s[4:5], exec
	s_cselect_b32 s15, s17, s23
	s_cselect_b32 s56, s16, s22
	s_ashr_i32 s13, s12, 31
	s_lshl_b64 s[18:19], s[12:13], 19
	v_readlane_b32 s26, v254, 15
	v_readlane_b32 s27, v254, 16
	s_add_u32 s18, s26, s18
	s_addc_u32 s19, s27, s19
	s_and_b64 s[26:27], s[4:5], exec
	s_cselect_b32 s13, s19, s25
	s_cselect_b32 s57, s18, s24
	s_add_u32 s22, s22, 0x40080
	s_addc_u32 s23, s23, 0
	s_add_u32 s58, s24, 0x100
	s_addc_u32 s59, s25, 0
	s_mov_b32 s60, -2
	s_waitcnt vmcnt(0)
	v_lshl_add_u32 v130, s20, 8, v175
	v_ashrrev_i32_e32 v131, 31, v130
	v_lshlrev_b64 v[130:131], 6, v[130:131]
	v_lshl_add_u64 v[130:131], v[150:151], 0, v[130:131]
	global_load_dwordx4 v[238:241], v[130:131], off
	global_load_dwordx4 v[242:245], v[130:131], off offset:1024
	global_load_dwordx4 v[246:249], v[130:131], off offset:2048
	global_load_dwordx4 v[250:253], v[130:131], off offset:3072
	ds_read_b128 v[130:133], v187
	ds_read_b128 v[134:137], v187 offset:1024
	ds_read_b128 v[138:141], v187 offset:2048
	ds_read_b128 v[160:163], v187 offset:3072
	ds_read_b128 v[164:167], v188
	ds_read_b128 v[182:185], v188 offset:1024
	ds_read_b128 v[192:195], v188 offset:2048
	ds_read_b128 v[196:199], v188 offset:3072
	s_add_u32 s24, s22, 0xfffc0080
	s_addc_u32 s25, s23, -1
	s_cmp_eq_u32 s60, 12
	s_cselect_b32 s27, s15, s25
	s_cselect_b32 s26, s56, s24
	s_cselect_b32 s25, s13, s59
	s_cselect_b32 s24, s57, s58
	s_add_i32 m0, s29, 0xc000
	ds_read_b128 v[200:203], v189
	ds_read_b128 v[204:207], v189 offset:1024
	ds_read_b128 v[208:211], v189 offset:2048
	ds_read_b128 v[212:215], v189 offset:3072
	ds_read_b128 v[216:219], v189 offset:4096
	ds_read_b128 v[220:223], v189 offset:5120
	ds_read_b128 v[224:227], v189 offset:6144
	ds_read_b128 v[230:233], v189 offset:7168
	global_load_lds_dwordx4 v152, s[22:23]
	s_add_i32 m0, s29, 0xe000
	s_nop 0
	global_load_lds_dwordx4 v154, s[22:23]
	s_waitcnt vmcnt(8)
	s_waitcnt lgkmcnt(0)
	s_barrier
	s_setprio 3
	s_waitcnt lgkmcnt(0)
	v_mfma_f32_16x16x32_bf16 v[126:129], v[130:133], v[200:203], 0
	v_mfma_f32_16x16x32_bf16 v[122:125], v[138:141], v[200:203], 0
	v_mfma_f32_16x16x32_bf16 v[110:113], v[130:133], v[208:211], 0
	v_mfma_f32_16x16x32_bf16 v[106:109], v[138:141], v[208:211], 0
	v_mfma_f32_16x16x32_bf16 v[94:97], v[130:133], v[216:219], 0
	v_mfma_f32_16x16x32_bf16 v[90:93], v[138:141], v[216:219], 0
	v_mfma_f32_16x16x32_bf16 v[78:81], v[130:133], v[224:227], 0
	v_mfma_f32_16x16x32_bf16 v[74:77], v[138:141], v[224:227], 0
	v_mfma_f32_16x16x32_bf16 v[126:129], v[134:137], v[204:207], v[126:129]
	v_mfma_f32_16x16x32_bf16 v[122:125], v[160:163], v[204:207], v[122:125]
	v_mfma_f32_16x16x32_bf16 v[110:113], v[134:137], v[212:215], v[110:113]
	v_mfma_f32_16x16x32_bf16 v[106:109], v[160:163], v[212:215], v[106:109]
	v_mfma_f32_16x16x32_bf16 v[94:97], v[134:137], v[220:223], v[94:97]
	v_mfma_f32_16x16x32_bf16 v[90:93], v[160:163], v[220:223], v[90:93]
	v_mfma_f32_16x16x32_bf16 v[78:81], v[134:137], v[230:233], v[78:81]
	v_mfma_f32_16x16x32_bf16 v[74:77], v[160:163], v[230:233], v[74:77]
	v_mfma_f32_16x16x32_bf16 v[118:121], v[164:167], v[200:203], 0
	v_mfma_f32_16x16x32_bf16 v[114:117], v[192:195], v[200:203], 0
	v_mfma_f32_16x16x32_bf16 v[102:105], v[164:167], v[208:211], 0
	v_mfma_f32_16x16x32_bf16 v[98:101], v[192:195], v[208:211], 0
	v_mfma_f32_16x16x32_bf16 v[86:89], v[164:167], v[216:219], 0
	v_mfma_f32_16x16x32_bf16 v[82:85], v[192:195], v[216:219], 0
	v_mfma_f32_16x16x32_bf16 v[70:73], v[164:167], v[224:227], 0
	v_mfma_f32_16x16x32_bf16 v[66:69], v[192:195], v[224:227], 0
	v_mfma_f32_16x16x32_bf16 v[118:121], v[182:185], v[204:207], v[118:121]
	v_mfma_f32_16x16x32_bf16 v[114:117], v[196:199], v[204:207], v[114:117]
	v_mfma_f32_16x16x32_bf16 v[102:105], v[182:185], v[212:215], v[102:105]
	v_mfma_f32_16x16x32_bf16 v[98:101], v[196:199], v[212:215], v[98:101]
	v_mfma_f32_16x16x32_bf16 v[86:89], v[182:185], v[220:223], v[86:89]
	v_mfma_f32_16x16x32_bf16 v[82:85], v[196:199], v[220:223], v[82:85]
	v_mfma_f32_16x16x32_bf16 v[70:73], v[182:185], v[230:233], v[70:73]
	v_mfma_f32_16x16x32_bf16 v[66:69], v[196:199], v[230:233], v[66:69]
	s_setprio 0
	s_barrier
	s_add_i32 s61, s39, s2
	v_lshl_add_u64 v[168:169], s[24:25], 0, v[146:147]
	s_mov_b32 m0, s61
	ds_read_b128 v[200:203], v189 offset:16384
	ds_read_b128 v[204:207], v189 offset:17408
	ds_read_b128 v[208:211], v189 offset:18432
	ds_read_b128 v[212:215], v189 offset:19456
	ds_read_b128 v[216:219], v189 offset:20480
	ds_read_b128 v[220:223], v189 offset:21504
	ds_read_b128 v[224:227], v189 offset:22528
	ds_read_b128 v[230:233], v189 offset:23552
	global_load_lds_dwordx4 v[168:169], off
	s_add_i32 m0, s61, 0x2000
	s_add_u32 s62, s24, 0x40000
	v_lshl_add_u64 v[172:173], s[24:25], 0, v[142:143]
	s_addc_u32 s63, s25, 0
	s_add_i32 s61, s48, s2
	global_load_lds_dwordx4 v[172:173], off
	s_mov_b32 m0, s61
	v_lshl_add_u64 v[234:235], s[26:27], 0, v[144:145]
	global_load_lds_dwordx4 v146, s[62:63]
	s_add_i32 m0, s61, 0x2000
	s_nop 0
	global_load_lds_dwordx4 v142, s[62:63]
	v_lshl_add_u64 v[176:177], s[26:27], 0, v[148:149]
	s_mov_b32 m0, s29
	s_nop 0
	global_load_lds_dwordx4 v[176:177], off
	s_mov_b32 m0, s30
	s_nop 0
	global_load_lds_dwordx4 v[234:235], off
	s_waitcnt vmcnt(8)
	s_waitcnt lgkmcnt(0)
	s_barrier
; #define PG8_STAGE_A(b, h, ptr, NX) do { if constexpr (Sched::GATHER) { unsigned gs_[2]; gs_[0] = ((NX) && last_) ? gN[h][0] : gA[h][0]; gs_[1] = ((NX) && last_) ? gN[h][1] : gA[h][1]; PG8_STAGE(PG8_SA(b, h), ptr, gs_); } \
;         else PG8_STAGE(PG8_SA(b, h), (ptr) + ((h) ? hstep : (size_t)0), voffA); } while (0)
; #define PG8_LDA(dst, b, h) do { _Pragma("unroll") for (int m = 0; m < 4; ++m) _Pragma("unroll") for (int k = 0; k < 2; ++k) dst[m][k] = *(const PG8_LAS bf16x8*)(lds + PG8_SA(b, h) + aoff + m * 2048 + k * 1024); } while (0)
; #define PG8_LDB(dst, b, h) do { _Pragma("unroll") for (int n = 0; n < 2; ++n) _Pragma("unroll") for (int k = 0; k < 2; ++k) dst[n][k] = *(const PG8_LAS bf16x8*)(lds + PG8_SB(b, h) + boff + n * 2048 + k * 1024); } while (0)
; #define PG8_MMA(ai, bj, At, Bt) do { __builtin_amdgcn_s_setprio(1); _Pragma("unroll") for (int m = 0; m < 4; ++m) _Pragma("unroll") for (int n = 0; n < 2; ++n) _Pragma("unroll") for (int k = 0; k < 2; ++k) \
;         acc[ai][bj][m][n] = __builtin_amdgcn_mfma_f32_16x16x32_bf16(Bt[n][k], At[m][k], acc[ai][bj][m][n], 0, 0, 0); __builtin_amdgcn_s_setprio(0); } while (0)
; #define PG8_WAIT_V(n) asm volatile("s_waitcnt vmcnt(" #n ")" ::: "memory")
; #define PG8_WAIT_L(n) asm volatile("s_waitcnt lgkmcnt(" #n ")" ::: "memory")
; #define PG8_BAR __builtin_amdgcn_s_barrier()
; #define PG8_SCHED __builtin_amdgcn_sched_barrier(0)
; template <class Epi, class Sched, bool ALIGN_EPI = false, bool SP2 = false>
; __device__ __forceinline__ void gemm_phase(PG8_LAS unsigned char* lds, const Gemm g, const Sched& S, const Epi& E, const bool skip_epi = false) {
;     ...
;             PG8_WAIT_V(8); PG8_WAIT_L(0); PG8_BAR; PG8_MMA(1, 0, At, B0); PG8_MMA(1, 1, At, B1); PG8_BAR; PG8_SCHED;
;             PG8_LDB(B0, 1, 0); PG8_LDB(B1, 1, 1); PG8_SCHED; PG8_LDA(At, 1, 0); PG8_STAGE_A(0, 1, a2, true);
;             PG8_WAIT_V(8); PG8_WAIT_L(0); PG8_BAR; PG8_MMA(0, 0, At, B0); PG8_MMA(0, 1, At, B1); PG8_BAR; PG8_SCHED;
	s_setprio 3
	s_waitcnt lgkmcnt(0)
	v_mfma_f32_16x16x32_bf16 v[62:65], v[130:133], v[200:203], 0
	v_mfma_f32_16x16x32_bf16 v[58:61], v[138:141], v[200:203], 0
	v_mfma_f32_16x16x32_bf16 v[46:49], v[130:133], v[208:211], 0
	v_mfma_f32_16x16x32_bf16 v[42:45], v[138:141], v[208:211], 0
	v_mfma_f32_16x16x32_bf16 v[30:33], v[130:133], v[216:219], 0
	v_mfma_f32_16x16x32_bf16 v[26:29], v[138:141], v[216:219], 0
	v_mfma_f32_16x16x32_bf16 v[14:17], v[130:133], v[224:227], 0
	v_mfma_f32_16x16x32_bf16 v[10:13], v[138:141], v[224:227], 0
	v_mfma_f32_16x16x32_bf16 v[62:65], v[134:137], v[204:207], v[62:65]
	v_mfma_f32_16x16x32_bf16 v[58:61], v[160:163], v[204:207], v[58:61]
	v_mfma_f32_16x16x32_bf16 v[46:49], v[134:137], v[212:215], v[46:49]
	v_mfma_f32_16x16x32_bf16 v[42:45], v[160:163], v[212:215], v[42:45]
	v_mfma_f32_16x16x32_bf16 v[30:33], v[134:137], v[220:223], v[30:33]
	v_mfma_f32_16x16x32_bf16 v[26:29], v[160:163], v[220:223], v[26:29]
	v_mfma_f32_16x16x32_bf16 v[14:17], v[134:137], v[230:233], v[14:17]
	v_mfma_f32_16x16x32_bf16 v[10:13], v[160:163], v[230:233], v[10:13]
	v_mfma_f32_16x16x32_bf16 v[54:57], v[164:167], v[200:203], 0
	v_mfma_f32_16x16x32_bf16 v[50:53], v[192:195], v[200:203], 0
	v_mfma_f32_16x16x32_bf16 v[38:41], v[164:167], v[208:211], 0
	v_mfma_f32_16x16x32_bf16 v[34:37], v[192:195], v[208:211], 0
	v_mfma_f32_16x16x32_bf16 v[22:25], v[164:167], v[216:219], 0
	v_mfma_f32_16x16x32_bf16 v[18:21], v[192:195], v[216:219], 0
	v_mfma_f32_16x16x32_bf16 v[6:9], v[164:167], v[224:227], 0
	v_mfma_f32_16x16x32_bf16 v[2:5], v[192:195], v[224:227], 0
	v_mfma_f32_16x16x32_bf16 v[54:57], v[182:185], v[204:207], v[54:57]
	v_mfma_f32_16x16x32_bf16 v[50:53], v[196:199], v[204:207], v[50:53]
	v_mfma_f32_16x16x32_bf16 v[38:41], v[182:185], v[212:215], v[38:41]
	v_mfma_f32_16x16x32_bf16 v[34:37], v[196:199], v[212:215], v[34:37]
	v_mfma_f32_16x16x32_bf16 v[22:25], v[182:185], v[220:223], v[22:25]
	v_mfma_f32_16x16x32_bf16 v[18:21], v[196:199], v[220:223], v[18:21]
	v_mfma_f32_16x16x32_bf16 v[6:9], v[182:185], v[230:233], v[6:9]
	v_mfma_f32_16x16x32_bf16 v[2:5], v[196:199], v[230:233], v[2:5]
	s_setprio 0
	s_barrier
	s_add_i32 s61, 0, 0x18000
	s_add_i32 s62, 0, 0x1c000
	v_add_u32_e32 v160, s61, v1
	v_add_u32_e32 v170, s62, v1
	ds_read_b128 v[130:133], v160
	ds_read_b128 v[134:137], v160 offset:1024
	ds_read_b128 v[138:141], v160 offset:2048
	ds_read_b128 v[160:163], v160 offset:3072
	ds_read_b128 v[164:167], v170
	ds_read_b128 v[182:185], v170 offset:1024
	ds_read_b128 v[192:195], v170 offset:2048
	ds_read_b128 v[196:199], v170 offset:3072
	s_add_u32 s26, s26, 0x40000
	s_addc_u32 s27, s27, 0
	s_mov_b32 m0, s31
	ds_read_b128 v[200:203], v189 offset:32768
	ds_read_b128 v[204:207], v189 offset:33792
	ds_read_b128 v[208:211], v189 offset:34816
	ds_read_b128 v[212:215], v189 offset:35840
	ds_read_b128 v[216:219], v189 offset:36864
	ds_read_b128 v[220:223], v189 offset:37888
	ds_read_b128 v[224:227], v189 offset:38912
	ds_read_b128 v[230:233], v189 offset:39936
	global_load_lds_dwordx4 v148, s[26:27]
	s_mov_b32 m0, s34
	s_nop 0
	global_load_lds_dwordx4 v144, s[26:27]
	s_waitcnt vmcnt(8)
	s_waitcnt lgkmcnt(0)
	s_barrier
	s_setprio 3
	s_waitcnt lgkmcnt(0)
	v_mfma_f32_16x16x32_bf16 v[126:129], v[130:133], v[200:203], v[126:129]
	v_mfma_f32_16x16x32_bf16 v[122:125], v[138:141], v[200:203], v[122:125]
	v_mfma_f32_16x16x32_bf16 v[110:113], v[130:133], v[208:211], v[110:113]
	v_mfma_f32_16x16x32_bf16 v[106:109], v[138:141], v[208:211], v[106:109]
	v_mfma_f32_16x16x32_bf16 v[94:97], v[130:133], v[216:219], v[94:97]
	v_mfma_f32_16x16x32_bf16 v[90:93], v[138:141], v[216:219], v[90:93]
	v_mfma_f32_16x16x32_bf16 v[78:81], v[130:133], v[224:227], v[78:81]
	v_mfma_f32_16x16x32_bf16 v[74:77], v[138:141], v[224:227], v[74:77]
	v_mfma_f32_16x16x32_bf16 v[126:129], v[134:137], v[204:207], v[126:129]
	v_mfma_f32_16x16x32_bf16 v[122:125], v[160:163], v[204:207], v[122:125]
	v_mfma_f32_16x16x32_bf16 v[110:113], v[134:137], v[212:215], v[110:113]
	v_mfma_f32_16x16x32_bf16 v[106:109], v[160:163], v[212:215], v[106:109]
	v_mfma_f32_16x16x32_bf16 v[94:97], v[134:137], v[220:223], v[94:97]
	v_mfma_f32_16x16x32_bf16 v[90:93], v[160:163], v[220:223], v[90:93]
	v_mfma_f32_16x16x32_bf16 v[78:81], v[134:137], v[230:233], v[78:81]
	v_mfma_f32_16x16x32_bf16 v[74:77], v[160:163], v[230:233], v[74:77]
	v_mfma_f32_16x16x32_bf16 v[118:121], v[164:167], v[200:203], v[118:121]
	v_mfma_f32_16x16x32_bf16 v[114:117], v[192:195], v[200:203], v[114:117]
	v_mfma_f32_16x16x32_bf16 v[102:105], v[164:167], v[208:211], v[102:105]
	v_mfma_f32_16x16x32_bf16 v[98:101], v[192:195], v[208:211], v[98:101]
	v_mfma_f32_16x16x32_bf16 v[86:89], v[164:167], v[216:219], v[86:89]
	v_mfma_f32_16x16x32_bf16 v[82:85], v[192:195], v[216:219], v[82:85]
	v_mfma_f32_16x16x32_bf16 v[70:73], v[164:167], v[224:227], v[70:73]
	v_mfma_f32_16x16x32_bf16 v[66:69], v[192:195], v[224:227], v[66:69]
	v_mfma_f32_16x16x32_bf16 v[118:121], v[182:185], v[204:207], v[118:121]
	v_mfma_f32_16x16x32_bf16 v[114:117], v[196:199], v[204:207], v[114:117]
	v_mfma_f32_16x16x32_bf16 v[102:105], v[182:185], v[212:215], v[102:105]
	v_mfma_f32_16x16x32_bf16 v[98:101], v[196:199], v[212:215], v[98:101]
	v_mfma_f32_16x16x32_bf16 v[86:89], v[182:185], v[220:223], v[86:89]
	v_mfma_f32_16x16x32_bf16 v[82:85], v[196:199], v[220:223], v[82:85]
	v_mfma_f32_16x16x32_bf16 v[70:73], v[182:185], v[230:233], v[70:73]
	v_mfma_f32_16x16x32_bf16 v[66:69], v[196:199], v[230:233], v[66:69]
	s_setprio 0
	s_barrier
; #define PG8_STAGE_A(b, h, ptr, NX) do { if constexpr (Sched::GATHER) { unsigned gs_[2]; gs_[0] = ((NX) && last_) ? gN[h][0] : gA[h][0]; gs_[1] = ((NX) && last_) ? gN[h][1] : gA[h][1]; PG8_STAGE(PG8_SA(b, h), ptr, gs_); } \
;         else PG8_STAGE(PG8_SA(b, h), (ptr) + ((h) ? hstep : (size_t)0), voffA); } while (0)
; #define PG8_STAGE(bufoff, gbase, voff) do { _Pragma("unroll") for (int _i = 0; _i < 2; ++_i) \
;         __builtin_amdgcn_global_load_lds((const unsigned*)((const char*)(gbase) + (voff)[_i]), (PG8_LAS unsigned*)(lds + (bufoff) + ldsw + _i * 8192), 16, 0, 0); } while (0)
; #define PG8_LDA(dst, b, h) do { _Pragma("unroll") for (int m = 0; m < 4; ++m) _Pragma("unroll") for (int k = 0; k < 2; ++k) dst[m][k] = *(const PG8_LAS bf16x8*)(lds + PG8_SA(b, h) + aoff + m * 2048 + k * 1024); } while (0)
; #define PG8_LDB(dst, b, h) do { _Pragma("unroll") for (int n = 0; n < 2; ++n) _Pragma("unroll") for (int k = 0; k < 2; ++k) dst[n][k] = *(const PG8_LAS bf16x8*)(lds + PG8_SB(b, h) + boff + n * 2048 + k * 1024); } while (0)
; #define PG8_WAIT_V(n) asm volatile("s_waitcnt vmcnt(" #n ")" ::: "memory")
; #define PG8_BAR __builtin_amdgcn_s_barrier()
; template <class Epi, class Sched, bool ALIGN_EPI = false, bool SP2 = false>
; __device__ __forceinline__ void gemm_phase(PG8_LAS unsigned char* lds, const Gemm g, const Sched& S, const Epi& E, const bool skip_epi = false) {
;     ...
;             PG8_LDB(B0, 0, 0); PG8_LDB(B1, 0, 1); PG8_SCHED; PG8_LDA(At, 0, 0); PG8_STAGE_A(1, 1, a1, false);
;             PG8_WAIT_V(8); PG8_WAIT_L(0); PG8_BAR; PG8_MMA(0, 0, At, B0); PG8_MMA(0, 1, At, B1); PG8_BAR; PG8_SCHED;
;             PG8_LDA(At, 0, 1); PG8_STAGE(PG8_SB(0, 0), b2, voffB); PG8_STAGE(PG8_SB(0, 1), b2 + hstep, voffB); PG8_STAGE_A(0, 0, a2, true);
;             PG8_WAIT_V(8); PG8_WAIT_L(0); PG8_BAR; PG8_MMA(1, 0, At, B0); PG8_MMA(1, 1, At, B1); PG8_BAR; PG8_SCHED;
;             PG8_LDB(B0, 1, 0); PG8_LDB(B1, 1, 1); PG8_SCHED; PG8_LDA(At, 1, 0); PG8_STAGE_A(0, 1, a2, true);
;             PG8_WAIT_V(8); PG8_WAIT_L(0); PG8_BAR; PG8_MMA(0, 0, At, B0); PG8_MMA(0, 1, At, B1); PG8_BAR; PG8_SCHED;
;             PG8_LDA(At, 1, 1); PG8_STAGE(PG8_SB(1, 0), b3, voffB); PG8_STAGE(PG8_SB(1, 1), b3 + hstep, voffB); PG8_STAGE_A(1, 0, a3, true);
;             PG8_WAIT_V(8); PG8_WAIT_L(0); PG8_BAR; PG8_MMA(1, 0, At, B0); PG8_MMA(1, 1, At, B1); PG8_BAR; PG8_SCHED;
	s_add_i32 s26, s61, s2
	s_add_i32 m0, s26, 0xffffff80
	ds_read_b128 v[200:203], v189 offset:49152
	ds_read_b128 v[204:207], v189 offset:50176
	ds_read_b128 v[208:211], v189 offset:51200
	ds_read_b128 v[212:215], v189 offset:52224
	ds_read_b128 v[216:219], v189 offset:53248
	ds_read_b128 v[220:223], v189 offset:54272
	ds_read_b128 v[224:227], v189 offset:55296
	ds_read_b128 v[230:233], v189 offset:56320
	global_load_lds_dwordx4 v[168:169], off offset:128
	s_add_i32 m0, s26, 0x1f80
	s_add_u32 s24, s24, 0x40080
	s_addc_u32 s25, s25, 0
	s_add_i32 s26, s62, s2
	global_load_lds_dwordx4 v[172:173], off offset:128
	s_mov_b32 m0, s26
	s_nop 0
	global_load_lds_dwordx4 v146, s[24:25]
	s_add_i32 m0, s26, 0x2000
	s_nop 0
	global_load_lds_dwordx4 v142, s[24:25]
	s_add_i32 m0, s36, 0xffffff80
	s_nop 0
	global_load_lds_dwordx4 v[176:177], off offset:128
	s_add_i32 m0, s37, 0xffffff80
	s_nop 0
	global_load_lds_dwordx4 v[234:235], off offset:128
	s_waitcnt vmcnt(8)
	s_waitcnt lgkmcnt(0)
	s_barrier
	s_setprio 3
	s_waitcnt lgkmcnt(0)
	v_mfma_f32_16x16x32_bf16 v[62:65], v[130:133], v[200:203], v[62:65]
	v_mfma_f32_16x16x32_bf16 v[58:61], v[138:141], v[200:203], v[58:61]
	v_mfma_f32_16x16x32_bf16 v[46:49], v[130:133], v[208:211], v[46:49]
	v_mfma_f32_16x16x32_bf16 v[42:45], v[138:141], v[208:211], v[42:45]
	v_mfma_f32_16x16x32_bf16 v[30:33], v[130:133], v[216:219], v[30:33]
	v_mfma_f32_16x16x32_bf16 v[26:29], v[138:141], v[216:219], v[26:29]
	v_mfma_f32_16x16x32_bf16 v[14:17], v[130:133], v[224:227], v[14:17]
	v_mfma_f32_16x16x32_bf16 v[10:13], v[138:141], v[224:227], v[10:13]
	v_mfma_f32_16x16x32_bf16 v[62:65], v[134:137], v[204:207], v[62:65]
	v_mfma_f32_16x16x32_bf16 v[58:61], v[160:163], v[204:207], v[58:61]
	v_mfma_f32_16x16x32_bf16 v[46:49], v[134:137], v[212:215], v[46:49]
	v_mfma_f32_16x16x32_bf16 v[42:45], v[160:163], v[212:215], v[42:45]
	v_mfma_f32_16x16x32_bf16 v[30:33], v[134:137], v[220:223], v[30:33]
	v_mfma_f32_16x16x32_bf16 v[26:29], v[160:163], v[220:223], v[26:29]
	v_mfma_f32_16x16x32_bf16 v[14:17], v[134:137], v[230:233], v[14:17]
	v_mfma_f32_16x16x32_bf16 v[10:13], v[160:163], v[230:233], v[10:13]
	v_mfma_f32_16x16x32_bf16 v[54:57], v[164:167], v[200:203], v[54:57]
	v_mfma_f32_16x16x32_bf16 v[50:53], v[192:195], v[200:203], v[50:53]
	v_mfma_f32_16x16x32_bf16 v[38:41], v[164:167], v[208:211], v[38:41]
	v_mfma_f32_16x16x32_bf16 v[34:37], v[192:195], v[208:211], v[34:37]
	v_mfma_f32_16x16x32_bf16 v[22:25], v[164:167], v[216:219], v[22:25]
	v_mfma_f32_16x16x32_bf16 v[18:21], v[192:195], v[216:219], v[18:21]
	v_mfma_f32_16x16x32_bf16 v[6:9], v[164:167], v[224:227], v[6:9]
	v_mfma_f32_16x16x32_bf16 v[2:5], v[192:195], v[224:227], v[2:5]
	v_mfma_f32_16x16x32_bf16 v[54:57], v[182:185], v[204:207], v[54:57]
	v_mfma_f32_16x16x32_bf16 v[50:53], v[196:199], v[204:207], v[50:53]
	v_mfma_f32_16x16x32_bf16 v[38:41], v[182:185], v[212:215], v[38:41]
	v_mfma_f32_16x16x32_bf16 v[34:37], v[196:199], v[212:215], v[34:37]
	v_mfma_f32_16x16x32_bf16 v[22:25], v[182:185], v[220:223], v[22:25]
	v_mfma_f32_16x16x32_bf16 v[18:21], v[196:199], v[220:223], v[18:21]
	v_mfma_f32_16x16x32_bf16 v[6:9], v[182:185], v[230:233], v[6:9]
	v_mfma_f32_16x16x32_bf16 v[2:5], v[196:199], v[230:233], v[2:5]
	s_setprio 0
	s_barrier
	s_add_i32 s60, s60, 2
	s_add_u32 s22, s22, 0x100
	s_addc_u32 s23, s23, 0
	s_add_u32 s58, s58, 0x100
	s_addc_u32 s59, s59, 0
	s_cmp_gt_u32 s60, 13
.LBB0_721:
	ds_read_b128 v[130:133], v187
	ds_read_b128 v[134:137], v187 offset:1024
	ds_read_b128 v[138:141], v187 offset:2048
	ds_read_b128 v[160:163], v187 offset:3072
	ds_read_b128 v[164:167], v188
	ds_read_b128 v[182:185], v188 offset:1024
	ds_read_b128 v[192:195], v188 offset:2048
	ds_read_b128 v[196:199], v188 offset:3072
	s_add_u32 s24, s22, 0xfffc0080
	s_addc_u32 s25, s23, -1
	s_cmp_eq_u32 s60, 12
	s_cselect_b32 s27, s15, s25
	s_cselect_b32 s26, s56, s24
	s_cselect_b32 s25, s13, s59
	s_cselect_b32 s24, s57, s58
	s_add_i32 m0, s29, 0xc000
	ds_read_b128 v[200:203], v189
	ds_read_b128 v[204:207], v189 offset:1024
	ds_read_b128 v[208:211], v189 offset:2048
	ds_read_b128 v[212:215], v189 offset:3072
	ds_read_b128 v[216:219], v189 offset:4096
	ds_read_b128 v[220:223], v189 offset:5120
	ds_read_b128 v[224:227], v189 offset:6144
	ds_read_b128 v[230:233], v189 offset:7168
	global_load_lds_dwordx4 v152, s[22:23]
	s_add_i32 m0, s29, 0xe000
	s_nop 0
	global_load_lds_dwordx4 v154, s[22:23]
	s_waitcnt vmcnt(8)
	s_waitcnt lgkmcnt(0)
	s_barrier
	s_setprio 3
	s_waitcnt lgkmcnt(0)
	v_mfma_f32_16x16x32_bf16 v[126:129], v[130:133], v[200:203], v[126:129]
	v_mfma_f32_16x16x32_bf16 v[122:125], v[138:141], v[200:203], v[122:125]
	v_mfma_f32_16x16x32_bf16 v[110:113], v[130:133], v[208:211], v[110:113]
	v_mfma_f32_16x16x32_bf16 v[106:109], v[138:141], v[208:211], v[106:109]
	v_mfma_f32_16x16x32_bf16 v[94:97], v[130:133], v[216:219], v[94:97]
	v_mfma_f32_16x16x32_bf16 v[90:93], v[138:141], v[216:219], v[90:93]
	v_mfma_f32_16x16x32_bf16 v[78:81], v[130:133], v[224:227], v[78:81]
	v_mfma_f32_16x16x32_bf16 v[74:77], v[138:141], v[224:227], v[74:77]
	v_mfma_f32_16x16x32_bf16 v[126:129], v[134:137], v[204:207], v[126:129]
	v_mfma_f32_16x16x32_bf16 v[122:125], v[160:163], v[204:207], v[122:125]
	v_mfma_f32_16x16x32_bf16 v[110:113], v[134:137], v[212:215], v[110:113]
	v_mfma_f32_16x16x32_bf16 v[106:109], v[160:163], v[212:215], v[106:109]
	v_mfma_f32_16x16x32_bf16 v[94:97], v[134:137], v[220:223], v[94:97]
	v_mfma_f32_16x16x32_bf16 v[90:93], v[160:163], v[220:223], v[90:93]
	v_mfma_f32_16x16x32_bf16 v[78:81], v[134:137], v[230:233], v[78:81]
	v_mfma_f32_16x16x32_bf16 v[74:77], v[160:163], v[230:233], v[74:77]
	v_mfma_f32_16x16x32_bf16 v[118:121], v[164:167], v[200:203], v[118:121]
	v_mfma_f32_16x16x32_bf16 v[114:117], v[192:195], v[200:203], v[114:117]
	v_mfma_f32_16x16x32_bf16 v[102:105], v[164:167], v[208:211], v[102:105]
	v_mfma_f32_16x16x32_bf16 v[98:101], v[192:195], v[208:211], v[98:101]
	v_mfma_f32_16x16x32_bf16 v[86:89], v[164:167], v[216:219], v[86:89]
	v_mfma_f32_16x16x32_bf16 v[82:85], v[192:195], v[216:219], v[82:85]
	v_mfma_f32_16x16x32_bf16 v[70:73], v[164:167], v[224:227], v[70:73]
	v_mfma_f32_16x16x32_bf16 v[66:69], v[192:195], v[224:227], v[66:69]
	v_mfma_f32_16x16x32_bf16 v[118:121], v[182:185], v[204:207], v[118:121]
	v_mfma_f32_16x16x32_bf16 v[114:117], v[196:199], v[204:207], v[114:117]
	v_mfma_f32_16x16x32_bf16 v[102:105], v[182:185], v[212:215], v[102:105]
	v_mfma_f32_16x16x32_bf16 v[98:101], v[196:199], v[212:215], v[98:101]
	v_mfma_f32_16x16x32_bf16 v[86:89], v[182:185], v[220:223], v[86:89]
	v_mfma_f32_16x16x32_bf16 v[82:85], v[196:199], v[220:223], v[82:85]
	v_mfma_f32_16x16x32_bf16 v[70:73], v[182:185], v[230:233], v[70:73]
	v_mfma_f32_16x16x32_bf16 v[66:69], v[196:199], v[230:233], v[66:69]
	s_setprio 0
	s_barrier
; #define PG8_STAGE_A(b, h, ptr, NX) do { if constexpr (Sched::GATHER) { unsigned gs_[2]; gs_[0] = ((NX) && last_) ? gN[h][0] : gA[h][0]; gs_[1] = ((NX) && last_) ? gN[h][1] : gA[h][1]; PG8_STAGE(PG8_SA(b, h), ptr, gs_); } \
;         else PG8_STAGE(PG8_SA(b, h), (ptr) + ((h) ? hstep : (size_t)0), voffA); } while (0)
; #define PG8_STAGE(bufoff, gbase, voff) do { _Pragma("unroll") for (int _i = 0; _i < 2; ++_i) \
;         __builtin_amdgcn_global_load_lds((const unsigned*)((const char*)(gbase) + (voff)[_i]), (PG8_LAS unsigned*)(lds + (bufoff) + ldsw + _i * 8192), 16, 0, 0); } while (0)
; #define PG8_LDA(dst, b, h) do { _Pragma("unroll") for (int m = 0; m < 4; ++m) _Pragma("unroll") for (int k = 0; k < 2; ++k) dst[m][k] = *(const PG8_LAS bf16x8*)(lds + PG8_SA(b, h) + aoff + m * 2048 + k * 1024); } while (0)
; #define PG8_LDB(dst, b, h) do { _Pragma("unroll") for (int n = 0; n < 2; ++n) _Pragma("unroll") for (int k = 0; k < 2; ++k) dst[n][k] = *(const PG8_LAS bf16x8*)(lds + PG8_SB(b, h) + boff + n * 2048 + k * 1024); } while (0)
; #define PG8_MMA(ai, bj, At, Bt) do { __builtin_amdgcn_s_setprio(1); _Pragma("unroll") for (int m = 0; m < 4; ++m) _Pragma("unroll") for (int n = 0; n < 2; ++n) _Pragma("unroll") for (int k = 0; k < 2; ++k) \
;         acc[ai][bj][m][n] = __builtin_amdgcn_mfma_f32_16x16x32_bf16(Bt[n][k], At[m][k], acc[ai][bj][m][n], 0, 0, 0); __builtin_amdgcn_s_setprio(0); } while (0)
; #define PG8_WAIT_V(n) asm volatile("s_waitcnt vmcnt(" #n ")" ::: "memory")
; #define PG8_WAIT_L(n) asm volatile("s_waitcnt lgkmcnt(" #n ")" ::: "memory")
; #define PG8_BAR __builtin_amdgcn_s_barrier()
; #define PG8_SCHED __builtin_amdgcn_sched_barrier(0)
; template <class Epi, class Sched, bool ALIGN_EPI = false, bool SP2 = false>
; __device__ __forceinline__ void gemm_phase(PG8_LAS unsigned char* lds, const Gemm g, const Sched& S, const Epi& E, const bool skip_epi = false) {
;     ...
;             PG8_LDA(At, 0, 1); PG8_STAGE(PG8_SB(0, 0), b2, voffB); PG8_STAGE(PG8_SB(0, 1), b2 + hstep, voffB); PG8_STAGE_A(0, 0, a2, true);
;             PG8_WAIT_V(8); PG8_WAIT_L(0); PG8_BAR; PG8_MMA(1, 0, At, B0); PG8_MMA(1, 1, At, B1); PG8_BAR; PG8_SCHED;
;             PG8_LDB(B0, 1, 0); PG8_LDB(B1, 1, 1); PG8_SCHED; PG8_LDA(At, 1, 0); PG8_STAGE_A(0, 1, a2, true);
;             PG8_WAIT_V(8); PG8_WAIT_L(0); PG8_BAR; PG8_MMA(0, 0, At, B0); PG8_MMA(0, 1, At, B1); PG8_BAR; PG8_SCHED;
	s_add_i32 s61, s39, s2
	v_lshl_add_u64 v[168:169], s[24:25], 0, v[146:147]
	s_mov_b32 m0, s61
	ds_read_b128 v[200:203], v189 offset:16384
	ds_read_b128 v[204:207], v189 offset:17408
	ds_read_b128 v[208:211], v189 offset:18432
	ds_read_b128 v[212:215], v189 offset:19456
	ds_read_b128 v[216:219], v189 offset:20480
	ds_read_b128 v[220:223], v189 offset:21504
	ds_read_b128 v[224:227], v189 offset:22528
	ds_read_b128 v[230:233], v189 offset:23552
	global_load_lds_dwordx4 v[168:169], off
	s_add_i32 m0, s61, 0x2000
	s_add_u32 s62, s24, 0x40000
	v_lshl_add_u64 v[172:173], s[24:25], 0, v[142:143]
	s_addc_u32 s63, s25, 0
	s_add_i32 s61, s48, s2
	global_load_lds_dwordx4 v[172:173], off
	s_mov_b32 m0, s61
	v_lshl_add_u64 v[234:235], s[26:27], 0, v[144:145]
	global_load_lds_dwordx4 v146, s[62:63]
	s_add_i32 m0, s61, 0x2000
	s_nop 0
	global_load_lds_dwordx4 v142, s[62:63]
	v_lshl_add_u64 v[176:177], s[26:27], 0, v[148:149]
	s_mov_b32 m0, s29
	s_nop 0
	global_load_lds_dwordx4 v[176:177], off
	s_mov_b32 m0, s30
	s_nop 0
	global_load_lds_dwordx4 v[234:235], off
	s_waitcnt vmcnt(8)
	s_waitcnt lgkmcnt(0)
	s_barrier
	s_setprio 3
	s_waitcnt lgkmcnt(0)
	v_mfma_f32_16x16x32_bf16 v[62:65], v[130:133], v[200:203], v[62:65]
	v_mfma_f32_16x16x32_bf16 v[58:61], v[138:141], v[200:203], v[58:61]
	v_mfma_f32_16x16x32_bf16 v[46:49], v[130:133], v[208:211], v[46:49]
	v_mfma_f32_16x16x32_bf16 v[42:45], v[138:141], v[208:211], v[42:45]
	v_mfma_f32_16x16x32_bf16 v[30:33], v[130:133], v[216:219], v[30:33]
	v_mfma_f32_16x16x32_bf16 v[26:29], v[138:141], v[216:219], v[26:29]
	v_mfma_f32_16x16x32_bf16 v[14:17], v[130:133], v[224:227], v[14:17]
	v_mfma_f32_16x16x32_bf16 v[10:13], v[138:141], v[224:227], v[10:13]
	v_mfma_f32_16x16x32_bf16 v[62:65], v[134:137], v[204:207], v[62:65]
	v_mfma_f32_16x16x32_bf16 v[58:61], v[160:163], v[204:207], v[58:61]
	v_mfma_f32_16x16x32_bf16 v[46:49], v[134:137], v[212:215], v[46:49]
	v_mfma_f32_16x16x32_bf16 v[42:45], v[160:163], v[212:215], v[42:45]
	v_mfma_f32_16x16x32_bf16 v[30:33], v[134:137], v[220:223], v[30:33]
	v_mfma_f32_16x16x32_bf16 v[26:29], v[160:163], v[220:223], v[26:29]
	v_mfma_f32_16x16x32_bf16 v[14:17], v[134:137], v[230:233], v[14:17]
	v_mfma_f32_16x16x32_bf16 v[10:13], v[160:163], v[230:233], v[10:13]
	v_mfma_f32_16x16x32_bf16 v[54:57], v[164:167], v[200:203], v[54:57]
	v_mfma_f32_16x16x32_bf16 v[50:53], v[192:195], v[200:203], v[50:53]
	v_mfma_f32_16x16x32_bf16 v[38:41], v[164:167], v[208:211], v[38:41]
	v_mfma_f32_16x16x32_bf16 v[34:37], v[192:195], v[208:211], v[34:37]
	v_mfma_f32_16x16x32_bf16 v[22:25], v[164:167], v[216:219], v[22:25]
	v_mfma_f32_16x16x32_bf16 v[18:21], v[192:195], v[216:219], v[18:21]
	v_mfma_f32_16x16x32_bf16 v[6:9], v[164:167], v[224:227], v[6:9]
	v_mfma_f32_16x16x32_bf16 v[2:5], v[192:195], v[224:227], v[2:5]
	v_mfma_f32_16x16x32_bf16 v[54:57], v[182:185], v[204:207], v[54:57]
	v_mfma_f32_16x16x32_bf16 v[50:53], v[196:199], v[204:207], v[50:53]
	v_mfma_f32_16x16x32_bf16 v[38:41], v[182:185], v[212:215], v[38:41]
	v_mfma_f32_16x16x32_bf16 v[34:37], v[196:199], v[212:215], v[34:37]
	v_mfma_f32_16x16x32_bf16 v[22:25], v[182:185], v[220:223], v[22:25]
	v_mfma_f32_16x16x32_bf16 v[18:21], v[196:199], v[220:223], v[18:21]
	v_mfma_f32_16x16x32_bf16 v[6:9], v[182:185], v[230:233], v[6:9]
	v_mfma_f32_16x16x32_bf16 v[2:5], v[196:199], v[230:233], v[2:5]
	s_setprio 0
	s_barrier
	s_add_i32 s61, 0, 0x18000
	s_add_i32 s62, 0, 0x1c000
	v_add_u32_e32 v160, s61, v1
	v_add_u32_e32 v170, s62, v1
	ds_read_b128 v[130:133], v160
	ds_read_b128 v[134:137], v160 offset:1024
	ds_read_b128 v[138:141], v160 offset:2048
	ds_read_b128 v[160:163], v160 offset:3072
	ds_read_b128 v[164:167], v170
	ds_read_b128 v[182:185], v170 offset:1024
	ds_read_b128 v[192:195], v170 offset:2048
	ds_read_b128 v[196:199], v170 offset:3072
	s_add_u32 s26, s26, 0x40000
	s_addc_u32 s27, s27, 0
	s_mov_b32 m0, s31
	ds_read_b128 v[200:203], v189 offset:32768
	ds_read_b128 v[204:207], v189 offset:33792
	ds_read_b128 v[208:211], v189 offset:34816
	ds_read_b128 v[212:215], v189 offset:35840
	ds_read_b128 v[216:219], v189 offset:36864
	ds_read_b128 v[220:223], v189 offset:37888
	ds_read_b128 v[224:227], v189 offset:38912
	ds_read_b128 v[230:233], v189 offset:39936
	global_load_lds_dwordx4 v148, s[26:27]
	s_mov_b32 m0, s34
	s_nop 0
	global_load_lds_dwordx4 v144, s[26:27]
	s_waitcnt vmcnt(8)
	s_waitcnt lgkmcnt(0)
	s_barrier
; #define PG8_STAGE_A(b, h, ptr, NX) do { if constexpr (Sched::GATHER) { unsigned gs_[2]; gs_[0] = ((NX) && last_) ? gN[h][0] : gA[h][0]; gs_[1] = ((NX) && last_) ? gN[h][1] : gA[h][1]; PG8_STAGE(PG8_SA(b, h), ptr, gs_); } \
;         else PG8_STAGE(PG8_SA(b, h), (ptr) + ((h) ? hstep : (size_t)0), voffA); } while (0)
; #define PG8_STAGE(bufoff, gbase, voff) do { _Pragma("unroll") for (int _i = 0; _i < 2; ++_i) \
;         __builtin_amdgcn_global_load_lds((const unsigned*)((const char*)(gbase) + (voff)[_i]), (PG8_LAS unsigned*)(lds + (bufoff) + ldsw + _i * 8192), 16, 0, 0); } while (0)
; #define PG8_LDA(dst, b, h) do { _Pragma("unroll") for (int m = 0; m < 4; ++m) _Pragma("unroll") for (int k = 0; k < 2; ++k) dst[m][k] = *(const PG8_LAS bf16x8*)(lds + PG8_SA(b, h) + aoff + m * 2048 + k * 1024); } while (0)
; #define PG8_MMA(ai, bj, At, Bt) do { __builtin_amdgcn_s_setprio(1); _Pragma("unroll") for (int m = 0; m < 4; ++m) _Pragma("unroll") for (int n = 0; n < 2; ++n) _Pragma("unroll") for (int k = 0; k < 2; ++k) \
;         acc[ai][bj][m][n] = __builtin_amdgcn_mfma_f32_16x16x32_bf16(Bt[n][k], At[m][k], acc[ai][bj][m][n], 0, 0, 0); __builtin_amdgcn_s_setprio(0); } while (0)
; #define PG8_WAIT_V(n) asm volatile("s_waitcnt vmcnt(" #n ")" ::: "memory")
; #define PG8_WAIT_L(n) asm volatile("s_waitcnt lgkmcnt(" #n ")" ::: "memory")
; #define PG8_BAR __builtin_amdgcn_s_barrier()
; #define PG8_SCHED __builtin_amdgcn_sched_barrier(0)
; template <class Epi, class Sched, bool ALIGN_EPI = false, bool SP2 = false>
; __device__ __forceinline__ void gemm_phase(PG8_LAS unsigned char* lds, const Gemm g, const Sched& S, const Epi& E, const bool skip_epi = false) {
;     ...
;             PG8_WAIT_V(8); PG8_WAIT_L(0); PG8_BAR; PG8_MMA(0, 0, At, B0); PG8_MMA(0, 1, At, B1); PG8_BAR; PG8_SCHED;
;             PG8_LDA(At, 1, 1); PG8_STAGE(PG8_SB(1, 0), b3, voffB); PG8_STAGE(PG8_SB(1, 1), b3 + hstep, voffB); PG8_STAGE_A(1, 0, a3, true);
;             PG8_WAIT_V(8); PG8_WAIT_L(0); PG8_BAR; PG8_MMA(1, 0, At, B0); PG8_MMA(1, 1, At, B1); PG8_BAR; PG8_SCHED;
;     ...
;         if constexpr (ALIGN_EPI) { if (wr == 0) PG8_BAR; }
	s_setprio 3
	s_waitcnt lgkmcnt(0)
	v_mfma_f32_16x16x32_bf16 v[126:129], v[130:133], v[200:203], v[126:129]
	v_mfma_f32_16x16x32_bf16 v[122:125], v[138:141], v[200:203], v[122:125]
	v_mfma_f32_16x16x32_bf16 v[110:113], v[130:133], v[208:211], v[110:113]
	v_mfma_f32_16x16x32_bf16 v[106:109], v[138:141], v[208:211], v[106:109]
	v_mfma_f32_16x16x32_bf16 v[94:97], v[130:133], v[216:219], v[94:97]
	v_mfma_f32_16x16x32_bf16 v[90:93], v[138:141], v[216:219], v[90:93]
	v_mfma_f32_16x16x32_bf16 v[78:81], v[130:133], v[224:227], v[78:81]
	v_mfma_f32_16x16x32_bf16 v[74:77], v[138:141], v[224:227], v[74:77]
	v_mfma_f32_16x16x32_bf16 v[126:129], v[134:137], v[204:207], v[126:129]
	v_mfma_f32_16x16x32_bf16 v[122:125], v[160:163], v[204:207], v[122:125]
	v_mfma_f32_16x16x32_bf16 v[110:113], v[134:137], v[212:215], v[110:113]
	v_mfma_f32_16x16x32_bf16 v[106:109], v[160:163], v[212:215], v[106:109]
	v_mfma_f32_16x16x32_bf16 v[94:97], v[134:137], v[220:223], v[94:97]
	v_mfma_f32_16x16x32_bf16 v[90:93], v[160:163], v[220:223], v[90:93]
	v_mfma_f32_16x16x32_bf16 v[78:81], v[134:137], v[230:233], v[78:81]
	v_mfma_f32_16x16x32_bf16 v[74:77], v[160:163], v[230:233], v[74:77]
	v_mfma_f32_16x16x32_bf16 v[118:121], v[164:167], v[200:203], v[118:121]
	v_mfma_f32_16x16x32_bf16 v[114:117], v[192:195], v[200:203], v[114:117]
	v_mfma_f32_16x16x32_bf16 v[102:105], v[164:167], v[208:211], v[102:105]
	v_mfma_f32_16x16x32_bf16 v[98:101], v[192:195], v[208:211], v[98:101]
	v_mfma_f32_16x16x32_bf16 v[86:89], v[164:167], v[216:219], v[86:89]
	v_mfma_f32_16x16x32_bf16 v[82:85], v[192:195], v[216:219], v[82:85]
	v_mfma_f32_16x16x32_bf16 v[70:73], v[164:167], v[224:227], v[70:73]
	v_mfma_f32_16x16x32_bf16 v[66:69], v[192:195], v[224:227], v[66:69]
	v_mfma_f32_16x16x32_bf16 v[118:121], v[182:185], v[204:207], v[118:121]
	v_mfma_f32_16x16x32_bf16 v[114:117], v[196:199], v[204:207], v[114:117]
	v_mfma_f32_16x16x32_bf16 v[102:105], v[182:185], v[212:215], v[102:105]
	v_mfma_f32_16x16x32_bf16 v[98:101], v[196:199], v[212:215], v[98:101]
	v_mfma_f32_16x16x32_bf16 v[86:89], v[182:185], v[220:223], v[86:89]
	v_mfma_f32_16x16x32_bf16 v[82:85], v[196:199], v[220:223], v[82:85]
	v_mfma_f32_16x16x32_bf16 v[70:73], v[182:185], v[230:233], v[70:73]
	v_mfma_f32_16x16x32_bf16 v[66:69], v[196:199], v[230:233], v[66:69]
	s_setprio 0
	s_barrier
	s_add_i32 s26, s61, s2
	s_add_i32 m0, s26, 0xffffff80
	ds_read_b128 v[200:203], v189 offset:49152
	ds_read_b128 v[204:207], v189 offset:50176
	ds_read_b128 v[208:211], v189 offset:51200
	ds_read_b128 v[212:215], v189 offset:52224
	ds_read_b128 v[216:219], v189 offset:53248
	ds_read_b128 v[220:223], v189 offset:54272
	ds_read_b128 v[224:227], v189 offset:55296
	ds_read_b128 v[230:233], v189 offset:56320
	global_load_lds_dwordx4 v[168:169], off offset:128
	s_add_i32 m0, s26, 0x1f80
	s_add_u32 s24, s24, 0x40080
	s_addc_u32 s25, s25, 0
	s_add_i32 s26, s62, s2
	global_load_lds_dwordx4 v[172:173], off offset:128
	s_mov_b32 m0, s26
	s_nop 0
	global_load_lds_dwordx4 v146, s[24:25]
	s_add_i32 m0, s26, 0x2000
	s_nop 0
	global_load_lds_dwordx4 v142, s[24:25]
	s_add_i32 m0, s36, 0xffffff80
	s_nop 0
	global_load_lds_dwordx4 v[176:177], off offset:128
	s_add_i32 m0, s37, 0xffffff80
	s_nop 0
	global_load_lds_dwordx4 v[234:235], off offset:128
	s_waitcnt vmcnt(8)
	s_waitcnt lgkmcnt(0)
	s_barrier
	s_setprio 3
	s_waitcnt lgkmcnt(0)
	v_mfma_f32_16x16x32_bf16 v[62:65], v[130:133], v[200:203], v[62:65]
	v_mfma_f32_16x16x32_bf16 v[58:61], v[138:141], v[200:203], v[58:61]
	v_mfma_f32_16x16x32_bf16 v[46:49], v[130:133], v[208:211], v[46:49]
	v_mfma_f32_16x16x32_bf16 v[42:45], v[138:141], v[208:211], v[42:45]
	v_mfma_f32_16x16x32_bf16 v[30:33], v[130:133], v[216:219], v[30:33]
	v_mfma_f32_16x16x32_bf16 v[26:29], v[138:141], v[216:219], v[26:29]
	v_mfma_f32_16x16x32_bf16 v[14:17], v[130:133], v[224:227], v[14:17]
	v_mfma_f32_16x16x32_bf16 v[10:13], v[138:141], v[224:227], v[10:13]
	v_mfma_f32_16x16x32_bf16 v[62:65], v[134:137], v[204:207], v[62:65]
	v_mfma_f32_16x16x32_bf16 v[58:61], v[160:163], v[204:207], v[58:61]
	v_mfma_f32_16x16x32_bf16 v[46:49], v[134:137], v[212:215], v[46:49]
	v_mfma_f32_16x16x32_bf16 v[42:45], v[160:163], v[212:215], v[42:45]
	v_mfma_f32_16x16x32_bf16 v[30:33], v[134:137], v[220:223], v[30:33]
	v_mfma_f32_16x16x32_bf16 v[26:29], v[160:163], v[220:223], v[26:29]
	v_mfma_f32_16x16x32_bf16 v[14:17], v[134:137], v[230:233], v[14:17]
	v_mfma_f32_16x16x32_bf16 v[10:13], v[160:163], v[230:233], v[10:13]
	v_mfma_f32_16x16x32_bf16 v[54:57], v[164:167], v[200:203], v[54:57]
	v_mfma_f32_16x16x32_bf16 v[50:53], v[192:195], v[200:203], v[50:53]
	v_mfma_f32_16x16x32_bf16 v[38:41], v[164:167], v[208:211], v[38:41]
	v_mfma_f32_16x16x32_bf16 v[34:37], v[192:195], v[208:211], v[34:37]
	v_mfma_f32_16x16x32_bf16 v[22:25], v[164:167], v[216:219], v[22:25]
	v_mfma_f32_16x16x32_bf16 v[18:21], v[192:195], v[216:219], v[18:21]
	v_mfma_f32_16x16x32_bf16 v[6:9], v[164:167], v[224:227], v[6:9]
	v_mfma_f32_16x16x32_bf16 v[2:5], v[192:195], v[224:227], v[2:5]
	v_mfma_f32_16x16x32_bf16 v[54:57], v[182:185], v[204:207], v[54:57]
	v_mfma_f32_16x16x32_bf16 v[50:53], v[196:199], v[204:207], v[50:53]
	v_mfma_f32_16x16x32_bf16 v[38:41], v[182:185], v[212:215], v[38:41]
	v_mfma_f32_16x16x32_bf16 v[34:37], v[196:199], v[212:215], v[34:37]
	v_mfma_f32_16x16x32_bf16 v[22:25], v[182:185], v[220:223], v[22:25]
	v_mfma_f32_16x16x32_bf16 v[18:21], v[196:199], v[220:223], v[18:21]
	v_mfma_f32_16x16x32_bf16 v[6:9], v[182:185], v[230:233], v[6:9]
	v_mfma_f32_16x16x32_bf16 v[2:5], v[196:199], v[230:233], v[2:5]
	s_setprio 0
	s_barrier
	s_add_i32 s60, s60, 2
	s_add_u32 s22, s22, 0x100
	s_addc_u32 s23, s23, 0
	s_add_u32 s58, s58, 0x100
	s_addc_u32 s59, s59, 0
	s_cmp_gt_u32 s60, 13
	s_cbranch_scc0 .LBB0_721
	s_and_b64 vcc, exec, s[10:11]
	s_cbranch_vccz .LBB0_724
	s_barrier

; #define PG8_STAGE_A(b, h, ptr, NX) do { if constexpr (Sched::GATHER) { unsigned gs_[2]; gs_[0] = ((NX) && last_) ? gN[h][0] : gA[h][0]; gs_[1] = ((NX) && last_) ? gN[h][1] : gA[h][1]; PG8_STAGE(PG8_SA(b, h), ptr, gs_); } \
;         else PG8_STAGE(PG8_SA(b, h), (ptr) + ((h) ? hstep : (size_t)0), voffA); } while (0)
; #define PG8_STAGE(bufoff, gbase, voff) do { _Pragma("unroll") for (int _i = 0; _i < 2; ++_i) \
;         __builtin_amdgcn_global_load_lds((const unsigned*)((const char*)(gbase) + (voff)[_i]), (PG8_LAS unsigned*)(lds + (bufoff) + ldsw + _i * 8192), 16, 0, 0); } while (0)
; #define PG8_LDA(dst, b, h) do { _Pragma("unroll") for (int m = 0; m < 4; ++m) _Pragma("unroll") for (int k = 0; k < 2; ++k) dst[m][k] = *(const PG8_LAS bf16x8*)(lds + PG8_SA(b, h) + aoff + m * 2048 + k * 1024); } while (0)
; #define PG8_WAIT_V(n) asm volatile("s_waitcnt vmcnt(" #n ")" ::: "memory")
; #define PG8_WAIT_L(n) asm volatile("s_waitcnt lgkmcnt(" #n ")" ::: "memory")
; #define PG8_BAR __builtin_amdgcn_s_barrier()
; template <class Epi, class Sched, bool ALIGN_EPI = false, bool SP2 = false>
; __device__ __forceinline__ void gemm_phase(PG8_LAS unsigned char* lds, const Gemm g, const Sched& S, const Epi& E, const bool skip_epi = false) {
;     ...
;         const char* nA = has_next ? (const char*)g.A + (size_t)nxt.pm * pmstepA + nxt.ko : cA; const char* nB = has_next ? (const char*)g.Bt + (size_t)nxt.pn * tstep + nxt.ko : cB;
;         for (int t = 0; t < nt; t += 2) {
;             const bool last = (t == nt - 2); last_ = last && has_next;
;             const char* a1 = cA + (size_t)(t + 1) * kstep;
;             const char* a2 = last ? nA : cA + (size_t)(t + 2) * kstep; const char* b2 = last ? nB : cB + (size_t)(t + 2) * kstep;
;             const char* a3 = a2 + kstep; const char* b3 = b2 + kstep;
;             if (last && has_next) S.a_ready(nxt);
;             if constexpr (SP2) {
;             PG8_LDB(B0, 0, 0); PG8_LDB(B1, 0, 1); PG8_SCHED; PG8_LDA(At, 0, 0); PG8_STAGE_A(1, 1, a1, false);
;             PG8_WAIT_V(8); PG8_WAIT_L(0); PG8_BAR; PG8_MMA(0, 0, At, B0); PG8_MMA(0, 1, At, B1); PG8_BAR; PG8_SCHED;
;             PG8_LDA(At, 0, 1); PG8_STAGE(PG8_SB(0, 0), b2, voffB); PG8_STAGE(PG8_SB(0, 1), b2 + hstep, voffB); PG8_STAGE_A(0, 0, a2, true);
;             PG8_WAIT_V(8); PG8_WAIT_L(0); PG8_BAR; PG8_MMA(1, 0, At, B0); PG8_MMA(1, 1, At, B1); PG8_BAR; PG8_SCHED;
.LBB0_856:
	s_add_u32 s55, s22, 0x100
	s_addc_u32 s56, s23, 0
	s_mov_b32 s57, -2
	s_waitcnt vmcnt(0)
	s_waitcnt lgkmcnt(0)
	ds_read_b128 v[98:101], v234
	ds_read_b128 v[110:113], v234 offset:1024
	ds_read_b128 v[122:125], v234 offset:2048
	ds_read_b128 v[126:129], v234 offset:3072
	ds_read_b128 v[138:141], v235
	ds_read_b128 v[142:145], v235 offset:1024
	ds_read_b128 v[146:149], v235 offset:2048
	ds_read_b128 v[150:153], v235 offset:3072
	s_add_u32 s22, s20, 0x100
	s_addc_u32 s23, s21, 0
	s_cmp_eq_u32 s57, 40
	s_cselect_b32 s27, s9, s23
	s_cselect_b32 s26, s8, s22
	s_cselect_b32 s25, s19, s56
	s_cselect_b32 s24, s18, s55
	v_lshl_add_u64 v[210:211], s[20:21], 0, v[198:199]
	s_add_i32 m0, s3, 0xc000
	ds_read_b128 v[154:157], v236
	ds_read_b128 v[166:169], v236 offset:1024
	ds_read_b128 v[170:173], v236 offset:2048
	ds_read_b128 v[174:177], v236 offset:3072
	ds_read_b128 v[178:181], v236 offset:4096
	ds_read_b128 v[182:185], v236 offset:5120
	ds_read_b128 v[186:189], v236 offset:6144
	ds_read_b128 v[206:209], v236 offset:7168
	global_load_lds_dwordx4 v[210:211], off
	v_lshl_add_u64 v[210:211], s[20:21], 0, v[200:201]
	s_add_i32 m0, s3, 0xe000
	s_nop 0
	global_load_lds_dwordx4 v[210:211], off
	s_waitcnt vmcnt(8)
	s_waitcnt lgkmcnt(0)
	s_barrier
	s_setprio 3
	s_waitcnt lgkmcnt(0)
	v_mfma_f32_16x16x32_bf16 v[162:165], v[98:101], v[154:157], 0
	v_mfma_f32_16x16x32_bf16 v[158:161], v[122:125], v[154:157], 0
	v_mfma_f32_16x16x32_bf16 v[118:121], v[98:101], v[170:173], 0
	v_mfma_f32_16x16x32_bf16 v[114:117], v[122:125], v[170:173], 0
	v_mfma_f32_16x16x32_bf16 v[94:97], v[98:101], v[178:181], 0
	v_mfma_f32_16x16x32_bf16 v[90:93], v[122:125], v[178:181], 0
	v_mfma_f32_16x16x32_bf16 v[78:81], v[98:101], v[186:189], 0
	v_mfma_f32_16x16x32_bf16 v[74:77], v[122:125], v[186:189], 0
	v_mfma_f32_16x16x32_bf16 v[162:165], v[110:113], v[166:169], v[162:165]
	v_mfma_f32_16x16x32_bf16 v[158:161], v[126:129], v[166:169], v[158:161]
	v_mfma_f32_16x16x32_bf16 v[118:121], v[110:113], v[174:177], v[118:121]
	v_mfma_f32_16x16x32_bf16 v[114:117], v[126:129], v[174:177], v[114:117]
	v_mfma_f32_16x16x32_bf16 v[94:97], v[110:113], v[182:185], v[94:97]
	v_mfma_f32_16x16x32_bf16 v[90:93], v[126:129], v[182:185], v[90:93]
	v_mfma_f32_16x16x32_bf16 v[78:81], v[110:113], v[206:209], v[78:81]
	v_mfma_f32_16x16x32_bf16 v[74:77], v[126:129], v[206:209], v[74:77]
	v_mfma_f32_16x16x32_bf16 v[134:137], v[138:141], v[154:157], 0
	v_mfma_f32_16x16x32_bf16 v[130:133], v[146:149], v[154:157], 0
	v_mfma_f32_16x16x32_bf16 v[106:109], v[138:141], v[170:173], 0
	v_mfma_f32_16x16x32_bf16 v[102:105], v[146:149], v[170:173], 0
	v_mfma_f32_16x16x32_bf16 v[86:89], v[138:141], v[178:181], 0
	v_mfma_f32_16x16x32_bf16 v[82:85], v[146:149], v[178:181], 0
	v_mfma_f32_16x16x32_bf16 v[70:73], v[138:141], v[186:189], 0
	v_mfma_f32_16x16x32_bf16 v[66:69], v[146:149], v[186:189], 0
	v_mfma_f32_16x16x32_bf16 v[134:137], v[142:145], v[166:169], v[134:137]
	v_mfma_f32_16x16x32_bf16 v[130:133], v[150:153], v[166:169], v[130:133]
	v_mfma_f32_16x16x32_bf16 v[106:109], v[142:145], v[174:177], v[106:109]
	v_mfma_f32_16x16x32_bf16 v[102:105], v[150:153], v[174:177], v[102:105]
	v_mfma_f32_16x16x32_bf16 v[86:89], v[142:145], v[182:185], v[86:89]
	v_mfma_f32_16x16x32_bf16 v[82:85], v[150:153], v[182:185], v[82:85]
	v_mfma_f32_16x16x32_bf16 v[70:73], v[142:145], v[206:209], v[70:73]
	v_mfma_f32_16x16x32_bf16 v[66:69], v[150:153], v[206:209], v[66:69]
	s_setprio 0
	s_barrier
	s_add_i32 s20, s39, s2
	v_lshl_add_u64 v[210:211], s[24:25], 0, v[192:193]
	s_mov_b32 m0, s20
	ds_read_b128 v[154:157], v236 offset:16384
	ds_read_b128 v[166:169], v236 offset:17408
	ds_read_b128 v[170:173], v236 offset:18432
	ds_read_b128 v[174:177], v236 offset:19456
	ds_read_b128 v[178:181], v236 offset:20480
	ds_read_b128 v[182:185], v236 offset:21504
	ds_read_b128 v[186:189], v236 offset:22528
	ds_read_b128 v[206:209], v236 offset:23552
	global_load_lds_dwordx4 v[210:211], off
	s_add_i32 m0, s20, 0x2000
	s_add_u32 s20, s24, 0xb0000
	v_lshl_add_u64 v[212:213], s[24:25], 0, v[196:197]
	s_addc_u32 s21, s25, 0
	s_add_i32 s58, s48, s2
	global_load_lds_dwordx4 v[212:213], off
	s_mov_b32 m0, s58
	v_lshl_add_u64 v[216:217], s[26:27], 0, v[194:195]
	global_load_lds_dwordx4 v192, s[20:21]
	s_add_i32 m0, s58, 0x2000
	s_nop 0
	global_load_lds_dwordx4 v196, s[20:21]
	v_lshl_add_u64 v[214:215], s[26:27], 0, v[190:191]
	s_mov_b32 m0, s3
	s_nop 0
	global_load_lds_dwordx4 v[214:215], off
	s_mov_b32 m0, s28
	s_nop 0
	global_load_lds_dwordx4 v[216:217], off
	s_waitcnt vmcnt(8)
	s_waitcnt lgkmcnt(0)
	s_barrier
; #define PG8_STAGE_A(b, h, ptr, NX) do { if constexpr (Sched::GATHER) { unsigned gs_[2]; gs_[0] = ((NX) && last_) ? gN[h][0] : gA[h][0]; gs_[1] = ((NX) && last_) ? gN[h][1] : gA[h][1]; PG8_STAGE(PG8_SA(b, h), ptr, gs_); } \
;         else PG8_STAGE(PG8_SA(b, h), (ptr) + ((h) ? hstep : (size_t)0), voffA); } while (0)
; #define PG8_LDA(dst, b, h) do { _Pragma("unroll") for (int m = 0; m < 4; ++m) _Pragma("unroll") for (int k = 0; k < 2; ++k) dst[m][k] = *(const PG8_LAS bf16x8*)(lds + PG8_SA(b, h) + aoff + m * 2048 + k * 1024); } while (0)
; #define PG8_LDB(dst, b, h) do { _Pragma("unroll") for (int n = 0; n < 2; ++n) _Pragma("unroll") for (int k = 0; k < 2; ++k) dst[n][k] = *(const PG8_LAS bf16x8*)(lds + PG8_SB(b, h) + boff + n * 2048 + k * 1024); } while (0)
; #define PG8_MMA(ai, bj, At, Bt) do { __builtin_amdgcn_s_setprio(1); _Pragma("unroll") for (int m = 0; m < 4; ++m) _Pragma("unroll") for (int n = 0; n < 2; ++n) _Pragma("unroll") for (int k = 0; k < 2; ++k) \
;         acc[ai][bj][m][n] = __builtin_amdgcn_mfma_f32_16x16x32_bf16(Bt[n][k], At[m][k], acc[ai][bj][m][n], 0, 0, 0); __builtin_amdgcn_s_setprio(0); } while (0)
; #define PG8_WAIT_V(n) asm volatile("s_waitcnt vmcnt(" #n ")" ::: "memory")
; #define PG8_WAIT_L(n) asm volatile("s_waitcnt lgkmcnt(" #n ")" ::: "memory")
; #define PG8_BAR __builtin_amdgcn_s_barrier()
; #define PG8_SCHED __builtin_amdgcn_sched_barrier(0)
; template <class Epi, class Sched, bool ALIGN_EPI = false, bool SP2 = false>
; __device__ __forceinline__ void gemm_phase(PG8_LAS unsigned char* lds, const Gemm g, const Sched& S, const Epi& E, const bool skip_epi = false) {
;     ...
;             PG8_WAIT_V(8); PG8_WAIT_L(0); PG8_BAR; PG8_MMA(1, 0, At, B0); PG8_MMA(1, 1, At, B1); PG8_BAR; PG8_SCHED;
;             PG8_LDB(B0, 1, 0); PG8_LDB(B1, 1, 1); PG8_SCHED; PG8_LDA(At, 1, 0); PG8_STAGE_A(0, 1, a2, true);
;             PG8_WAIT_V(8); PG8_WAIT_L(0); PG8_BAR; PG8_MMA(0, 0, At, B0); PG8_MMA(0, 1, At, B1); PG8_BAR; PG8_SCHED;
	s_setprio 3
	s_waitcnt lgkmcnt(0)
	v_mfma_f32_16x16x32_bf16 v[62:65], v[98:101], v[154:157], 0
	v_mfma_f32_16x16x32_bf16 v[58:61], v[122:125], v[154:157], 0
	v_mfma_f32_16x16x32_bf16 v[46:49], v[98:101], v[170:173], 0
	v_mfma_f32_16x16x32_bf16 v[42:45], v[122:125], v[170:173], 0
	v_mfma_f32_16x16x32_bf16 v[30:33], v[98:101], v[178:181], 0
	v_mfma_f32_16x16x32_bf16 v[26:29], v[122:125], v[178:181], 0
	v_mfma_f32_16x16x32_bf16 v[14:17], v[98:101], v[186:189], 0
	v_mfma_f32_16x16x32_bf16 v[10:13], v[122:125], v[186:189], 0
	v_mfma_f32_16x16x32_bf16 v[62:65], v[110:113], v[166:169], v[62:65]
	v_mfma_f32_16x16x32_bf16 v[58:61], v[126:129], v[166:169], v[58:61]
	v_mfma_f32_16x16x32_bf16 v[46:49], v[110:113], v[174:177], v[46:49]
	v_mfma_f32_16x16x32_bf16 v[42:45], v[126:129], v[174:177], v[42:45]
	v_mfma_f32_16x16x32_bf16 v[30:33], v[110:113], v[182:185], v[30:33]
	v_mfma_f32_16x16x32_bf16 v[26:29], v[126:129], v[182:185], v[26:29]
	v_mfma_f32_16x16x32_bf16 v[14:17], v[110:113], v[206:209], v[14:17]
	v_mfma_f32_16x16x32_bf16 v[10:13], v[126:129], v[206:209], v[10:13]
	v_mfma_f32_16x16x32_bf16 v[54:57], v[138:141], v[154:157], 0
	v_mfma_f32_16x16x32_bf16 v[50:53], v[146:149], v[154:157], 0
	v_mfma_f32_16x16x32_bf16 v[38:41], v[138:141], v[170:173], 0
	v_mfma_f32_16x16x32_bf16 v[34:37], v[146:149], v[170:173], 0
	v_mfma_f32_16x16x32_bf16 v[22:25], v[138:141], v[178:181], 0
	v_mfma_f32_16x16x32_bf16 v[18:21], v[146:149], v[178:181], 0
	v_mfma_f32_16x16x32_bf16 v[6:9], v[138:141], v[186:189], 0
	v_mfma_f32_16x16x32_bf16 v[2:5], v[146:149], v[186:189], 0
	v_mfma_f32_16x16x32_bf16 v[54:57], v[142:145], v[166:169], v[54:57]
	v_mfma_f32_16x16x32_bf16 v[50:53], v[150:153], v[166:169], v[50:53]
	v_mfma_f32_16x16x32_bf16 v[38:41], v[142:145], v[174:177], v[38:41]
	v_mfma_f32_16x16x32_bf16 v[34:37], v[150:153], v[174:177], v[34:37]
	v_mfma_f32_16x16x32_bf16 v[22:25], v[142:145], v[182:185], v[22:25]
	v_mfma_f32_16x16x32_bf16 v[18:21], v[150:153], v[182:185], v[18:21]
	v_mfma_f32_16x16x32_bf16 v[6:9], v[142:145], v[206:209], v[6:9]
	v_mfma_f32_16x16x32_bf16 v[2:5], v[150:153], v[206:209], v[2:5]
	s_setprio 0
	s_barrier
	s_add_i32 s58, 0, 0x18000
	s_add_i32 s59, 0, 0x1c000
	v_add_u32_e32 v126, s58, v229
	v_add_u32_e32 v150, s59, v229
	ds_read_b128 v[98:101], v126
	ds_read_b128 v[110:113], v126 offset:1024
	ds_read_b128 v[122:125], v126 offset:2048
	ds_read_b128 v[126:129], v126 offset:3072
	ds_read_b128 v[138:141], v150
	ds_read_b128 v[142:145], v150 offset:1024
	ds_read_b128 v[146:149], v150 offset:2048
	ds_read_b128 v[150:153], v150 offset:3072
	s_add_u32 s20, s26, 0xb0000
	s_addc_u32 s21, s27, 0
	s_mov_b32 m0, s29
	ds_read_b128 v[154:157], v236 offset:32768
	ds_read_b128 v[166:169], v236 offset:33792
	ds_read_b128 v[170:173], v236 offset:34816
	ds_read_b128 v[174:177], v236 offset:35840
	ds_read_b128 v[178:181], v236 offset:36864
	ds_read_b128 v[182:185], v236 offset:37888
	ds_read_b128 v[186:189], v236 offset:38912
	ds_read_b128 v[206:209], v236 offset:39936
	global_load_lds_dwordx4 v190, s[20:21]
	s_mov_b32 m0, s30
	s_nop 0
	global_load_lds_dwordx4 v194, s[20:21]
	s_waitcnt vmcnt(8)
	s_waitcnt lgkmcnt(0)
	s_barrier
	s_setprio 3
	s_waitcnt lgkmcnt(0)
	v_mfma_f32_16x16x32_bf16 v[162:165], v[98:101], v[154:157], v[162:165]
	v_mfma_f32_16x16x32_bf16 v[158:161], v[122:125], v[154:157], v[158:161]
	v_mfma_f32_16x16x32_bf16 v[118:121], v[98:101], v[170:173], v[118:121]
	v_mfma_f32_16x16x32_bf16 v[114:117], v[122:125], v[170:173], v[114:117]
	v_mfma_f32_16x16x32_bf16 v[94:97], v[98:101], v[178:181], v[94:97]
	v_mfma_f32_16x16x32_bf16 v[90:93], v[122:125], v[178:181], v[90:93]
	v_mfma_f32_16x16x32_bf16 v[78:81], v[98:101], v[186:189], v[78:81]
	v_mfma_f32_16x16x32_bf16 v[74:77], v[122:125], v[186:189], v[74:77]
	v_mfma_f32_16x16x32_bf16 v[162:165], v[110:113], v[166:169], v[162:165]
	v_mfma_f32_16x16x32_bf16 v[158:161], v[126:129], v[166:169], v[158:161]
	v_mfma_f32_16x16x32_bf16 v[118:121], v[110:113], v[174:177], v[118:121]
	v_mfma_f32_16x16x32_bf16 v[114:117], v[126:129], v[174:177], v[114:117]
	v_mfma_f32_16x16x32_bf16 v[94:97], v[110:113], v[182:185], v[94:97]
	v_mfma_f32_16x16x32_bf16 v[90:93], v[126:129], v[182:185], v[90:93]
	v_mfma_f32_16x16x32_bf16 v[78:81], v[110:113], v[206:209], v[78:81]
	v_mfma_f32_16x16x32_bf16 v[74:77], v[126:129], v[206:209], v[74:77]
	v_mfma_f32_16x16x32_bf16 v[134:137], v[138:141], v[154:157], v[134:137]
	v_mfma_f32_16x16x32_bf16 v[130:133], v[146:149], v[154:157], v[130:133]
	v_mfma_f32_16x16x32_bf16 v[106:109], v[138:141], v[170:173], v[106:109]
	v_mfma_f32_16x16x32_bf16 v[102:105], v[146:149], v[170:173], v[102:105]
	v_mfma_f32_16x16x32_bf16 v[86:89], v[138:141], v[178:181], v[86:89]
	v_mfma_f32_16x16x32_bf16 v[82:85], v[146:149], v[178:181], v[82:85]
	v_mfma_f32_16x16x32_bf16 v[70:73], v[138:141], v[186:189], v[70:73]
	v_mfma_f32_16x16x32_bf16 v[66:69], v[146:149], v[186:189], v[66:69]
	v_mfma_f32_16x16x32_bf16 v[134:137], v[142:145], v[166:169], v[134:137]
	v_mfma_f32_16x16x32_bf16 v[130:133], v[150:153], v[166:169], v[130:133]
	v_mfma_f32_16x16x32_bf16 v[106:109], v[142:145], v[174:177], v[106:109]
	v_mfma_f32_16x16x32_bf16 v[102:105], v[150:153], v[174:177], v[102:105]
	v_mfma_f32_16x16x32_bf16 v[86:89], v[142:145], v[182:185], v[86:89]
	v_mfma_f32_16x16x32_bf16 v[82:85], v[150:153], v[182:185], v[82:85]
	v_mfma_f32_16x16x32_bf16 v[70:73], v[142:145], v[206:209], v[70:73]
	v_mfma_f32_16x16x32_bf16 v[66:69], v[150:153], v[206:209], v[66:69]
	s_setprio 0
	s_barrier
; #define PG8_STAGE_A(b, h, ptr, NX) do { if constexpr (Sched::GATHER) { unsigned gs_[2]; gs_[0] = ((NX) && last_) ? gN[h][0] : gA[h][0]; gs_[1] = ((NX) && last_) ? gN[h][1] : gA[h][1]; PG8_STAGE(PG8_SA(b, h), ptr, gs_); } \
;         else PG8_STAGE(PG8_SA(b, h), (ptr) + ((h) ? hstep : (size_t)0), voffA); } while (0)
; #define PG8_STAGE(bufoff, gbase, voff) do { _Pragma("unroll") for (int _i = 0; _i < 2; ++_i) \
;         __builtin_amdgcn_global_load_lds((const unsigned*)((const char*)(gbase) + (voff)[_i]), (PG8_LAS unsigned*)(lds + (bufoff) + ldsw + _i * 8192), 16, 0, 0); } while (0)
; #define PG8_LDA(dst, b, h) do { _Pragma("unroll") for (int m = 0; m < 4; ++m) _Pragma("unroll") for (int k = 0; k < 2; ++k) dst[m][k] = *(const PG8_LAS bf16x8*)(lds + PG8_SA(b, h) + aoff + m * 2048 + k * 1024); } while (0)
; #define PG8_LDB(dst, b, h) do { _Pragma("unroll") for (int n = 0; n < 2; ++n) _Pragma("unroll") for (int k = 0; k < 2; ++k) dst[n][k] = *(const PG8_LAS bf16x8*)(lds + PG8_SB(b, h) + boff + n * 2048 + k * 1024); } while (0)
; #define PG8_WAIT_V(n) asm volatile("s_waitcnt vmcnt(" #n ")" ::: "memory")
; #define PG8_BAR __builtin_amdgcn_s_barrier()
; template <class Epi, class Sched, bool ALIGN_EPI = false, bool SP2 = false>
; __device__ __forceinline__ void gemm_phase(PG8_LAS unsigned char* lds, const Gemm g, const Sched& S, const Epi& E, const bool skip_epi = false) {
;     ...
;             PG8_LDB(B0, 0, 0); PG8_LDB(B1, 0, 1); PG8_SCHED; PG8_LDA(At, 0, 0); PG8_STAGE_A(1, 1, a1, false);
;             PG8_WAIT_V(8); PG8_WAIT_L(0); PG8_BAR; PG8_MMA(0, 0, At, B0); PG8_MMA(0, 1, At, B1); PG8_BAR; PG8_SCHED;
;             PG8_LDA(At, 0, 1); PG8_STAGE(PG8_SB(0, 0), b2, voffB); PG8_STAGE(PG8_SB(0, 1), b2 + hstep, voffB); PG8_STAGE_A(0, 0, a2, true);
;             PG8_WAIT_V(8); PG8_WAIT_L(0); PG8_BAR; PG8_MMA(1, 0, At, B0); PG8_MMA(1, 1, At, B1); PG8_BAR; PG8_SCHED;
;             PG8_LDB(B0, 1, 0); PG8_LDB(B1, 1, 1); PG8_SCHED; PG8_LDA(At, 1, 0); PG8_STAGE_A(0, 1, a2, true);
;             PG8_WAIT_V(8); PG8_WAIT_L(0); PG8_BAR; PG8_MMA(0, 0, At, B0); PG8_MMA(0, 1, At, B1); PG8_BAR; PG8_SCHED;
;             PG8_LDA(At, 1, 1); PG8_STAGE(PG8_SB(1, 0), b3, voffB); PG8_STAGE(PG8_SB(1, 1), b3 + hstep, voffB); PG8_STAGE_A(1, 0, a3, true);
;             PG8_WAIT_V(8); PG8_WAIT_L(0); PG8_BAR; PG8_MMA(1, 0, At, B0); PG8_MMA(1, 1, At, B1); PG8_BAR; PG8_SCHED;
	s_add_i32 s20, s58, s2
	s_add_i32 m0, s20, 0xffffff80
	ds_read_b128 v[154:157], v236 offset:49152
	ds_read_b128 v[166:169], v236 offset:50176
	ds_read_b128 v[170:173], v236 offset:51200
	ds_read_b128 v[174:177], v236 offset:52224
	ds_read_b128 v[178:181], v236 offset:53248
	ds_read_b128 v[182:185], v236 offset:54272
	ds_read_b128 v[186:189], v236 offset:55296
	ds_read_b128 v[206:209], v236 offset:56320
	global_load_lds_dwordx4 v[210:211], off offset:128
	s_add_i32 m0, s20, 0x1f80
	s_add_u32 s20, s24, 0xb0080
	s_addc_u32 s21, s25, 0
	s_add_i32 s24, s59, s2
	global_load_lds_dwordx4 v[212:213], off offset:128
	s_mov_b32 m0, s24
	s_nop 0
	global_load_lds_dwordx4 v192, s[20:21]
	s_add_i32 m0, s24, 0x2000
	s_nop 0
	global_load_lds_dwordx4 v196, s[20:21]
	s_add_i32 m0, s35, 0xffffff80
	s_nop 0
	global_load_lds_dwordx4 v[214:215], off offset:128
	s_add_i32 m0, s36, 0xffffff80
	s_nop 0
	global_load_lds_dwordx4 v[216:217], off offset:128
	s_waitcnt vmcnt(8)
	s_waitcnt lgkmcnt(0)
	s_barrier
	s_setprio 3
	s_waitcnt lgkmcnt(0)
	v_mfma_f32_16x16x32_bf16 v[62:65], v[98:101], v[154:157], v[62:65]
	v_mfma_f32_16x16x32_bf16 v[58:61], v[122:125], v[154:157], v[58:61]
	v_mfma_f32_16x16x32_bf16 v[46:49], v[98:101], v[170:173], v[46:49]
	v_mfma_f32_16x16x32_bf16 v[42:45], v[122:125], v[170:173], v[42:45]
	v_mfma_f32_16x16x32_bf16 v[30:33], v[98:101], v[178:181], v[30:33]
	v_mfma_f32_16x16x32_bf16 v[26:29], v[122:125], v[178:181], v[26:29]
	v_mfma_f32_16x16x32_bf16 v[14:17], v[98:101], v[186:189], v[14:17]
	v_mfma_f32_16x16x32_bf16 v[10:13], v[122:125], v[186:189], v[10:13]
	v_mfma_f32_16x16x32_bf16 v[62:65], v[110:113], v[166:169], v[62:65]
	v_mfma_f32_16x16x32_bf16 v[58:61], v[126:129], v[166:169], v[58:61]
	v_mfma_f32_16x16x32_bf16 v[46:49], v[110:113], v[174:177], v[46:49]
	v_mfma_f32_16x16x32_bf16 v[42:45], v[126:129], v[174:177], v[42:45]
	v_mfma_f32_16x16x32_bf16 v[30:33], v[110:113], v[182:185], v[30:33]
	v_mfma_f32_16x16x32_bf16 v[26:29], v[126:129], v[182:185], v[26:29]
	v_mfma_f32_16x16x32_bf16 v[14:17], v[110:113], v[206:209], v[14:17]
	v_mfma_f32_16x16x32_bf16 v[10:13], v[126:129], v[206:209], v[10:13]
	v_mfma_f32_16x16x32_bf16 v[54:57], v[138:141], v[154:157], v[54:57]
	v_mfma_f32_16x16x32_bf16 v[50:53], v[146:149], v[154:157], v[50:53]
	v_mfma_f32_16x16x32_bf16 v[38:41], v[138:141], v[170:173], v[38:41]
	v_mfma_f32_16x16x32_bf16 v[34:37], v[146:149], v[170:173], v[34:37]
	v_mfma_f32_16x16x32_bf16 v[22:25], v[138:141], v[178:181], v[22:25]
	v_mfma_f32_16x16x32_bf16 v[18:21], v[146:149], v[178:181], v[18:21]
	v_mfma_f32_16x16x32_bf16 v[6:9], v[138:141], v[186:189], v[6:9]
	v_mfma_f32_16x16x32_bf16 v[2:5], v[146:149], v[186:189], v[2:5]
	v_mfma_f32_16x16x32_bf16 v[54:57], v[142:145], v[166:169], v[54:57]
	v_mfma_f32_16x16x32_bf16 v[50:53], v[150:153], v[166:169], v[50:53]
	v_mfma_f32_16x16x32_bf16 v[38:41], v[142:145], v[174:177], v[38:41]
	v_mfma_f32_16x16x32_bf16 v[34:37], v[150:153], v[174:177], v[34:37]
	v_mfma_f32_16x16x32_bf16 v[22:25], v[142:145], v[182:185], v[22:25]
	v_mfma_f32_16x16x32_bf16 v[18:21], v[150:153], v[182:185], v[18:21]
	v_mfma_f32_16x16x32_bf16 v[6:9], v[142:145], v[206:209], v[6:9]
	v_mfma_f32_16x16x32_bf16 v[2:5], v[150:153], v[206:209], v[2:5]
	s_setprio 0
	s_barrier
	s_add_i32 s57, s57, 2
	s_add_u32 s55, s55, 0x100
	s_addc_u32 s56, s56, 0
	s_cmp_gt_u32 s57, 41
	s_mov_b64 s[20:21], s[22:23]
.LBB0_857:
	ds_read_b128 v[98:101], v234
	ds_read_b128 v[110:113], v234 offset:1024
	ds_read_b128 v[122:125], v234 offset:2048
	ds_read_b128 v[126:129], v234 offset:3072
	ds_read_b128 v[138:141], v235
	ds_read_b128 v[142:145], v235 offset:1024
	ds_read_b128 v[146:149], v235 offset:2048
	ds_read_b128 v[150:153], v235 offset:3072
	s_add_u32 s22, s20, 0x100
	s_addc_u32 s23, s21, 0
	s_cmp_eq_u32 s57, 40
	s_cselect_b32 s27, s9, s23
	s_cselect_b32 s26, s8, s22
	s_cselect_b32 s25, s19, s56
	s_cselect_b32 s24, s18, s55
	v_lshl_add_u64 v[210:211], s[20:21], 0, v[198:199]
	s_add_i32 m0, s3, 0xc000
	ds_read_b128 v[154:157], v236
	ds_read_b128 v[166:169], v236 offset:1024
	ds_read_b128 v[170:173], v236 offset:2048
	ds_read_b128 v[174:177], v236 offset:3072
	ds_read_b128 v[178:181], v236 offset:4096
	ds_read_b128 v[182:185], v236 offset:5120
	ds_read_b128 v[186:189], v236 offset:6144
	ds_read_b128 v[206:209], v236 offset:7168
	global_load_lds_dwordx4 v[210:211], off
	v_lshl_add_u64 v[210:211], s[20:21], 0, v[200:201]
	s_add_i32 m0, s3, 0xe000
	s_nop 0
	global_load_lds_dwordx4 v[210:211], off
	s_waitcnt vmcnt(8)
	s_waitcnt lgkmcnt(0)
	s_barrier
; #define PG8_STAGE_A(b, h, ptr, NX) do { if constexpr (Sched::GATHER) { unsigned gs_[2]; gs_[0] = ((NX) && last_) ? gN[h][0] : gA[h][0]; gs_[1] = ((NX) && last_) ? gN[h][1] : gA[h][1]; PG8_STAGE(PG8_SA(b, h), ptr, gs_); } \
;         else PG8_STAGE(PG8_SA(b, h), (ptr) + ((h) ? hstep : (size_t)0), voffA); } while (0)
; #define PG8_STAGE(bufoff, gbase, voff) do { _Pragma("unroll") for (int _i = 0; _i < 2; ++_i) \
;         __builtin_amdgcn_global_load_lds((const unsigned*)((const char*)(gbase) + (voff)[_i]), (PG8_LAS unsigned*)(lds + (bufoff) + ldsw + _i * 8192), 16, 0, 0); } while (0)
; #define PG8_LDA(dst, b, h) do { _Pragma("unroll") for (int m = 0; m < 4; ++m) _Pragma("unroll") for (int k = 0; k < 2; ++k) dst[m][k] = *(const PG8_LAS bf16x8*)(lds + PG8_SA(b, h) + aoff + m * 2048 + k * 1024); } while (0)
; #define PG8_MMA(ai, bj, At, Bt) do { __builtin_amdgcn_s_setprio(1); _Pragma("unroll") for (int m = 0; m < 4; ++m) _Pragma("unroll") for (int n = 0; n < 2; ++n) _Pragma("unroll") for (int k = 0; k < 2; ++k) \
;         acc[ai][bj][m][n] = __builtin_amdgcn_mfma_f32_16x16x32_bf16(Bt[n][k], At[m][k], acc[ai][bj][m][n], 0, 0, 0); __builtin_amdgcn_s_setprio(0); } while (0)
; #define PG8_WAIT_V(n) asm volatile("s_waitcnt vmcnt(" #n ")" ::: "memory")
; #define PG8_WAIT_L(n) asm volatile("s_waitcnt lgkmcnt(" #n ")" ::: "memory")
; #define PG8_BAR __builtin_amdgcn_s_barrier()
; #define PG8_SCHED __builtin_amdgcn_sched_barrier(0)
; template <class Epi, class Sched, bool ALIGN_EPI = false, bool SP2 = false>
; __device__ __forceinline__ void gemm_phase(PG8_LAS unsigned char* lds, const Gemm g, const Sched& S, const Epi& E, const bool skip_epi = false) {
;     ...
;             PG8_WAIT_V(8); PG8_WAIT_L(0); PG8_BAR; PG8_MMA(0, 0, At, B0); PG8_MMA(0, 1, At, B1); PG8_BAR; PG8_SCHED;
;             PG8_LDA(At, 0, 1); PG8_STAGE(PG8_SB(0, 0), b2, voffB); PG8_STAGE(PG8_SB(0, 1), b2 + hstep, voffB); PG8_STAGE_A(0, 0, a2, true);
;             PG8_WAIT_V(8); PG8_WAIT_L(0); PG8_BAR; PG8_MMA(1, 0, At, B0); PG8_MMA(1, 1, At, B1); PG8_BAR; PG8_SCHED;
	s_setprio 3
	s_waitcnt lgkmcnt(0)
	v_mfma_f32_16x16x32_bf16 v[162:165], v[98:101], v[154:157], v[162:165]
	v_mfma_f32_16x16x32_bf16 v[158:161], v[122:125], v[154:157], v[158:161]
	v_mfma_f32_16x16x32_bf16 v[118:121], v[98:101], v[170:173], v[118:121]
	v_mfma_f32_16x16x32_bf16 v[114:117], v[122:125], v[170:173], v[114:117]
	v_mfma_f32_16x16x32_bf16 v[94:97], v[98:101], v[178:181], v[94:97]
	v_mfma_f32_16x16x32_bf16 v[90:93], v[122:125], v[178:181], v[90:93]
	v_mfma_f32_16x16x32_bf16 v[78:81], v[98:101], v[186:189], v[78:81]
	v_mfma_f32_16x16x32_bf16 v[74:77], v[122:125], v[186:189], v[74:77]
	v_mfma_f32_16x16x32_bf16 v[162:165], v[110:113], v[166:169], v[162:165]
	v_mfma_f32_16x16x32_bf16 v[158:161], v[126:129], v[166:169], v[158:161]
	v_mfma_f32_16x16x32_bf16 v[118:121], v[110:113], v[174:177], v[118:121]
	v_mfma_f32_16x16x32_bf16 v[114:117], v[126:129], v[174:177], v[114:117]
	v_mfma_f32_16x16x32_bf16 v[94:97], v[110:113], v[182:185], v[94:97]
	v_mfma_f32_16x16x32_bf16 v[90:93], v[126:129], v[182:185], v[90:93]
	v_mfma_f32_16x16x32_bf16 v[78:81], v[110:113], v[206:209], v[78:81]
	v_mfma_f32_16x16x32_bf16 v[74:77], v[126:129], v[206:209], v[74:77]
	v_mfma_f32_16x16x32_bf16 v[134:137], v[138:141], v[154:157], v[134:137]
	v_mfma_f32_16x16x32_bf16 v[130:133], v[146:149], v[154:157], v[130:133]
	v_mfma_f32_16x16x32_bf16 v[106:109], v[138:141], v[170:173], v[106:109]
	v_mfma_f32_16x16x32_bf16 v[102:105], v[146:149], v[170:173], v[102:105]
	v_mfma_f32_16x16x32_bf16 v[86:89], v[138:141], v[178:181], v[86:89]
	v_mfma_f32_16x16x32_bf16 v[82:85], v[146:149], v[178:181], v[82:85]
	v_mfma_f32_16x16x32_bf16 v[70:73], v[138:141], v[186:189], v[70:73]
	v_mfma_f32_16x16x32_bf16 v[66:69], v[146:149], v[186:189], v[66:69]
	v_mfma_f32_16x16x32_bf16 v[134:137], v[142:145], v[166:169], v[134:137]
	v_mfma_f32_16x16x32_bf16 v[130:133], v[150:153], v[166:169], v[130:133]
	v_mfma_f32_16x16x32_bf16 v[106:109], v[142:145], v[174:177], v[106:109]
	v_mfma_f32_16x16x32_bf16 v[102:105], v[150:153], v[174:177], v[102:105]
	v_mfma_f32_16x16x32_bf16 v[86:89], v[142:145], v[182:185], v[86:89]
	v_mfma_f32_16x16x32_bf16 v[82:85], v[150:153], v[182:185], v[82:85]
	v_mfma_f32_16x16x32_bf16 v[70:73], v[142:145], v[206:209], v[70:73]
	v_mfma_f32_16x16x32_bf16 v[66:69], v[150:153], v[206:209], v[66:69]
	s_setprio 0
	s_barrier
	s_add_i32 s20, s39, s2
	v_lshl_add_u64 v[210:211], s[24:25], 0, v[192:193]
	s_mov_b32 m0, s20
	ds_read_b128 v[154:157], v236 offset:16384
	ds_read_b128 v[166:169], v236 offset:17408
	ds_read_b128 v[170:173], v236 offset:18432
	ds_read_b128 v[174:177], v236 offset:19456
	ds_read_b128 v[178:181], v236 offset:20480
	ds_read_b128 v[182:185], v236 offset:21504
	ds_read_b128 v[186:189], v236 offset:22528
	ds_read_b128 v[206:209], v236 offset:23552
	global_load_lds_dwordx4 v[210:211], off
	s_add_i32 m0, s20, 0x2000
	s_add_u32 s20, s24, 0xb0000
	v_lshl_add_u64 v[212:213], s[24:25], 0, v[196:197]
	s_addc_u32 s21, s25, 0
	s_add_i32 s58, s48, s2
	global_load_lds_dwordx4 v[212:213], off
	s_mov_b32 m0, s58
	v_lshl_add_u64 v[216:217], s[26:27], 0, v[194:195]
	global_load_lds_dwordx4 v192, s[20:21]
	s_add_i32 m0, s58, 0x2000
	s_nop 0
	global_load_lds_dwordx4 v196, s[20:21]
	v_lshl_add_u64 v[214:215], s[26:27], 0, v[190:191]
	s_mov_b32 m0, s3
	s_nop 0
	global_load_lds_dwordx4 v[214:215], off
	s_mov_b32 m0, s28
	s_nop 0
	global_load_lds_dwordx4 v[216:217], off
	s_waitcnt vmcnt(8)
	s_waitcnt lgkmcnt(0)
	s_barrier
	s_setprio 3
	s_waitcnt lgkmcnt(0)
	v_mfma_f32_16x16x32_bf16 v[62:65], v[98:101], v[154:157], v[62:65]
	v_mfma_f32_16x16x32_bf16 v[58:61], v[122:125], v[154:157], v[58:61]
	v_mfma_f32_16x16x32_bf16 v[46:49], v[98:101], v[170:173], v[46:49]
	v_mfma_f32_16x16x32_bf16 v[42:45], v[122:125], v[170:173], v[42:45]
	v_mfma_f32_16x16x32_bf16 v[30:33], v[98:101], v[178:181], v[30:33]
	v_mfma_f32_16x16x32_bf16 v[26:29], v[122:125], v[178:181], v[26:29]
	v_mfma_f32_16x16x32_bf16 v[14:17], v[98:101], v[186:189], v[14:17]
	v_mfma_f32_16x16x32_bf16 v[10:13], v[122:125], v[186:189], v[10:13]
	v_mfma_f32_16x16x32_bf16 v[62:65], v[110:113], v[166:169], v[62:65]
	v_mfma_f32_16x16x32_bf16 v[58:61], v[126:129], v[166:169], v[58:61]
	v_mfma_f32_16x16x32_bf16 v[46:49], v[110:113], v[174:177], v[46:49]
	v_mfma_f32_16x16x32_bf16 v[42:45], v[126:129], v[174:177], v[42:45]
	v_mfma_f32_16x16x32_bf16 v[30:33], v[110:113], v[182:185], v[30:33]
	v_mfma_f32_16x16x32_bf16 v[26:29], v[126:129], v[182:185], v[26:29]
	v_mfma_f32_16x16x32_bf16 v[14:17], v[110:113], v[206:209], v[14:17]
	v_mfma_f32_16x16x32_bf16 v[10:13], v[126:129], v[206:209], v[10:13]
	v_mfma_f32_16x16x32_bf16 v[54:57], v[138:141], v[154:157], v[54:57]
	v_mfma_f32_16x16x32_bf16 v[50:53], v[146:149], v[154:157], v[50:53]
	v_mfma_f32_16x16x32_bf16 v[38:41], v[138:141], v[170:173], v[38:41]
	v_mfma_f32_16x16x32_bf16 v[34:37], v[146:149], v[170:173], v[34:37]
	v_mfma_f32_16x16x32_bf16 v[22:25], v[138:141], v[178:181], v[22:25]
	v_mfma_f32_16x16x32_bf16 v[18:21], v[146:149], v[178:181], v[18:21]
	v_mfma_f32_16x16x32_bf16 v[6:9], v[138:141], v[186:189], v[6:9]
	v_mfma_f32_16x16x32_bf16 v[2:5], v[146:149], v[186:189], v[2:5]
	v_mfma_f32_16x16x32_bf16 v[54:57], v[142:145], v[166:169], v[54:57]
	v_mfma_f32_16x16x32_bf16 v[50:53], v[150:153], v[166:169], v[50:53]
	v_mfma_f32_16x16x32_bf16 v[38:41], v[142:145], v[174:177], v[38:41]
	v_mfma_f32_16x16x32_bf16 v[34:37], v[150:153], v[174:177], v[34:37]
	v_mfma_f32_16x16x32_bf16 v[22:25], v[142:145], v[182:185], v[22:25]
	v_mfma_f32_16x16x32_bf16 v[18:21], v[150:153], v[182:185], v[18:21]
	v_mfma_f32_16x16x32_bf16 v[6:9], v[142:145], v[206:209], v[6:9]
	v_mfma_f32_16x16x32_bf16 v[2:5], v[150:153], v[206:209], v[2:5]
	s_setprio 0
	s_barrier
; #define PG8_STAGE_A(b, h, ptr, NX) do { if constexpr (Sched::GATHER) { unsigned gs_[2]; gs_[0] = ((NX) && last_) ? gN[h][0] : gA[h][0]; gs_[1] = ((NX) && last_) ? gN[h][1] : gA[h][1]; PG8_STAGE(PG8_SA(b, h), ptr, gs_); } \
;         else PG8_STAGE(PG8_SA(b, h), (ptr) + ((h) ? hstep : (size_t)0), voffA); } while (0)
; #define PG8_STAGE(bufoff, gbase, voff) do { _Pragma("unroll") for (int _i = 0; _i < 2; ++_i) \
;         __builtin_amdgcn_global_load_lds((const unsigned*)((const char*)(gbase) + (voff)[_i]), (PG8_LAS unsigned*)(lds + (bufoff) + ldsw + _i * 8192), 16, 0, 0); } while (0)
; #define PG8_LDA(dst, b, h) do { _Pragma("unroll") for (int m = 0; m < 4; ++m) _Pragma("unroll") for (int k = 0; k < 2; ++k) dst[m][k] = *(const PG8_LAS bf16x8*)(lds + PG8_SA(b, h) + aoff + m * 2048 + k * 1024); } while (0)
; #define PG8_LDB(dst, b, h) do { _Pragma("unroll") for (int n = 0; n < 2; ++n) _Pragma("unroll") for (int k = 0; k < 2; ++k) dst[n][k] = *(const PG8_LAS bf16x8*)(lds + PG8_SB(b, h) + boff + n * 2048 + k * 1024); } while (0)
; #define PG8_MMA(ai, bj, At, Bt) do { __builtin_amdgcn_s_setprio(1); _Pragma("unroll") for (int m = 0; m < 4; ++m) _Pragma("unroll") for (int n = 0; n < 2; ++n) _Pragma("unroll") for (int k = 0; k < 2; ++k) \
;         acc[ai][bj][m][n] = __builtin_amdgcn_mfma_f32_16x16x32_bf16(Bt[n][k], At[m][k], acc[ai][bj][m][n], 0, 0, 0); __builtin_amdgcn_s_setprio(0); } while (0)
; #define PG8_WAIT_V(n) asm volatile("s_waitcnt vmcnt(" #n ")" ::: "memory")
; #define PG8_WAIT_L(n) asm volatile("s_waitcnt lgkmcnt(" #n ")" ::: "memory")
; #define PG8_BAR __builtin_amdgcn_s_barrier()
; #define PG8_SCHED __builtin_amdgcn_sched_barrier(0)
; template <class Epi, class Sched, bool ALIGN_EPI = false, bool SP2 = false>
; __device__ __forceinline__ void gemm_phase(PG8_LAS unsigned char* lds, const Gemm g, const Sched& S, const Epi& E, const bool skip_epi = false) {
;     ...
;             PG8_LDB(B0, 1, 0); PG8_LDB(B1, 1, 1); PG8_SCHED; PG8_LDA(At, 1, 0); PG8_STAGE_A(0, 1, a2, true);
;             PG8_WAIT_V(8); PG8_WAIT_L(0); PG8_BAR; PG8_MMA(0, 0, At, B0); PG8_MMA(0, 1, At, B1); PG8_BAR; PG8_SCHED;
;             PG8_LDA(At, 1, 1); PG8_STAGE(PG8_SB(1, 0), b3, voffB); PG8_STAGE(PG8_SB(1, 1), b3 + hstep, voffB); PG8_STAGE_A(1, 0, a3, true);
;             PG8_WAIT_V(8); PG8_WAIT_L(0); PG8_BAR; PG8_MMA(1, 0, At, B0); PG8_MMA(1, 1, At, B1); PG8_BAR; PG8_SCHED;
	s_add_i32 s58, 0, 0x18000
	s_add_i32 s59, 0, 0x1c000
	v_add_u32_e32 v126, s58, v229
	v_add_u32_e32 v150, s59, v229
	ds_read_b128 v[98:101], v126
	ds_read_b128 v[110:113], v126 offset:1024
	ds_read_b128 v[122:125], v126 offset:2048
	ds_read_b128 v[126:129], v126 offset:3072
	ds_read_b128 v[138:141], v150
	ds_read_b128 v[142:145], v150 offset:1024
	ds_read_b128 v[146:149], v150 offset:2048
	ds_read_b128 v[150:153], v150 offset:3072
	s_add_u32 s20, s26, 0xb0000
	s_addc_u32 s21, s27, 0
	s_mov_b32 m0, s29
	ds_read_b128 v[154:157], v236 offset:32768
	ds_read_b128 v[166:169], v236 offset:33792
	ds_read_b128 v[170:173], v236 offset:34816
	ds_read_b128 v[174:177], v236 offset:35840
	ds_read_b128 v[178:181], v236 offset:36864
	ds_read_b128 v[182:185], v236 offset:37888
	ds_read_b128 v[186:189], v236 offset:38912
	ds_read_b128 v[206:209], v236 offset:39936
	global_load_lds_dwordx4 v190, s[20:21]
	s_mov_b32 m0, s30
	s_nop 0
	global_load_lds_dwordx4 v194, s[20:21]
	s_waitcnt vmcnt(8)
	s_waitcnt lgkmcnt(0)
	s_barrier
	s_setprio 3
	s_waitcnt lgkmcnt(0)
	v_mfma_f32_16x16x32_bf16 v[162:165], v[98:101], v[154:157], v[162:165]
	v_mfma_f32_16x16x32_bf16 v[158:161], v[122:125], v[154:157], v[158:161]
	v_mfma_f32_16x16x32_bf16 v[118:121], v[98:101], v[170:173], v[118:121]
	v_mfma_f32_16x16x32_bf16 v[114:117], v[122:125], v[170:173], v[114:117]
	v_mfma_f32_16x16x32_bf16 v[94:97], v[98:101], v[178:181], v[94:97]
	v_mfma_f32_16x16x32_bf16 v[90:93], v[122:125], v[178:181], v[90:93]
	v_mfma_f32_16x16x32_bf16 v[78:81], v[98:101], v[186:189], v[78:81]
	v_mfma_f32_16x16x32_bf16 v[74:77], v[122:125], v[186:189], v[74:77]
	v_mfma_f32_16x16x32_bf16 v[162:165], v[110:113], v[166:169], v[162:165]
	v_mfma_f32_16x16x32_bf16 v[158:161], v[126:129], v[166:169], v[158:161]
	v_mfma_f32_16x16x32_bf16 v[118:121], v[110:113], v[174:177], v[118:121]
	v_mfma_f32_16x16x32_bf16 v[114:117], v[126:129], v[174:177], v[114:117]
	v_mfma_f32_16x16x32_bf16 v[94:97], v[110:113], v[182:185], v[94:97]
	v_mfma_f32_16x16x32_bf16 v[90:93], v[126:129], v[182:185], v[90:93]
	v_mfma_f32_16x16x32_bf16 v[78:81], v[110:113], v[206:209], v[78:81]
	v_mfma_f32_16x16x32_bf16 v[74:77], v[126:129], v[206:209], v[74:77]
	v_mfma_f32_16x16x32_bf16 v[134:137], v[138:141], v[154:157], v[134:137]
	v_mfma_f32_16x16x32_bf16 v[130:133], v[146:149], v[154:157], v[130:133]
	v_mfma_f32_16x16x32_bf16 v[106:109], v[138:141], v[170:173], v[106:109]
	v_mfma_f32_16x16x32_bf16 v[102:105], v[146:149], v[170:173], v[102:105]
	v_mfma_f32_16x16x32_bf16 v[86:89], v[138:141], v[178:181], v[86:89]
	v_mfma_f32_16x16x32_bf16 v[82:85], v[146:149], v[178:181], v[82:85]
	v_mfma_f32_16x16x32_bf16 v[70:73], v[138:141], v[186:189], v[70:73]
	v_mfma_f32_16x16x32_bf16 v[66:69], v[146:149], v[186:189], v[66:69]
	v_mfma_f32_16x16x32_bf16 v[134:137], v[142:145], v[166:169], v[134:137]
	v_mfma_f32_16x16x32_bf16 v[130:133], v[150:153], v[166:169], v[130:133]
	v_mfma_f32_16x16x32_bf16 v[106:109], v[142:145], v[174:177], v[106:109]
	v_mfma_f32_16x16x32_bf16 v[102:105], v[150:153], v[174:177], v[102:105]
	v_mfma_f32_16x16x32_bf16 v[86:89], v[142:145], v[182:185], v[86:89]
	v_mfma_f32_16x16x32_bf16 v[82:85], v[150:153], v[182:185], v[82:85]
	v_mfma_f32_16x16x32_bf16 v[70:73], v[142:145], v[206:209], v[70:73]
	v_mfma_f32_16x16x32_bf16 v[66:69], v[150:153], v[206:209], v[66:69]
	s_setprio 0
	s_barrier
	s_add_i32 s20, s58, s2
	s_add_i32 m0, s20, 0xffffff80
	ds_read_b128 v[154:157], v236 offset:49152
	ds_read_b128 v[166:169], v236 offset:50176
	ds_read_b128 v[170:173], v236 offset:51200
	ds_read_b128 v[174:177], v236 offset:52224
	ds_read_b128 v[178:181], v236 offset:53248
	ds_read_b128 v[182:185], v236 offset:54272
	ds_read_b128 v[186:189], v236 offset:55296
	ds_read_b128 v[206:209], v236 offset:56320
	global_load_lds_dwordx4 v[210:211], off offset:128
	s_add_i32 m0, s20, 0x1f80
	s_add_u32 s20, s24, 0xb0080
	s_addc_u32 s21, s25, 0
	s_add_i32 s24, s59, s2
	global_load_lds_dwordx4 v[212:213], off offset:128
	s_mov_b32 m0, s24
	s_nop 0
	global_load_lds_dwordx4 v192, s[20:21]
	s_add_i32 m0, s24, 0x2000
	s_nop 0
	global_load_lds_dwordx4 v196, s[20:21]
	s_add_i32 m0, s35, 0xffffff80
	s_nop 0
	global_load_lds_dwordx4 v[214:215], off offset:128
	s_add_i32 m0, s36, 0xffffff80
	s_nop 0
	global_load_lds_dwordx4 v[216:217], off offset:128
	s_waitcnt vmcnt(8)
	s_waitcnt lgkmcnt(0)
	s_barrier
	s_setprio 3
	s_waitcnt lgkmcnt(0)
	v_mfma_f32_16x16x32_bf16 v[62:65], v[98:101], v[154:157], v[62:65]
	v_mfma_f32_16x16x32_bf16 v[58:61], v[122:125], v[154:157], v[58:61]
	v_mfma_f32_16x16x32_bf16 v[46:49], v[98:101], v[170:173], v[46:49]
	v_mfma_f32_16x16x32_bf16 v[42:45], v[122:125], v[170:173], v[42:45]
	v_mfma_f32_16x16x32_bf16 v[30:33], v[98:101], v[178:181], v[30:33]
	v_mfma_f32_16x16x32_bf16 v[26:29], v[122:125], v[178:181], v[26:29]
	v_mfma_f32_16x16x32_bf16 v[14:17], v[98:101], v[186:189], v[14:17]
	v_mfma_f32_16x16x32_bf16 v[10:13], v[122:125], v[186:189], v[10:13]
	v_mfma_f32_16x16x32_bf16 v[62:65], v[110:113], v[166:169], v[62:65]
	v_mfma_f32_16x16x32_bf16 v[58:61], v[126:129], v[166:169], v[58:61]
	v_mfma_f32_16x16x32_bf16 v[46:49], v[110:113], v[174:177], v[46:49]
	v_mfma_f32_16x16x32_bf16 v[42:45], v[126:129], v[174:177], v[42:45]
	v_mfma_f32_16x16x32_bf16 v[30:33], v[110:113], v[182:185], v[30:33]
	v_mfma_f32_16x16x32_bf16 v[26:29], v[126:129], v[182:185], v[26:29]
	v_mfma_f32_16x16x32_bf16 v[14:17], v[110:113], v[206:209], v[14:17]
	v_mfma_f32_16x16x32_bf16 v[10:13], v[126:129], v[206:209], v[10:13]
	v_mfma_f32_16x16x32_bf16 v[54:57], v[138:141], v[154:157], v[54:57]
	v_mfma_f32_16x16x32_bf16 v[50:53], v[146:149], v[154:157], v[50:53]
	v_mfma_f32_16x16x32_bf16 v[38:41], v[138:141], v[170:173], v[38:41]
	v_mfma_f32_16x16x32_bf16 v[34:37], v[146:149], v[170:173], v[34:37]
	v_mfma_f32_16x16x32_bf16 v[22:25], v[138:141], v[178:181], v[22:25]
	v_mfma_f32_16x16x32_bf16 v[18:21], v[146:149], v[178:181], v[18:21]
	v_mfma_f32_16x16x32_bf16 v[6:9], v[138:141], v[186:189], v[6:9]
	v_mfma_f32_16x16x32_bf16 v[2:5], v[146:149], v[186:189], v[2:5]
	v_mfma_f32_16x16x32_bf16 v[54:57], v[142:145], v[166:169], v[54:57]
	v_mfma_f32_16x16x32_bf16 v[50:53], v[150:153], v[166:169], v[50:53]
	v_mfma_f32_16x16x32_bf16 v[38:41], v[142:145], v[174:177], v[38:41]
	v_mfma_f32_16x16x32_bf16 v[34:37], v[150:153], v[174:177], v[34:37]
	v_mfma_f32_16x16x32_bf16 v[22:25], v[142:145], v[182:185], v[22:25]
	v_mfma_f32_16x16x32_bf16 v[18:21], v[150:153], v[182:185], v[18:21]
	v_mfma_f32_16x16x32_bf16 v[6:9], v[142:145], v[206:209], v[6:9]
	v_mfma_f32_16x16x32_bf16 v[2:5], v[150:153], v[206:209], v[2:5]
	s_setprio 0
	s_barrier
	s_add_i32 s57, s57, 2
	s_add_u32 s55, s55, 0x100
	s_addc_u32 s56, s56, 0
	s_cmp_gt_u32 s57, 41
	s_mov_b64 s[20:21], s[22:23]
	s_cbranch_scc0 .LBB0_857
	s_and_b64 vcc, exec, s[16:17]
	s_cbranch_vccz .LBB0_860
	s_barrier

; #define PG8_STAGE_A(b, h, ptr, NX) do { if constexpr (Sched::GATHER) { unsigned gs_[2]; gs_[0] = ((NX) && last_) ? gN[h][0] : gA[h][0]; gs_[1] = ((NX) && last_) ? gN[h][1] : gA[h][1]; PG8_STAGE(PG8_SA(b, h), ptr, gs_); } \
;         else PG8_STAGE(PG8_SA(b, h), (ptr) + ((h) ? hstep : (size_t)0), voffA); } while (0)
; #define PG8_STAGE(bufoff, gbase, voff) do { _Pragma("unroll") for (int _i = 0; _i < 2; ++_i) \
;         __builtin_amdgcn_global_load_lds((const unsigned*)((const char*)(gbase) + (voff)[_i]), (PG8_LAS unsigned*)(lds + (bufoff) + ldsw + _i * 8192), 16, 0, 0); } while (0)
; #define PG8_LDA(dst, b, h) do { _Pragma("unroll") for (int m = 0; m < 4; ++m) _Pragma("unroll") for (int k = 0; k < 2; ++k) dst[m][k] = *(const PG8_LAS bf16x8*)(lds + PG8_SA(b, h) + aoff + m * 2048 + k * 1024); } while (0)
; #define PG8_WAIT_V(n) asm volatile("s_waitcnt vmcnt(" #n ")" ::: "memory")
; #define PG8_WAIT_L(n) asm volatile("s_waitcnt lgkmcnt(" #n ")" ::: "memory")
; #define PG8_BAR __builtin_amdgcn_s_barrier()
; template <class Epi, class Sched, bool ALIGN_EPI = false, bool SP2 = false>
; __device__ __forceinline__ void gemm_phase(PG8_LAS unsigned char* lds, const Gemm g, const Sched& S, const Epi& E, const bool skip_epi = false) {
;     ...
;         const char* nA = has_next ? (const char*)g.A + (size_t)nxt.pm * pmstepA + nxt.ko : cA; const char* nB = has_next ? (const char*)g.Bt + (size_t)nxt.pn * tstep + nxt.ko : cB;
;         for (int t = 0; t < nt; t += 2) {
;             const bool last = (t == nt - 2); last_ = last && has_next;
;             const char* a1 = cA + (size_t)(t + 1) * kstep;
;             const char* a2 = last ? nA : cA + (size_t)(t + 2) * kstep; const char* b2 = last ? nB : cB + (size_t)(t + 2) * kstep;
;             const char* a3 = a2 + kstep; const char* b3 = b2 + kstep;
;             if (last && has_next) S.a_ready(nxt);
;             if constexpr (SP2) {
;             PG8_LDB(B0, 0, 0); PG8_LDB(B1, 0, 1); PG8_SCHED; PG8_LDA(At, 0, 0); PG8_STAGE_A(1, 1, a1, false);
;             PG8_WAIT_V(8); PG8_WAIT_L(0); PG8_BAR; PG8_MMA(0, 0, At, B0); PG8_MMA(0, 1, At, B1); PG8_BAR; PG8_SCHED;
;             PG8_LDA(At, 0, 1); PG8_STAGE(PG8_SB(0, 0), b2, voffB); PG8_STAGE(PG8_SB(0, 1), b2 + hstep, voffB); PG8_STAGE_A(0, 0, a2, true);
;             PG8_WAIT_V(8); PG8_WAIT_L(0); PG8_BAR; PG8_MMA(1, 0, At, B0); PG8_MMA(1, 1, At, B1); PG8_BAR; PG8_SCHED;
.LBB0_943:
	s_ashr_i32 s15, s14, 31
	s_lshl_b64 s[16:17], s[14:15], 19
	s_add_u32 s16, s86, s16
	s_addc_u32 s17, s87, s17
	s_and_b64 s[18:19], s[4:5], exec
	s_cselect_b32 s15, s17, s23
	s_cselect_b32 s54, s16, s22
	s_ashr_i32 s13, s12, 31
	s_lshl_b64 s[18:19], s[12:13], 19
	s_add_u32 s18, s2, s18
	s_addc_u32 s19, s3, s19
	s_and_b64 s[26:27], s[4:5], exec
	s_cselect_b32 s13, s19, s25
	s_cselect_b32 s55, s18, s24
	s_add_u32 s22, s22, 0x40080
	s_addc_u32 s23, s23, 0
	s_add_u32 s56, s24, 0x100
	s_addc_u32 s57, s25, 0
	s_mov_b32 s58, -2
	s_waitcnt vmcnt(0)
	ds_read_b128 v[148:151], v170
	ds_read_b128 v[152:155], v170 offset:1024
	ds_read_b128 v[156:159], v170 offset:2048
	ds_read_b128 v[160:163], v170 offset:3072
	ds_read_b128 v[176:179], v171
	ds_read_b128 v[180:183], v171 offset:1024
	ds_read_b128 v[184:187], v171 offset:2048
	ds_read_b128 v[188:191], v171 offset:3072
	s_add_u32 s24, s22, 0xfffc0080
	s_addc_u32 s25, s23, -1
	s_cmp_eq_u32 s58, 12
	s_cselect_b32 s27, s15, s25
	s_cselect_b32 s26, s54, s24
	s_cselect_b32 s25, s13, s57
	s_cselect_b32 s24, s55, s56
	s_add_i32 m0, s21, 0xc000
	ds_read_b128 v[192:195], v172
	ds_read_b128 v[196:199], v172 offset:1024
	ds_read_b128 v[200:203], v172 offset:2048
	ds_read_b128 v[204:207], v172 offset:3072
	ds_read_b128 v[208:211], v172 offset:4096
	ds_read_b128 v[212:215], v172 offset:5120
	ds_read_b128 v[216:219], v172 offset:6144
	ds_read_b128 v[220:223], v172 offset:7168
	global_load_lds_dwordx4 v140, s[22:23]
	s_add_i32 m0, s21, 0xe000
	s_nop 0
	global_load_lds_dwordx4 v142, s[22:23]
	s_waitcnt vmcnt(8)
	s_waitcnt lgkmcnt(0)
	s_barrier
	s_setprio 3
	s_waitcnt lgkmcnt(0)
	v_mfma_f32_16x16x32_bf16 v[126:129], v[148:151], v[192:195], 0
	v_mfma_f32_16x16x32_bf16 v[122:125], v[156:159], v[192:195], 0
	v_mfma_f32_16x16x32_bf16 v[114:117], v[148:151], v[200:203], 0
	v_mfma_f32_16x16x32_bf16 v[106:109], v[156:159], v[200:203], 0
	v_mfma_f32_16x16x32_bf16 v[98:101], v[148:151], v[208:211], 0
	v_mfma_f32_16x16x32_bf16 v[90:93], v[156:159], v[208:211], 0
	v_mfma_f32_16x16x32_bf16 v[82:85], v[148:151], v[216:219], 0
	v_mfma_f32_16x16x32_bf16 v[74:77], v[156:159], v[216:219], 0
	v_mfma_f32_16x16x32_bf16 v[126:129], v[152:155], v[196:199], v[126:129]
	v_mfma_f32_16x16x32_bf16 v[122:125], v[160:163], v[196:199], v[122:125]
	v_mfma_f32_16x16x32_bf16 v[114:117], v[152:155], v[204:207], v[114:117]
	v_mfma_f32_16x16x32_bf16 v[106:109], v[160:163], v[204:207], v[106:109]
	v_mfma_f32_16x16x32_bf16 v[98:101], v[152:155], v[212:215], v[98:101]
	v_mfma_f32_16x16x32_bf16 v[90:93], v[160:163], v[212:215], v[90:93]
	v_mfma_f32_16x16x32_bf16 v[82:85], v[152:155], v[220:223], v[82:85]
	v_mfma_f32_16x16x32_bf16 v[74:77], v[160:163], v[220:223], v[74:77]
	v_mfma_f32_16x16x32_bf16 v[118:121], v[176:179], v[192:195], 0
	v_mfma_f32_16x16x32_bf16 v[110:113], v[184:187], v[192:195], 0
	v_mfma_f32_16x16x32_bf16 v[102:105], v[176:179], v[200:203], 0
	v_mfma_f32_16x16x32_bf16 v[94:97], v[184:187], v[200:203], 0
	v_mfma_f32_16x16x32_bf16 v[86:89], v[176:179], v[208:211], 0
	v_mfma_f32_16x16x32_bf16 v[78:81], v[184:187], v[208:211], 0
	v_mfma_f32_16x16x32_bf16 v[70:73], v[176:179], v[216:219], 0
	v_mfma_f32_16x16x32_bf16 v[66:69], v[184:187], v[216:219], 0
	v_mfma_f32_16x16x32_bf16 v[118:121], v[180:183], v[196:199], v[118:121]
	v_mfma_f32_16x16x32_bf16 v[110:113], v[188:191], v[196:199], v[110:113]
	v_mfma_f32_16x16x32_bf16 v[102:105], v[180:183], v[204:207], v[102:105]
	v_mfma_f32_16x16x32_bf16 v[94:97], v[188:191], v[204:207], v[94:97]
	v_mfma_f32_16x16x32_bf16 v[86:89], v[180:183], v[212:215], v[86:89]
	v_mfma_f32_16x16x32_bf16 v[78:81], v[188:191], v[212:215], v[78:81]
	v_mfma_f32_16x16x32_bf16 v[70:73], v[180:183], v[220:223], v[70:73]
	v_mfma_f32_16x16x32_bf16 v[66:69], v[188:191], v[220:223], v[66:69]
	s_setprio 0
	s_barrier
	s_add_i32 s59, s48, s28
	v_lshl_add_u64 v[164:165], s[24:25], 0, v[134:135]
	s_mov_b32 m0, s59
	ds_read_b128 v[192:195], v172 offset:16384
	ds_read_b128 v[196:199], v172 offset:17408
	ds_read_b128 v[200:203], v172 offset:18432
	ds_read_b128 v[204:207], v172 offset:19456
	ds_read_b128 v[208:211], v172 offset:20480
	ds_read_b128 v[212:215], v172 offset:21504
	ds_read_b128 v[216:219], v172 offset:22528
	ds_read_b128 v[220:223], v172 offset:23552
	global_load_lds_dwordx4 v[164:165], off
	s_add_i32 m0, s59, 0x2000
	s_add_u32 s60, s24, 0x40000
	v_lshl_add_u64 v[224:225], s[24:25], 0, v[130:131]
	s_addc_u32 s61, s25, 0
	s_add_i32 s59, s49, s28
	global_load_lds_dwordx4 v[224:225], off
	s_mov_b32 m0, s59
	v_lshl_add_u64 v[230:231], s[26:27], 0, v[132:133]
	global_load_lds_dwordx4 v134, s[60:61]
	s_add_i32 m0, s59, 0x2000
	s_nop 0
	global_load_lds_dwordx4 v130, s[60:61]
	v_lshl_add_u64 v[226:227], s[26:27], 0, v[136:137]
	s_mov_b32 m0, s21
	s_nop 0
	global_load_lds_dwordx4 v[226:227], off
	s_mov_b32 m0, s31
	s_nop 0
	global_load_lds_dwordx4 v[230:231], off
	s_waitcnt vmcnt(8)
	s_waitcnt lgkmcnt(0)
	s_barrier
; #define PG8_STAGE_A(b, h, ptr, NX) do { if constexpr (Sched::GATHER) { unsigned gs_[2]; gs_[0] = ((NX) && last_) ? gN[h][0] : gA[h][0]; gs_[1] = ((NX) && last_) ? gN[h][1] : gA[h][1]; PG8_STAGE(PG8_SA(b, h), ptr, gs_); } \
;         else PG8_STAGE(PG8_SA(b, h), (ptr) + ((h) ? hstep : (size_t)0), voffA); } while (0)
; #define PG8_LDA(dst, b, h) do { _Pragma("unroll") for (int m = 0; m < 4; ++m) _Pragma("unroll") for (int k = 0; k < 2; ++k) dst[m][k] = *(const PG8_LAS bf16x8*)(lds + PG8_SA(b, h) + aoff + m * 2048 + k * 1024); } while (0)
; #define PG8_LDB(dst, b, h) do { _Pragma("unroll") for (int n = 0; n < 2; ++n) _Pragma("unroll") for (int k = 0; k < 2; ++k) dst[n][k] = *(const PG8_LAS bf16x8*)(lds + PG8_SB(b, h) + boff + n * 2048 + k * 1024); } while (0)
; #define PG8_MMA(ai, bj, At, Bt) do { __builtin_amdgcn_s_setprio(1); _Pragma("unroll") for (int m = 0; m < 4; ++m) _Pragma("unroll") for (int n = 0; n < 2; ++n) _Pragma("unroll") for (int k = 0; k < 2; ++k) \
;         acc[ai][bj][m][n] = __builtin_amdgcn_mfma_f32_16x16x32_bf16(Bt[n][k], At[m][k], acc[ai][bj][m][n], 0, 0, 0); __builtin_amdgcn_s_setprio(0); } while (0)
; #define PG8_WAIT_V(n) asm volatile("s_waitcnt vmcnt(" #n ")" ::: "memory")
; #define PG8_WAIT_L(n) asm volatile("s_waitcnt lgkmcnt(" #n ")" ::: "memory")
; #define PG8_BAR __builtin_amdgcn_s_barrier()
; #define PG8_SCHED __builtin_amdgcn_sched_barrier(0)
; template <class Epi, class Sched, bool ALIGN_EPI = false, bool SP2 = false>
; __device__ __forceinline__ void gemm_phase(PG8_LAS unsigned char* lds, const Gemm g, const Sched& S, const Epi& E, const bool skip_epi = false) {
;     ...
;             PG8_WAIT_V(8); PG8_WAIT_L(0); PG8_BAR; PG8_MMA(1, 0, At, B0); PG8_MMA(1, 1, At, B1); PG8_BAR; PG8_SCHED;
;             PG8_LDB(B0, 1, 0); PG8_LDB(B1, 1, 1); PG8_SCHED; PG8_LDA(At, 1, 0); PG8_STAGE_A(0, 1, a2, true);
;             PG8_WAIT_V(8); PG8_WAIT_L(0); PG8_BAR; PG8_MMA(0, 0, At, B0); PG8_MMA(0, 1, At, B1); PG8_BAR; PG8_SCHED;
	s_setprio 3
	s_waitcnt lgkmcnt(0)
	v_mfma_f32_16x16x32_bf16 v[62:65], v[148:151], v[192:195], 0
	v_mfma_f32_16x16x32_bf16 v[58:61], v[156:159], v[192:195], 0
	v_mfma_f32_16x16x32_bf16 v[50:53], v[148:151], v[200:203], 0
	v_mfma_f32_16x16x32_bf16 v[42:45], v[156:159], v[200:203], 0
	v_mfma_f32_16x16x32_bf16 v[34:37], v[148:151], v[208:211], 0
	v_mfma_f32_16x16x32_bf16 v[26:29], v[156:159], v[208:211], 0
	v_mfma_f32_16x16x32_bf16 v[18:21], v[148:151], v[216:219], 0
	v_mfma_f32_16x16x32_bf16 v[10:13], v[156:159], v[216:219], 0
	v_mfma_f32_16x16x32_bf16 v[62:65], v[152:155], v[196:199], v[62:65]
	v_mfma_f32_16x16x32_bf16 v[58:61], v[160:163], v[196:199], v[58:61]
	v_mfma_f32_16x16x32_bf16 v[50:53], v[152:155], v[204:207], v[50:53]
	v_mfma_f32_16x16x32_bf16 v[42:45], v[160:163], v[204:207], v[42:45]
	v_mfma_f32_16x16x32_bf16 v[34:37], v[152:155], v[212:215], v[34:37]
	v_mfma_f32_16x16x32_bf16 v[26:29], v[160:163], v[212:215], v[26:29]
	v_mfma_f32_16x16x32_bf16 v[18:21], v[152:155], v[220:223], v[18:21]
	v_mfma_f32_16x16x32_bf16 v[10:13], v[160:163], v[220:223], v[10:13]
	v_mfma_f32_16x16x32_bf16 v[54:57], v[176:179], v[192:195], 0
	v_mfma_f32_16x16x32_bf16 v[46:49], v[184:187], v[192:195], 0
	v_mfma_f32_16x16x32_bf16 v[38:41], v[176:179], v[200:203], 0
	v_mfma_f32_16x16x32_bf16 v[30:33], v[184:187], v[200:203], 0
	v_mfma_f32_16x16x32_bf16 v[22:25], v[176:179], v[208:211], 0
	v_mfma_f32_16x16x32_bf16 v[14:17], v[184:187], v[208:211], 0
	v_mfma_f32_16x16x32_bf16 v[6:9], v[176:179], v[216:219], 0
	v_mfma_f32_16x16x32_bf16 v[2:5], v[184:187], v[216:219], 0
	v_mfma_f32_16x16x32_bf16 v[54:57], v[180:183], v[196:199], v[54:57]
	v_mfma_f32_16x16x32_bf16 v[46:49], v[188:191], v[196:199], v[46:49]
	v_mfma_f32_16x16x32_bf16 v[38:41], v[180:183], v[204:207], v[38:41]
	v_mfma_f32_16x16x32_bf16 v[30:33], v[188:191], v[204:207], v[30:33]
	v_mfma_f32_16x16x32_bf16 v[22:25], v[180:183], v[212:215], v[22:25]
	v_mfma_f32_16x16x32_bf16 v[14:17], v[188:191], v[212:215], v[14:17]
	v_mfma_f32_16x16x32_bf16 v[6:9], v[180:183], v[220:223], v[6:9]
	v_mfma_f32_16x16x32_bf16 v[2:5], v[188:191], v[220:223], v[2:5]
	s_setprio 0
	s_barrier
	s_add_i32 s59, 0, 0x18000
	s_add_i32 s60, 0, 0x1c000
	v_add_u32_e32 v160, s59, v1
	v_add_u32_e32 v188, s60, v1
	ds_read_b128 v[148:151], v160
	ds_read_b128 v[152:155], v160 offset:1024
	ds_read_b128 v[156:159], v160 offset:2048
	ds_read_b128 v[160:163], v160 offset:3072
	ds_read_b128 v[176:179], v188
	ds_read_b128 v[180:183], v188 offset:1024
	ds_read_b128 v[184:187], v188 offset:2048
	ds_read_b128 v[188:191], v188 offset:3072
	s_add_u32 s26, s26, 0x40000
	s_addc_u32 s27, s27, 0
	s_mov_b32 m0, s34
	ds_read_b128 v[192:195], v172 offset:32768
	ds_read_b128 v[196:199], v172 offset:33792
	ds_read_b128 v[200:203], v172 offset:34816
	ds_read_b128 v[204:207], v172 offset:35840
	ds_read_b128 v[208:211], v172 offset:36864
	ds_read_b128 v[212:215], v172 offset:37888
	ds_read_b128 v[216:219], v172 offset:38912
	ds_read_b128 v[220:223], v172 offset:39936
	global_load_lds_dwordx4 v136, s[26:27]
	s_mov_b32 m0, s35
	s_nop 0
	global_load_lds_dwordx4 v132, s[26:27]
	s_waitcnt vmcnt(8)
	s_waitcnt lgkmcnt(0)
	s_barrier
	s_setprio 3
	s_waitcnt lgkmcnt(0)
	v_mfma_f32_16x16x32_bf16 v[126:129], v[148:151], v[192:195], v[126:129]
	v_mfma_f32_16x16x32_bf16 v[122:125], v[156:159], v[192:195], v[122:125]
	v_mfma_f32_16x16x32_bf16 v[114:117], v[148:151], v[200:203], v[114:117]
	v_mfma_f32_16x16x32_bf16 v[106:109], v[156:159], v[200:203], v[106:109]
	v_mfma_f32_16x16x32_bf16 v[98:101], v[148:151], v[208:211], v[98:101]
	v_mfma_f32_16x16x32_bf16 v[90:93], v[156:159], v[208:211], v[90:93]
	v_mfma_f32_16x16x32_bf16 v[82:85], v[148:151], v[216:219], v[82:85]
	v_mfma_f32_16x16x32_bf16 v[74:77], v[156:159], v[216:219], v[74:77]
	v_mfma_f32_16x16x32_bf16 v[126:129], v[152:155], v[196:199], v[126:129]
	v_mfma_f32_16x16x32_bf16 v[122:125], v[160:163], v[196:199], v[122:125]
	v_mfma_f32_16x16x32_bf16 v[114:117], v[152:155], v[204:207], v[114:117]
	v_mfma_f32_16x16x32_bf16 v[106:109], v[160:163], v[204:207], v[106:109]
	v_mfma_f32_16x16x32_bf16 v[98:101], v[152:155], v[212:215], v[98:101]
	v_mfma_f32_16x16x32_bf16 v[90:93], v[160:163], v[212:215], v[90:93]
	v_mfma_f32_16x16x32_bf16 v[82:85], v[152:155], v[220:223], v[82:85]
	v_mfma_f32_16x16x32_bf16 v[74:77], v[160:163], v[220:223], v[74:77]
	v_mfma_f32_16x16x32_bf16 v[118:121], v[176:179], v[192:195], v[118:121]
	v_mfma_f32_16x16x32_bf16 v[110:113], v[184:187], v[192:195], v[110:113]
	v_mfma_f32_16x16x32_bf16 v[102:105], v[176:179], v[200:203], v[102:105]
	v_mfma_f32_16x16x32_bf16 v[94:97], v[184:187], v[200:203], v[94:97]
	v_mfma_f32_16x16x32_bf16 v[86:89], v[176:179], v[208:211], v[86:89]
	v_mfma_f32_16x16x32_bf16 v[78:81], v[184:187], v[208:211], v[78:81]
	v_mfma_f32_16x16x32_bf16 v[70:73], v[176:179], v[216:219], v[70:73]
	v_mfma_f32_16x16x32_bf16 v[66:69], v[184:187], v[216:219], v[66:69]
	v_mfma_f32_16x16x32_bf16 v[118:121], v[180:183], v[196:199], v[118:121]
	v_mfma_f32_16x16x32_bf16 v[110:113], v[188:191], v[196:199], v[110:113]
	v_mfma_f32_16x16x32_bf16 v[102:105], v[180:183], v[204:207], v[102:105]
	v_mfma_f32_16x16x32_bf16 v[94:97], v[188:191], v[204:207], v[94:97]
	v_mfma_f32_16x16x32_bf16 v[86:89], v[180:183], v[212:215], v[86:89]
	v_mfma_f32_16x16x32_bf16 v[78:81], v[188:191], v[212:215], v[78:81]
	v_mfma_f32_16x16x32_bf16 v[70:73], v[180:183], v[220:223], v[70:73]
	v_mfma_f32_16x16x32_bf16 v[66:69], v[188:191], v[220:223], v[66:69]
	s_setprio 0
	s_barrier
; #define PG8_STAGE_A(b, h, ptr, NX) do { if constexpr (Sched::GATHER) { unsigned gs_[2]; gs_[0] = ((NX) && last_) ? gN[h][0] : gA[h][0]; gs_[1] = ((NX) && last_) ? gN[h][1] : gA[h][1]; PG8_STAGE(PG8_SA(b, h), ptr, gs_); } \
;         else PG8_STAGE(PG8_SA(b, h), (ptr) + ((h) ? hstep : (size_t)0), voffA); } while (0)
; #define PG8_STAGE(bufoff, gbase, voff) do { _Pragma("unroll") for (int _i = 0; _i < 2; ++_i) \
;         __builtin_amdgcn_global_load_lds((const unsigned*)((const char*)(gbase) + (voff)[_i]), (PG8_LAS unsigned*)(lds + (bufoff) + ldsw + _i * 8192), 16, 0, 0); } while (0)
; #define PG8_LDA(dst, b, h) do { _Pragma("unroll") for (int m = 0; m < 4; ++m) _Pragma("unroll") for (int k = 0; k < 2; ++k) dst[m][k] = *(const PG8_LAS bf16x8*)(lds + PG8_SA(b, h) + aoff + m * 2048 + k * 1024); } while (0)
; #define PG8_LDB(dst, b, h) do { _Pragma("unroll") for (int n = 0; n < 2; ++n) _Pragma("unroll") for (int k = 0; k < 2; ++k) dst[n][k] = *(const PG8_LAS bf16x8*)(lds + PG8_SB(b, h) + boff + n * 2048 + k * 1024); } while (0)
; #define PG8_WAIT_V(n) asm volatile("s_waitcnt vmcnt(" #n ")" ::: "memory")
; #define PG8_BAR __builtin_amdgcn_s_barrier()
; template <class Epi, class Sched, bool ALIGN_EPI = false, bool SP2 = false>
; __device__ __forceinline__ void gemm_phase(PG8_LAS unsigned char* lds, const Gemm g, const Sched& S, const Epi& E, const bool skip_epi = false) {
;     ...
;             PG8_LDB(B0, 0, 0); PG8_LDB(B1, 0, 1); PG8_SCHED; PG8_LDA(At, 0, 0); PG8_STAGE_A(1, 1, a1, false);
;             PG8_WAIT_V(8); PG8_WAIT_L(0); PG8_BAR; PG8_MMA(0, 0, At, B0); PG8_MMA(0, 1, At, B1); PG8_BAR; PG8_SCHED;
;             PG8_LDA(At, 0, 1); PG8_STAGE(PG8_SB(0, 0), b2, voffB); PG8_STAGE(PG8_SB(0, 1), b2 + hstep, voffB); PG8_STAGE_A(0, 0, a2, true);
;             PG8_WAIT_V(8); PG8_WAIT_L(0); PG8_BAR; PG8_MMA(1, 0, At, B0); PG8_MMA(1, 1, At, B1); PG8_BAR; PG8_SCHED;
;             PG8_LDB(B0, 1, 0); PG8_LDB(B1, 1, 1); PG8_SCHED; PG8_LDA(At, 1, 0); PG8_STAGE_A(0, 1, a2, true);
;             PG8_WAIT_V(8); PG8_WAIT_L(0); PG8_BAR; PG8_MMA(0, 0, At, B0); PG8_MMA(0, 1, At, B1); PG8_BAR; PG8_SCHED;
;             PG8_LDA(At, 1, 1); PG8_STAGE(PG8_SB(1, 0), b3, voffB); PG8_STAGE(PG8_SB(1, 1), b3 + hstep, voffB); PG8_STAGE_A(1, 0, a3, true);
;             PG8_WAIT_V(8); PG8_WAIT_L(0); PG8_BAR; PG8_MMA(1, 0, At, B0); PG8_MMA(1, 1, At, B1); PG8_BAR; PG8_SCHED;
	s_add_i32 s26, s59, s28
	s_add_i32 m0, s26, 0xffffff80
	ds_read_b128 v[192:195], v172 offset:49152
	ds_read_b128 v[196:199], v172 offset:50176
	ds_read_b128 v[200:203], v172 offset:51200
	ds_read_b128 v[204:207], v172 offset:52224
	ds_read_b128 v[208:211], v172 offset:53248
	ds_read_b128 v[212:215], v172 offset:54272
	ds_read_b128 v[216:219], v172 offset:55296
	ds_read_b128 v[220:223], v172 offset:56320
	global_load_lds_dwordx4 v[164:165], off offset:128
	s_add_i32 m0, s26, 0x1f80
	s_add_u32 s24, s24, 0x40080
	s_addc_u32 s25, s25, 0
	s_add_i32 s26, s60, s28
	global_load_lds_dwordx4 v[224:225], off offset:128
	s_mov_b32 m0, s26
	s_nop 0
	global_load_lds_dwordx4 v134, s[24:25]
	s_add_i32 m0, s26, 0x2000
	s_nop 0
	global_load_lds_dwordx4 v130, s[24:25]
	s_add_i32 m0, s37, 0xffffff80
	s_nop 0
	global_load_lds_dwordx4 v[226:227], off offset:128
	s_add_i32 m0, s38, 0xffffff80
	s_nop 0
	global_load_lds_dwordx4 v[230:231], off offset:128
	s_waitcnt vmcnt(8)
	s_waitcnt lgkmcnt(0)
	s_barrier
	s_setprio 3
	s_waitcnt lgkmcnt(0)
	v_mfma_f32_16x16x32_bf16 v[62:65], v[148:151], v[192:195], v[62:65]
	v_mfma_f32_16x16x32_bf16 v[58:61], v[156:159], v[192:195], v[58:61]
	v_mfma_f32_16x16x32_bf16 v[50:53], v[148:151], v[200:203], v[50:53]
	v_mfma_f32_16x16x32_bf16 v[42:45], v[156:159], v[200:203], v[42:45]
	v_mfma_f32_16x16x32_bf16 v[34:37], v[148:151], v[208:211], v[34:37]
	v_mfma_f32_16x16x32_bf16 v[26:29], v[156:159], v[208:211], v[26:29]
	v_mfma_f32_16x16x32_bf16 v[18:21], v[148:151], v[216:219], v[18:21]
	v_mfma_f32_16x16x32_bf16 v[10:13], v[156:159], v[216:219], v[10:13]
	v_mfma_f32_16x16x32_bf16 v[62:65], v[152:155], v[196:199], v[62:65]
	v_mfma_f32_16x16x32_bf16 v[58:61], v[160:163], v[196:199], v[58:61]
	v_mfma_f32_16x16x32_bf16 v[50:53], v[152:155], v[204:207], v[50:53]
	v_mfma_f32_16x16x32_bf16 v[42:45], v[160:163], v[204:207], v[42:45]
	v_mfma_f32_16x16x32_bf16 v[34:37], v[152:155], v[212:215], v[34:37]
	v_mfma_f32_16x16x32_bf16 v[26:29], v[160:163], v[212:215], v[26:29]
	v_mfma_f32_16x16x32_bf16 v[18:21], v[152:155], v[220:223], v[18:21]
	v_mfma_f32_16x16x32_bf16 v[10:13], v[160:163], v[220:223], v[10:13]
	v_mfma_f32_16x16x32_bf16 v[54:57], v[176:179], v[192:195], v[54:57]
	v_mfma_f32_16x16x32_bf16 v[46:49], v[184:187], v[192:195], v[46:49]
	v_mfma_f32_16x16x32_bf16 v[38:41], v[176:179], v[200:203], v[38:41]
	v_mfma_f32_16x16x32_bf16 v[30:33], v[184:187], v[200:203], v[30:33]
	v_mfma_f32_16x16x32_bf16 v[22:25], v[176:179], v[208:211], v[22:25]
	v_mfma_f32_16x16x32_bf16 v[14:17], v[184:187], v[208:211], v[14:17]
	v_mfma_f32_16x16x32_bf16 v[6:9], v[176:179], v[216:219], v[6:9]
	v_mfma_f32_16x16x32_bf16 v[2:5], v[184:187], v[216:219], v[2:5]
	v_mfma_f32_16x16x32_bf16 v[54:57], v[180:183], v[196:199], v[54:57]
	v_mfma_f32_16x16x32_bf16 v[46:49], v[188:191], v[196:199], v[46:49]
	v_mfma_f32_16x16x32_bf16 v[38:41], v[180:183], v[204:207], v[38:41]
	v_mfma_f32_16x16x32_bf16 v[30:33], v[188:191], v[204:207], v[30:33]
	v_mfma_f32_16x16x32_bf16 v[22:25], v[180:183], v[212:215], v[22:25]
	v_mfma_f32_16x16x32_bf16 v[14:17], v[188:191], v[212:215], v[14:17]
	v_mfma_f32_16x16x32_bf16 v[6:9], v[180:183], v[220:223], v[6:9]
	v_mfma_f32_16x16x32_bf16 v[2:5], v[188:191], v[220:223], v[2:5]
	s_setprio 0
	s_barrier
	s_add_i32 s58, s58, 2
	s_add_u32 s22, s22, 0x100
	s_addc_u32 s23, s23, 0
	s_add_u32 s56, s56, 0x100
	s_addc_u32 s57, s57, 0
	s_cmp_gt_u32 s58, 13
.LBB0_944:
	ds_read_b128 v[148:151], v170
	ds_read_b128 v[152:155], v170 offset:1024
	ds_read_b128 v[156:159], v170 offset:2048
	ds_read_b128 v[160:163], v170 offset:3072
	ds_read_b128 v[176:179], v171
	ds_read_b128 v[180:183], v171 offset:1024
	ds_read_b128 v[184:187], v171 offset:2048
	ds_read_b128 v[188:191], v171 offset:3072
	s_add_u32 s24, s22, 0xfffc0080
	s_addc_u32 s25, s23, -1
	s_cmp_eq_u32 s58, 12
	s_cselect_b32 s27, s15, s25
	s_cselect_b32 s26, s54, s24
	s_cselect_b32 s25, s13, s57
	s_cselect_b32 s24, s55, s56
	s_add_i32 m0, s21, 0xc000
	ds_read_b128 v[192:195], v172
	ds_read_b128 v[196:199], v172 offset:1024
	ds_read_b128 v[200:203], v172 offset:2048
	ds_read_b128 v[204:207], v172 offset:3072
	ds_read_b128 v[208:211], v172 offset:4096
	ds_read_b128 v[212:215], v172 offset:5120
	ds_read_b128 v[216:219], v172 offset:6144
	ds_read_b128 v[220:223], v172 offset:7168
	global_load_lds_dwordx4 v140, s[22:23]
	s_add_i32 m0, s21, 0xe000
	s_nop 0
	global_load_lds_dwordx4 v142, s[22:23]
	s_waitcnt vmcnt(8)
	s_waitcnt lgkmcnt(0)
	s_barrier
	s_setprio 3
	s_waitcnt lgkmcnt(0)
	v_mfma_f32_16x16x32_bf16 v[126:129], v[148:151], v[192:195], v[126:129]
	v_mfma_f32_16x16x32_bf16 v[122:125], v[156:159], v[192:195], v[122:125]
	v_mfma_f32_16x16x32_bf16 v[114:117], v[148:151], v[200:203], v[114:117]
	v_mfma_f32_16x16x32_bf16 v[106:109], v[156:159], v[200:203], v[106:109]
	v_mfma_f32_16x16x32_bf16 v[98:101], v[148:151], v[208:211], v[98:101]
	v_mfma_f32_16x16x32_bf16 v[90:93], v[156:159], v[208:211], v[90:93]
	v_mfma_f32_16x16x32_bf16 v[82:85], v[148:151], v[216:219], v[82:85]
	v_mfma_f32_16x16x32_bf16 v[74:77], v[156:159], v[216:219], v[74:77]
	v_mfma_f32_16x16x32_bf16 v[126:129], v[152:155], v[196:199], v[126:129]
	v_mfma_f32_16x16x32_bf16 v[122:125], v[160:163], v[196:199], v[122:125]
	v_mfma_f32_16x16x32_bf16 v[114:117], v[152:155], v[204:207], v[114:117]
	v_mfma_f32_16x16x32_bf16 v[106:109], v[160:163], v[204:207], v[106:109]
	v_mfma_f32_16x16x32_bf16 v[98:101], v[152:155], v[212:215], v[98:101]
	v_mfma_f32_16x16x32_bf16 v[90:93], v[160:163], v[212:215], v[90:93]
	v_mfma_f32_16x16x32_bf16 v[82:85], v[152:155], v[220:223], v[82:85]
	v_mfma_f32_16x16x32_bf16 v[74:77], v[160:163], v[220:223], v[74:77]
	v_mfma_f32_16x16x32_bf16 v[118:121], v[176:179], v[192:195], v[118:121]
	v_mfma_f32_16x16x32_bf16 v[110:113], v[184:187], v[192:195], v[110:113]
	v_mfma_f32_16x16x32_bf16 v[102:105], v[176:179], v[200:203], v[102:105]
	v_mfma_f32_16x16x32_bf16 v[94:97], v[184:187], v[200:203], v[94:97]
	v_mfma_f32_16x16x32_bf16 v[86:89], v[176:179], v[208:211], v[86:89]
	v_mfma_f32_16x16x32_bf16 v[78:81], v[184:187], v[208:211], v[78:81]
	v_mfma_f32_16x16x32_bf16 v[70:73], v[176:179], v[216:219], v[70:73]
	v_mfma_f32_16x16x32_bf16 v[66:69], v[184:187], v[216:219], v[66:69]
	v_mfma_f32_16x16x32_bf16 v[118:121], v[180:183], v[196:199], v[118:121]
	v_mfma_f32_16x16x32_bf16 v[110:113], v[188:191], v[196:199], v[110:113]
	v_mfma_f32_16x16x32_bf16 v[102:105], v[180:183], v[204:207], v[102:105]
	v_mfma_f32_16x16x32_bf16 v[94:97], v[188:191], v[204:207], v[94:97]
	v_mfma_f32_16x16x32_bf16 v[86:89], v[180:183], v[212:215], v[86:89]
	v_mfma_f32_16x16x32_bf16 v[78:81], v[188:191], v[212:215], v[78:81]
	v_mfma_f32_16x16x32_bf16 v[70:73], v[180:183], v[220:223], v[70:73]
	v_mfma_f32_16x16x32_bf16 v[66:69], v[188:191], v[220:223], v[66:69]
	s_setprio 0
	s_barrier
; #define PG8_STAGE_A(b, h, ptr, NX) do { if constexpr (Sched::GATHER) { unsigned gs_[2]; gs_[0] = ((NX) && last_) ? gN[h][0] : gA[h][0]; gs_[1] = ((NX) && last_) ? gN[h][1] : gA[h][1]; PG8_STAGE(PG8_SA(b, h), ptr, gs_); } \
;         else PG8_STAGE(PG8_SA(b, h), (ptr) + ((h) ? hstep : (size_t)0), voffA); } while (0)
; #define PG8_STAGE(bufoff, gbase, voff) do { _Pragma("unroll") for (int _i = 0; _i < 2; ++_i) \
;         __builtin_amdgcn_global_load_lds((const unsigned*)((const char*)(gbase) + (voff)[_i]), (PG8_LAS unsigned*)(lds + (bufoff) + ldsw + _i * 8192), 16, 0, 0); } while (0)
; #define PG8_LDA(dst, b, h) do { _Pragma("unroll") for (int m = 0; m < 4; ++m) _Pragma("unroll") for (int k = 0; k < 2; ++k) dst[m][k] = *(const PG8_LAS bf16x8*)(lds + PG8_SA(b, h) + aoff + m * 2048 + k * 1024); } while (0)
; #define PG8_LDB(dst, b, h) do { _Pragma("unroll") for (int n = 0; n < 2; ++n) _Pragma("unroll") for (int k = 0; k < 2; ++k) dst[n][k] = *(const PG8_LAS bf16x8*)(lds + PG8_SB(b, h) + boff + n * 2048 + k * 1024); } while (0)
; #define PG8_MMA(ai, bj, At, Bt) do { __builtin_amdgcn_s_setprio(1); _Pragma("unroll") for (int m = 0; m < 4; ++m) _Pragma("unroll") for (int n = 0; n < 2; ++n) _Pragma("unroll") for (int k = 0; k < 2; ++k) \
;         acc[ai][bj][m][n] = __builtin_amdgcn_mfma_f32_16x16x32_bf16(Bt[n][k], At[m][k], acc[ai][bj][m][n], 0, 0, 0); __builtin_amdgcn_s_setprio(0); } while (0)
; #define PG8_WAIT_V(n) asm volatile("s_waitcnt vmcnt(" #n ")" ::: "memory")
; #define PG8_WAIT_L(n) asm volatile("s_waitcnt lgkmcnt(" #n ")" ::: "memory")
; #define PG8_BAR __builtin_amdgcn_s_barrier()
; #define PG8_SCHED __builtin_amdgcn_sched_barrier(0)
; template <class Epi, class Sched, bool ALIGN_EPI = false, bool SP2 = false>
; __device__ __forceinline__ void gemm_phase(PG8_LAS unsigned char* lds, const Gemm g, const Sched& S, const Epi& E, const bool skip_epi = false) {
;     ...
;             PG8_LDA(At, 0, 1); PG8_STAGE(PG8_SB(0, 0), b2, voffB); PG8_STAGE(PG8_SB(0, 1), b2 + hstep, voffB); PG8_STAGE_A(0, 0, a2, true);
;             PG8_WAIT_V(8); PG8_WAIT_L(0); PG8_BAR; PG8_MMA(1, 0, At, B0); PG8_MMA(1, 1, At, B1); PG8_BAR; PG8_SCHED;
;             PG8_LDB(B0, 1, 0); PG8_LDB(B1, 1, 1); PG8_SCHED; PG8_LDA(At, 1, 0); PG8_STAGE_A(0, 1, a2, true);
;             PG8_WAIT_V(8); PG8_WAIT_L(0); PG8_BAR; PG8_MMA(0, 0, At, B0); PG8_MMA(0, 1, At, B1); PG8_BAR; PG8_SCHED;
	s_add_i32 s59, s48, s28
	v_lshl_add_u64 v[164:165], s[24:25], 0, v[134:135]
	s_mov_b32 m0, s59
	ds_read_b128 v[192:195], v172 offset:16384
	ds_read_b128 v[196:199], v172 offset:17408
	ds_read_b128 v[200:203], v172 offset:18432
	ds_read_b128 v[204:207], v172 offset:19456
	ds_read_b128 v[208:211], v172 offset:20480
	ds_read_b128 v[212:215], v172 offset:21504
	ds_read_b128 v[216:219], v172 offset:22528
	ds_read_b128 v[220:223], v172 offset:23552
	global_load_lds_dwordx4 v[164:165], off
	s_add_i32 m0, s59, 0x2000
	s_add_u32 s60, s24, 0x40000
	v_lshl_add_u64 v[224:225], s[24:25], 0, v[130:131]
	s_addc_u32 s61, s25, 0
	s_add_i32 s59, s49, s28
	global_load_lds_dwordx4 v[224:225], off
	s_mov_b32 m0, s59
	v_lshl_add_u64 v[230:231], s[26:27], 0, v[132:133]
	global_load_lds_dwordx4 v134, s[60:61]
	s_add_i32 m0, s59, 0x2000
	s_nop 0
	global_load_lds_dwordx4 v130, s[60:61]
	v_lshl_add_u64 v[226:227], s[26:27], 0, v[136:137]
	s_mov_b32 m0, s21
	s_nop 0
	global_load_lds_dwordx4 v[226:227], off
	s_mov_b32 m0, s31
	s_nop 0
	global_load_lds_dwordx4 v[230:231], off
	s_waitcnt vmcnt(8)
	s_waitcnt lgkmcnt(0)
	s_barrier
	s_setprio 3
	s_waitcnt lgkmcnt(0)
	v_mfma_f32_16x16x32_bf16 v[62:65], v[148:151], v[192:195], v[62:65]
	v_mfma_f32_16x16x32_bf16 v[58:61], v[156:159], v[192:195], v[58:61]
	v_mfma_f32_16x16x32_bf16 v[50:53], v[148:151], v[200:203], v[50:53]
	v_mfma_f32_16x16x32_bf16 v[42:45], v[156:159], v[200:203], v[42:45]
	v_mfma_f32_16x16x32_bf16 v[34:37], v[148:151], v[208:211], v[34:37]
	v_mfma_f32_16x16x32_bf16 v[26:29], v[156:159], v[208:211], v[26:29]
	v_mfma_f32_16x16x32_bf16 v[18:21], v[148:151], v[216:219], v[18:21]
	v_mfma_f32_16x16x32_bf16 v[10:13], v[156:159], v[216:219], v[10:13]
	v_mfma_f32_16x16x32_bf16 v[62:65], v[152:155], v[196:199], v[62:65]
	v_mfma_f32_16x16x32_bf16 v[58:61], v[160:163], v[196:199], v[58:61]
	v_mfma_f32_16x16x32_bf16 v[50:53], v[152:155], v[204:207], v[50:53]
	v_mfma_f32_16x16x32_bf16 v[42:45], v[160:163], v[204:207], v[42:45]
	v_mfma_f32_16x16x32_bf16 v[34:37], v[152:155], v[212:215], v[34:37]
	v_mfma_f32_16x16x32_bf16 v[26:29], v[160:163], v[212:215], v[26:29]
	v_mfma_f32_16x16x32_bf16 v[18:21], v[152:155], v[220:223], v[18:21]
	v_mfma_f32_16x16x32_bf16 v[10:13], v[160:163], v[220:223], v[10:13]
	v_mfma_f32_16x16x32_bf16 v[54:57], v[176:179], v[192:195], v[54:57]
	v_mfma_f32_16x16x32_bf16 v[46:49], v[184:187], v[192:195], v[46:49]
	v_mfma_f32_16x16x32_bf16 v[38:41], v[176:179], v[200:203], v[38:41]
	v_mfma_f32_16x16x32_bf16 v[30:33], v[184:187], v[200:203], v[30:33]
	v_mfma_f32_16x16x32_bf16 v[22:25], v[176:179], v[208:211], v[22:25]
	v_mfma_f32_16x16x32_bf16 v[14:17], v[184:187], v[208:211], v[14:17]
	v_mfma_f32_16x16x32_bf16 v[6:9], v[176:179], v[216:219], v[6:9]
	v_mfma_f32_16x16x32_bf16 v[2:5], v[184:187], v[216:219], v[2:5]
	v_mfma_f32_16x16x32_bf16 v[54:57], v[180:183], v[196:199], v[54:57]
	v_mfma_f32_16x16x32_bf16 v[46:49], v[188:191], v[196:199], v[46:49]
	v_mfma_f32_16x16x32_bf16 v[38:41], v[180:183], v[204:207], v[38:41]
	v_mfma_f32_16x16x32_bf16 v[30:33], v[188:191], v[204:207], v[30:33]
	v_mfma_f32_16x16x32_bf16 v[22:25], v[180:183], v[212:215], v[22:25]
	v_mfma_f32_16x16x32_bf16 v[14:17], v[188:191], v[212:215], v[14:17]
	v_mfma_f32_16x16x32_bf16 v[6:9], v[180:183], v[220:223], v[6:9]
	v_mfma_f32_16x16x32_bf16 v[2:5], v[188:191], v[220:223], v[2:5]
	s_setprio 0
	s_barrier
	s_add_i32 s59, 0, 0x18000
	s_add_i32 s60, 0, 0x1c000
	v_add_u32_e32 v160, s59, v1
	v_add_u32_e32 v188, s60, v1
	ds_read_b128 v[148:151], v160
	ds_read_b128 v[152:155], v160 offset:1024
	ds_read_b128 v[156:159], v160 offset:2048
	ds_read_b128 v[160:163], v160 offset:3072
	ds_read_b128 v[176:179], v188
	ds_read_b128 v[180:183], v188 offset:1024
	ds_read_b128 v[184:187], v188 offset:2048
	ds_read_b128 v[188:191], v188 offset:3072
	s_add_u32 s26, s26, 0x40000
	s_addc_u32 s27, s27, 0
	s_mov_b32 m0, s34
	ds_read_b128 v[192:195], v172 offset:32768
	ds_read_b128 v[196:199], v172 offset:33792
	ds_read_b128 v[200:203], v172 offset:34816
	ds_read_b128 v[204:207], v172 offset:35840
	ds_read_b128 v[208:211], v172 offset:36864
	ds_read_b128 v[212:215], v172 offset:37888
	ds_read_b128 v[216:219], v172 offset:38912
	ds_read_b128 v[220:223], v172 offset:39936
	global_load_lds_dwordx4 v136, s[26:27]
	s_mov_b32 m0, s35
	s_nop 0
	global_load_lds_dwordx4 v132, s[26:27]
	s_waitcnt vmcnt(8)
	s_waitcnt lgkmcnt(0)
	s_barrier
; #define PG8_STAGE_A(b, h, ptr, NX) do { if constexpr (Sched::GATHER) { unsigned gs_[2]; gs_[0] = ((NX) && last_) ? gN[h][0] : gA[h][0]; gs_[1] = ((NX) && last_) ? gN[h][1] : gA[h][1]; PG8_STAGE(PG8_SA(b, h), ptr, gs_); } \
;         else PG8_STAGE(PG8_SA(b, h), (ptr) + ((h) ? hstep : (size_t)0), voffA); } while (0)
; #define PG8_STAGE(bufoff, gbase, voff) do { _Pragma("unroll") for (int _i = 0; _i < 2; ++_i) \
;         __builtin_amdgcn_global_load_lds((const unsigned*)((const char*)(gbase) + (voff)[_i]), (PG8_LAS unsigned*)(lds + (bufoff) + ldsw + _i * 8192), 16, 0, 0); } while (0)
; #define PG8_LDA(dst, b, h) do { _Pragma("unroll") for (int m = 0; m < 4; ++m) _Pragma("unroll") for (int k = 0; k < 2; ++k) dst[m][k] = *(const PG8_LAS bf16x8*)(lds + PG8_SA(b, h) + aoff + m * 2048 + k * 1024); } while (0)
; #define PG8_LDB(dst, b, h) do { _Pragma("unroll") for (int n = 0; n < 2; ++n) _Pragma("unroll") for (int k = 0; k < 2; ++k) dst[n][k] = *(const PG8_LAS bf16x8*)(lds + PG8_SB(b, h) + boff + n * 2048 + k * 1024); } while (0)
; #define PG8_MMA(ai, bj, At, Bt) do { __builtin_amdgcn_s_setprio(1); _Pragma("unroll") for (int m = 0; m < 4; ++m) _Pragma("unroll") for (int n = 0; n < 2; ++n) _Pragma("unroll") for (int k = 0; k < 2; ++k) \
;         acc[ai][bj][m][n] = __builtin_amdgcn_mfma_f32_16x16x32_bf16(Bt[n][k], At[m][k], acc[ai][bj][m][n], 0, 0, 0); __builtin_amdgcn_s_setprio(0); } while (0)
; __device__ __forceinline__ void rstd8(const float* SS, int rowb, int lane, float (&rs)[2][4]) {
;     ...
;         for (int m = 0; m < 4; ++m) p[ai][m] = *(const f32x4*)(SS + (size_t)(rowb + HALF * ai + 16 * m + (lane >> 2)) * 16 + 4 * (lane & 3));
; template <class Epi, class Sched, bool ALIGN_EPI = false, bool SP2 = false>
; __device__ __forceinline__ void gemm_phase(PG8_LAS unsigned char* lds, const Gemm g, const Sched& S, const Epi& E, const bool skip_epi = false) {
;     ...
;             PG8_LDB(B0, 1, 0); PG8_LDB(B1, 1, 1); PG8_SCHED; PG8_LDA(At, 1, 0); PG8_STAGE_A(0, 1, a2, true);
;             PG8_WAIT_V(8); PG8_WAIT_L(0); PG8_BAR; PG8_MMA(0, 0, At, B0); PG8_MMA(0, 1, At, B1); PG8_BAR; PG8_SCHED;
;             PG8_LDA(At, 1, 1); PG8_STAGE(PG8_SB(1, 0), b3, voffB); PG8_STAGE(PG8_SB(1, 1), b3 + hstep, voffB); PG8_STAGE_A(1, 0, a3, true);
;             PG8_WAIT_V(8); PG8_WAIT_L(0); PG8_BAR; PG8_MMA(1, 0, At, B0); PG8_MMA(1, 1, At, B1); PG8_BAR; PG8_SCHED;
	s_setprio 3
	s_waitcnt lgkmcnt(0)
	v_mfma_f32_16x16x32_bf16 v[126:129], v[148:151], v[192:195], v[126:129]
	v_mfma_f32_16x16x32_bf16 v[122:125], v[156:159], v[192:195], v[122:125]
	v_mfma_f32_16x16x32_bf16 v[114:117], v[148:151], v[200:203], v[114:117]
	v_mfma_f32_16x16x32_bf16 v[106:109], v[156:159], v[200:203], v[106:109]
	v_mfma_f32_16x16x32_bf16 v[98:101], v[148:151], v[208:211], v[98:101]
	v_mfma_f32_16x16x32_bf16 v[90:93], v[156:159], v[208:211], v[90:93]
	v_mfma_f32_16x16x32_bf16 v[82:85], v[148:151], v[216:219], v[82:85]
	v_mfma_f32_16x16x32_bf16 v[74:77], v[156:159], v[216:219], v[74:77]
	v_mfma_f32_16x16x32_bf16 v[126:129], v[152:155], v[196:199], v[126:129]
	v_mfma_f32_16x16x32_bf16 v[122:125], v[160:163], v[196:199], v[122:125]
	v_mfma_f32_16x16x32_bf16 v[114:117], v[152:155], v[204:207], v[114:117]
	v_mfma_f32_16x16x32_bf16 v[106:109], v[160:163], v[204:207], v[106:109]
	v_mfma_f32_16x16x32_bf16 v[98:101], v[152:155], v[212:215], v[98:101]
	v_mfma_f32_16x16x32_bf16 v[90:93], v[160:163], v[212:215], v[90:93]
	v_mfma_f32_16x16x32_bf16 v[82:85], v[152:155], v[220:223], v[82:85]
	v_mfma_f32_16x16x32_bf16 v[74:77], v[160:163], v[220:223], v[74:77]
	v_mfma_f32_16x16x32_bf16 v[118:121], v[176:179], v[192:195], v[118:121]
	v_mfma_f32_16x16x32_bf16 v[110:113], v[184:187], v[192:195], v[110:113]
	v_mfma_f32_16x16x32_bf16 v[102:105], v[176:179], v[200:203], v[102:105]
	v_mfma_f32_16x16x32_bf16 v[94:97], v[184:187], v[200:203], v[94:97]
	v_mfma_f32_16x16x32_bf16 v[86:89], v[176:179], v[208:211], v[86:89]
	v_mfma_f32_16x16x32_bf16 v[78:81], v[184:187], v[208:211], v[78:81]
	v_mfma_f32_16x16x32_bf16 v[70:73], v[176:179], v[216:219], v[70:73]
	v_mfma_f32_16x16x32_bf16 v[66:69], v[184:187], v[216:219], v[66:69]
	v_mfma_f32_16x16x32_bf16 v[118:121], v[180:183], v[196:199], v[118:121]
	v_mfma_f32_16x16x32_bf16 v[110:113], v[188:191], v[196:199], v[110:113]
	v_mfma_f32_16x16x32_bf16 v[102:105], v[180:183], v[204:207], v[102:105]
	v_mfma_f32_16x16x32_bf16 v[94:97], v[188:191], v[204:207], v[94:97]
	v_mfma_f32_16x16x32_bf16 v[86:89], v[180:183], v[212:215], v[86:89]
	v_mfma_f32_16x16x32_bf16 v[78:81], v[188:191], v[212:215], v[78:81]
	v_mfma_f32_16x16x32_bf16 v[70:73], v[180:183], v[220:223], v[70:73]
	v_mfma_f32_16x16x32_bf16 v[66:69], v[188:191], v[220:223], v[66:69]
	s_setprio 0
	s_barrier
	s_add_i32 s26, s59, s28
	s_add_i32 m0, s26, 0xffffff80
	ds_read_b128 v[192:195], v172 offset:49152
	ds_read_b128 v[196:199], v172 offset:50176
	ds_read_b128 v[200:203], v172 offset:51200
	ds_read_b128 v[204:207], v172 offset:52224
	ds_read_b128 v[208:211], v172 offset:53248
	ds_read_b128 v[212:215], v172 offset:54272
	ds_read_b128 v[216:219], v172 offset:55296
	ds_read_b128 v[220:223], v172 offset:56320
	global_load_lds_dwordx4 v[164:165], off offset:128
	s_add_i32 m0, s26, 0x1f80
	s_add_u32 s24, s24, 0x40080
	s_addc_u32 s25, s25, 0
	s_add_i32 s26, s60, s28
	global_load_lds_dwordx4 v[224:225], off offset:128
	s_mov_b32 m0, s26
	s_nop 0
	global_load_lds_dwordx4 v134, s[24:25]
	s_add_i32 m0, s26, 0x2000
	s_nop 0
	global_load_lds_dwordx4 v130, s[24:25]
	s_add_i32 m0, s37, 0xffffff80
	s_nop 0
	global_load_lds_dwordx4 v[226:227], off offset:128
	s_add_i32 m0, s38, 0xffffff80
	s_nop 0
	global_load_lds_dwordx4 v[230:231], off offset:128
	s_waitcnt vmcnt(8)
	s_waitcnt lgkmcnt(0)
	s_barrier
	s_setprio 3
	s_waitcnt lgkmcnt(0)
	v_mfma_f32_16x16x32_bf16 v[62:65], v[148:151], v[192:195], v[62:65]
	v_mfma_f32_16x16x32_bf16 v[58:61], v[156:159], v[192:195], v[58:61]
	v_mfma_f32_16x16x32_bf16 v[50:53], v[148:151], v[200:203], v[50:53]
	v_mfma_f32_16x16x32_bf16 v[42:45], v[156:159], v[200:203], v[42:45]
	v_mfma_f32_16x16x32_bf16 v[34:37], v[148:151], v[208:211], v[34:37]
	v_mfma_f32_16x16x32_bf16 v[26:29], v[156:159], v[208:211], v[26:29]
	v_mfma_f32_16x16x32_bf16 v[18:21], v[148:151], v[216:219], v[18:21]
	v_mfma_f32_16x16x32_bf16 v[10:13], v[156:159], v[216:219], v[10:13]
	v_mfma_f32_16x16x32_bf16 v[62:65], v[152:155], v[196:199], v[62:65]
	v_mfma_f32_16x16x32_bf16 v[58:61], v[160:163], v[196:199], v[58:61]
	v_mfma_f32_16x16x32_bf16 v[50:53], v[152:155], v[204:207], v[50:53]
	v_mfma_f32_16x16x32_bf16 v[42:45], v[160:163], v[204:207], v[42:45]
	v_mfma_f32_16x16x32_bf16 v[34:37], v[152:155], v[212:215], v[34:37]
	v_mfma_f32_16x16x32_bf16 v[26:29], v[160:163], v[212:215], v[26:29]
	v_mfma_f32_16x16x32_bf16 v[18:21], v[152:155], v[220:223], v[18:21]
	v_mfma_f32_16x16x32_bf16 v[10:13], v[160:163], v[220:223], v[10:13]
	v_mfma_f32_16x16x32_bf16 v[54:57], v[176:179], v[192:195], v[54:57]
	v_mfma_f32_16x16x32_bf16 v[46:49], v[184:187], v[192:195], v[46:49]
	v_mfma_f32_16x16x32_bf16 v[38:41], v[176:179], v[200:203], v[38:41]
	v_mfma_f32_16x16x32_bf16 v[30:33], v[184:187], v[200:203], v[30:33]
	v_mfma_f32_16x16x32_bf16 v[22:25], v[176:179], v[208:211], v[22:25]
	v_mfma_f32_16x16x32_bf16 v[14:17], v[184:187], v[208:211], v[14:17]
	v_mfma_f32_16x16x32_bf16 v[6:9], v[176:179], v[216:219], v[6:9]
	v_mfma_f32_16x16x32_bf16 v[2:5], v[184:187], v[216:219], v[2:5]
	v_mfma_f32_16x16x32_bf16 v[54:57], v[180:183], v[196:199], v[54:57]
	v_mfma_f32_16x16x32_bf16 v[46:49], v[188:191], v[196:199], v[46:49]
	v_mfma_f32_16x16x32_bf16 v[38:41], v[180:183], v[204:207], v[38:41]
	v_mfma_f32_16x16x32_bf16 v[30:33], v[188:191], v[204:207], v[30:33]
	v_mfma_f32_16x16x32_bf16 v[22:25], v[180:183], v[212:215], v[22:25]
	v_mfma_f32_16x16x32_bf16 v[14:17], v[188:191], v[212:215], v[14:17]
	v_mfma_f32_16x16x32_bf16 v[6:9], v[180:183], v[220:223], v[6:9]
	v_mfma_f32_16x16x32_bf16 v[2:5], v[188:191], v[220:223], v[2:5]
	s_setprio 0
	s_barrier
	s_add_i32 s58, s58, 2
	s_add_u32 s22, s22, 0x100
	s_addc_u32 s23, s23, 0
	s_add_u32 s56, s56, 0x100
	s_addc_u32 s57, s57, 0
	s_cmp_gt_u32 s58, 13
	s_cbranch_scc0 .LBB0_944
	v_lshl_add_u32 v164, s20, 8, v167
	v_ashrrev_i32_e32 v165, 31, v164
	v_lshlrev_b64 v[148:149], 6, v[164:165]
	v_lshl_add_u64 v[148:149], v[138:139], 0, v[148:149]
	v_add_co_u32_e32 v150, vcc, 0x2000, v148
	v_addc_co_u32_e32 v151, vcc, 0, v149, vcc
	global_load_dwordx4 v[176:179], v[148:149], off
	global_load_dwordx4 v[180:183], v[148:149], off offset:1024
	global_load_dwordx4 v[184:187], v[148:149], off offset:2048
	global_load_dwordx4 v[188:191], v[148:149], off offset:3072
	global_load_dwordx4 v[192:195], v[150:151], off
	global_load_dwordx4 v[196:199], v[150:151], off offset:1024
	global_load_dwordx4 v[200:203], v[150:151], off offset:2048
	global_load_dwordx4 v[204:207], v[150:151], off offset:3072
	s_and_b64 vcc, exec, s[10:11]
	s_cbranch_vccz .LBB0_947
	s_barrier

; #define PG8_STAGE_A(b, h, ptr, NX) do { if constexpr (Sched::GATHER) { unsigned gs_[2]; gs_[0] = ((NX) && last_) ? gN[h][0] : gA[h][0]; gs_[1] = ((NX) && last_) ? gN[h][1] : gA[h][1]; PG8_STAGE(PG8_SA(b, h), ptr, gs_); } \
;         else PG8_STAGE(PG8_SA(b, h), (ptr) + ((h) ? hstep : (size_t)0), voffA); } while (0)
; #define PG8_STAGE(bufoff, gbase, voff) do { _Pragma("unroll") for (int _i = 0; _i < 2; ++_i) \
;         __builtin_amdgcn_global_load_lds((const unsigned*)((const char*)(gbase) + (voff)[_i]), (PG8_LAS unsigned*)(lds + (bufoff) + ldsw + _i * 8192), 16, 0, 0); } while (0)
; #define PG8_LDA(dst, b, h) do { _Pragma("unroll") for (int m = 0; m < 4; ++m) _Pragma("unroll") for (int k = 0; k < 2; ++k) dst[m][k] = *(const PG8_LAS bf16x8*)(lds + PG8_SA(b, h) + aoff + m * 2048 + k * 1024); } while (0)
; #define PG8_LDB(dst, b, h) do { _Pragma("unroll") for (int n = 0; n < 2; ++n) _Pragma("unroll") for (int k = 0; k < 2; ++k) dst[n][k] = *(const PG8_LAS bf16x8*)(lds + PG8_SB(b, h) + boff + n * 2048 + k * 1024); } while (0)
; #define PG8_WAIT_V(n) asm volatile("s_waitcnt vmcnt(" #n ")" ::: "memory")
; template <class Epi, class Sched, bool ALIGN_EPI = false, bool SP2 = false>
; __device__ __forceinline__ void gemm_phase(PG8_LAS unsigned char* lds, const Gemm g, const Sched& S, const Epi& E, const bool skip_epi = false) {
;     ...
;         const char* nA = has_next ? (const char*)g.A + (size_t)nxt.pm * pmstepA + nxt.ko : cA; const char* nB = has_next ? (const char*)g.Bt + (size_t)nxt.pn * tstep + nxt.ko : cB;
;         for (int t = 0; t < nt; t += 2) {
;             const bool last = (t == nt - 2); last_ = last && has_next;
;             const char* a1 = cA + (size_t)(t + 1) * kstep;
;             const char* a2 = last ? nA : cA + (size_t)(t + 2) * kstep; const char* b2 = last ? nB : cB + (size_t)(t + 2) * kstep;
;             const char* a3 = a2 + kstep; const char* b3 = b2 + kstep;
;             if (last && has_next) S.a_ready(nxt);
;             if constexpr (SP2) {
;             PG8_LDB(B0, 0, 0); PG8_LDB(B1, 0, 1); PG8_SCHED; PG8_LDA(At, 0, 0); PG8_STAGE_A(1, 1, a1, false);
;             PG8_WAIT_V(8); PG8_WAIT_L(0); PG8_BAR; PG8_MMA(0, 0, At, B0); PG8_MMA(0, 1, At, B1); PG8_BAR; PG8_SCHED;
;             PG8_LDA(At, 0, 1); PG8_STAGE(PG8_SB(0, 0), b2, voffB); PG8_STAGE(PG8_SB(0, 1), b2 + hstep, voffB); PG8_STAGE_A(0, 0, a2, true);
.LBB0_1323:
	s_ashr_i32 s25, s24, 31
	s_lshl_b64 s[26:27], s[24:25], 19
	s_add_u32 s26, s46, s26
	s_addc_u32 s27, s47, s27
	s_and_b64 s[28:29], s[6:7], exec
	s_cselect_b32 s25, s27, s35
	s_cselect_b32 s31, s26, s34
	s_ashr_i32 s23, s22, 31
	s_lshl_b64 s[28:29], s[22:23], 19
	s_add_u32 s28, s2, s28
	s_addc_u32 s29, s3, s29
	s_and_b64 s[38:39], s[6:7], exec
	s_cselect_b32 s23, s29, s37
	s_cselect_b32 s60, s28, s36
	s_add_u32 s34, s34, 0x40080
	s_addc_u32 s35, s35, 0
	s_add_u32 s61, s36, 0x100
	s_addc_u32 s62, s37, 0
	s_mov_b32 s63, -2
	s_waitcnt vmcnt(0)
	s_waitcnt lgkmcnt(0)
	ds_read_b128 v[98:101], v225
	ds_read_b128 v[110:113], v225 offset:1024
	ds_read_b128 v[122:125], v225 offset:2048
	ds_read_b128 v[130:133], v225 offset:3072
	ds_read_b128 v[146:149], v226
	ds_read_b128 v[150:153], v226 offset:1024
	ds_read_b128 v[154:157], v226 offset:2048
	ds_read_b128 v[158:161], v226 offset:3072
	s_add_u32 s36, s34, 0xfffc0080
	s_addc_u32 s37, s35, -1
	s_cmp_eq_u32 s63, 12
	s_cselect_b32 s39, s25, s37
	s_cselect_b32 s38, s31, s36
	s_cselect_b32 s37, s23, s62
	s_cselect_b32 s36, s60, s61
	s_add_i32 m0, s41, 0xc000
	ds_read_b128 v[162:165], v227
	ds_read_b128 v[166:169], v227 offset:1024
	ds_read_b128 v[170:173], v227 offset:2048
	ds_read_b128 v[174:177], v227 offset:3072
	ds_read_b128 v[178:181], v227 offset:4096
	ds_read_b128 v[182:185], v227 offset:5120
	ds_read_b128 v[202:205], v227 offset:6144
	ds_read_b128 v[206:209], v227 offset:7168
	global_load_lds_dwordx4 v194, s[34:35]
	s_add_i32 m0, s41, 0xe000
	s_nop 0
	global_load_lds_dwordx4 v196, s[34:35]
	s_waitcnt vmcnt(8)
	s_waitcnt lgkmcnt(0)
	s_barrier
	s_setprio 3
	s_waitcnt lgkmcnt(0)
	v_mfma_f32_16x16x32_bf16 v[142:145], v[98:101], v[162:165], 0
	v_mfma_f32_16x16x32_bf16 v[138:141], v[122:125], v[162:165], 0
	v_mfma_f32_16x16x32_bf16 v[118:121], v[98:101], v[170:173], 0
	v_mfma_f32_16x16x32_bf16 v[114:117], v[122:125], v[170:173], 0
	v_mfma_f32_16x16x32_bf16 v[94:97], v[98:101], v[178:181], 0
	v_mfma_f32_16x16x32_bf16 v[90:93], v[122:125], v[178:181], 0
	v_mfma_f32_16x16x32_bf16 v[78:81], v[98:101], v[202:205], 0
	v_mfma_f32_16x16x32_bf16 v[74:77], v[122:125], v[202:205], 0
	v_mfma_f32_16x16x32_bf16 v[142:145], v[110:113], v[166:169], v[142:145]
	v_mfma_f32_16x16x32_bf16 v[138:141], v[130:133], v[166:169], v[138:141]
	v_mfma_f32_16x16x32_bf16 v[118:121], v[110:113], v[174:177], v[118:121]
	v_mfma_f32_16x16x32_bf16 v[114:117], v[130:133], v[174:177], v[114:117]
	v_mfma_f32_16x16x32_bf16 v[94:97], v[110:113], v[182:185], v[94:97]
	v_mfma_f32_16x16x32_bf16 v[90:93], v[130:133], v[182:185], v[90:93]
	v_mfma_f32_16x16x32_bf16 v[78:81], v[110:113], v[206:209], v[78:81]
	v_mfma_f32_16x16x32_bf16 v[74:77], v[130:133], v[206:209], v[74:77]
	v_mfma_f32_16x16x32_bf16 v[134:137], v[146:149], v[162:165], 0
	v_mfma_f32_16x16x32_bf16 v[126:129], v[154:157], v[162:165], 0
	v_mfma_f32_16x16x32_bf16 v[106:109], v[146:149], v[170:173], 0
	v_mfma_f32_16x16x32_bf16 v[102:105], v[154:157], v[170:173], 0
	v_mfma_f32_16x16x32_bf16 v[86:89], v[146:149], v[178:181], 0
	v_mfma_f32_16x16x32_bf16 v[82:85], v[154:157], v[178:181], 0
	v_mfma_f32_16x16x32_bf16 v[70:73], v[146:149], v[202:205], 0
	v_mfma_f32_16x16x32_bf16 v[66:69], v[154:157], v[202:205], 0
	v_mfma_f32_16x16x32_bf16 v[134:137], v[150:153], v[166:169], v[134:137]
	v_mfma_f32_16x16x32_bf16 v[126:129], v[158:161], v[166:169], v[126:129]
	v_mfma_f32_16x16x32_bf16 v[106:109], v[150:153], v[174:177], v[106:109]
	v_mfma_f32_16x16x32_bf16 v[102:105], v[158:161], v[174:177], v[102:105]
	v_mfma_f32_16x16x32_bf16 v[86:89], v[150:153], v[182:185], v[86:89]
	v_mfma_f32_16x16x32_bf16 v[82:85], v[158:161], v[182:185], v[82:85]
	v_mfma_f32_16x16x32_bf16 v[70:73], v[150:153], v[206:209], v[70:73]
	v_mfma_f32_16x16x32_bf16 v[66:69], v[158:161], v[206:209], v[66:69]
	s_setprio 0
	s_barrier
	s_add_i32 s64, s57, s40
	v_lshl_add_u64 v[210:211], s[36:37], 0, v[188:189]
	s_mov_b32 m0, s64
	ds_read_b128 v[162:165], v227 offset:16384
	ds_read_b128 v[166:169], v227 offset:17408
	ds_read_b128 v[170:173], v227 offset:18432
	ds_read_b128 v[174:177], v227 offset:19456
	ds_read_b128 v[178:181], v227 offset:20480
	ds_read_b128 v[182:185], v227 offset:21504
	ds_read_b128 v[202:205], v227 offset:22528
	ds_read_b128 v[206:209], v227 offset:23552
	global_load_lds_dwordx4 v[210:211], off
	s_add_i32 m0, s64, 0x2000
	s_add_u32 s64, s36, 0x40000
	v_lshl_add_u64 v[212:213], s[36:37], 0, v[192:193]
	s_addc_u32 s65, s37, 0
	s_add_i32 s66, s58, s40
	global_load_lds_dwordx4 v[212:213], off
	s_mov_b32 m0, s66
	v_lshl_add_u64 v[216:217], s[38:39], 0, v[190:191]
	global_load_lds_dwordx4 v188, s[64:65]
	s_add_i32 m0, s66, 0x2000
	s_nop 0
	global_load_lds_dwordx4 v192, s[64:65]
	v_lshl_add_u64 v[214:215], s[38:39], 0, v[186:187]
	s_mov_b32 m0, s41
	s_nop 0
	global_load_lds_dwordx4 v[214:215], off
	s_mov_b32 m0, s44
	s_nop 0
	global_load_lds_dwordx4 v[216:217], off
	s_waitcnt vmcnt(8)
	s_waitcnt lgkmcnt(0)
	s_barrier
; #define PG8_STAGE_A(b, h, ptr, NX) do { if constexpr (Sched::GATHER) { unsigned gs_[2]; gs_[0] = ((NX) && last_) ? gN[h][0] : gA[h][0]; gs_[1] = ((NX) && last_) ? gN[h][1] : gA[h][1]; PG8_STAGE(PG8_SA(b, h), ptr, gs_); } \
;         else PG8_STAGE(PG8_SA(b, h), (ptr) + ((h) ? hstep : (size_t)0), voffA); } while (0)
; #define PG8_STAGE(bufoff, gbase, voff) do { _Pragma("unroll") for (int _i = 0; _i < 2; ++_i) \
;         __builtin_amdgcn_global_load_lds((const unsigned*)((const char*)(gbase) + (voff)[_i]), (PG8_LAS unsigned*)(lds + (bufoff) + ldsw + _i * 8192), 16, 0, 0); } while (0)
; #define PG8_LDA(dst, b, h) do { _Pragma("unroll") for (int m = 0; m < 4; ++m) _Pragma("unroll") for (int k = 0; k < 2; ++k) dst[m][k] = *(const PG8_LAS bf16x8*)(lds + PG8_SA(b, h) + aoff + m * 2048 + k * 1024); } while (0)
; #define PG8_LDB(dst, b, h) do { _Pragma("unroll") for (int n = 0; n < 2; ++n) _Pragma("unroll") for (int k = 0; k < 2; ++k) dst[n][k] = *(const PG8_LAS bf16x8*)(lds + PG8_SB(b, h) + boff + n * 2048 + k * 1024); } while (0)
; #define PG8_MMA(ai, bj, At, Bt) do { __builtin_amdgcn_s_setprio(1); _Pragma("unroll") for (int m = 0; m < 4; ++m) _Pragma("unroll") for (int n = 0; n < 2; ++n) _Pragma("unroll") for (int k = 0; k < 2; ++k) \
;         acc[ai][bj][m][n] = __builtin_amdgcn_mfma_f32_16x16x32_bf16(Bt[n][k], At[m][k], acc[ai][bj][m][n], 0, 0, 0); __builtin_amdgcn_s_setprio(0); } while (0)
; #define PG8_WAIT_V(n) asm volatile("s_waitcnt vmcnt(" #n ")" ::: "memory")
; #define PG8_WAIT_L(n) asm volatile("s_waitcnt lgkmcnt(" #n ")" ::: "memory")
; #define PG8_BAR __builtin_amdgcn_s_barrier()
; #define PG8_SCHED __builtin_amdgcn_sched_barrier(0)
; template <class Epi, class Sched, bool ALIGN_EPI = false, bool SP2 = false>
; __device__ __forceinline__ void gemm_phase(PG8_LAS unsigned char* lds, const Gemm g, const Sched& S, const Epi& E, const bool skip_epi = false) {
;     ...
;             PG8_LDA(At, 0, 1); PG8_STAGE(PG8_SB(0, 0), b2, voffB); PG8_STAGE(PG8_SB(0, 1), b2 + hstep, voffB); PG8_STAGE_A(0, 0, a2, true);
;             PG8_WAIT_V(8); PG8_WAIT_L(0); PG8_BAR; PG8_MMA(1, 0, At, B0); PG8_MMA(1, 1, At, B1); PG8_BAR; PG8_SCHED;
;             PG8_LDB(B0, 1, 0); PG8_LDB(B1, 1, 1); PG8_SCHED; PG8_LDA(At, 1, 0); PG8_STAGE_A(0, 1, a2, true);
;             PG8_WAIT_V(8); PG8_WAIT_L(0); PG8_BAR; PG8_MMA(0, 0, At, B0); PG8_MMA(0, 1, At, B1); PG8_BAR; PG8_SCHED;
	s_setprio 3
	s_waitcnt lgkmcnt(0)
	v_mfma_f32_16x16x32_bf16 v[62:65], v[98:101], v[162:165], 0
	v_mfma_f32_16x16x32_bf16 v[58:61], v[122:125], v[162:165], 0
	v_mfma_f32_16x16x32_bf16 v[46:49], v[98:101], v[170:173], 0
	v_mfma_f32_16x16x32_bf16 v[42:45], v[122:125], v[170:173], 0
	v_mfma_f32_16x16x32_bf16 v[30:33], v[98:101], v[178:181], 0
	v_mfma_f32_16x16x32_bf16 v[26:29], v[122:125], v[178:181], 0
	v_mfma_f32_16x16x32_bf16 v[14:17], v[98:101], v[202:205], 0
	v_mfma_f32_16x16x32_bf16 v[10:13], v[122:125], v[202:205], 0
	v_mfma_f32_16x16x32_bf16 v[62:65], v[110:113], v[166:169], v[62:65]
	v_mfma_f32_16x16x32_bf16 v[58:61], v[130:133], v[166:169], v[58:61]
	v_mfma_f32_16x16x32_bf16 v[46:49], v[110:113], v[174:177], v[46:49]
	v_mfma_f32_16x16x32_bf16 v[42:45], v[130:133], v[174:177], v[42:45]
	v_mfma_f32_16x16x32_bf16 v[30:33], v[110:113], v[182:185], v[30:33]
	v_mfma_f32_16x16x32_bf16 v[26:29], v[130:133], v[182:185], v[26:29]
	v_mfma_f32_16x16x32_bf16 v[14:17], v[110:113], v[206:209], v[14:17]
	v_mfma_f32_16x16x32_bf16 v[10:13], v[130:133], v[206:209], v[10:13]
	v_mfma_f32_16x16x32_bf16 v[54:57], v[146:149], v[162:165], 0
	v_mfma_f32_16x16x32_bf16 v[50:53], v[154:157], v[162:165], 0
	v_mfma_f32_16x16x32_bf16 v[38:41], v[146:149], v[170:173], 0
	v_mfma_f32_16x16x32_bf16 v[34:37], v[154:157], v[170:173], 0
	v_mfma_f32_16x16x32_bf16 v[22:25], v[146:149], v[178:181], 0
	v_mfma_f32_16x16x32_bf16 v[18:21], v[154:157], v[178:181], 0
	v_mfma_f32_16x16x32_bf16 v[6:9], v[146:149], v[202:205], 0
	v_mfma_f32_16x16x32_bf16 v[2:5], v[154:157], v[202:205], 0
	v_mfma_f32_16x16x32_bf16 v[54:57], v[150:153], v[166:169], v[54:57]
	v_mfma_f32_16x16x32_bf16 v[50:53], v[158:161], v[166:169], v[50:53]
	v_mfma_f32_16x16x32_bf16 v[38:41], v[150:153], v[174:177], v[38:41]
	v_mfma_f32_16x16x32_bf16 v[34:37], v[158:161], v[174:177], v[34:37]
	v_mfma_f32_16x16x32_bf16 v[22:25], v[150:153], v[182:185], v[22:25]
	v_mfma_f32_16x16x32_bf16 v[18:21], v[158:161], v[182:185], v[18:21]
	v_mfma_f32_16x16x32_bf16 v[6:9], v[150:153], v[206:209], v[6:9]
	v_mfma_f32_16x16x32_bf16 v[2:5], v[158:161], v[206:209], v[2:5]
	s_setprio 0
	s_barrier
	s_add_i32 s64, 0, 0x18000
	s_add_i32 s65, 0, 0x1c000
	v_add_u32_e32 v130, s64, v220
	v_add_u32_e32 v158, s65, v220
	ds_read_b128 v[98:101], v130
	ds_read_b128 v[110:113], v130 offset:1024
	ds_read_b128 v[122:125], v130 offset:2048
	ds_read_b128 v[130:133], v130 offset:3072
	ds_read_b128 v[146:149], v158
	ds_read_b128 v[150:153], v158 offset:1024
	ds_read_b128 v[154:157], v158 offset:2048
	ds_read_b128 v[158:161], v158 offset:3072
	s_add_u32 s38, s38, 0x40000
	s_addc_u32 s39, s39, 0
	s_mov_b32 m0, s45
	ds_read_b128 v[162:165], v227 offset:32768
	ds_read_b128 v[166:169], v227 offset:33792
	ds_read_b128 v[170:173], v227 offset:34816
	ds_read_b128 v[174:177], v227 offset:35840
	ds_read_b128 v[178:181], v227 offset:36864
	ds_read_b128 v[182:185], v227 offset:37888
	ds_read_b128 v[202:205], v227 offset:38912
	ds_read_b128 v[206:209], v227 offset:39936
	global_load_lds_dwordx4 v186, s[38:39]
	s_mov_b32 m0, s48
	s_nop 0
	global_load_lds_dwordx4 v190, s[38:39]
	s_waitcnt vmcnt(8)
	s_waitcnt lgkmcnt(0)
	s_barrier
	s_setprio 3
	s_waitcnt lgkmcnt(0)
	v_mfma_f32_16x16x32_bf16 v[142:145], v[98:101], v[162:165], v[142:145]
	v_mfma_f32_16x16x32_bf16 v[138:141], v[122:125], v[162:165], v[138:141]
	v_mfma_f32_16x16x32_bf16 v[118:121], v[98:101], v[170:173], v[118:121]
	v_mfma_f32_16x16x32_bf16 v[114:117], v[122:125], v[170:173], v[114:117]
	v_mfma_f32_16x16x32_bf16 v[94:97], v[98:101], v[178:181], v[94:97]
	v_mfma_f32_16x16x32_bf16 v[90:93], v[122:125], v[178:181], v[90:93]
	v_mfma_f32_16x16x32_bf16 v[78:81], v[98:101], v[202:205], v[78:81]
	v_mfma_f32_16x16x32_bf16 v[74:77], v[122:125], v[202:205], v[74:77]
	v_mfma_f32_16x16x32_bf16 v[142:145], v[110:113], v[166:169], v[142:145]
	v_mfma_f32_16x16x32_bf16 v[138:141], v[130:133], v[166:169], v[138:141]
	v_mfma_f32_16x16x32_bf16 v[118:121], v[110:113], v[174:177], v[118:121]
	v_mfma_f32_16x16x32_bf16 v[114:117], v[130:133], v[174:177], v[114:117]
	v_mfma_f32_16x16x32_bf16 v[94:97], v[110:113], v[182:185], v[94:97]
	v_mfma_f32_16x16x32_bf16 v[90:93], v[130:133], v[182:185], v[90:93]
	v_mfma_f32_16x16x32_bf16 v[78:81], v[110:113], v[206:209], v[78:81]
	v_mfma_f32_16x16x32_bf16 v[74:77], v[130:133], v[206:209], v[74:77]
	v_mfma_f32_16x16x32_bf16 v[134:137], v[146:149], v[162:165], v[134:137]
	v_mfma_f32_16x16x32_bf16 v[126:129], v[154:157], v[162:165], v[126:129]
	v_mfma_f32_16x16x32_bf16 v[106:109], v[146:149], v[170:173], v[106:109]
	v_mfma_f32_16x16x32_bf16 v[102:105], v[154:157], v[170:173], v[102:105]
	v_mfma_f32_16x16x32_bf16 v[86:89], v[146:149], v[178:181], v[86:89]
	v_mfma_f32_16x16x32_bf16 v[82:85], v[154:157], v[178:181], v[82:85]
	v_mfma_f32_16x16x32_bf16 v[70:73], v[146:149], v[202:205], v[70:73]
	v_mfma_f32_16x16x32_bf16 v[66:69], v[154:157], v[202:205], v[66:69]
	v_mfma_f32_16x16x32_bf16 v[134:137], v[150:153], v[166:169], v[134:137]
	v_mfma_f32_16x16x32_bf16 v[126:129], v[158:161], v[166:169], v[126:129]
	v_mfma_f32_16x16x32_bf16 v[106:109], v[150:153], v[174:177], v[106:109]
	v_mfma_f32_16x16x32_bf16 v[102:105], v[158:161], v[174:177], v[102:105]
	v_mfma_f32_16x16x32_bf16 v[86:89], v[150:153], v[182:185], v[86:89]
	v_mfma_f32_16x16x32_bf16 v[82:85], v[158:161], v[182:185], v[82:85]
	v_mfma_f32_16x16x32_bf16 v[70:73], v[150:153], v[206:209], v[70:73]
	v_mfma_f32_16x16x32_bf16 v[66:69], v[158:161], v[206:209], v[66:69]
	s_setprio 0
	s_barrier
; #define PG8_STAGE_A(b, h, ptr, NX) do { if constexpr (Sched::GATHER) { unsigned gs_[2]; gs_[0] = ((NX) && last_) ? gN[h][0] : gA[h][0]; gs_[1] = ((NX) && last_) ? gN[h][1] : gA[h][1]; PG8_STAGE(PG8_SA(b, h), ptr, gs_); } \
;         else PG8_STAGE(PG8_SA(b, h), (ptr) + ((h) ? hstep : (size_t)0), voffA); } while (0)
; #define PG8_STAGE(bufoff, gbase, voff) do { _Pragma("unroll") for (int _i = 0; _i < 2; ++_i) \
;         __builtin_amdgcn_global_load_lds((const unsigned*)((const char*)(gbase) + (voff)[_i]), (PG8_LAS unsigned*)(lds + (bufoff) + ldsw + _i * 8192), 16, 0, 0); } while (0)
; #define PG8_LDA(dst, b, h) do { _Pragma("unroll") for (int m = 0; m < 4; ++m) _Pragma("unroll") for (int k = 0; k < 2; ++k) dst[m][k] = *(const PG8_LAS bf16x8*)(lds + PG8_SA(b, h) + aoff + m * 2048 + k * 1024); } while (0)
; #define PG8_LDB(dst, b, h) do { _Pragma("unroll") for (int n = 0; n < 2; ++n) _Pragma("unroll") for (int k = 0; k < 2; ++k) dst[n][k] = *(const PG8_LAS bf16x8*)(lds + PG8_SB(b, h) + boff + n * 2048 + k * 1024); } while (0)
; #define PG8_WAIT_V(n) asm volatile("s_waitcnt vmcnt(" #n ")" ::: "memory")
; #define PG8_WAIT_L(n) asm volatile("s_waitcnt lgkmcnt(" #n ")" ::: "memory")
; template <class Epi, class Sched, bool ALIGN_EPI = false, bool SP2 = false>
; __device__ __forceinline__ void gemm_phase(PG8_LAS unsigned char* lds, const Gemm g, const Sched& S, const Epi& E, const bool skip_epi = false) {
;     ...
;         for (int t = 0; t < nt; t += 2) {
;             const bool last = (t == nt - 2); last_ = last && has_next;
;             const char* a1 = cA + (size_t)(t + 1) * kstep;
;             const char* a2 = last ? nA : cA + (size_t)(t + 2) * kstep; const char* b2 = last ? nB : cB + (size_t)(t + 2) * kstep;
;             const char* a3 = a2 + kstep; const char* b3 = b2 + kstep;
;             if (last && has_next) S.a_ready(nxt);
;             if constexpr (SP2) {
;             PG8_LDB(B0, 0, 0); PG8_LDB(B1, 0, 1); PG8_SCHED; PG8_LDA(At, 0, 0); PG8_STAGE_A(1, 1, a1, false);
;             PG8_WAIT_V(8); PG8_WAIT_L(0); PG8_BAR; PG8_MMA(0, 0, At, B0); PG8_MMA(0, 1, At, B1); PG8_BAR; PG8_SCHED;
;     ...
;             PG8_LDA(At, 1, 1); PG8_STAGE(PG8_SB(1, 0), b3, voffB); PG8_STAGE(PG8_SB(1, 1), b3 + hstep, voffB); PG8_STAGE_A(1, 0, a3, true);
;             PG8_WAIT_V(8); PG8_WAIT_L(0); PG8_BAR; PG8_MMA(1, 0, At, B0); PG8_MMA(1, 1, At, B1); PG8_BAR; PG8_SCHED;
	s_add_i32 s38, s64, s40
	s_add_i32 m0, s38, 0xffffff80
	ds_read_b128 v[162:165], v227 offset:49152
	ds_read_b128 v[166:169], v227 offset:50176
	ds_read_b128 v[170:173], v227 offset:51200
	ds_read_b128 v[174:177], v227 offset:52224
	ds_read_b128 v[178:181], v227 offset:53248
	ds_read_b128 v[182:185], v227 offset:54272
	ds_read_b128 v[202:205], v227 offset:55296
	ds_read_b128 v[206:209], v227 offset:56320
	global_load_lds_dwordx4 v[210:211], off offset:128
	s_add_i32 m0, s38, 0x1f80
	s_add_u32 s36, s36, 0x40080
	s_addc_u32 s37, s37, 0
	s_add_i32 s38, s65, s40
	global_load_lds_dwordx4 v[212:213], off offset:128
	s_mov_b32 m0, s38
	s_nop 0
	global_load_lds_dwordx4 v188, s[36:37]
	s_add_i32 m0, s38, 0x2000
	s_nop 0
	global_load_lds_dwordx4 v192, s[36:37]
	s_add_i32 m0, s53, 0xffffff80
	s_nop 0
	global_load_lds_dwordx4 v[214:215], off offset:128
	s_add_i32 m0, s54, 0xffffff80
	s_nop 0
	global_load_lds_dwordx4 v[216:217], off offset:128
	s_waitcnt vmcnt(8)
	s_waitcnt lgkmcnt(0)
	s_barrier
	s_setprio 3
	s_waitcnt lgkmcnt(0)
	v_mfma_f32_16x16x32_bf16 v[62:65], v[98:101], v[162:165], v[62:65]
	v_mfma_f32_16x16x32_bf16 v[58:61], v[122:125], v[162:165], v[58:61]
	v_mfma_f32_16x16x32_bf16 v[46:49], v[98:101], v[170:173], v[46:49]
	v_mfma_f32_16x16x32_bf16 v[42:45], v[122:125], v[170:173], v[42:45]
	v_mfma_f32_16x16x32_bf16 v[30:33], v[98:101], v[178:181], v[30:33]
	v_mfma_f32_16x16x32_bf16 v[26:29], v[122:125], v[178:181], v[26:29]
	v_mfma_f32_16x16x32_bf16 v[14:17], v[98:101], v[202:205], v[14:17]
	v_mfma_f32_16x16x32_bf16 v[10:13], v[122:125], v[202:205], v[10:13]
	v_mfma_f32_16x16x32_bf16 v[62:65], v[110:113], v[166:169], v[62:65]
	v_mfma_f32_16x16x32_bf16 v[58:61], v[130:133], v[166:169], v[58:61]
	v_mfma_f32_16x16x32_bf16 v[46:49], v[110:113], v[174:177], v[46:49]
	v_mfma_f32_16x16x32_bf16 v[42:45], v[130:133], v[174:177], v[42:45]
	v_mfma_f32_16x16x32_bf16 v[30:33], v[110:113], v[182:185], v[30:33]
	v_mfma_f32_16x16x32_bf16 v[26:29], v[130:133], v[182:185], v[26:29]
	v_mfma_f32_16x16x32_bf16 v[14:17], v[110:113], v[206:209], v[14:17]
	v_mfma_f32_16x16x32_bf16 v[10:13], v[130:133], v[206:209], v[10:13]
	v_mfma_f32_16x16x32_bf16 v[54:57], v[146:149], v[162:165], v[54:57]
	v_mfma_f32_16x16x32_bf16 v[50:53], v[154:157], v[162:165], v[50:53]
	v_mfma_f32_16x16x32_bf16 v[38:41], v[146:149], v[170:173], v[38:41]
	v_mfma_f32_16x16x32_bf16 v[34:37], v[154:157], v[170:173], v[34:37]
	v_mfma_f32_16x16x32_bf16 v[22:25], v[146:149], v[178:181], v[22:25]
	v_mfma_f32_16x16x32_bf16 v[18:21], v[154:157], v[178:181], v[18:21]
	v_mfma_f32_16x16x32_bf16 v[6:9], v[146:149], v[202:205], v[6:9]
	v_mfma_f32_16x16x32_bf16 v[2:5], v[154:157], v[202:205], v[2:5]
	v_mfma_f32_16x16x32_bf16 v[54:57], v[150:153], v[166:169], v[54:57]
	v_mfma_f32_16x16x32_bf16 v[50:53], v[158:161], v[166:169], v[50:53]
	v_mfma_f32_16x16x32_bf16 v[38:41], v[150:153], v[174:177], v[38:41]
	v_mfma_f32_16x16x32_bf16 v[34:37], v[158:161], v[174:177], v[34:37]
	v_mfma_f32_16x16x32_bf16 v[22:25], v[150:153], v[182:185], v[22:25]
	v_mfma_f32_16x16x32_bf16 v[18:21], v[158:161], v[182:185], v[18:21]
	v_mfma_f32_16x16x32_bf16 v[6:9], v[150:153], v[206:209], v[6:9]
	v_mfma_f32_16x16x32_bf16 v[2:5], v[158:161], v[206:209], v[2:5]
	s_setprio 0
	s_barrier
	s_add_i32 s63, s63, 2
	s_add_u32 s34, s34, 0x100
	s_addc_u32 s35, s35, 0
	s_add_u32 s61, s61, 0x100
	s_addc_u32 s62, s62, 0
	s_cmp_gt_u32 s63, 13
.LBB0_1324:
	ds_read_b128 v[98:101], v225
	ds_read_b128 v[110:113], v225 offset:1024
	ds_read_b128 v[122:125], v225 offset:2048
	ds_read_b128 v[130:133], v225 offset:3072
	ds_read_b128 v[146:149], v226
	ds_read_b128 v[150:153], v226 offset:1024
	ds_read_b128 v[154:157], v226 offset:2048
	ds_read_b128 v[158:161], v226 offset:3072
	s_add_u32 s36, s34, 0xfffc0080
	s_addc_u32 s37, s35, -1
	s_cmp_eq_u32 s63, 12
	s_cselect_b32 s39, s25, s37
	s_cselect_b32 s38, s31, s36
	s_cselect_b32 s37, s23, s62
	s_cselect_b32 s36, s60, s61
	s_add_i32 m0, s41, 0xc000
	ds_read_b128 v[162:165], v227
	ds_read_b128 v[166:169], v227 offset:1024
	ds_read_b128 v[170:173], v227 offset:2048
	ds_read_b128 v[174:177], v227 offset:3072
	ds_read_b128 v[178:181], v227 offset:4096
	ds_read_b128 v[182:185], v227 offset:5120
	ds_read_b128 v[202:205], v227 offset:6144
	ds_read_b128 v[206:209], v227 offset:7168
	global_load_lds_dwordx4 v194, s[34:35]
	s_add_i32 m0, s41, 0xe000
	s_nop 0
	global_load_lds_dwordx4 v196, s[34:35]
	s_waitcnt vmcnt(8)
	s_waitcnt lgkmcnt(0)
	s_barrier
	s_setprio 3
	s_waitcnt lgkmcnt(0)
	v_mfma_f32_16x16x32_bf16 v[142:145], v[98:101], v[162:165], v[142:145]
	v_mfma_f32_16x16x32_bf16 v[138:141], v[122:125], v[162:165], v[138:141]
	v_mfma_f32_16x16x32_bf16 v[118:121], v[98:101], v[170:173], v[118:121]
	v_mfma_f32_16x16x32_bf16 v[114:117], v[122:125], v[170:173], v[114:117]
	v_mfma_f32_16x16x32_bf16 v[94:97], v[98:101], v[178:181], v[94:97]
	v_mfma_f32_16x16x32_bf16 v[90:93], v[122:125], v[178:181], v[90:93]
	v_mfma_f32_16x16x32_bf16 v[78:81], v[98:101], v[202:205], v[78:81]
	v_mfma_f32_16x16x32_bf16 v[74:77], v[122:125], v[202:205], v[74:77]
	v_mfma_f32_16x16x32_bf16 v[142:145], v[110:113], v[166:169], v[142:145]
	v_mfma_f32_16x16x32_bf16 v[138:141], v[130:133], v[166:169], v[138:141]
	v_mfma_f32_16x16x32_bf16 v[118:121], v[110:113], v[174:177], v[118:121]
	v_mfma_f32_16x16x32_bf16 v[114:117], v[130:133], v[174:177], v[114:117]
	v_mfma_f32_16x16x32_bf16 v[94:97], v[110:113], v[182:185], v[94:97]
	v_mfma_f32_16x16x32_bf16 v[90:93], v[130:133], v[182:185], v[90:93]
	v_mfma_f32_16x16x32_bf16 v[78:81], v[110:113], v[206:209], v[78:81]
	v_mfma_f32_16x16x32_bf16 v[74:77], v[130:133], v[206:209], v[74:77]
	v_mfma_f32_16x16x32_bf16 v[134:137], v[146:149], v[162:165], v[134:137]
	v_mfma_f32_16x16x32_bf16 v[126:129], v[154:157], v[162:165], v[126:129]
	v_mfma_f32_16x16x32_bf16 v[106:109], v[146:149], v[170:173], v[106:109]
	v_mfma_f32_16x16x32_bf16 v[102:105], v[154:157], v[170:173], v[102:105]
	v_mfma_f32_16x16x32_bf16 v[86:89], v[146:149], v[178:181], v[86:89]
	v_mfma_f32_16x16x32_bf16 v[82:85], v[154:157], v[178:181], v[82:85]
	v_mfma_f32_16x16x32_bf16 v[70:73], v[146:149], v[202:205], v[70:73]
	v_mfma_f32_16x16x32_bf16 v[66:69], v[154:157], v[202:205], v[66:69]
	v_mfma_f32_16x16x32_bf16 v[134:137], v[150:153], v[166:169], v[134:137]
	v_mfma_f32_16x16x32_bf16 v[126:129], v[158:161], v[166:169], v[126:129]
	v_mfma_f32_16x16x32_bf16 v[106:109], v[150:153], v[174:177], v[106:109]
	v_mfma_f32_16x16x32_bf16 v[102:105], v[158:161], v[174:177], v[102:105]
	v_mfma_f32_16x16x32_bf16 v[86:89], v[150:153], v[182:185], v[86:89]
	v_mfma_f32_16x16x32_bf16 v[82:85], v[158:161], v[182:185], v[82:85]
	v_mfma_f32_16x16x32_bf16 v[70:73], v[150:153], v[206:209], v[70:73]
	v_mfma_f32_16x16x32_bf16 v[66:69], v[158:161], v[206:209], v[66:69]
	s_setprio 0
	s_barrier
; #define PG8_STAGE_A(b, h, ptr, NX) do { if constexpr (Sched::GATHER) { unsigned gs_[2]; gs_[0] = ((NX) && last_) ? gN[h][0] : gA[h][0]; gs_[1] = ((NX) && last_) ? gN[h][1] : gA[h][1]; PG8_STAGE(PG8_SA(b, h), ptr, gs_); } \
;         else PG8_STAGE(PG8_SA(b, h), (ptr) + ((h) ? hstep : (size_t)0), voffA); } while (0)
; #define PG8_STAGE(bufoff, gbase, voff) do { _Pragma("unroll") for (int _i = 0; _i < 2; ++_i) \
;         __builtin_amdgcn_global_load_lds((const unsigned*)((const char*)(gbase) + (voff)[_i]), (PG8_LAS unsigned*)(lds + (bufoff) + ldsw + _i * 8192), 16, 0, 0); } while (0)
; #define PG8_LDA(dst, b, h) do { _Pragma("unroll") for (int m = 0; m < 4; ++m) _Pragma("unroll") for (int k = 0; k < 2; ++k) dst[m][k] = *(const PG8_LAS bf16x8*)(lds + PG8_SA(b, h) + aoff + m * 2048 + k * 1024); } while (0)
; #define PG8_LDB(dst, b, h) do { _Pragma("unroll") for (int n = 0; n < 2; ++n) _Pragma("unroll") for (int k = 0; k < 2; ++k) dst[n][k] = *(const PG8_LAS bf16x8*)(lds + PG8_SB(b, h) + boff + n * 2048 + k * 1024); } while (0)
; #define PG8_MMA(ai, bj, At, Bt) do { __builtin_amdgcn_s_setprio(1); _Pragma("unroll") for (int m = 0; m < 4; ++m) _Pragma("unroll") for (int n = 0; n < 2; ++n) _Pragma("unroll") for (int k = 0; k < 2; ++k) \
;         acc[ai][bj][m][n] = __builtin_amdgcn_mfma_f32_16x16x32_bf16(Bt[n][k], At[m][k], acc[ai][bj][m][n], 0, 0, 0); __builtin_amdgcn_s_setprio(0); } while (0)
; #define PG8_WAIT_V(n) asm volatile("s_waitcnt vmcnt(" #n ")" ::: "memory")
; #define PG8_WAIT_L(n) asm volatile("s_waitcnt lgkmcnt(" #n ")" ::: "memory")
; template <class Epi, class Sched, bool ALIGN_EPI = false, bool SP2 = false>
; __device__ __forceinline__ void gemm_phase(PG8_LAS unsigned char* lds, const Gemm g, const Sched& S, const Epi& E, const bool skip_epi = false) {
;     ...
;             PG8_LDB(B0, 0, 0); PG8_LDB(B1, 0, 1); PG8_SCHED; PG8_LDA(At, 0, 0); PG8_STAGE_A(1, 1, a1, false);
;             PG8_WAIT_V(8); PG8_WAIT_L(0); PG8_BAR; PG8_MMA(0, 0, At, B0); PG8_MMA(0, 1, At, B1); PG8_BAR; PG8_SCHED;
;             PG8_LDA(At, 0, 1); PG8_STAGE(PG8_SB(0, 0), b2, voffB); PG8_STAGE(PG8_SB(0, 1), b2 + hstep, voffB); PG8_STAGE_A(0, 0, a2, true);
;             PG8_WAIT_V(8); PG8_WAIT_L(0); PG8_BAR; PG8_MMA(1, 0, At, B0); PG8_MMA(1, 1, At, B1); PG8_BAR; PG8_SCHED;
;             PG8_LDB(B0, 1, 0); PG8_LDB(B1, 1, 1); PG8_SCHED; PG8_LDA(At, 1, 0); PG8_STAGE_A(0, 1, a2, true);
	s_add_i32 s64, s57, s40
	v_lshl_add_u64 v[210:211], s[36:37], 0, v[188:189]
	s_mov_b32 m0, s64
	ds_read_b128 v[162:165], v227 offset:16384
	ds_read_b128 v[166:169], v227 offset:17408
	ds_read_b128 v[170:173], v227 offset:18432
	ds_read_b128 v[174:177], v227 offset:19456
	ds_read_b128 v[178:181], v227 offset:20480
	ds_read_b128 v[182:185], v227 offset:21504
	ds_read_b128 v[202:205], v227 offset:22528
	ds_read_b128 v[206:209], v227 offset:23552
	global_load_lds_dwordx4 v[210:211], off
	s_add_i32 m0, s64, 0x2000
	s_add_u32 s64, s36, 0x40000
	v_lshl_add_u64 v[212:213], s[36:37], 0, v[192:193]
	s_addc_u32 s65, s37, 0
	s_add_i32 s66, s58, s40
	global_load_lds_dwordx4 v[212:213], off
	s_mov_b32 m0, s66
	v_lshl_add_u64 v[216:217], s[38:39], 0, v[190:191]
	global_load_lds_dwordx4 v188, s[64:65]
	s_add_i32 m0, s66, 0x2000
	s_nop 0
	global_load_lds_dwordx4 v192, s[64:65]
	v_lshl_add_u64 v[214:215], s[38:39], 0, v[186:187]
	s_mov_b32 m0, s41
	s_nop 0
	global_load_lds_dwordx4 v[214:215], off
	s_mov_b32 m0, s44
	s_nop 0
	global_load_lds_dwordx4 v[216:217], off
	s_waitcnt vmcnt(8)
	s_waitcnt lgkmcnt(0)
	s_barrier
	s_setprio 3
	s_waitcnt lgkmcnt(0)
	v_mfma_f32_16x16x32_bf16 v[62:65], v[98:101], v[162:165], v[62:65]
	v_mfma_f32_16x16x32_bf16 v[58:61], v[122:125], v[162:165], v[58:61]
	v_mfma_f32_16x16x32_bf16 v[46:49], v[98:101], v[170:173], v[46:49]
	v_mfma_f32_16x16x32_bf16 v[42:45], v[122:125], v[170:173], v[42:45]
	v_mfma_f32_16x16x32_bf16 v[30:33], v[98:101], v[178:181], v[30:33]
	v_mfma_f32_16x16x32_bf16 v[26:29], v[122:125], v[178:181], v[26:29]
	v_mfma_f32_16x16x32_bf16 v[14:17], v[98:101], v[202:205], v[14:17]
	v_mfma_f32_16x16x32_bf16 v[10:13], v[122:125], v[202:205], v[10:13]
	v_mfma_f32_16x16x32_bf16 v[62:65], v[110:113], v[166:169], v[62:65]
	v_mfma_f32_16x16x32_bf16 v[58:61], v[130:133], v[166:169], v[58:61]
	v_mfma_f32_16x16x32_bf16 v[46:49], v[110:113], v[174:177], v[46:49]
	v_mfma_f32_16x16x32_bf16 v[42:45], v[130:133], v[174:177], v[42:45]
	v_mfma_f32_16x16x32_bf16 v[30:33], v[110:113], v[182:185], v[30:33]
	v_mfma_f32_16x16x32_bf16 v[26:29], v[130:133], v[182:185], v[26:29]
	v_mfma_f32_16x16x32_bf16 v[14:17], v[110:113], v[206:209], v[14:17]
	v_mfma_f32_16x16x32_bf16 v[10:13], v[130:133], v[206:209], v[10:13]
	v_mfma_f32_16x16x32_bf16 v[54:57], v[146:149], v[162:165], v[54:57]
	v_mfma_f32_16x16x32_bf16 v[50:53], v[154:157], v[162:165], v[50:53]
	v_mfma_f32_16x16x32_bf16 v[38:41], v[146:149], v[170:173], v[38:41]
	v_mfma_f32_16x16x32_bf16 v[34:37], v[154:157], v[170:173], v[34:37]
	v_mfma_f32_16x16x32_bf16 v[22:25], v[146:149], v[178:181], v[22:25]
	v_mfma_f32_16x16x32_bf16 v[18:21], v[154:157], v[178:181], v[18:21]
	v_mfma_f32_16x16x32_bf16 v[6:9], v[146:149], v[202:205], v[6:9]
	v_mfma_f32_16x16x32_bf16 v[2:5], v[154:157], v[202:205], v[2:5]
	v_mfma_f32_16x16x32_bf16 v[54:57], v[150:153], v[166:169], v[54:57]
	v_mfma_f32_16x16x32_bf16 v[50:53], v[158:161], v[166:169], v[50:53]
	v_mfma_f32_16x16x32_bf16 v[38:41], v[150:153], v[174:177], v[38:41]
	v_mfma_f32_16x16x32_bf16 v[34:37], v[158:161], v[174:177], v[34:37]
	v_mfma_f32_16x16x32_bf16 v[22:25], v[150:153], v[182:185], v[22:25]
	v_mfma_f32_16x16x32_bf16 v[18:21], v[158:161], v[182:185], v[18:21]
	v_mfma_f32_16x16x32_bf16 v[6:9], v[150:153], v[206:209], v[6:9]
	v_mfma_f32_16x16x32_bf16 v[2:5], v[158:161], v[206:209], v[2:5]
	s_setprio 0
	s_barrier
	s_add_i32 s64, 0, 0x18000
	s_add_i32 s65, 0, 0x1c000
	v_add_u32_e32 v130, s64, v220
	v_add_u32_e32 v158, s65, v220
	ds_read_b128 v[98:101], v130
	ds_read_b128 v[110:113], v130 offset:1024
	ds_read_b128 v[122:125], v130 offset:2048
	ds_read_b128 v[130:133], v130 offset:3072
	ds_read_b128 v[146:149], v158
	ds_read_b128 v[150:153], v158 offset:1024
	ds_read_b128 v[154:157], v158 offset:2048
	ds_read_b128 v[158:161], v158 offset:3072
	s_add_u32 s38, s38, 0x40000
	s_addc_u32 s39, s39, 0
	s_mov_b32 m0, s45
	ds_read_b128 v[162:165], v227 offset:32768
	ds_read_b128 v[166:169], v227 offset:33792
	ds_read_b128 v[170:173], v227 offset:34816
	ds_read_b128 v[174:177], v227 offset:35840
	ds_read_b128 v[178:181], v227 offset:36864
	ds_read_b128 v[182:185], v227 offset:37888
	ds_read_b128 v[202:205], v227 offset:38912
	ds_read_b128 v[206:209], v227 offset:39936
	global_load_lds_dwordx4 v186, s[38:39]
	s_mov_b32 m0, s48
	s_nop 0
	global_load_lds_dwordx4 v190, s[38:39]
	s_waitcnt vmcnt(8)
	s_waitcnt lgkmcnt(0)
	s_barrier
; #define PG8_STAGE_A(b, h, ptr, NX) do { if constexpr (Sched::GATHER) { unsigned gs_[2]; gs_[0] = ((NX) && last_) ? gN[h][0] : gA[h][0]; gs_[1] = ((NX) && last_) ? gN[h][1] : gA[h][1]; PG8_STAGE(PG8_SA(b, h), ptr, gs_); } \
;         else PG8_STAGE(PG8_SA(b, h), (ptr) + ((h) ? hstep : (size_t)0), voffA); } while (0)
; #define PG8_STAGE(bufoff, gbase, voff) do { _Pragma("unroll") for (int _i = 0; _i < 2; ++_i) \
;         __builtin_amdgcn_global_load_lds((const unsigned*)((const char*)(gbase) + (voff)[_i]), (PG8_LAS unsigned*)(lds + (bufoff) + ldsw + _i * 8192), 16, 0, 0); } while (0)
; #define PG8_LDA(dst, b, h) do { _Pragma("unroll") for (int m = 0; m < 4; ++m) _Pragma("unroll") for (int k = 0; k < 2; ++k) dst[m][k] = *(const PG8_LAS bf16x8*)(lds + PG8_SA(b, h) + aoff + m * 2048 + k * 1024); } while (0)
; #define PG8_LDB(dst, b, h) do { _Pragma("unroll") for (int n = 0; n < 2; ++n) _Pragma("unroll") for (int k = 0; k < 2; ++k) dst[n][k] = *(const PG8_LAS bf16x8*)(lds + PG8_SB(b, h) + boff + n * 2048 + k * 1024); } while (0)
; #define PG8_MMA(ai, bj, At, Bt) do { __builtin_amdgcn_s_setprio(1); _Pragma("unroll") for (int m = 0; m < 4; ++m) _Pragma("unroll") for (int n = 0; n < 2; ++n) _Pragma("unroll") for (int k = 0; k < 2; ++k) \
;         acc[ai][bj][m][n] = __builtin_amdgcn_mfma_f32_16x16x32_bf16(Bt[n][k], At[m][k], acc[ai][bj][m][n], 0, 0, 0); __builtin_amdgcn_s_setprio(0); } while (0)
; #define PG8_WAIT_V(n) asm volatile("s_waitcnt vmcnt(" #n ")" ::: "memory")
; #define PG8_WAIT_L(n) asm volatile("s_waitcnt lgkmcnt(" #n ")" ::: "memory")
; #define PG8_BAR __builtin_amdgcn_s_barrier()
; template <class Epi, class Sched, bool ALIGN_EPI = false, bool SP2 = false>
; __device__ __forceinline__ void gemm_phase(PG8_LAS unsigned char* lds, const Gemm g, const Sched& S, const Epi& E, const bool skip_epi = false) {
;     ...
;             PG8_LDB(B0, 1, 0); PG8_LDB(B1, 1, 1); PG8_SCHED; PG8_LDA(At, 1, 0); PG8_STAGE_A(0, 1, a2, true);
;             PG8_WAIT_V(8); PG8_WAIT_L(0); PG8_BAR; PG8_MMA(0, 0, At, B0); PG8_MMA(0, 1, At, B1); PG8_BAR; PG8_SCHED;
;             PG8_LDA(At, 1, 1); PG8_STAGE(PG8_SB(1, 0), b3, voffB); PG8_STAGE(PG8_SB(1, 1), b3 + hstep, voffB); PG8_STAGE_A(1, 0, a3, true);
;             PG8_WAIT_V(8); PG8_WAIT_L(0); PG8_BAR; PG8_MMA(1, 0, At, B0); PG8_MMA(1, 1, At, B1); PG8_BAR; PG8_SCHED;
;     ...
;         if constexpr (ALIGN_EPI) { if (wr == 0) PG8_BAR; }
	s_setprio 3
	s_waitcnt lgkmcnt(0)
	v_mfma_f32_16x16x32_bf16 v[142:145], v[98:101], v[162:165], v[142:145]
	v_mfma_f32_16x16x32_bf16 v[138:141], v[122:125], v[162:165], v[138:141]
	v_mfma_f32_16x16x32_bf16 v[118:121], v[98:101], v[170:173], v[118:121]
	v_mfma_f32_16x16x32_bf16 v[114:117], v[122:125], v[170:173], v[114:117]
	v_mfma_f32_16x16x32_bf16 v[94:97], v[98:101], v[178:181], v[94:97]
	v_mfma_f32_16x16x32_bf16 v[90:93], v[122:125], v[178:181], v[90:93]
	v_mfma_f32_16x16x32_bf16 v[78:81], v[98:101], v[202:205], v[78:81]
	v_mfma_f32_16x16x32_bf16 v[74:77], v[122:125], v[202:205], v[74:77]
	v_mfma_f32_16x16x32_bf16 v[142:145], v[110:113], v[166:169], v[142:145]
	v_mfma_f32_16x16x32_bf16 v[138:141], v[130:133], v[166:169], v[138:141]
	v_mfma_f32_16x16x32_bf16 v[118:121], v[110:113], v[174:177], v[118:121]
	v_mfma_f32_16x16x32_bf16 v[114:117], v[130:133], v[174:177], v[114:117]
	v_mfma_f32_16x16x32_bf16 v[94:97], v[110:113], v[182:185], v[94:97]
	v_mfma_f32_16x16x32_bf16 v[90:93], v[130:133], v[182:185], v[90:93]
	v_mfma_f32_16x16x32_bf16 v[78:81], v[110:113], v[206:209], v[78:81]
	v_mfma_f32_16x16x32_bf16 v[74:77], v[130:133], v[206:209], v[74:77]
	v_mfma_f32_16x16x32_bf16 v[134:137], v[146:149], v[162:165], v[134:137]
	v_mfma_f32_16x16x32_bf16 v[126:129], v[154:157], v[162:165], v[126:129]
	v_mfma_f32_16x16x32_bf16 v[106:109], v[146:149], v[170:173], v[106:109]
	v_mfma_f32_16x16x32_bf16 v[102:105], v[154:157], v[170:173], v[102:105]
	v_mfma_f32_16x16x32_bf16 v[86:89], v[146:149], v[178:181], v[86:89]
	v_mfma_f32_16x16x32_bf16 v[82:85], v[154:157], v[178:181], v[82:85]
	v_mfma_f32_16x16x32_bf16 v[70:73], v[146:149], v[202:205], v[70:73]
	v_mfma_f32_16x16x32_bf16 v[66:69], v[154:157], v[202:205], v[66:69]
	v_mfma_f32_16x16x32_bf16 v[134:137], v[150:153], v[166:169], v[134:137]
	v_mfma_f32_16x16x32_bf16 v[126:129], v[158:161], v[166:169], v[126:129]
	v_mfma_f32_16x16x32_bf16 v[106:109], v[150:153], v[174:177], v[106:109]
	v_mfma_f32_16x16x32_bf16 v[102:105], v[158:161], v[174:177], v[102:105]
	v_mfma_f32_16x16x32_bf16 v[86:89], v[150:153], v[182:185], v[86:89]
	v_mfma_f32_16x16x32_bf16 v[82:85], v[158:161], v[182:185], v[82:85]
	v_mfma_f32_16x16x32_bf16 v[70:73], v[150:153], v[206:209], v[70:73]
	v_mfma_f32_16x16x32_bf16 v[66:69], v[158:161], v[206:209], v[66:69]
	s_setprio 0
	s_barrier
	s_add_i32 s38, s64, s40
	s_add_i32 m0, s38, 0xffffff80
	ds_read_b128 v[162:165], v227 offset:49152
	ds_read_b128 v[166:169], v227 offset:50176
	ds_read_b128 v[170:173], v227 offset:51200
	ds_read_b128 v[174:177], v227 offset:52224
	ds_read_b128 v[178:181], v227 offset:53248
	ds_read_b128 v[182:185], v227 offset:54272
	ds_read_b128 v[202:205], v227 offset:55296
	ds_read_b128 v[206:209], v227 offset:56320
	global_load_lds_dwordx4 v[210:211], off offset:128
	s_add_i32 m0, s38, 0x1f80
	s_add_u32 s36, s36, 0x40080
	s_addc_u32 s37, s37, 0
	s_add_i32 s38, s65, s40
	global_load_lds_dwordx4 v[212:213], off offset:128
	s_mov_b32 m0, s38
	s_nop 0
	global_load_lds_dwordx4 v188, s[36:37]
	s_add_i32 m0, s38, 0x2000
	s_nop 0
	global_load_lds_dwordx4 v192, s[36:37]
	s_add_i32 m0, s53, 0xffffff80
	s_nop 0
	global_load_lds_dwordx4 v[214:215], off offset:128
	s_add_i32 m0, s54, 0xffffff80
	s_nop 0
	global_load_lds_dwordx4 v[216:217], off offset:128
	s_waitcnt vmcnt(8)
	s_waitcnt lgkmcnt(0)
	s_barrier
	s_setprio 3
	s_waitcnt lgkmcnt(0)
	v_mfma_f32_16x16x32_bf16 v[62:65], v[98:101], v[162:165], v[62:65]
	v_mfma_f32_16x16x32_bf16 v[58:61], v[122:125], v[162:165], v[58:61]
	v_mfma_f32_16x16x32_bf16 v[46:49], v[98:101], v[170:173], v[46:49]
	v_mfma_f32_16x16x32_bf16 v[42:45], v[122:125], v[170:173], v[42:45]
	v_mfma_f32_16x16x32_bf16 v[30:33], v[98:101], v[178:181], v[30:33]
	v_mfma_f32_16x16x32_bf16 v[26:29], v[122:125], v[178:181], v[26:29]
	v_mfma_f32_16x16x32_bf16 v[14:17], v[98:101], v[202:205], v[14:17]
	v_mfma_f32_16x16x32_bf16 v[10:13], v[122:125], v[202:205], v[10:13]
	v_mfma_f32_16x16x32_bf16 v[62:65], v[110:113], v[166:169], v[62:65]
	v_mfma_f32_16x16x32_bf16 v[58:61], v[130:133], v[166:169], v[58:61]
	v_mfma_f32_16x16x32_bf16 v[46:49], v[110:113], v[174:177], v[46:49]
	v_mfma_f32_16x16x32_bf16 v[42:45], v[130:133], v[174:177], v[42:45]
	v_mfma_f32_16x16x32_bf16 v[30:33], v[110:113], v[182:185], v[30:33]
	v_mfma_f32_16x16x32_bf16 v[26:29], v[130:133], v[182:185], v[26:29]
	v_mfma_f32_16x16x32_bf16 v[14:17], v[110:113], v[206:209], v[14:17]
	v_mfma_f32_16x16x32_bf16 v[10:13], v[130:133], v[206:209], v[10:13]
	v_mfma_f32_16x16x32_bf16 v[54:57], v[146:149], v[162:165], v[54:57]
	v_mfma_f32_16x16x32_bf16 v[50:53], v[154:157], v[162:165], v[50:53]
	v_mfma_f32_16x16x32_bf16 v[38:41], v[146:149], v[170:173], v[38:41]
	v_mfma_f32_16x16x32_bf16 v[34:37], v[154:157], v[170:173], v[34:37]
	v_mfma_f32_16x16x32_bf16 v[22:25], v[146:149], v[178:181], v[22:25]
	v_mfma_f32_16x16x32_bf16 v[18:21], v[154:157], v[178:181], v[18:21]
	v_mfma_f32_16x16x32_bf16 v[6:9], v[146:149], v[202:205], v[6:9]
	v_mfma_f32_16x16x32_bf16 v[2:5], v[154:157], v[202:205], v[2:5]
	v_mfma_f32_16x16x32_bf16 v[54:57], v[150:153], v[166:169], v[54:57]
	v_mfma_f32_16x16x32_bf16 v[50:53], v[158:161], v[166:169], v[50:53]
	v_mfma_f32_16x16x32_bf16 v[38:41], v[150:153], v[174:177], v[38:41]
	v_mfma_f32_16x16x32_bf16 v[34:37], v[158:161], v[174:177], v[34:37]
	v_mfma_f32_16x16x32_bf16 v[22:25], v[150:153], v[182:185], v[22:25]
	v_mfma_f32_16x16x32_bf16 v[18:21], v[158:161], v[182:185], v[18:21]
	v_mfma_f32_16x16x32_bf16 v[6:9], v[150:153], v[206:209], v[6:9]
	v_mfma_f32_16x16x32_bf16 v[2:5], v[158:161], v[206:209], v[2:5]
	s_setprio 0
	s_barrier
	s_add_i32 s63, s63, 2
	s_add_u32 s34, s34, 0x100
	s_addc_u32 s35, s35, 0
	s_add_u32 s61, s61, 0x100
	s_addc_u32 s62, s62, 0
	s_cmp_gt_u32 s63, 13
	s_cbranch_scc0 .LBB0_1324
	s_and_b64 vcc, exec, s[14:15]
	s_cbranch_vccz .LBB0_1327
	s_barrier

; #define PG8_STAGE_A(b, h, ptr, NX) do { if constexpr (Sched::GATHER) { unsigned gs_[2]; gs_[0] = ((NX) && last_) ? gN[h][0] : gA[h][0]; gs_[1] = ((NX) && last_) ? gN[h][1] : gA[h][1]; PG8_STAGE(PG8_SA(b, h), ptr, gs_); } \
;         else PG8_STAGE(PG8_SA(b, h), (ptr) + ((h) ? hstep : (size_t)0), voffA); } while (0)
; #define PG8_STAGE(bufoff, gbase, voff) do { _Pragma("unroll") for (int _i = 0; _i < 2; ++_i) \
;         __builtin_amdgcn_global_load_lds((const unsigned*)((const char*)(gbase) + (voff)[_i]), (PG8_LAS unsigned*)(lds + (bufoff) + ldsw + _i * 8192), 16, 0, 0); } while (0)
; #define PG8_LDA(dst, b, h) do { _Pragma("unroll") for (int m = 0; m < 4; ++m) _Pragma("unroll") for (int k = 0; k < 2; ++k) dst[m][k] = *(const PG8_LAS bf16x8*)(lds + PG8_SA(b, h) + aoff + m * 2048 + k * 1024); } while (0)
; #define PG8_LDB(dst, b, h) do { _Pragma("unroll") for (int n = 0; n < 2; ++n) _Pragma("unroll") for (int k = 0; k < 2; ++k) dst[n][k] = *(const PG8_LAS bf16x8*)(lds + PG8_SB(b, h) + boff + n * 2048 + k * 1024); } while (0)
; #define PG8_MMA(ai, bj, At, Bt) do { __builtin_amdgcn_s_setprio(1); _Pragma("unroll") for (int m = 0; m < 4; ++m) _Pragma("unroll") for (int n = 0; n < 2; ++n) _Pragma("unroll") for (int k = 0; k < 2; ++k) \
;         acc[ai][bj][m][n] = __builtin_amdgcn_mfma_f32_16x16x32_bf16(Bt[n][k], At[m][k], acc[ai][bj][m][n], 0, 0, 0); __builtin_amdgcn_s_setprio(0); } while (0)
; #define PG8_WAIT_V(n) asm volatile("s_waitcnt vmcnt(" #n ")" ::: "memory")
; #define PG8_WAIT_L(n) asm volatile("s_waitcnt lgkmcnt(" #n ")" ::: "memory")
; #define PG8_BAR __builtin_amdgcn_s_barrier()
; #define PG8_SCHED __builtin_amdgcn_sched_barrier(0)
; template <class Epi, class Sched, bool ALIGN_EPI = false, bool SP2 = false>
; __device__ __forceinline__ void gemm_phase(PG8_LAS unsigned char* lds, const Gemm g, const Sched& S, const Epi& E, const bool skip_epi = false) {
;     ...
;             PG8_LDB(B0, 0, 0); PG8_LDB(B1, 0, 1); PG8_SCHED; PG8_LDA(At, 0, 0); PG8_STAGE_A(1, 1, a1, false);
;             PG8_WAIT_V(8); PG8_WAIT_L(0); PG8_BAR; PG8_MMA(0, 0, At, B0); PG8_MMA(0, 1, At, B1); PG8_BAR; PG8_SCHED;
;             PG8_LDA(At, 0, 1); PG8_STAGE(PG8_SB(0, 0), b2, voffB); PG8_STAGE(PG8_SB(0, 1), b2 + hstep, voffB); PG8_STAGE_A(0, 0, a2, true);
.Lg5_zero:
.LBB0_1727:
	s_mov_b32 s29, s41
	s_mov_b32 s31, s40
	v_mov_b32_e32 v143, v133
	v_mov_b32_e32 v141, v133
	s_add_u32 s61, s40, 0x100
	v_lshl_add_u64 v[146:147], s[24:25], 0, v[140:141]
	v_lshl_add_u64 v[148:149], s[24:25], 0, v[142:143]
	s_addc_u32 s62, s41, 0
	s_mov_b32 s63, -2
	s_mov_b64 s[40:41], 0
	ds_read_b128 v[166:169], v158
	ds_read_b128 v[170:173], v158 offset:1024
	ds_read_b128 v[174:177], v158 offset:2048
	ds_read_b128 v[178:181], v158 offset:3072
	ds_read_b128 v[182:185], v159
	ds_read_b128 v[186:189], v159 offset:1024
	ds_read_b128 v[190:193], v159 offset:2048
	ds_read_b128 v[194:197], v159 offset:3072
	s_add_u32 s42, s78, s40
	s_addc_u32 s43, s79, s41
	s_add_u32 s44, s42, 0x1aa00100
	s_addc_u32 s45, s43, 0
	s_add_u32 s66, s61, s40
	s_addc_u32 s67, s62, s41
	s_cmpk_eq_i32 s40, 0x700
	s_cselect_b64 s[64:65], -1, 0
	s_and_b64 s[42:43], s[64:65], exec
	s_cselect_b32 s45, s87, s45
	s_cselect_b32 s44, s86, s44
	s_cselect_b32 s42, s31, s66
	s_cselect_b32 s43, s29, s67
	s_and_b64 vcc, s[6:7], s[64:65]
	v_lshl_add_u64 v[226:227], v[148:149], 0, s[40:41]
	s_add_i32 m0, s37, 0xc000
	ds_read_b128 v[198:201], v160
	ds_read_b128 v[202:205], v160 offset:1024
	ds_read_b128 v[206:209], v160 offset:2048
	ds_read_b128 v[210:213], v160 offset:3072
	ds_read_b128 v[214:217], v160 offset:4096
	ds_read_b128 v[218:221], v160 offset:5120
	ds_read_b128 v[222:225], v160 offset:6144
	ds_read_b128 v[230:233], v160 offset:7168
	global_load_lds_dwordx4 v[226:227], off
	v_lshl_add_u64 v[226:227], v[146:147], 0, s[40:41]
	s_add_i32 m0, s37, 0xe000
	s_nop 0
	global_load_lds_dwordx4 v[226:227], off
	s_waitcnt vmcnt(8)
	s_waitcnt lgkmcnt(0)
	s_barrier
	s_setprio 3
	s_waitcnt lgkmcnt(0)
	v_mfma_f32_16x16x32_bf16 v[126:129], v[166:169], v[198:201], 0
	v_mfma_f32_16x16x32_bf16 v[122:125], v[174:177], v[198:201], 0
	v_mfma_f32_16x16x32_bf16 v[110:113], v[166:169], v[206:209], 0
	v_mfma_f32_16x16x32_bf16 v[106:109], v[174:177], v[206:209], 0
	v_mfma_f32_16x16x32_bf16 v[94:97], v[166:169], v[214:217], 0
	v_mfma_f32_16x16x32_bf16 v[90:93], v[174:177], v[214:217], 0
	v_mfma_f32_16x16x32_bf16 v[78:81], v[166:169], v[222:225], 0
	v_mfma_f32_16x16x32_bf16 v[74:77], v[174:177], v[222:225], 0
	v_mfma_f32_16x16x32_bf16 v[126:129], v[170:173], v[202:205], v[126:129]
	v_mfma_f32_16x16x32_bf16 v[122:125], v[178:181], v[202:205], v[122:125]
	v_mfma_f32_16x16x32_bf16 v[110:113], v[170:173], v[210:213], v[110:113]
	v_mfma_f32_16x16x32_bf16 v[106:109], v[178:181], v[210:213], v[106:109]
	v_mfma_f32_16x16x32_bf16 v[94:97], v[170:173], v[218:221], v[94:97]
	v_mfma_f32_16x16x32_bf16 v[90:93], v[178:181], v[218:221], v[90:93]
	v_mfma_f32_16x16x32_bf16 v[78:81], v[170:173], v[230:233], v[78:81]
	v_mfma_f32_16x16x32_bf16 v[74:77], v[178:181], v[230:233], v[74:77]
	v_mfma_f32_16x16x32_bf16 v[118:121], v[182:185], v[198:201], 0
	v_mfma_f32_16x16x32_bf16 v[114:117], v[190:193], v[198:201], 0
	v_mfma_f32_16x16x32_bf16 v[102:105], v[182:185], v[206:209], 0
	v_mfma_f32_16x16x32_bf16 v[98:101], v[190:193], v[206:209], 0
	v_mfma_f32_16x16x32_bf16 v[86:89], v[182:185], v[214:217], 0
	v_mfma_f32_16x16x32_bf16 v[82:85], v[190:193], v[214:217], 0
	v_mfma_f32_16x16x32_bf16 v[70:73], v[182:185], v[222:225], 0
	v_mfma_f32_16x16x32_bf16 v[66:69], v[190:193], v[222:225], 0
	v_mfma_f32_16x16x32_bf16 v[118:121], v[186:189], v[202:205], v[118:121]
	v_mfma_f32_16x16x32_bf16 v[114:117], v[194:197], v[202:205], v[114:117]
	v_mfma_f32_16x16x32_bf16 v[102:105], v[186:189], v[210:213], v[102:105]
	v_mfma_f32_16x16x32_bf16 v[98:101], v[194:197], v[210:213], v[98:101]
	v_mfma_f32_16x16x32_bf16 v[86:89], v[186:189], v[218:221], v[86:89]
	v_mfma_f32_16x16x32_bf16 v[82:85], v[194:197], v[218:221], v[82:85]
	v_mfma_f32_16x16x32_bf16 v[70:73], v[186:189], v[230:233], v[70:73]
	v_mfma_f32_16x16x32_bf16 v[66:69], v[194:197], v[230:233], v[66:69]
	s_setprio 0
	s_barrier
	s_add_i32 s64, s58, s50
	v_lshl_add_u64 v[226:227], s[42:43], 0, v[134:135]
	s_mov_b32 m0, s64
	ds_read_b128 v[198:201], v160 offset:16384
	ds_read_b128 v[202:205], v160 offset:17408
	ds_read_b128 v[206:209], v160 offset:18432
	ds_read_b128 v[210:213], v160 offset:19456
	ds_read_b128 v[214:217], v160 offset:20480
	ds_read_b128 v[218:221], v160 offset:21504
	ds_read_b128 v[222:225], v160 offset:22528
	ds_read_b128 v[230:233], v160 offset:23552
	global_load_lds_dwordx4 v[226:227], off
	s_add_i32 m0, s64, 0x2000
	s_add_u32 s64, s42, 0x40000
	v_lshl_add_u64 v[234:235], s[42:43], 0, v[136:137]
	s_addc_u32 s65, s43, 0
	s_add_i32 s66, s59, s50
	global_load_lds_dwordx4 v[234:235], off
	s_mov_b32 m0, s66
	v_cndmask_b32_e32 v132, v130, v164, vcc
	global_load_lds_dwordx4 v134, s[64:65]
	s_add_i32 m0, s66, 0x2000
	v_lshl_add_u64 v[238:239], s[44:45], 0, v[132:133]
	global_load_lds_dwordx4 v136, s[64:65]
	s_mov_b32 m0, s37
	v_cndmask_b32_e32 v236, v144, v163, vcc
	global_load_lds_dwordx4 v132, s[44:45]
	s_mov_b32 m0, s39
	v_mov_b32_e32 v237, v133
	global_load_lds_dwordx4 v236, s[44:45]
	s_waitcnt vmcnt(8)
	s_waitcnt lgkmcnt(0)
	v_lshl_add_u64 v[236:237], s[44:45], 0, v[236:237]
	s_barrier
; #define PG8_STAGE_A(b, h, ptr, NX) do { if constexpr (Sched::GATHER) { unsigned gs_[2]; gs_[0] = ((NX) && last_) ? gN[h][0] : gA[h][0]; gs_[1] = ((NX) && last_) ? gN[h][1] : gA[h][1]; PG8_STAGE(PG8_SA(b, h), ptr, gs_); } \
;         else PG8_STAGE(PG8_SA(b, h), (ptr) + ((h) ? hstep : (size_t)0), voffA); } while (0)
; #define PG8_STAGE(bufoff, gbase, voff) do { _Pragma("unroll") for (int _i = 0; _i < 2; ++_i) \
;         __builtin_amdgcn_global_load_lds((const unsigned*)((const char*)(gbase) + (voff)[_i]), (PG8_LAS unsigned*)(lds + (bufoff) + ldsw + _i * 8192), 16, 0, 0); } while (0)
; #define PG8_LDA(dst, b, h) do { _Pragma("unroll") for (int m = 0; m < 4; ++m) _Pragma("unroll") for (int k = 0; k < 2; ++k) dst[m][k] = *(const PG8_LAS bf16x8*)(lds + PG8_SA(b, h) + aoff + m * 2048 + k * 1024); } while (0)
; #define PG8_LDB(dst, b, h) do { _Pragma("unroll") for (int n = 0; n < 2; ++n) _Pragma("unroll") for (int k = 0; k < 2; ++k) dst[n][k] = *(const PG8_LAS bf16x8*)(lds + PG8_SB(b, h) + boff + n * 2048 + k * 1024); } while (0)
; #define PG8_MMA(ai, bj, At, Bt) do { __builtin_amdgcn_s_setprio(1); _Pragma("unroll") for (int m = 0; m < 4; ++m) _Pragma("unroll") for (int n = 0; n < 2; ++n) _Pragma("unroll") for (int k = 0; k < 2; ++k) \
;         acc[ai][bj][m][n] = __builtin_amdgcn_mfma_f32_16x16x32_bf16(Bt[n][k], At[m][k], acc[ai][bj][m][n], 0, 0, 0); __builtin_amdgcn_s_setprio(0); } while (0)
; #define PG8_WAIT_V(n) asm volatile("s_waitcnt vmcnt(" #n ")" ::: "memory")
; #define PG8_WAIT_L(n) asm volatile("s_waitcnt lgkmcnt(" #n ")" ::: "memory")
; #define PG8_BAR __builtin_amdgcn_s_barrier()
; #define PG8_SCHED __builtin_amdgcn_sched_barrier(0)
; template <class Epi, class Sched, bool ALIGN_EPI = false, bool SP2 = false>
; __device__ __forceinline__ void gemm_phase(PG8_LAS unsigned char* lds, const Gemm g, const Sched& S, const Epi& E, const bool skip_epi = false) {
;     ...
;             PG8_LDA(At, 0, 1); PG8_STAGE(PG8_SB(0, 0), b2, voffB); PG8_STAGE(PG8_SB(0, 1), b2 + hstep, voffB); PG8_STAGE_A(0, 0, a2, true);
;             PG8_WAIT_V(8); PG8_WAIT_L(0); PG8_BAR; PG8_MMA(1, 0, At, B0); PG8_MMA(1, 1, At, B1); PG8_BAR; PG8_SCHED;
;             PG8_LDB(B0, 1, 0); PG8_LDB(B1, 1, 1); PG8_SCHED; PG8_LDA(At, 1, 0); PG8_STAGE_A(0, 1, a2, true);
;             PG8_WAIT_V(8); PG8_WAIT_L(0); PG8_BAR; PG8_MMA(0, 0, At, B0); PG8_MMA(0, 1, At, B1); PG8_BAR; PG8_SCHED;
	s_setprio 3
	s_waitcnt lgkmcnt(0)
	v_mfma_f32_16x16x32_bf16 v[62:65], v[166:169], v[198:201], 0
	v_mfma_f32_16x16x32_bf16 v[58:61], v[174:177], v[198:201], 0
	v_mfma_f32_16x16x32_bf16 v[38:41], v[166:169], v[206:209], 0
	v_mfma_f32_16x16x32_bf16 v[34:37], v[174:177], v[206:209], 0
	v_mfma_f32_16x16x32_bf16 v[22:25], v[166:169], v[214:217], 0
	v_mfma_f32_16x16x32_bf16 v[18:21], v[174:177], v[214:217], 0
	v_mfma_f32_16x16x32_bf16 v[6:9], v[166:169], v[222:225], 0
	v_mfma_f32_16x16x32_bf16 v[2:5], v[174:177], v[222:225], 0
	v_mfma_f32_16x16x32_bf16 v[62:65], v[170:173], v[202:205], v[62:65]
	v_mfma_f32_16x16x32_bf16 v[58:61], v[178:181], v[202:205], v[58:61]
	v_mfma_f32_16x16x32_bf16 v[38:41], v[170:173], v[210:213], v[38:41]
	v_mfma_f32_16x16x32_bf16 v[34:37], v[178:181], v[210:213], v[34:37]
	v_mfma_f32_16x16x32_bf16 v[22:25], v[170:173], v[218:221], v[22:25]
	v_mfma_f32_16x16x32_bf16 v[18:21], v[178:181], v[218:221], v[18:21]
	v_mfma_f32_16x16x32_bf16 v[6:9], v[170:173], v[230:233], v[6:9]
	v_mfma_f32_16x16x32_bf16 v[2:5], v[178:181], v[230:233], v[2:5]
	v_mfma_f32_16x16x32_bf16 v[50:53], v[182:185], v[198:201], 0
	v_mfma_f32_16x16x32_bf16 v[42:45], v[190:193], v[198:201], 0
	v_mfma_f32_16x16x32_bf16 v[54:57], v[182:185], v[206:209], 0
	v_mfma_f32_16x16x32_bf16 v[46:49], v[190:193], v[206:209], 0
	v_mfma_f32_16x16x32_bf16 v[30:33], v[182:185], v[214:217], 0
	v_mfma_f32_16x16x32_bf16 v[26:29], v[190:193], v[214:217], 0
	v_mfma_f32_16x16x32_bf16 v[14:17], v[182:185], v[222:225], 0
	v_mfma_f32_16x16x32_bf16 v[10:13], v[190:193], v[222:225], 0
	v_mfma_f32_16x16x32_bf16 v[50:53], v[186:189], v[202:205], v[50:53]
	v_mfma_f32_16x16x32_bf16 v[42:45], v[194:197], v[202:205], v[42:45]
	v_mfma_f32_16x16x32_bf16 v[54:57], v[186:189], v[210:213], v[54:57]
	v_mfma_f32_16x16x32_bf16 v[46:49], v[194:197], v[210:213], v[46:49]
	v_mfma_f32_16x16x32_bf16 v[30:33], v[186:189], v[218:221], v[30:33]
	v_mfma_f32_16x16x32_bf16 v[26:29], v[194:197], v[218:221], v[26:29]
	v_mfma_f32_16x16x32_bf16 v[14:17], v[186:189], v[230:233], v[14:17]
	v_mfma_f32_16x16x32_bf16 v[10:13], v[194:197], v[230:233], v[10:13]
	s_setprio 0
	s_barrier
	s_add_i32 s64, 0, 0x18000
	v_add_u32_e32 v132, s64, v154
	s_add_i32 s65, 0, 0x1c000
	ds_read_b128 v[166:169], v132
	ds_read_b128 v[170:173], v132 offset:1024
	ds_read_b128 v[174:177], v132 offset:2048
	ds_read_b128 v[178:181], v132 offset:3072
	v_add_u32_e32 v132, s65, v154
	ds_read_b128 v[182:185], v132
	ds_read_b128 v[186:189], v132 offset:1024
	ds_read_b128 v[190:193], v132 offset:2048
	ds_read_b128 v[194:197], v132 offset:3072
	s_mov_b32 m0, s51
	v_cndmask_b32_e32 v132, v142, v162, vcc
	ds_read_b128 v[198:201], v160 offset:32768
	ds_read_b128 v[202:205], v160 offset:33792
	ds_read_b128 v[206:209], v160 offset:34816
	ds_read_b128 v[210:213], v160 offset:35840
	ds_read_b128 v[214:217], v160 offset:36864
	ds_read_b128 v[218:221], v160 offset:37888
	ds_read_b128 v[222:225], v160 offset:38912
	ds_read_b128 v[230:233], v160 offset:39936
	v_cndmask_b32_e32 v141, v140, v161, vcc
	global_load_lds_dwordx4 v132, s[44:45]
	s_mov_b32 m0, s52
	s_nop 0
	global_load_lds_dwordx4 v141, s[44:45]
	s_waitcnt vmcnt(8)
	s_waitcnt lgkmcnt(0)
	s_barrier
	s_setprio 3
	s_waitcnt lgkmcnt(0)
	v_mfma_f32_16x16x32_bf16 v[126:129], v[166:169], v[198:201], v[126:129]
	v_mfma_f32_16x16x32_bf16 v[122:125], v[174:177], v[198:201], v[122:125]
	v_mfma_f32_16x16x32_bf16 v[110:113], v[166:169], v[206:209], v[110:113]
	v_mfma_f32_16x16x32_bf16 v[106:109], v[174:177], v[206:209], v[106:109]
	v_mfma_f32_16x16x32_bf16 v[94:97], v[166:169], v[214:217], v[94:97]
	v_mfma_f32_16x16x32_bf16 v[90:93], v[174:177], v[214:217], v[90:93]
	v_mfma_f32_16x16x32_bf16 v[78:81], v[166:169], v[222:225], v[78:81]
	v_mfma_f32_16x16x32_bf16 v[74:77], v[174:177], v[222:225], v[74:77]
	v_mfma_f32_16x16x32_bf16 v[126:129], v[170:173], v[202:205], v[126:129]
	v_mfma_f32_16x16x32_bf16 v[122:125], v[178:181], v[202:205], v[122:125]
	v_mfma_f32_16x16x32_bf16 v[110:113], v[170:173], v[210:213], v[110:113]
	v_mfma_f32_16x16x32_bf16 v[106:109], v[178:181], v[210:213], v[106:109]
	v_mfma_f32_16x16x32_bf16 v[94:97], v[170:173], v[218:221], v[94:97]
	v_mfma_f32_16x16x32_bf16 v[90:93], v[178:181], v[218:221], v[90:93]
	v_mfma_f32_16x16x32_bf16 v[78:81], v[170:173], v[230:233], v[78:81]
	v_mfma_f32_16x16x32_bf16 v[74:77], v[178:181], v[230:233], v[74:77]
	v_mfma_f32_16x16x32_bf16 v[118:121], v[182:185], v[198:201], v[118:121]
	v_mfma_f32_16x16x32_bf16 v[114:117], v[190:193], v[198:201], v[114:117]
	v_mfma_f32_16x16x32_bf16 v[102:105], v[182:185], v[206:209], v[102:105]
	v_mfma_f32_16x16x32_bf16 v[98:101], v[190:193], v[206:209], v[98:101]
	v_mfma_f32_16x16x32_bf16 v[86:89], v[182:185], v[214:217], v[86:89]
	v_mfma_f32_16x16x32_bf16 v[82:85], v[190:193], v[214:217], v[82:85]
	v_mfma_f32_16x16x32_bf16 v[70:73], v[182:185], v[222:225], v[70:73]
	v_mfma_f32_16x16x32_bf16 v[66:69], v[190:193], v[222:225], v[66:69]
	v_mfma_f32_16x16x32_bf16 v[118:121], v[186:189], v[202:205], v[118:121]
	v_mfma_f32_16x16x32_bf16 v[114:117], v[194:197], v[202:205], v[114:117]
	v_mfma_f32_16x16x32_bf16 v[102:105], v[186:189], v[210:213], v[102:105]
	v_mfma_f32_16x16x32_bf16 v[98:101], v[194:197], v[210:213], v[98:101]
	v_mfma_f32_16x16x32_bf16 v[86:89], v[186:189], v[218:221], v[86:89]
	v_mfma_f32_16x16x32_bf16 v[82:85], v[194:197], v[218:221], v[82:85]
	v_mfma_f32_16x16x32_bf16 v[70:73], v[186:189], v[230:233], v[70:73]
	v_mfma_f32_16x16x32_bf16 v[66:69], v[194:197], v[230:233], v[66:69]
	s_setprio 0
	s_barrier
; #define PG8_GIDX(G_, PM_) do { if constexpr (Sched::GATHER) { _Pragma("unroll") for (int h_ = 0; h_ < 2; ++h_) _Pragma("unroll") for (int i_ = 0; i_ < 2; ++i_) { int R_, C_; stage_rc(tid * 16 + i_ * 8192, R_, C_); \
;         const int src_ = S.rowsrc[(PM_) * BM + h_ * HALF + R_]; G_[h_][i_] = (unsigned)(src_ * K + C_) * 2u; } } } while (0)
; #define PG8_STAGE_A(b, h, ptr, NX) do { if constexpr (Sched::GATHER) { unsigned gs_[2]; gs_[0] = ((NX) && last_) ? gN[h][0] : gA[h][0]; gs_[1] = ((NX) && last_) ? gN[h][1] : gA[h][1]; PG8_STAGE(PG8_SA(b, h), ptr, gs_); } \
;         else PG8_STAGE(PG8_SA(b, h), (ptr) + ((h) ? hstep : (size_t)0), voffA); } while (0)
; #define PG8_STAGE(bufoff, gbase, voff) do { _Pragma("unroll") for (int _i = 0; _i < 2; ++_i) \
;         __builtin_amdgcn_global_load_lds((const unsigned*)((const char*)(gbase) + (voff)[_i]), (PG8_LAS unsigned*)(lds + (bufoff) + ldsw + _i * 8192), 16, 0, 0); } while (0)
; #define PG8_LDA(dst, b, h) do { _Pragma("unroll") for (int m = 0; m < 4; ++m) _Pragma("unroll") for (int k = 0; k < 2; ++k) dst[m][k] = *(const PG8_LAS bf16x8*)(lds + PG8_SA(b, h) + aoff + m * 2048 + k * 1024); } while (0)
; #define PG8_WAIT_V(n) asm volatile("s_waitcnt vmcnt(" #n ")" ::: "memory")
; #define PG8_WAIT_L(n) asm volatile("s_waitcnt lgkmcnt(" #n ")" ::: "memory")
; #define PG8_BAR __builtin_amdgcn_s_barrier()
; #define PG8_SCHED __builtin_amdgcn_sched_barrier(0)
;     __device__ bool next(int i, Unit& u) const {
;     ...
;         const int p = fm + rr % gsz; u.pm = p; u.pn = panel_e[p] * NT + rr / gsz; u.ko = 0; return true;
; template <class Epi, class Sched, bool ALIGN_EPI = false, bool SP2 = false>
; __device__ __forceinline__ void gemm_phase(PG8_LAS unsigned char* lds, const Gemm g, const Sched& S, const Epi& E, const bool skip_epi = false) {
;     ...
;         if (has_next) PG8_GIDX(gN, nxt.pm);
;         const char* nA = has_next ? (const char*)g.A + (size_t)nxt.pm * pmstepA + nxt.ko : cA; const char* nB = has_next ? (const char*)g.Bt + (size_t)nxt.pn * tstep + nxt.ko : cB;
;     ...
;             PG8_LDA(At, 1, 1); PG8_STAGE(PG8_SB(1, 0), b3, voffB); PG8_STAGE(PG8_SB(1, 1), b3 + hstep, voffB); PG8_STAGE_A(1, 0, a3, true);
;             PG8_WAIT_V(8); PG8_WAIT_L(0); PG8_BAR; PG8_MMA(1, 0, At, B0); PG8_MMA(1, 1, At, B1); PG8_BAR; PG8_SCHED;
	s_add_i32 s44, s64, s50
	s_add_i32 m0, s44, 0xffffff80
	ds_read_b128 v[198:201], v160 offset:49152
	ds_read_b128 v[202:205], v160 offset:50176
	ds_read_b128 v[206:209], v160 offset:51200
	ds_read_b128 v[210:213], v160 offset:52224
	ds_read_b128 v[214:217], v160 offset:53248
	ds_read_b128 v[218:221], v160 offset:54272
	ds_read_b128 v[222:225], v160 offset:55296
	ds_read_b128 v[230:233], v160 offset:56320
	global_load_lds_dwordx4 v[226:227], off offset:128
	s_add_i32 m0, s44, 0x1f80
	s_add_u32 s42, s42, 0x40080
	s_addc_u32 s43, s43, 0
	s_add_i32 s44, s65, s50
	global_load_lds_dwordx4 v[234:235], off offset:128
	s_mov_b32 m0, s44
	s_nop 0
	global_load_lds_dwordx4 v134, s[42:43]
	s_add_i32 m0, s44, 0x2000
	s_nop 0
	global_load_lds_dwordx4 v136, s[42:43]
	s_add_i32 m0, s55, 0xffffff80
	s_nop 0
	global_load_lds_dwordx4 v[238:239], off offset:128
	s_add_i32 m0, s56, 0xffffff80
	s_nop 0
	global_load_lds_dwordx4 v[236:237], off offset:128
	s_waitcnt vmcnt(8)
	s_waitcnt lgkmcnt(0)
	s_barrier
	s_setprio 3
	s_waitcnt lgkmcnt(0)
	v_mfma_f32_16x16x32_bf16 v[62:65], v[166:169], v[198:201], v[62:65]
	v_mfma_f32_16x16x32_bf16 v[58:61], v[174:177], v[198:201], v[58:61]
	v_mfma_f32_16x16x32_bf16 v[38:41], v[166:169], v[206:209], v[38:41]
	v_mfma_f32_16x16x32_bf16 v[34:37], v[174:177], v[206:209], v[34:37]
	v_mfma_f32_16x16x32_bf16 v[22:25], v[166:169], v[214:217], v[22:25]
	v_mfma_f32_16x16x32_bf16 v[18:21], v[174:177], v[214:217], v[18:21]
	v_mfma_f32_16x16x32_bf16 v[6:9], v[166:169], v[222:225], v[6:9]
	v_mfma_f32_16x16x32_bf16 v[2:5], v[174:177], v[222:225], v[2:5]
	v_mfma_f32_16x16x32_bf16 v[62:65], v[170:173], v[202:205], v[62:65]
	v_mfma_f32_16x16x32_bf16 v[58:61], v[178:181], v[202:205], v[58:61]
	v_mfma_f32_16x16x32_bf16 v[38:41], v[170:173], v[210:213], v[38:41]
	v_mfma_f32_16x16x32_bf16 v[34:37], v[178:181], v[210:213], v[34:37]
	v_mfma_f32_16x16x32_bf16 v[22:25], v[170:173], v[218:221], v[22:25]
	v_mfma_f32_16x16x32_bf16 v[18:21], v[178:181], v[218:221], v[18:21]
	v_mfma_f32_16x16x32_bf16 v[6:9], v[170:173], v[230:233], v[6:9]
	v_mfma_f32_16x16x32_bf16 v[2:5], v[178:181], v[230:233], v[2:5]
	v_mfma_f32_16x16x32_bf16 v[50:53], v[182:185], v[198:201], v[50:53]
	v_mfma_f32_16x16x32_bf16 v[42:45], v[190:193], v[198:201], v[42:45]
	v_mfma_f32_16x16x32_bf16 v[54:57], v[182:185], v[206:209], v[54:57]
	v_mfma_f32_16x16x32_bf16 v[46:49], v[190:193], v[206:209], v[46:49]
	v_mfma_f32_16x16x32_bf16 v[30:33], v[182:185], v[214:217], v[30:33]
	v_mfma_f32_16x16x32_bf16 v[26:29], v[190:193], v[214:217], v[26:29]
	v_mfma_f32_16x16x32_bf16 v[14:17], v[182:185], v[222:225], v[14:17]
	v_mfma_f32_16x16x32_bf16 v[10:13], v[190:193], v[222:225], v[10:13]
	v_mfma_f32_16x16x32_bf16 v[50:53], v[186:189], v[202:205], v[50:53]
	v_mfma_f32_16x16x32_bf16 v[42:45], v[194:197], v[202:205], v[42:45]
	v_mfma_f32_16x16x32_bf16 v[54:57], v[186:189], v[210:213], v[54:57]
	v_mfma_f32_16x16x32_bf16 v[46:49], v[194:197], v[210:213], v[46:49]
	v_mfma_f32_16x16x32_bf16 v[30:33], v[186:189], v[218:221], v[30:33]
	v_mfma_f32_16x16x32_bf16 v[26:29], v[194:197], v[218:221], v[26:29]
	v_mfma_f32_16x16x32_bf16 v[14:17], v[186:189], v[230:233], v[14:17]
	v_mfma_f32_16x16x32_bf16 v[10:13], v[194:197], v[230:233], v[10:13]
	s_setprio 0
	s_barrier
	s_add_i32 s63, s63, 2
	s_add_u32 s40, s40, 0x100
	s_addc_u32 s41, s41, 0
	s_cmp_gt_u32 s63, 13
	s_andn2_b64 vcc, exec, s[6:7]
	s_cbranch_vccnz .Lg5_nonext
	s_waitcnt vmcnt(8)
	v_readfirstlane_b32 s34, v250
	v_lshl_add_u32 v164, v229, 11, v152
	v_lshl_add_u32 v163, v251, 11, v153
	v_lshl_add_u32 v162, v252, 11, v152
	v_lshl_add_u32 v161, v253, 11, v153
	s_mul_i32 s34, s34, 28
	s_add_i32 s30, s34, s30
	s_ashr_i32 s31, s30, 31
	s_lshl_b64 s[34:35], s[30:31], 19
	v_readlane_b32 s42, v254, 29
	v_readlane_b32 s43, v254, 30
	s_add_u32 s34, s42, s34
	s_addc_u32 s35, s43, s35
	s_mov_b32 s29, s35
	s_mov_b32 s31, s34
.Lg5_nonext:
.LBB0_1728:
	ds_read_b128 v[166:169], v158
	ds_read_b128 v[170:173], v158 offset:1024
	ds_read_b128 v[174:177], v158 offset:2048
	ds_read_b128 v[178:181], v158 offset:3072
	ds_read_b128 v[182:185], v159
	ds_read_b128 v[186:189], v159 offset:1024
	ds_read_b128 v[190:193], v159 offset:2048
	ds_read_b128 v[194:197], v159 offset:3072
	s_add_u32 s42, s78, s40
	s_addc_u32 s43, s79, s41
	s_add_u32 s44, s42, 0x1aa00100
	s_addc_u32 s45, s43, 0
	s_add_u32 s66, s61, s40
	s_addc_u32 s67, s62, s41
	s_cmpk_eq_i32 s40, 0x700
	s_cselect_b64 s[64:65], -1, 0
	s_and_b64 s[42:43], s[64:65], exec
	s_cselect_b32 s45, s87, s45
	s_cselect_b32 s44, s86, s44
	s_cselect_b32 s42, s31, s66
	s_cselect_b32 s43, s29, s67
	s_and_b64 vcc, s[6:7], s[64:65]
	v_lshl_add_u64 v[226:227], v[148:149], 0, s[40:41]
	s_add_i32 m0, s37, 0xc000
	ds_read_b128 v[198:201], v160
	ds_read_b128 v[202:205], v160 offset:1024
	ds_read_b128 v[206:209], v160 offset:2048
	ds_read_b128 v[210:213], v160 offset:3072
	ds_read_b128 v[214:217], v160 offset:4096
	ds_read_b128 v[218:221], v160 offset:5120
	ds_read_b128 v[222:225], v160 offset:6144
	ds_read_b128 v[230:233], v160 offset:7168
	global_load_lds_dwordx4 v[226:227], off
	v_lshl_add_u64 v[226:227], v[146:147], 0, s[40:41]
	s_add_i32 m0, s37, 0xe000
	s_nop 0
	global_load_lds_dwordx4 v[226:227], off
	s_waitcnt vmcnt(8)
	s_waitcnt lgkmcnt(0)
	s_barrier
; #define PG8_STAGE_A(b, h, ptr, NX) do { if constexpr (Sched::GATHER) { unsigned gs_[2]; gs_[0] = ((NX) && last_) ? gN[h][0] : gA[h][0]; gs_[1] = ((NX) && last_) ? gN[h][1] : gA[h][1]; PG8_STAGE(PG8_SA(b, h), ptr, gs_); } \
;         else PG8_STAGE(PG8_SA(b, h), (ptr) + ((h) ? hstep : (size_t)0), voffA); } while (0)
; #define PG8_STAGE(bufoff, gbase, voff) do { _Pragma("unroll") for (int _i = 0; _i < 2; ++_i) \
;         __builtin_amdgcn_global_load_lds((const unsigned*)((const char*)(gbase) + (voff)[_i]), (PG8_LAS unsigned*)(lds + (bufoff) + ldsw + _i * 8192), 16, 0, 0); } while (0)
; #define PG8_LDA(dst, b, h) do { _Pragma("unroll") for (int m = 0; m < 4; ++m) _Pragma("unroll") for (int k = 0; k < 2; ++k) dst[m][k] = *(const PG8_LAS bf16x8*)(lds + PG8_SA(b, h) + aoff + m * 2048 + k * 1024); } while (0)
; #define PG8_MMA(ai, bj, At, Bt) do { __builtin_amdgcn_s_setprio(1); _Pragma("unroll") for (int m = 0; m < 4; ++m) _Pragma("unroll") for (int n = 0; n < 2; ++n) _Pragma("unroll") for (int k = 0; k < 2; ++k) \
;         acc[ai][bj][m][n] = __builtin_amdgcn_mfma_f32_16x16x32_bf16(Bt[n][k], At[m][k], acc[ai][bj][m][n], 0, 0, 0); __builtin_amdgcn_s_setprio(0); } while (0)
; #define PG8_WAIT_V(n) asm volatile("s_waitcnt vmcnt(" #n ")" ::: "memory")
; #define PG8_WAIT_L(n) asm volatile("s_waitcnt lgkmcnt(" #n ")" ::: "memory")
; #define PG8_BAR __builtin_amdgcn_s_barrier()
; #define PG8_SCHED __builtin_amdgcn_sched_barrier(0)
; template <class Epi, class Sched, bool ALIGN_EPI = false, bool SP2 = false>
; __device__ __forceinline__ void gemm_phase(PG8_LAS unsigned char* lds, const Gemm g, const Sched& S, const Epi& E, const bool skip_epi = false) {
;     ...
;             PG8_WAIT_V(8); PG8_WAIT_L(0); PG8_BAR; PG8_MMA(0, 0, At, B0); PG8_MMA(0, 1, At, B1); PG8_BAR; PG8_SCHED;
;             PG8_LDA(At, 0, 1); PG8_STAGE(PG8_SB(0, 0), b2, voffB); PG8_STAGE(PG8_SB(0, 1), b2 + hstep, voffB); PG8_STAGE_A(0, 0, a2, true);
;             PG8_WAIT_V(8); PG8_WAIT_L(0); PG8_BAR; PG8_MMA(1, 0, At, B0); PG8_MMA(1, 1, At, B1); PG8_BAR; PG8_SCHED;
	s_setprio 3
	s_waitcnt lgkmcnt(0)
	v_mfma_f32_16x16x32_bf16 v[126:129], v[166:169], v[198:201], v[126:129]
	v_mfma_f32_16x16x32_bf16 v[122:125], v[174:177], v[198:201], v[122:125]
	v_mfma_f32_16x16x32_bf16 v[110:113], v[166:169], v[206:209], v[110:113]
	v_mfma_f32_16x16x32_bf16 v[106:109], v[174:177], v[206:209], v[106:109]
	v_mfma_f32_16x16x32_bf16 v[94:97], v[166:169], v[214:217], v[94:97]
	v_mfma_f32_16x16x32_bf16 v[90:93], v[174:177], v[214:217], v[90:93]
	v_mfma_f32_16x16x32_bf16 v[78:81], v[166:169], v[222:225], v[78:81]
	v_mfma_f32_16x16x32_bf16 v[74:77], v[174:177], v[222:225], v[74:77]
	v_mfma_f32_16x16x32_bf16 v[126:129], v[170:173], v[202:205], v[126:129]
	v_mfma_f32_16x16x32_bf16 v[122:125], v[178:181], v[202:205], v[122:125]
	v_mfma_f32_16x16x32_bf16 v[110:113], v[170:173], v[210:213], v[110:113]
	v_mfma_f32_16x16x32_bf16 v[106:109], v[178:181], v[210:213], v[106:109]
	v_mfma_f32_16x16x32_bf16 v[94:97], v[170:173], v[218:221], v[94:97]
	v_mfma_f32_16x16x32_bf16 v[90:93], v[178:181], v[218:221], v[90:93]
	v_mfma_f32_16x16x32_bf16 v[78:81], v[170:173], v[230:233], v[78:81]
	v_mfma_f32_16x16x32_bf16 v[74:77], v[178:181], v[230:233], v[74:77]
	v_mfma_f32_16x16x32_bf16 v[118:121], v[182:185], v[198:201], v[118:121]
	v_mfma_f32_16x16x32_bf16 v[114:117], v[190:193], v[198:201], v[114:117]
	v_mfma_f32_16x16x32_bf16 v[102:105], v[182:185], v[206:209], v[102:105]
	v_mfma_f32_16x16x32_bf16 v[98:101], v[190:193], v[206:209], v[98:101]
	v_mfma_f32_16x16x32_bf16 v[86:89], v[182:185], v[214:217], v[86:89]
	v_mfma_f32_16x16x32_bf16 v[82:85], v[190:193], v[214:217], v[82:85]
	v_mfma_f32_16x16x32_bf16 v[70:73], v[182:185], v[222:225], v[70:73]
	v_mfma_f32_16x16x32_bf16 v[66:69], v[190:193], v[222:225], v[66:69]
	v_mfma_f32_16x16x32_bf16 v[118:121], v[186:189], v[202:205], v[118:121]
	v_mfma_f32_16x16x32_bf16 v[114:117], v[194:197], v[202:205], v[114:117]
	v_mfma_f32_16x16x32_bf16 v[102:105], v[186:189], v[210:213], v[102:105]
	v_mfma_f32_16x16x32_bf16 v[98:101], v[194:197], v[210:213], v[98:101]
	v_mfma_f32_16x16x32_bf16 v[86:89], v[186:189], v[218:221], v[86:89]
	v_mfma_f32_16x16x32_bf16 v[82:85], v[194:197], v[218:221], v[82:85]
	v_mfma_f32_16x16x32_bf16 v[70:73], v[186:189], v[230:233], v[70:73]
	v_mfma_f32_16x16x32_bf16 v[66:69], v[194:197], v[230:233], v[66:69]
	s_setprio 0
	s_barrier
	s_add_i32 s64, s58, s50
	v_lshl_add_u64 v[226:227], s[42:43], 0, v[134:135]
	s_mov_b32 m0, s64
	ds_read_b128 v[198:201], v160 offset:16384
	ds_read_b128 v[202:205], v160 offset:17408
	ds_read_b128 v[206:209], v160 offset:18432
	ds_read_b128 v[210:213], v160 offset:19456
	ds_read_b128 v[214:217], v160 offset:20480
	ds_read_b128 v[218:221], v160 offset:21504
	ds_read_b128 v[222:225], v160 offset:22528
	ds_read_b128 v[230:233], v160 offset:23552
	global_load_lds_dwordx4 v[226:227], off
	s_add_i32 m0, s64, 0x2000
	s_add_u32 s64, s42, 0x40000
	v_lshl_add_u64 v[234:235], s[42:43], 0, v[136:137]
	s_addc_u32 s65, s43, 0
	s_add_i32 s66, s59, s50
	global_load_lds_dwordx4 v[234:235], off
	s_mov_b32 m0, s66
	v_cndmask_b32_e32 v132, v130, v164, vcc
	global_load_lds_dwordx4 v134, s[64:65]
	s_add_i32 m0, s66, 0x2000
	v_lshl_add_u64 v[238:239], s[44:45], 0, v[132:133]
	global_load_lds_dwordx4 v136, s[64:65]
	s_mov_b32 m0, s37
	v_cndmask_b32_e32 v236, v144, v163, vcc
	global_load_lds_dwordx4 v132, s[44:45]
	s_mov_b32 m0, s39
	v_mov_b32_e32 v237, v133
	global_load_lds_dwordx4 v236, s[44:45]
	s_waitcnt vmcnt(8)
	s_waitcnt lgkmcnt(0)
	v_lshl_add_u64 v[236:237], s[44:45], 0, v[236:237]
	s_barrier
	s_setprio 3
	s_waitcnt lgkmcnt(0)
	v_mfma_f32_16x16x32_bf16 v[62:65], v[166:169], v[198:201], v[62:65]
	v_mfma_f32_16x16x32_bf16 v[58:61], v[174:177], v[198:201], v[58:61]
	v_mfma_f32_16x16x32_bf16 v[38:41], v[166:169], v[206:209], v[38:41]
	v_mfma_f32_16x16x32_bf16 v[34:37], v[174:177], v[206:209], v[34:37]
	v_mfma_f32_16x16x32_bf16 v[22:25], v[166:169], v[214:217], v[22:25]
	v_mfma_f32_16x16x32_bf16 v[18:21], v[174:177], v[214:217], v[18:21]
	v_mfma_f32_16x16x32_bf16 v[6:9], v[166:169], v[222:225], v[6:9]
	v_mfma_f32_16x16x32_bf16 v[2:5], v[174:177], v[222:225], v[2:5]
	v_mfma_f32_16x16x32_bf16 v[62:65], v[170:173], v[202:205], v[62:65]
	v_mfma_f32_16x16x32_bf16 v[58:61], v[178:181], v[202:205], v[58:61]
	v_mfma_f32_16x16x32_bf16 v[38:41], v[170:173], v[210:213], v[38:41]
	v_mfma_f32_16x16x32_bf16 v[34:37], v[178:181], v[210:213], v[34:37]
	v_mfma_f32_16x16x32_bf16 v[22:25], v[170:173], v[218:221], v[22:25]
	v_mfma_f32_16x16x32_bf16 v[18:21], v[178:181], v[218:221], v[18:21]
	v_mfma_f32_16x16x32_bf16 v[6:9], v[170:173], v[230:233], v[6:9]
	v_mfma_f32_16x16x32_bf16 v[2:5], v[178:181], v[230:233], v[2:5]
	v_mfma_f32_16x16x32_bf16 v[50:53], v[182:185], v[198:201], v[50:53]
	v_mfma_f32_16x16x32_bf16 v[42:45], v[190:193], v[198:201], v[42:45]
	v_mfma_f32_16x16x32_bf16 v[54:57], v[182:185], v[206:209], v[54:57]
	v_mfma_f32_16x16x32_bf16 v[46:49], v[190:193], v[206:209], v[46:49]
	v_mfma_f32_16x16x32_bf16 v[30:33], v[182:185], v[214:217], v[30:33]
	v_mfma_f32_16x16x32_bf16 v[26:29], v[190:193], v[214:217], v[26:29]
	v_mfma_f32_16x16x32_bf16 v[14:17], v[182:185], v[222:225], v[14:17]
	v_mfma_f32_16x16x32_bf16 v[10:13], v[190:193], v[222:225], v[10:13]
	v_mfma_f32_16x16x32_bf16 v[50:53], v[186:189], v[202:205], v[50:53]
	v_mfma_f32_16x16x32_bf16 v[42:45], v[194:197], v[202:205], v[42:45]
	v_mfma_f32_16x16x32_bf16 v[54:57], v[186:189], v[210:213], v[54:57]
	v_mfma_f32_16x16x32_bf16 v[46:49], v[194:197], v[210:213], v[46:49]
	v_mfma_f32_16x16x32_bf16 v[30:33], v[186:189], v[218:221], v[30:33]
	v_mfma_f32_16x16x32_bf16 v[26:29], v[194:197], v[218:221], v[26:29]
	v_mfma_f32_16x16x32_bf16 v[14:17], v[186:189], v[230:233], v[14:17]
	v_mfma_f32_16x16x32_bf16 v[10:13], v[194:197], v[230:233], v[10:13]
	s_setprio 0
	s_barrier
; #define PG8_STAGE_A(b, h, ptr, NX) do { if constexpr (Sched::GATHER) { unsigned gs_[2]; gs_[0] = ((NX) && last_) ? gN[h][0] : gA[h][0]; gs_[1] = ((NX) && last_) ? gN[h][1] : gA[h][1]; PG8_STAGE(PG8_SA(b, h), ptr, gs_); } \
;         else PG8_STAGE(PG8_SA(b, h), (ptr) + ((h) ? hstep : (size_t)0), voffA); } while (0)
; #define PG8_STAGE(bufoff, gbase, voff) do { _Pragma("unroll") for (int _i = 0; _i < 2; ++_i) \
;         __builtin_amdgcn_global_load_lds((const unsigned*)((const char*)(gbase) + (voff)[_i]), (PG8_LAS unsigned*)(lds + (bufoff) + ldsw + _i * 8192), 16, 0, 0); } while (0)
; #define PG8_LDA(dst, b, h) do { _Pragma("unroll") for (int m = 0; m < 4; ++m) _Pragma("unroll") for (int k = 0; k < 2; ++k) dst[m][k] = *(const PG8_LAS bf16x8*)(lds + PG8_SA(b, h) + aoff + m * 2048 + k * 1024); } while (0)
; #define PG8_LDB(dst, b, h) do { _Pragma("unroll") for (int n = 0; n < 2; ++n) _Pragma("unroll") for (int k = 0; k < 2; ++k) dst[n][k] = *(const PG8_LAS bf16x8*)(lds + PG8_SB(b, h) + boff + n * 2048 + k * 1024); } while (0)
; #define PG8_MMA(ai, bj, At, Bt) do { __builtin_amdgcn_s_setprio(1); _Pragma("unroll") for (int m = 0; m < 4; ++m) _Pragma("unroll") for (int n = 0; n < 2; ++n) _Pragma("unroll") for (int k = 0; k < 2; ++k) \
;         acc[ai][bj][m][n] = __builtin_amdgcn_mfma_f32_16x16x32_bf16(Bt[n][k], At[m][k], acc[ai][bj][m][n], 0, 0, 0); __builtin_amdgcn_s_setprio(0); } while (0)
; #define PG8_WAIT_V(n) asm volatile("s_waitcnt vmcnt(" #n ")" ::: "memory")
; #define PG8_WAIT_L(n) asm volatile("s_waitcnt lgkmcnt(" #n ")" ::: "memory")
; #define PG8_BAR __builtin_amdgcn_s_barrier()
; template <class Epi, class Sched, bool ALIGN_EPI = false, bool SP2 = false>
; __device__ __forceinline__ void gemm_phase(PG8_LAS unsigned char* lds, const Gemm g, const Sched& S, const Epi& E, const bool skip_epi = false) {
;     ...
;             PG8_LDB(B0, 1, 0); PG8_LDB(B1, 1, 1); PG8_SCHED; PG8_LDA(At, 1, 0); PG8_STAGE_A(0, 1, a2, true);
;             PG8_WAIT_V(8); PG8_WAIT_L(0); PG8_BAR; PG8_MMA(0, 0, At, B0); PG8_MMA(0, 1, At, B1); PG8_BAR; PG8_SCHED;
;             PG8_LDA(At, 1, 1); PG8_STAGE(PG8_SB(1, 0), b3, voffB); PG8_STAGE(PG8_SB(1, 1), b3 + hstep, voffB); PG8_STAGE_A(1, 0, a3, true);
;             PG8_WAIT_V(8); PG8_WAIT_L(0); PG8_BAR; PG8_MMA(1, 0, At, B0); PG8_MMA(1, 1, At, B1); PG8_BAR; PG8_SCHED;
;     ...
;         if constexpr (ALIGN_EPI) { if (wr == 0) PG8_BAR; }
	s_add_i32 s64, 0, 0x18000
	v_add_u32_e32 v132, s64, v154
	s_add_i32 s65, 0, 0x1c000
	ds_read_b128 v[166:169], v132
	ds_read_b128 v[170:173], v132 offset:1024
	ds_read_b128 v[174:177], v132 offset:2048
	ds_read_b128 v[178:181], v132 offset:3072
	v_add_u32_e32 v132, s65, v154
	ds_read_b128 v[182:185], v132
	ds_read_b128 v[186:189], v132 offset:1024
	ds_read_b128 v[190:193], v132 offset:2048
	ds_read_b128 v[194:197], v132 offset:3072
	s_mov_b32 m0, s51
	v_cndmask_b32_e32 v132, v142, v162, vcc
	ds_read_b128 v[198:201], v160 offset:32768
	ds_read_b128 v[202:205], v160 offset:33792
	ds_read_b128 v[206:209], v160 offset:34816
	ds_read_b128 v[210:213], v160 offset:35840
	ds_read_b128 v[214:217], v160 offset:36864
	ds_read_b128 v[218:221], v160 offset:37888
	ds_read_b128 v[222:225], v160 offset:38912
	ds_read_b128 v[230:233], v160 offset:39936
	v_cndmask_b32_e32 v141, v140, v161, vcc
	global_load_lds_dwordx4 v132, s[44:45]
	s_mov_b32 m0, s52
	s_nop 0
	global_load_lds_dwordx4 v141, s[44:45]
	s_waitcnt vmcnt(8)
	s_waitcnt lgkmcnt(0)
	s_barrier
	s_setprio 3
	s_waitcnt lgkmcnt(0)
	v_mfma_f32_16x16x32_bf16 v[126:129], v[166:169], v[198:201], v[126:129]
	v_mfma_f32_16x16x32_bf16 v[122:125], v[174:177], v[198:201], v[122:125]
	v_mfma_f32_16x16x32_bf16 v[110:113], v[166:169], v[206:209], v[110:113]
	v_mfma_f32_16x16x32_bf16 v[106:109], v[174:177], v[206:209], v[106:109]
	v_mfma_f32_16x16x32_bf16 v[94:97], v[166:169], v[214:217], v[94:97]
	v_mfma_f32_16x16x32_bf16 v[90:93], v[174:177], v[214:217], v[90:93]
	v_mfma_f32_16x16x32_bf16 v[78:81], v[166:169], v[222:225], v[78:81]
	v_mfma_f32_16x16x32_bf16 v[74:77], v[174:177], v[222:225], v[74:77]
	v_mfma_f32_16x16x32_bf16 v[126:129], v[170:173], v[202:205], v[126:129]
	v_mfma_f32_16x16x32_bf16 v[122:125], v[178:181], v[202:205], v[122:125]
	v_mfma_f32_16x16x32_bf16 v[110:113], v[170:173], v[210:213], v[110:113]
	v_mfma_f32_16x16x32_bf16 v[106:109], v[178:181], v[210:213], v[106:109]
	v_mfma_f32_16x16x32_bf16 v[94:97], v[170:173], v[218:221], v[94:97]
	v_mfma_f32_16x16x32_bf16 v[90:93], v[178:181], v[218:221], v[90:93]
	v_mfma_f32_16x16x32_bf16 v[78:81], v[170:173], v[230:233], v[78:81]
	v_mfma_f32_16x16x32_bf16 v[74:77], v[178:181], v[230:233], v[74:77]
	v_mfma_f32_16x16x32_bf16 v[118:121], v[182:185], v[198:201], v[118:121]
	v_mfma_f32_16x16x32_bf16 v[114:117], v[190:193], v[198:201], v[114:117]
	v_mfma_f32_16x16x32_bf16 v[102:105], v[182:185], v[206:209], v[102:105]
	v_mfma_f32_16x16x32_bf16 v[98:101], v[190:193], v[206:209], v[98:101]
	v_mfma_f32_16x16x32_bf16 v[86:89], v[182:185], v[214:217], v[86:89]
	v_mfma_f32_16x16x32_bf16 v[82:85], v[190:193], v[214:217], v[82:85]
	v_mfma_f32_16x16x32_bf16 v[70:73], v[182:185], v[222:225], v[70:73]
	v_mfma_f32_16x16x32_bf16 v[66:69], v[190:193], v[222:225], v[66:69]
	v_mfma_f32_16x16x32_bf16 v[118:121], v[186:189], v[202:205], v[118:121]
	v_mfma_f32_16x16x32_bf16 v[114:117], v[194:197], v[202:205], v[114:117]
	v_mfma_f32_16x16x32_bf16 v[102:105], v[186:189], v[210:213], v[102:105]
	v_mfma_f32_16x16x32_bf16 v[98:101], v[194:197], v[210:213], v[98:101]
	v_mfma_f32_16x16x32_bf16 v[86:89], v[186:189], v[218:221], v[86:89]
	v_mfma_f32_16x16x32_bf16 v[82:85], v[194:197], v[218:221], v[82:85]
	v_mfma_f32_16x16x32_bf16 v[70:73], v[186:189], v[230:233], v[70:73]
	v_mfma_f32_16x16x32_bf16 v[66:69], v[194:197], v[230:233], v[66:69]
	s_setprio 0
	s_barrier
	s_add_i32 s44, s64, s50
	s_add_i32 m0, s44, 0xffffff80
	ds_read_b128 v[198:201], v160 offset:49152
	ds_read_b128 v[202:205], v160 offset:50176
	ds_read_b128 v[206:209], v160 offset:51200
	ds_read_b128 v[210:213], v160 offset:52224
	ds_read_b128 v[214:217], v160 offset:53248
	ds_read_b128 v[218:221], v160 offset:54272
	ds_read_b128 v[222:225], v160 offset:55296
	ds_read_b128 v[230:233], v160 offset:56320
	global_load_lds_dwordx4 v[226:227], off offset:128
	s_add_i32 m0, s44, 0x1f80
	s_add_u32 s42, s42, 0x40080
	s_addc_u32 s43, s43, 0
	s_add_i32 s44, s65, s50
	global_load_lds_dwordx4 v[234:235], off offset:128
	s_mov_b32 m0, s44
	s_nop 0
	global_load_lds_dwordx4 v134, s[42:43]
	s_add_i32 m0, s44, 0x2000
	s_nop 0
	global_load_lds_dwordx4 v136, s[42:43]
	s_add_i32 m0, s55, 0xffffff80
	s_nop 0
	global_load_lds_dwordx4 v[238:239], off offset:128
	s_add_i32 m0, s56, 0xffffff80
	s_nop 0
	global_load_lds_dwordx4 v[236:237], off offset:128
	s_waitcnt vmcnt(8)
	s_waitcnt lgkmcnt(0)
	s_barrier
	s_setprio 3
	s_waitcnt lgkmcnt(0)
	v_mfma_f32_16x16x32_bf16 v[62:65], v[166:169], v[198:201], v[62:65]
	v_mfma_f32_16x16x32_bf16 v[58:61], v[174:177], v[198:201], v[58:61]
	v_mfma_f32_16x16x32_bf16 v[38:41], v[166:169], v[206:209], v[38:41]
	v_mfma_f32_16x16x32_bf16 v[34:37], v[174:177], v[206:209], v[34:37]
	v_mfma_f32_16x16x32_bf16 v[22:25], v[166:169], v[214:217], v[22:25]
	v_mfma_f32_16x16x32_bf16 v[18:21], v[174:177], v[214:217], v[18:21]
	v_mfma_f32_16x16x32_bf16 v[6:9], v[166:169], v[222:225], v[6:9]
	v_mfma_f32_16x16x32_bf16 v[2:5], v[174:177], v[222:225], v[2:5]
	v_mfma_f32_16x16x32_bf16 v[62:65], v[170:173], v[202:205], v[62:65]
	v_mfma_f32_16x16x32_bf16 v[58:61], v[178:181], v[202:205], v[58:61]
	v_mfma_f32_16x16x32_bf16 v[38:41], v[170:173], v[210:213], v[38:41]
	v_mfma_f32_16x16x32_bf16 v[34:37], v[178:181], v[210:213], v[34:37]
	v_mfma_f32_16x16x32_bf16 v[22:25], v[170:173], v[218:221], v[22:25]
	v_mfma_f32_16x16x32_bf16 v[18:21], v[178:181], v[218:221], v[18:21]
	v_mfma_f32_16x16x32_bf16 v[6:9], v[170:173], v[230:233], v[6:9]
	v_mfma_f32_16x16x32_bf16 v[2:5], v[178:181], v[230:233], v[2:5]
	v_mfma_f32_16x16x32_bf16 v[50:53], v[182:185], v[198:201], v[50:53]
	v_mfma_f32_16x16x32_bf16 v[42:45], v[190:193], v[198:201], v[42:45]
	v_mfma_f32_16x16x32_bf16 v[54:57], v[182:185], v[206:209], v[54:57]
	v_mfma_f32_16x16x32_bf16 v[46:49], v[190:193], v[206:209], v[46:49]
	v_mfma_f32_16x16x32_bf16 v[30:33], v[182:185], v[214:217], v[30:33]
	v_mfma_f32_16x16x32_bf16 v[26:29], v[190:193], v[214:217], v[26:29]
	v_mfma_f32_16x16x32_bf16 v[14:17], v[182:185], v[222:225], v[14:17]
	v_mfma_f32_16x16x32_bf16 v[10:13], v[190:193], v[222:225], v[10:13]
	v_mfma_f32_16x16x32_bf16 v[50:53], v[186:189], v[202:205], v[50:53]
	v_mfma_f32_16x16x32_bf16 v[42:45], v[194:197], v[202:205], v[42:45]
	v_mfma_f32_16x16x32_bf16 v[54:57], v[186:189], v[210:213], v[54:57]
	v_mfma_f32_16x16x32_bf16 v[46:49], v[194:197], v[210:213], v[46:49]
	v_mfma_f32_16x16x32_bf16 v[30:33], v[186:189], v[218:221], v[30:33]
	v_mfma_f32_16x16x32_bf16 v[26:29], v[194:197], v[218:221], v[26:29]
	v_mfma_f32_16x16x32_bf16 v[14:17], v[186:189], v[230:233], v[14:17]
	v_mfma_f32_16x16x32_bf16 v[10:13], v[194:197], v[230:233], v[10:13]
	s_setprio 0
	s_barrier
	s_add_i32 s63, s63, 2
	s_add_u32 s40, s40, 0x100
	s_addc_u32 s41, s41, 0
	s_cmp_gt_u32 s63, 13
	s_cbranch_scc0 .LBB0_1728
	s_and_b64 vcc, exec, s[26:27]
	s_cbranch_vccz .LBB0_1731
	s_barrier

; #define PG8_STAGE_A(b, h, ptr, NX) do { if constexpr (Sched::GATHER) { unsigned gs_[2]; gs_[0] = ((NX) && last_) ? gN[h][0] : gA[h][0]; gs_[1] = ((NX) && last_) ? gN[h][1] : gA[h][1]; PG8_STAGE(PG8_SA(b, h), ptr, gs_); } \
;         else PG8_STAGE(PG8_SA(b, h), (ptr) + ((h) ? hstep : (size_t)0), voffA); } while (0)
; #define PG8_STAGE(bufoff, gbase, voff) do { _Pragma("unroll") for (int _i = 0; _i < 2; ++_i) \
;         __builtin_amdgcn_global_load_lds((const unsigned*)((const char*)(gbase) + (voff)[_i]), (PG8_LAS unsigned*)(lds + (bufoff) + ldsw + _i * 8192), 16, 0, 0); } while (0)
; #define PG8_LDA(dst, b, h) do { _Pragma("unroll") for (int m = 0; m < 4; ++m) _Pragma("unroll") for (int k = 0; k < 2; ++k) dst[m][k] = *(const PG8_LAS bf16x8*)(lds + PG8_SA(b, h) + aoff + m * 2048 + k * 1024); } while (0)
; #define PG8_LDB(dst, b, h) do { _Pragma("unroll") for (int n = 0; n < 2; ++n) _Pragma("unroll") for (int k = 0; k < 2; ++k) dst[n][k] = *(const PG8_LAS bf16x8*)(lds + PG8_SB(b, h) + boff + n * 2048 + k * 1024); } while (0)
; #define PG8_MMA(ai, bj, At, Bt) do { __builtin_amdgcn_s_setprio(1); _Pragma("unroll") for (int m = 0; m < 4; ++m) _Pragma("unroll") for (int n = 0; n < 2; ++n) _Pragma("unroll") for (int k = 0; k < 2; ++k) \
;         acc[ai][bj][m][n] = __builtin_amdgcn_mfma_f32_16x16x32_bf16(Bt[n][k], At[m][k], acc[ai][bj][m][n], 0, 0, 0); __builtin_amdgcn_s_setprio(0); } while (0)
; #define PG8_WAIT_V(n) asm volatile("s_waitcnt vmcnt(" #n ")" ::: "memory")
; #define PG8_WAIT_L(n) asm volatile("s_waitcnt lgkmcnt(" #n ")" ::: "memory")
; #define PG8_BAR __builtin_amdgcn_s_barrier()
; #define PG8_SCHED __builtin_amdgcn_sched_barrier(0)
; template <class Epi, class Sched, bool ALIGN_EPI = false, bool SP2 = false>
; __device__ __forceinline__ void gemm_phase(PG8_LAS unsigned char* lds, const Gemm g, const Sched& S, const Epi& E, const bool skip_epi = false) {
;     ...
;             PG8_LDB(B0, 0, 0); PG8_LDB(B1, 0, 1); PG8_SCHED; PG8_LDA(At, 0, 0); PG8_STAGE_A(1, 1, a1, false);
;             PG8_WAIT_V(8); PG8_WAIT_L(0); PG8_BAR; PG8_MMA(0, 0, At, B0); PG8_MMA(0, 1, At, B1); PG8_BAR; PG8_SCHED;
;             PG8_LDA(At, 0, 1); PG8_STAGE(PG8_SB(0, 0), b2, voffB); PG8_STAGE(PG8_SB(0, 1), b2 + hstep, voffB); PG8_STAGE_A(0, 0, a2, true);
;             PG8_WAIT_V(8); PG8_WAIT_L(0); PG8_BAR; PG8_MMA(1, 0, At, B0); PG8_MMA(1, 1, At, B1); PG8_BAR; PG8_SCHED;
.LBB0_1822:
	s_add_u32 s67, s40, 0x100
	s_addc_u32 s68, s41, 0
	s_mov_b32 s69, -2
	ds_read_b128 v[160:163], v157
	ds_read_b128 v[164:167], v157 offset:1024
	ds_read_b128 v[168:171], v157 offset:2048
	ds_read_b128 v[172:175], v157 offset:3072
	ds_read_b128 v[176:179], v158
	ds_read_b128 v[180:183], v158 offset:1024
	ds_read_b128 v[184:187], v158 offset:2048
	ds_read_b128 v[188:191], v158 offset:3072
	s_add_u32 s40, s38, 0x100
	s_addc_u32 s41, s39, 0
	s_cmp_eq_u32 s69, 52
	s_cselect_b32 s45, s7, s41
	s_cselect_b32 s44, s6, s40
	s_cselect_b32 s43, s35, s68
	s_cselect_b32 s42, s34, s67
	v_lshl_add_u64 v[152:153], s[38:39], 0, v[140:141]
	s_add_i32 m0, s37, 0xc000
	ds_read_b128 v[192:195], v159
	ds_read_b128 v[196:199], v159 offset:1024
	ds_read_b128 v[200:203], v159 offset:2048
	ds_read_b128 v[204:207], v159 offset:3072
	ds_read_b128 v[208:211], v159 offset:4096
	ds_read_b128 v[212:215], v159 offset:5120
	ds_read_b128 v[216:219], v159 offset:6144
	ds_read_b128 v[220:223], v159 offset:7168
	global_load_lds_dwordx4 v[152:153], off
	v_lshl_add_u64 v[152:153], s[38:39], 0, v[142:143]
	s_add_i32 m0, s37, 0xe000
	s_nop 0
	global_load_lds_dwordx4 v[152:153], off
	s_waitcnt vmcnt(8)
	s_waitcnt lgkmcnt(0)
	s_barrier
	s_setprio 3
	s_waitcnt lgkmcnt(0)
	v_mfma_f32_16x16x32_bf16 v[126:129], v[160:163], v[192:195], 0
	v_mfma_f32_16x16x32_bf16 v[122:125], v[168:171], v[192:195], 0
	v_mfma_f32_16x16x32_bf16 v[118:121], v[160:163], v[200:203], 0
	v_mfma_f32_16x16x32_bf16 v[114:117], v[168:171], v[200:203], 0
	v_mfma_f32_16x16x32_bf16 v[106:109], v[160:163], v[208:211], 0
	v_mfma_f32_16x16x32_bf16 v[98:101], v[168:171], v[208:211], 0
	v_mfma_f32_16x16x32_bf16 v[78:81], v[160:163], v[216:219], 0
	v_mfma_f32_16x16x32_bf16 v[74:77], v[168:171], v[216:219], 0
	v_mfma_f32_16x16x32_bf16 v[126:129], v[164:167], v[196:199], v[126:129]
	v_mfma_f32_16x16x32_bf16 v[122:125], v[172:175], v[196:199], v[122:125]
	v_mfma_f32_16x16x32_bf16 v[118:121], v[164:167], v[204:207], v[118:121]
	v_mfma_f32_16x16x32_bf16 v[114:117], v[172:175], v[204:207], v[114:117]
	v_mfma_f32_16x16x32_bf16 v[106:109], v[164:167], v[212:215], v[106:109]
	v_mfma_f32_16x16x32_bf16 v[98:101], v[172:175], v[212:215], v[98:101]
	v_mfma_f32_16x16x32_bf16 v[78:81], v[164:167], v[220:223], v[78:81]
	v_mfma_f32_16x16x32_bf16 v[74:77], v[172:175], v[220:223], v[74:77]
	v_mfma_f32_16x16x32_bf16 v[110:113], v[176:179], v[192:195], 0
	v_mfma_f32_16x16x32_bf16 v[102:105], v[184:187], v[192:195], 0
	v_mfma_f32_16x16x32_bf16 v[94:97], v[176:179], v[200:203], 0
	v_mfma_f32_16x16x32_bf16 v[90:93], v[184:187], v[200:203], 0
	v_mfma_f32_16x16x32_bf16 v[86:89], v[176:179], v[208:211], 0
	v_mfma_f32_16x16x32_bf16 v[82:85], v[184:187], v[208:211], 0
	v_mfma_f32_16x16x32_bf16 v[70:73], v[176:179], v[216:219], 0
	v_mfma_f32_16x16x32_bf16 v[66:69], v[184:187], v[216:219], 0
	v_mfma_f32_16x16x32_bf16 v[110:113], v[180:183], v[196:199], v[110:113]
	v_mfma_f32_16x16x32_bf16 v[102:105], v[188:191], v[196:199], v[102:105]
	v_mfma_f32_16x16x32_bf16 v[94:97], v[180:183], v[204:207], v[94:97]
	v_mfma_f32_16x16x32_bf16 v[90:93], v[188:191], v[204:207], v[90:93]
	v_mfma_f32_16x16x32_bf16 v[86:89], v[180:183], v[212:215], v[86:89]
	v_mfma_f32_16x16x32_bf16 v[82:85], v[188:191], v[212:215], v[82:85]
	v_mfma_f32_16x16x32_bf16 v[70:73], v[180:183], v[220:223], v[70:73]
	v_mfma_f32_16x16x32_bf16 v[66:69], v[188:191], v[220:223], v[66:69]
	s_setprio 0
	s_barrier
	s_add_i32 s38, s60, s51
	v_lshl_add_u64 v[152:153], s[42:43], 0, v[134:135]
	s_mov_b32 m0, s38
	ds_read_b128 v[192:195], v159 offset:16384
	ds_read_b128 v[196:199], v159 offset:17408
	ds_read_b128 v[200:203], v159 offset:18432
	ds_read_b128 v[204:207], v159 offset:19456
	ds_read_b128 v[208:211], v159 offset:20480
	ds_read_b128 v[212:215], v159 offset:21504
	ds_read_b128 v[216:219], v159 offset:22528
	ds_read_b128 v[220:223], v159 offset:23552
	global_load_lds_dwordx4 v[152:153], off
	s_add_i32 m0, s38, 0x2000
	s_add_u32 s38, s42, 0xe0000
	v_lshl_add_u64 v[224:225], s[42:43], 0, v[138:139]
	s_addc_u32 s39, s43, 0
	s_add_i32 s70, s61, s51
	global_load_lds_dwordx4 v[224:225], off
	s_mov_b32 m0, s70
	v_lshl_add_u64 v[230:231], s[44:45], 0, v[136:137]
	global_load_lds_dwordx4 v134, s[38:39]
	s_add_i32 m0, s70, 0x2000
	s_nop 0
	global_load_lds_dwordx4 v138, s[38:39]
	v_lshl_add_u64 v[226:227], s[44:45], 0, v[132:133]
	s_mov_b32 m0, s37
	s_nop 0
	global_load_lds_dwordx4 v[226:227], off
	s_mov_b32 m0, s52
	s_nop 0
	global_load_lds_dwordx4 v[230:231], off
	s_waitcnt vmcnt(8)
	s_waitcnt lgkmcnt(0)
	s_barrier
	s_setprio 3
	s_waitcnt lgkmcnt(0)
	v_mfma_f32_16x16x32_bf16 v[62:65], v[160:163], v[192:195], 0
	v_mfma_f32_16x16x32_bf16 v[58:61], v[168:171], v[192:195], 0
	v_mfma_f32_16x16x32_bf16 v[50:53], v[160:163], v[200:203], 0
	v_mfma_f32_16x16x32_bf16 v[42:45], v[168:171], v[200:203], 0
	v_mfma_f32_16x16x32_bf16 v[34:37], v[160:163], v[208:211], 0
	v_mfma_f32_16x16x32_bf16 v[26:29], v[168:171], v[208:211], 0
	v_mfma_f32_16x16x32_bf16 v[18:21], v[160:163], v[216:219], 0
	v_mfma_f32_16x16x32_bf16 v[10:13], v[168:171], v[216:219], 0
	v_mfma_f32_16x16x32_bf16 v[62:65], v[164:167], v[196:199], v[62:65]
	v_mfma_f32_16x16x32_bf16 v[58:61], v[172:175], v[196:199], v[58:61]
	v_mfma_f32_16x16x32_bf16 v[50:53], v[164:167], v[204:207], v[50:53]
	v_mfma_f32_16x16x32_bf16 v[42:45], v[172:175], v[204:207], v[42:45]
	v_mfma_f32_16x16x32_bf16 v[34:37], v[164:167], v[212:215], v[34:37]
	v_mfma_f32_16x16x32_bf16 v[26:29], v[172:175], v[212:215], v[26:29]
	v_mfma_f32_16x16x32_bf16 v[18:21], v[164:167], v[220:223], v[18:21]
	v_mfma_f32_16x16x32_bf16 v[10:13], v[172:175], v[220:223], v[10:13]
	v_mfma_f32_16x16x32_bf16 v[54:57], v[176:179], v[192:195], 0
	v_mfma_f32_16x16x32_bf16 v[46:49], v[184:187], v[192:195], 0
	v_mfma_f32_16x16x32_bf16 v[38:41], v[176:179], v[200:203], 0
	v_mfma_f32_16x16x32_bf16 v[30:33], v[184:187], v[200:203], 0
	v_mfma_f32_16x16x32_bf16 v[22:25], v[176:179], v[208:211], 0
	v_mfma_f32_16x16x32_bf16 v[14:17], v[184:187], v[208:211], 0
	v_mfma_f32_16x16x32_bf16 v[6:9], v[176:179], v[216:219], 0
	v_mfma_f32_16x16x32_bf16 v[2:5], v[184:187], v[216:219], 0
	v_mfma_f32_16x16x32_bf16 v[54:57], v[180:183], v[196:199], v[54:57]
	v_mfma_f32_16x16x32_bf16 v[46:49], v[188:191], v[196:199], v[46:49]
	v_mfma_f32_16x16x32_bf16 v[38:41], v[180:183], v[204:207], v[38:41]
	v_mfma_f32_16x16x32_bf16 v[30:33], v[188:191], v[204:207], v[30:33]
	v_mfma_f32_16x16x32_bf16 v[22:25], v[180:183], v[212:215], v[22:25]
	v_mfma_f32_16x16x32_bf16 v[14:17], v[188:191], v[212:215], v[14:17]
	v_mfma_f32_16x16x32_bf16 v[6:9], v[180:183], v[220:223], v[6:9]
	v_mfma_f32_16x16x32_bf16 v[2:5], v[188:191], v[220:223], v[2:5]
	s_setprio 0
	s_barrier
; #define PG8_STAGE_A(b, h, ptr, NX) do { if constexpr (Sched::GATHER) { unsigned gs_[2]; gs_[0] = ((NX) && last_) ? gN[h][0] : gA[h][0]; gs_[1] = ((NX) && last_) ? gN[h][1] : gA[h][1]; PG8_STAGE(PG8_SA(b, h), ptr, gs_); } \
;         else PG8_STAGE(PG8_SA(b, h), (ptr) + ((h) ? hstep : (size_t)0), voffA); } while (0)
; #define PG8_STAGE(bufoff, gbase, voff) do { _Pragma("unroll") for (int _i = 0; _i < 2; ++_i) \
;         __builtin_amdgcn_global_load_lds((const unsigned*)((const char*)(gbase) + (voff)[_i]), (PG8_LAS unsigned*)(lds + (bufoff) + ldsw + _i * 8192), 16, 0, 0); } while (0)
; #define PG8_LDA(dst, b, h) do { _Pragma("unroll") for (int m = 0; m < 4; ++m) _Pragma("unroll") for (int k = 0; k < 2; ++k) dst[m][k] = *(const PG8_LAS bf16x8*)(lds + PG8_SA(b, h) + aoff + m * 2048 + k * 1024); } while (0)
; #define PG8_LDB(dst, b, h) do { _Pragma("unroll") for (int n = 0; n < 2; ++n) _Pragma("unroll") for (int k = 0; k < 2; ++k) dst[n][k] = *(const PG8_LAS bf16x8*)(lds + PG8_SB(b, h) + boff + n * 2048 + k * 1024); } while (0)
; #define PG8_MMA(ai, bj, At, Bt) do { __builtin_amdgcn_s_setprio(1); _Pragma("unroll") for (int m = 0; m < 4; ++m) _Pragma("unroll") for (int n = 0; n < 2; ++n) _Pragma("unroll") for (int k = 0; k < 2; ++k) \
;         acc[ai][bj][m][n] = __builtin_amdgcn_mfma_f32_16x16x32_bf16(Bt[n][k], At[m][k], acc[ai][bj][m][n], 0, 0, 0); __builtin_amdgcn_s_setprio(0); } while (0)
; #define PG8_WAIT_V(n) asm volatile("s_waitcnt vmcnt(" #n ")" ::: "memory")
; #define PG8_WAIT_L(n) asm volatile("s_waitcnt lgkmcnt(" #n ")" ::: "memory")
; #define PG8_BAR __builtin_amdgcn_s_barrier()
; #define PG8_SCHED __builtin_amdgcn_sched_barrier(0)
; template <class Epi, class Sched, bool ALIGN_EPI = false, bool SP2 = false>
; __device__ __forceinline__ void gemm_phase(PG8_LAS unsigned char* lds, const Gemm g, const Sched& S, const Epi& E, const bool skip_epi = false) {
;     ...
;             PG8_LDB(B0, 1, 0); PG8_LDB(B1, 1, 1); PG8_SCHED; PG8_LDA(At, 1, 0); PG8_STAGE_A(0, 1, a2, true);
;             PG8_WAIT_V(8); PG8_WAIT_L(0); PG8_BAR; PG8_MMA(0, 0, At, B0); PG8_MMA(0, 1, At, B1); PG8_BAR; PG8_SCHED;
;             PG8_LDA(At, 1, 1); PG8_STAGE(PG8_SB(1, 0), b3, voffB); PG8_STAGE(PG8_SB(1, 1), b3 + hstep, voffB); PG8_STAGE_A(1, 0, a3, true);
;             PG8_WAIT_V(8); PG8_WAIT_L(0); PG8_BAR; PG8_MMA(1, 0, At, B0); PG8_MMA(1, 1, At, B1); PG8_BAR; PG8_SCHED;
	s_add_i32 s70, 0, 0x18000
	v_add_u32_e32 v130, s70, v147
	s_add_i32 s71, 0, 0x1c000
	ds_read_b128 v[160:163], v130
	ds_read_b128 v[164:167], v130 offset:1024
	ds_read_b128 v[168:171], v130 offset:2048
	ds_read_b128 v[172:175], v130 offset:3072
	v_add_u32_e32 v130, s71, v147
	ds_read_b128 v[176:179], v130
	ds_read_b128 v[180:183], v130 offset:1024
	ds_read_b128 v[184:187], v130 offset:2048
	ds_read_b128 v[188:191], v130 offset:3072
	s_add_u32 s38, s44, 0xe0000
	s_addc_u32 s39, s45, 0
	s_mov_b32 m0, s53
	ds_read_b128 v[192:195], v159 offset:32768
	ds_read_b128 v[196:199], v159 offset:33792
	ds_read_b128 v[200:203], v159 offset:34816
	ds_read_b128 v[204:207], v159 offset:35840
	ds_read_b128 v[208:211], v159 offset:36864
	ds_read_b128 v[212:215], v159 offset:37888
	ds_read_b128 v[216:219], v159 offset:38912
	ds_read_b128 v[220:223], v159 offset:39936
	global_load_lds_dwordx4 v132, s[38:39]
	s_mov_b32 m0, s54
	s_nop 0
	global_load_lds_dwordx4 v136, s[38:39]
	s_waitcnt vmcnt(8)
	s_waitcnt lgkmcnt(0)
	s_barrier
	s_setprio 3
	s_waitcnt lgkmcnt(0)
	v_mfma_f32_16x16x32_bf16 v[126:129], v[160:163], v[192:195], v[126:129]
	v_mfma_f32_16x16x32_bf16 v[122:125], v[168:171], v[192:195], v[122:125]
	v_mfma_f32_16x16x32_bf16 v[118:121], v[160:163], v[200:203], v[118:121]
	v_mfma_f32_16x16x32_bf16 v[114:117], v[168:171], v[200:203], v[114:117]
	v_mfma_f32_16x16x32_bf16 v[106:109], v[160:163], v[208:211], v[106:109]
	v_mfma_f32_16x16x32_bf16 v[98:101], v[168:171], v[208:211], v[98:101]
	v_mfma_f32_16x16x32_bf16 v[78:81], v[160:163], v[216:219], v[78:81]
	v_mfma_f32_16x16x32_bf16 v[74:77], v[168:171], v[216:219], v[74:77]
	v_mfma_f32_16x16x32_bf16 v[126:129], v[164:167], v[196:199], v[126:129]
	v_mfma_f32_16x16x32_bf16 v[122:125], v[172:175], v[196:199], v[122:125]
	v_mfma_f32_16x16x32_bf16 v[118:121], v[164:167], v[204:207], v[118:121]
	v_mfma_f32_16x16x32_bf16 v[114:117], v[172:175], v[204:207], v[114:117]
	v_mfma_f32_16x16x32_bf16 v[106:109], v[164:167], v[212:215], v[106:109]
	v_mfma_f32_16x16x32_bf16 v[98:101], v[172:175], v[212:215], v[98:101]
	v_mfma_f32_16x16x32_bf16 v[78:81], v[164:167], v[220:223], v[78:81]
	v_mfma_f32_16x16x32_bf16 v[74:77], v[172:175], v[220:223], v[74:77]
	v_mfma_f32_16x16x32_bf16 v[110:113], v[176:179], v[192:195], v[110:113]
	v_mfma_f32_16x16x32_bf16 v[102:105], v[184:187], v[192:195], v[102:105]
	v_mfma_f32_16x16x32_bf16 v[94:97], v[176:179], v[200:203], v[94:97]
	v_mfma_f32_16x16x32_bf16 v[90:93], v[184:187], v[200:203], v[90:93]
	v_mfma_f32_16x16x32_bf16 v[86:89], v[176:179], v[208:211], v[86:89]
	v_mfma_f32_16x16x32_bf16 v[82:85], v[184:187], v[208:211], v[82:85]
	v_mfma_f32_16x16x32_bf16 v[70:73], v[176:179], v[216:219], v[70:73]
	v_mfma_f32_16x16x32_bf16 v[66:69], v[184:187], v[216:219], v[66:69]
	v_mfma_f32_16x16x32_bf16 v[110:113], v[180:183], v[196:199], v[110:113]
	v_mfma_f32_16x16x32_bf16 v[102:105], v[188:191], v[196:199], v[102:105]
	v_mfma_f32_16x16x32_bf16 v[94:97], v[180:183], v[204:207], v[94:97]
	v_mfma_f32_16x16x32_bf16 v[90:93], v[188:191], v[204:207], v[90:93]
	v_mfma_f32_16x16x32_bf16 v[86:89], v[180:183], v[212:215], v[86:89]
	v_mfma_f32_16x16x32_bf16 v[82:85], v[188:191], v[212:215], v[82:85]
	v_mfma_f32_16x16x32_bf16 v[70:73], v[180:183], v[220:223], v[70:73]
	v_mfma_f32_16x16x32_bf16 v[66:69], v[188:191], v[220:223], v[66:69]
	s_setprio 0
	s_barrier
	s_add_i32 s38, s70, s51
	s_add_i32 m0, s38, 0xffffff80
	ds_read_b128 v[192:195], v159 offset:49152
	ds_read_b128 v[196:199], v159 offset:50176
	ds_read_b128 v[200:203], v159 offset:51200
	ds_read_b128 v[204:207], v159 offset:52224
	ds_read_b128 v[208:211], v159 offset:53248
	ds_read_b128 v[212:215], v159 offset:54272
	ds_read_b128 v[216:219], v159 offset:55296
	ds_read_b128 v[220:223], v159 offset:56320
	global_load_lds_dwordx4 v[152:153], off offset:128
	s_add_i32 m0, s38, 0x1f80
	s_add_u32 s38, s42, 0xe0080
	s_addc_u32 s39, s43, 0
	s_add_i32 s42, s71, s51
	global_load_lds_dwordx4 v[224:225], off offset:128
	s_mov_b32 m0, s42
	s_nop 0
	global_load_lds_dwordx4 v134, s[38:39]
	s_add_i32 m0, s42, 0x2000
	s_nop 0
	global_load_lds_dwordx4 v138, s[38:39]
	s_add_i32 m0, s57, 0xffffff80
	s_nop 0
	global_load_lds_dwordx4 v[226:227], off offset:128
	s_add_i32 m0, s58, 0xffffff80
	s_nop 0
	global_load_lds_dwordx4 v[230:231], off offset:128
	s_waitcnt vmcnt(8)
	s_waitcnt lgkmcnt(0)
	s_barrier
	s_setprio 3
	s_waitcnt lgkmcnt(0)
	v_mfma_f32_16x16x32_bf16 v[62:65], v[160:163], v[192:195], v[62:65]
	v_mfma_f32_16x16x32_bf16 v[58:61], v[168:171], v[192:195], v[58:61]
	v_mfma_f32_16x16x32_bf16 v[50:53], v[160:163], v[200:203], v[50:53]
	v_mfma_f32_16x16x32_bf16 v[42:45], v[168:171], v[200:203], v[42:45]
	v_mfma_f32_16x16x32_bf16 v[34:37], v[160:163], v[208:211], v[34:37]
	v_mfma_f32_16x16x32_bf16 v[26:29], v[168:171], v[208:211], v[26:29]
	v_mfma_f32_16x16x32_bf16 v[18:21], v[160:163], v[216:219], v[18:21]
	v_mfma_f32_16x16x32_bf16 v[10:13], v[168:171], v[216:219], v[10:13]
	v_mfma_f32_16x16x32_bf16 v[62:65], v[164:167], v[196:199], v[62:65]
	v_mfma_f32_16x16x32_bf16 v[58:61], v[172:175], v[196:199], v[58:61]
	v_mfma_f32_16x16x32_bf16 v[50:53], v[164:167], v[204:207], v[50:53]
	v_mfma_f32_16x16x32_bf16 v[42:45], v[172:175], v[204:207], v[42:45]
	v_mfma_f32_16x16x32_bf16 v[34:37], v[164:167], v[212:215], v[34:37]
	v_mfma_f32_16x16x32_bf16 v[26:29], v[172:175], v[212:215], v[26:29]
	v_mfma_f32_16x16x32_bf16 v[18:21], v[164:167], v[220:223], v[18:21]
	v_mfma_f32_16x16x32_bf16 v[10:13], v[172:175], v[220:223], v[10:13]
	v_mfma_f32_16x16x32_bf16 v[54:57], v[176:179], v[192:195], v[54:57]
	v_mfma_f32_16x16x32_bf16 v[46:49], v[184:187], v[192:195], v[46:49]
	v_mfma_f32_16x16x32_bf16 v[38:41], v[176:179], v[200:203], v[38:41]
	v_mfma_f32_16x16x32_bf16 v[30:33], v[184:187], v[200:203], v[30:33]
	v_mfma_f32_16x16x32_bf16 v[22:25], v[176:179], v[208:211], v[22:25]
	v_mfma_f32_16x16x32_bf16 v[14:17], v[184:187], v[208:211], v[14:17]
	v_mfma_f32_16x16x32_bf16 v[6:9], v[176:179], v[216:219], v[6:9]
	v_mfma_f32_16x16x32_bf16 v[2:5], v[184:187], v[216:219], v[2:5]
	v_mfma_f32_16x16x32_bf16 v[54:57], v[180:183], v[196:199], v[54:57]
	v_mfma_f32_16x16x32_bf16 v[46:49], v[188:191], v[196:199], v[46:49]
	v_mfma_f32_16x16x32_bf16 v[38:41], v[180:183], v[204:207], v[38:41]
	v_mfma_f32_16x16x32_bf16 v[30:33], v[188:191], v[204:207], v[30:33]
	v_mfma_f32_16x16x32_bf16 v[22:25], v[180:183], v[212:215], v[22:25]
	v_mfma_f32_16x16x32_bf16 v[14:17], v[188:191], v[212:215], v[14:17]
	v_mfma_f32_16x16x32_bf16 v[6:9], v[180:183], v[220:223], v[6:9]
	v_mfma_f32_16x16x32_bf16 v[2:5], v[188:191], v[220:223], v[2:5]
	s_setprio 0
	s_barrier
	s_add_i32 s69, s69, 2
	s_add_u32 s67, s67, 0x100
	s_addc_u32 s68, s68, 0
	s_cmp_gt_u32 s69, 53
	s_mov_b64 s[38:39], s[40:41]
; #define PG8_STAGE_A(b, h, ptr, NX) do { if constexpr (Sched::GATHER) { unsigned gs_[2]; gs_[0] = ((NX) && last_) ? gN[h][0] : gA[h][0]; gs_[1] = ((NX) && last_) ? gN[h][1] : gA[h][1]; PG8_STAGE(PG8_SA(b, h), ptr, gs_); } \
;         else PG8_STAGE(PG8_SA(b, h), (ptr) + ((h) ? hstep : (size_t)0), voffA); } while (0)
; #define PG8_STAGE(bufoff, gbase, voff) do { _Pragma("unroll") for (int _i = 0; _i < 2; ++_i) \
;         __builtin_amdgcn_global_load_lds((const unsigned*)((const char*)(gbase) + (voff)[_i]), (PG8_LAS unsigned*)(lds + (bufoff) + ldsw + _i * 8192), 16, 0, 0); } while (0)
; #define PG8_LDA(dst, b, h) do { _Pragma("unroll") for (int m = 0; m < 4; ++m) _Pragma("unroll") for (int k = 0; k < 2; ++k) dst[m][k] = *(const PG8_LAS bf16x8*)(lds + PG8_SA(b, h) + aoff + m * 2048 + k * 1024); } while (0)
; #define PG8_LDB(dst, b, h) do { _Pragma("unroll") for (int n = 0; n < 2; ++n) _Pragma("unroll") for (int k = 0; k < 2; ++k) dst[n][k] = *(const PG8_LAS bf16x8*)(lds + PG8_SB(b, h) + boff + n * 2048 + k * 1024); } while (0)
; #define PG8_MMA(ai, bj, At, Bt) do { __builtin_amdgcn_s_setprio(1); _Pragma("unroll") for (int m = 0; m < 4; ++m) _Pragma("unroll") for (int n = 0; n < 2; ++n) _Pragma("unroll") for (int k = 0; k < 2; ++k) \
;         acc[ai][bj][m][n] = __builtin_amdgcn_mfma_f32_16x16x32_bf16(Bt[n][k], At[m][k], acc[ai][bj][m][n], 0, 0, 0); __builtin_amdgcn_s_setprio(0); } while (0)
; #define PG8_WAIT_V(n) asm volatile("s_waitcnt vmcnt(" #n ")" ::: "memory")
; #define PG8_WAIT_L(n) asm volatile("s_waitcnt lgkmcnt(" #n ")" ::: "memory")
; #define PG8_BAR __builtin_amdgcn_s_barrier()
; #define PG8_SCHED __builtin_amdgcn_sched_barrier(0)
; template <class Epi, class Sched, bool ALIGN_EPI = false, bool SP2 = false>
; __device__ __forceinline__ void gemm_phase(PG8_LAS unsigned char* lds, const Gemm g, const Sched& S, const Epi& E, const bool skip_epi = false) {
;     ...
;             PG8_LDB(B0, 0, 0); PG8_LDB(B1, 0, 1); PG8_SCHED; PG8_LDA(At, 0, 0); PG8_STAGE_A(1, 1, a1, false);
;             PG8_WAIT_V(8); PG8_WAIT_L(0); PG8_BAR; PG8_MMA(0, 0, At, B0); PG8_MMA(0, 1, At, B1); PG8_BAR; PG8_SCHED;
;             PG8_LDA(At, 0, 1); PG8_STAGE(PG8_SB(0, 0), b2, voffB); PG8_STAGE(PG8_SB(0, 1), b2 + hstep, voffB); PG8_STAGE_A(0, 0, a2, true);
.LBB0_1823:
	ds_read_b128 v[160:163], v157
	ds_read_b128 v[164:167], v157 offset:1024
	ds_read_b128 v[168:171], v157 offset:2048
	ds_read_b128 v[172:175], v157 offset:3072
	ds_read_b128 v[176:179], v158
	ds_read_b128 v[180:183], v158 offset:1024
	ds_read_b128 v[184:187], v158 offset:2048
	ds_read_b128 v[188:191], v158 offset:3072
	s_add_u32 s40, s38, 0x100
	s_addc_u32 s41, s39, 0
	s_cmp_eq_u32 s69, 52
	s_cselect_b32 s45, s7, s41
	s_cselect_b32 s44, s6, s40
	s_cselect_b32 s43, s35, s68
	s_cselect_b32 s42, s34, s67
	v_lshl_add_u64 v[152:153], s[38:39], 0, v[140:141]
	s_add_i32 m0, s37, 0xc000
	ds_read_b128 v[192:195], v159
	ds_read_b128 v[196:199], v159 offset:1024
	ds_read_b128 v[200:203], v159 offset:2048
	ds_read_b128 v[204:207], v159 offset:3072
	ds_read_b128 v[208:211], v159 offset:4096
	ds_read_b128 v[212:215], v159 offset:5120
	ds_read_b128 v[216:219], v159 offset:6144
	ds_read_b128 v[220:223], v159 offset:7168
	global_load_lds_dwordx4 v[152:153], off
	v_lshl_add_u64 v[152:153], s[38:39], 0, v[142:143]
	s_add_i32 m0, s37, 0xe000
	s_nop 0
	global_load_lds_dwordx4 v[152:153], off
	s_waitcnt vmcnt(8)
	s_waitcnt lgkmcnt(0)
	s_barrier
	s_setprio 3
	s_waitcnt lgkmcnt(0)
	v_mfma_f32_16x16x32_bf16 v[126:129], v[160:163], v[192:195], v[126:129]
	v_mfma_f32_16x16x32_bf16 v[122:125], v[168:171], v[192:195], v[122:125]
	v_mfma_f32_16x16x32_bf16 v[118:121], v[160:163], v[200:203], v[118:121]
	v_mfma_f32_16x16x32_bf16 v[114:117], v[168:171], v[200:203], v[114:117]
	v_mfma_f32_16x16x32_bf16 v[106:109], v[160:163], v[208:211], v[106:109]
	v_mfma_f32_16x16x32_bf16 v[98:101], v[168:171], v[208:211], v[98:101]
	v_mfma_f32_16x16x32_bf16 v[78:81], v[160:163], v[216:219], v[78:81]
	v_mfma_f32_16x16x32_bf16 v[74:77], v[168:171], v[216:219], v[74:77]
	v_mfma_f32_16x16x32_bf16 v[126:129], v[164:167], v[196:199], v[126:129]
	v_mfma_f32_16x16x32_bf16 v[122:125], v[172:175], v[196:199], v[122:125]
	v_mfma_f32_16x16x32_bf16 v[118:121], v[164:167], v[204:207], v[118:121]
	v_mfma_f32_16x16x32_bf16 v[114:117], v[172:175], v[204:207], v[114:117]
	v_mfma_f32_16x16x32_bf16 v[106:109], v[164:167], v[212:215], v[106:109]
	v_mfma_f32_16x16x32_bf16 v[98:101], v[172:175], v[212:215], v[98:101]
	v_mfma_f32_16x16x32_bf16 v[78:81], v[164:167], v[220:223], v[78:81]
	v_mfma_f32_16x16x32_bf16 v[74:77], v[172:175], v[220:223], v[74:77]
	v_mfma_f32_16x16x32_bf16 v[110:113], v[176:179], v[192:195], v[110:113]
	v_mfma_f32_16x16x32_bf16 v[102:105], v[184:187], v[192:195], v[102:105]
	v_mfma_f32_16x16x32_bf16 v[94:97], v[176:179], v[200:203], v[94:97]
	v_mfma_f32_16x16x32_bf16 v[90:93], v[184:187], v[200:203], v[90:93]
	v_mfma_f32_16x16x32_bf16 v[86:89], v[176:179], v[208:211], v[86:89]
	v_mfma_f32_16x16x32_bf16 v[82:85], v[184:187], v[208:211], v[82:85]
	v_mfma_f32_16x16x32_bf16 v[70:73], v[176:179], v[216:219], v[70:73]
	v_mfma_f32_16x16x32_bf16 v[66:69], v[184:187], v[216:219], v[66:69]
	v_mfma_f32_16x16x32_bf16 v[110:113], v[180:183], v[196:199], v[110:113]
	v_mfma_f32_16x16x32_bf16 v[102:105], v[188:191], v[196:199], v[102:105]
	v_mfma_f32_16x16x32_bf16 v[94:97], v[180:183], v[204:207], v[94:97]
	v_mfma_f32_16x16x32_bf16 v[90:93], v[188:191], v[204:207], v[90:93]
	v_mfma_f32_16x16x32_bf16 v[86:89], v[180:183], v[212:215], v[86:89]
	v_mfma_f32_16x16x32_bf16 v[82:85], v[188:191], v[212:215], v[82:85]
	v_mfma_f32_16x16x32_bf16 v[70:73], v[180:183], v[220:223], v[70:73]
	v_mfma_f32_16x16x32_bf16 v[66:69], v[188:191], v[220:223], v[66:69]
	s_setprio 0
	s_barrier
	s_add_i32 s38, s60, s51
	v_lshl_add_u64 v[152:153], s[42:43], 0, v[134:135]
	s_mov_b32 m0, s38
	ds_read_b128 v[192:195], v159 offset:16384
	ds_read_b128 v[196:199], v159 offset:17408
	ds_read_b128 v[200:203], v159 offset:18432
	ds_read_b128 v[204:207], v159 offset:19456
	ds_read_b128 v[208:211], v159 offset:20480
	ds_read_b128 v[212:215], v159 offset:21504
	ds_read_b128 v[216:219], v159 offset:22528
	ds_read_b128 v[220:223], v159 offset:23552
	global_load_lds_dwordx4 v[152:153], off
	s_add_i32 m0, s38, 0x2000
	s_add_u32 s38, s42, 0xe0000
	v_lshl_add_u64 v[224:225], s[42:43], 0, v[138:139]
	s_addc_u32 s39, s43, 0
	s_add_i32 s70, s61, s51
	global_load_lds_dwordx4 v[224:225], off
	s_mov_b32 m0, s70
	v_lshl_add_u64 v[230:231], s[44:45], 0, v[136:137]
	global_load_lds_dwordx4 v134, s[38:39]
	s_add_i32 m0, s70, 0x2000
	s_nop 0
	global_load_lds_dwordx4 v138, s[38:39]
	v_lshl_add_u64 v[226:227], s[44:45], 0, v[132:133]
	s_mov_b32 m0, s37
	s_nop 0
	global_load_lds_dwordx4 v[226:227], off
	s_mov_b32 m0, s52
	s_nop 0
	global_load_lds_dwordx4 v[230:231], off
	s_waitcnt vmcnt(8)
	s_waitcnt lgkmcnt(0)
	s_barrier
; #define PG8_STAGE_A(b, h, ptr, NX) do { if constexpr (Sched::GATHER) { unsigned gs_[2]; gs_[0] = ((NX) && last_) ? gN[h][0] : gA[h][0]; gs_[1] = ((NX) && last_) ? gN[h][1] : gA[h][1]; PG8_STAGE(PG8_SA(b, h), ptr, gs_); } \
;         else PG8_STAGE(PG8_SA(b, h), (ptr) + ((h) ? hstep : (size_t)0), voffA); } while (0)
; #define PG8_STAGE(bufoff, gbase, voff) do { _Pragma("unroll") for (int _i = 0; _i < 2; ++_i) \
;         __builtin_amdgcn_global_load_lds((const unsigned*)((const char*)(gbase) + (voff)[_i]), (PG8_LAS unsigned*)(lds + (bufoff) + ldsw + _i * 8192), 16, 0, 0); } while (0)
; #define PG8_LDA(dst, b, h) do { _Pragma("unroll") for (int m = 0; m < 4; ++m) _Pragma("unroll") for (int k = 0; k < 2; ++k) dst[m][k] = *(const PG8_LAS bf16x8*)(lds + PG8_SA(b, h) + aoff + m * 2048 + k * 1024); } while (0)
; #define PG8_LDB(dst, b, h) do { _Pragma("unroll") for (int n = 0; n < 2; ++n) _Pragma("unroll") for (int k = 0; k < 2; ++k) dst[n][k] = *(const PG8_LAS bf16x8*)(lds + PG8_SB(b, h) + boff + n * 2048 + k * 1024); } while (0)
; #define PG8_MMA(ai, bj, At, Bt) do { __builtin_amdgcn_s_setprio(1); _Pragma("unroll") for (int m = 0; m < 4; ++m) _Pragma("unroll") for (int n = 0; n < 2; ++n) _Pragma("unroll") for (int k = 0; k < 2; ++k) \
;         acc[ai][bj][m][n] = __builtin_amdgcn_mfma_f32_16x16x32_bf16(Bt[n][k], At[m][k], acc[ai][bj][m][n], 0, 0, 0); __builtin_amdgcn_s_setprio(0); } while (0)
; #define PG8_WAIT_V(n) asm volatile("s_waitcnt vmcnt(" #n ")" ::: "memory")
; #define PG8_WAIT_L(n) asm volatile("s_waitcnt lgkmcnt(" #n ")" ::: "memory")
; #define PG8_BAR __builtin_amdgcn_s_barrier()
; #define PG8_SCHED __builtin_amdgcn_sched_barrier(0)
; template <class Epi, class Sched, bool ALIGN_EPI = false, bool SP2 = false>
; __device__ __forceinline__ void gemm_phase(PG8_LAS unsigned char* lds, const Gemm g, const Sched& S, const Epi& E, const bool skip_epi = false) {
;     ...
;             PG8_LDA(At, 0, 1); PG8_STAGE(PG8_SB(0, 0), b2, voffB); PG8_STAGE(PG8_SB(0, 1), b2 + hstep, voffB); PG8_STAGE_A(0, 0, a2, true);
;             PG8_WAIT_V(8); PG8_WAIT_L(0); PG8_BAR; PG8_MMA(1, 0, At, B0); PG8_MMA(1, 1, At, B1); PG8_BAR; PG8_SCHED;
;             PG8_LDB(B0, 1, 0); PG8_LDB(B1, 1, 1); PG8_SCHED; PG8_LDA(At, 1, 0); PG8_STAGE_A(0, 1, a2, true);
;             PG8_WAIT_V(8); PG8_WAIT_L(0); PG8_BAR; PG8_MMA(0, 0, At, B0); PG8_MMA(0, 1, At, B1); PG8_BAR; PG8_SCHED;
	s_setprio 3
	s_waitcnt lgkmcnt(0)
	v_mfma_f32_16x16x32_bf16 v[62:65], v[160:163], v[192:195], v[62:65]
	v_mfma_f32_16x16x32_bf16 v[58:61], v[168:171], v[192:195], v[58:61]
	v_mfma_f32_16x16x32_bf16 v[50:53], v[160:163], v[200:203], v[50:53]
	v_mfma_f32_16x16x32_bf16 v[42:45], v[168:171], v[200:203], v[42:45]
	v_mfma_f32_16x16x32_bf16 v[34:37], v[160:163], v[208:211], v[34:37]
	v_mfma_f32_16x16x32_bf16 v[26:29], v[168:171], v[208:211], v[26:29]
	v_mfma_f32_16x16x32_bf16 v[18:21], v[160:163], v[216:219], v[18:21]
	v_mfma_f32_16x16x32_bf16 v[10:13], v[168:171], v[216:219], v[10:13]
	v_mfma_f32_16x16x32_bf16 v[62:65], v[164:167], v[196:199], v[62:65]
	v_mfma_f32_16x16x32_bf16 v[58:61], v[172:175], v[196:199], v[58:61]
	v_mfma_f32_16x16x32_bf16 v[50:53], v[164:167], v[204:207], v[50:53]
	v_mfma_f32_16x16x32_bf16 v[42:45], v[172:175], v[204:207], v[42:45]
	v_mfma_f32_16x16x32_bf16 v[34:37], v[164:167], v[212:215], v[34:37]
	v_mfma_f32_16x16x32_bf16 v[26:29], v[172:175], v[212:215], v[26:29]
	v_mfma_f32_16x16x32_bf16 v[18:21], v[164:167], v[220:223], v[18:21]
	v_mfma_f32_16x16x32_bf16 v[10:13], v[172:175], v[220:223], v[10:13]
	v_mfma_f32_16x16x32_bf16 v[54:57], v[176:179], v[192:195], v[54:57]
	v_mfma_f32_16x16x32_bf16 v[46:49], v[184:187], v[192:195], v[46:49]
	v_mfma_f32_16x16x32_bf16 v[38:41], v[176:179], v[200:203], v[38:41]
	v_mfma_f32_16x16x32_bf16 v[30:33], v[184:187], v[200:203], v[30:33]
	v_mfma_f32_16x16x32_bf16 v[22:25], v[176:179], v[208:211], v[22:25]
	v_mfma_f32_16x16x32_bf16 v[14:17], v[184:187], v[208:211], v[14:17]
	v_mfma_f32_16x16x32_bf16 v[6:9], v[176:179], v[216:219], v[6:9]
	v_mfma_f32_16x16x32_bf16 v[2:5], v[184:187], v[216:219], v[2:5]
	v_mfma_f32_16x16x32_bf16 v[54:57], v[180:183], v[196:199], v[54:57]
	v_mfma_f32_16x16x32_bf16 v[46:49], v[188:191], v[196:199], v[46:49]
	v_mfma_f32_16x16x32_bf16 v[38:41], v[180:183], v[204:207], v[38:41]
	v_mfma_f32_16x16x32_bf16 v[30:33], v[188:191], v[204:207], v[30:33]
	v_mfma_f32_16x16x32_bf16 v[22:25], v[180:183], v[212:215], v[22:25]
	v_mfma_f32_16x16x32_bf16 v[14:17], v[188:191], v[212:215], v[14:17]
	v_mfma_f32_16x16x32_bf16 v[6:9], v[180:183], v[220:223], v[6:9]
	v_mfma_f32_16x16x32_bf16 v[2:5], v[188:191], v[220:223], v[2:5]
	s_setprio 0
	s_barrier
	s_add_i32 s70, 0, 0x18000
	v_add_u32_e32 v130, s70, v147
	s_add_i32 s71, 0, 0x1c000
	ds_read_b128 v[160:163], v130
	ds_read_b128 v[164:167], v130 offset:1024
	ds_read_b128 v[168:171], v130 offset:2048
	ds_read_b128 v[172:175], v130 offset:3072
	v_add_u32_e32 v130, s71, v147
	ds_read_b128 v[176:179], v130
	ds_read_b128 v[180:183], v130 offset:1024
	ds_read_b128 v[184:187], v130 offset:2048
	ds_read_b128 v[188:191], v130 offset:3072
	s_add_u32 s38, s44, 0xe0000
	s_addc_u32 s39, s45, 0
	s_mov_b32 m0, s53
	ds_read_b128 v[192:195], v159 offset:32768
	ds_read_b128 v[196:199], v159 offset:33792
	ds_read_b128 v[200:203], v159 offset:34816
	ds_read_b128 v[204:207], v159 offset:35840
	ds_read_b128 v[208:211], v159 offset:36864
	ds_read_b128 v[212:215], v159 offset:37888
	ds_read_b128 v[216:219], v159 offset:38912
	ds_read_b128 v[220:223], v159 offset:39936
	global_load_lds_dwordx4 v132, s[38:39]
	s_mov_b32 m0, s54
	s_nop 0
	global_load_lds_dwordx4 v136, s[38:39]
	s_waitcnt vmcnt(8)
	s_waitcnt lgkmcnt(0)
	s_barrier
	s_setprio 3
	s_waitcnt lgkmcnt(0)
	v_mfma_f32_16x16x32_bf16 v[126:129], v[160:163], v[192:195], v[126:129]
	v_mfma_f32_16x16x32_bf16 v[122:125], v[168:171], v[192:195], v[122:125]
	v_mfma_f32_16x16x32_bf16 v[118:121], v[160:163], v[200:203], v[118:121]
	v_mfma_f32_16x16x32_bf16 v[114:117], v[168:171], v[200:203], v[114:117]
	v_mfma_f32_16x16x32_bf16 v[106:109], v[160:163], v[208:211], v[106:109]
	v_mfma_f32_16x16x32_bf16 v[98:101], v[168:171], v[208:211], v[98:101]
	v_mfma_f32_16x16x32_bf16 v[78:81], v[160:163], v[216:219], v[78:81]
	v_mfma_f32_16x16x32_bf16 v[74:77], v[168:171], v[216:219], v[74:77]
	v_mfma_f32_16x16x32_bf16 v[126:129], v[164:167], v[196:199], v[126:129]
	v_mfma_f32_16x16x32_bf16 v[122:125], v[172:175], v[196:199], v[122:125]
	v_mfma_f32_16x16x32_bf16 v[118:121], v[164:167], v[204:207], v[118:121]
	v_mfma_f32_16x16x32_bf16 v[114:117], v[172:175], v[204:207], v[114:117]
	v_mfma_f32_16x16x32_bf16 v[106:109], v[164:167], v[212:215], v[106:109]
	v_mfma_f32_16x16x32_bf16 v[98:101], v[172:175], v[212:215], v[98:101]
	v_mfma_f32_16x16x32_bf16 v[78:81], v[164:167], v[220:223], v[78:81]
	v_mfma_f32_16x16x32_bf16 v[74:77], v[172:175], v[220:223], v[74:77]
	v_mfma_f32_16x16x32_bf16 v[110:113], v[176:179], v[192:195], v[110:113]
	v_mfma_f32_16x16x32_bf16 v[102:105], v[184:187], v[192:195], v[102:105]
	v_mfma_f32_16x16x32_bf16 v[94:97], v[176:179], v[200:203], v[94:97]
	v_mfma_f32_16x16x32_bf16 v[90:93], v[184:187], v[200:203], v[90:93]
	v_mfma_f32_16x16x32_bf16 v[86:89], v[176:179], v[208:211], v[86:89]
	v_mfma_f32_16x16x32_bf16 v[82:85], v[184:187], v[208:211], v[82:85]
	v_mfma_f32_16x16x32_bf16 v[70:73], v[176:179], v[216:219], v[70:73]
	v_mfma_f32_16x16x32_bf16 v[66:69], v[184:187], v[216:219], v[66:69]
	v_mfma_f32_16x16x32_bf16 v[110:113], v[180:183], v[196:199], v[110:113]
	v_mfma_f32_16x16x32_bf16 v[102:105], v[188:191], v[196:199], v[102:105]
	v_mfma_f32_16x16x32_bf16 v[94:97], v[180:183], v[204:207], v[94:97]
	v_mfma_f32_16x16x32_bf16 v[90:93], v[188:191], v[204:207], v[90:93]
	v_mfma_f32_16x16x32_bf16 v[86:89], v[180:183], v[212:215], v[86:89]
	v_mfma_f32_16x16x32_bf16 v[82:85], v[188:191], v[212:215], v[82:85]
	v_mfma_f32_16x16x32_bf16 v[70:73], v[180:183], v[220:223], v[70:73]
	v_mfma_f32_16x16x32_bf16 v[66:69], v[188:191], v[220:223], v[66:69]
	s_setprio 0
	s_barrier
; #define PG8_STAGE_A(b, h, ptr, NX) do { if constexpr (Sched::GATHER) { unsigned gs_[2]; gs_[0] = ((NX) && last_) ? gN[h][0] : gA[h][0]; gs_[1] = ((NX) && last_) ? gN[h][1] : gA[h][1]; PG8_STAGE(PG8_SA(b, h), ptr, gs_); } \
;         else PG8_STAGE(PG8_SA(b, h), (ptr) + ((h) ? hstep : (size_t)0), voffA); } while (0)
; #define PG8_STAGE(bufoff, gbase, voff) do { _Pragma("unroll") for (int _i = 0; _i < 2; ++_i) \
;         __builtin_amdgcn_global_load_lds((const unsigned*)((const char*)(gbase) + (voff)[_i]), (PG8_LAS unsigned*)(lds + (bufoff) + ldsw + _i * 8192), 16, 0, 0); } while (0)
; #define PG8_LDA(dst, b, h) do { _Pragma("unroll") for (int m = 0; m < 4; ++m) _Pragma("unroll") for (int k = 0; k < 2; ++k) dst[m][k] = *(const PG8_LAS bf16x8*)(lds + PG8_SA(b, h) + aoff + m * 2048 + k * 1024); } while (0)
; #define PG8_MMA(ai, bj, At, Bt) do { __builtin_amdgcn_s_setprio(1); _Pragma("unroll") for (int m = 0; m < 4; ++m) _Pragma("unroll") for (int n = 0; n < 2; ++n) _Pragma("unroll") for (int k = 0; k < 2; ++k) \
;         acc[ai][bj][m][n] = __builtin_amdgcn_mfma_f32_16x16x32_bf16(Bt[n][k], At[m][k], acc[ai][bj][m][n], 0, 0, 0); __builtin_amdgcn_s_setprio(0); } while (0)
; #define PG8_WAIT_V(n) asm volatile("s_waitcnt vmcnt(" #n ")" ::: "memory")
; #define PG8_WAIT_L(n) asm volatile("s_waitcnt lgkmcnt(" #n ")" ::: "memory")
; #define PG8_BAR __builtin_amdgcn_s_barrier()
; #define PG8_SCHED __builtin_amdgcn_sched_barrier(0)
; template <class Epi, class Sched, bool ALIGN_EPI = false, bool SP2 = false>
; __device__ __forceinline__ void gemm_phase(PG8_LAS unsigned char* lds, const Gemm g, const Sched& S, const Epi& E, const bool skip_epi = false) {
;     ...
;             PG8_LDA(At, 1, 1); PG8_STAGE(PG8_SB(1, 0), b3, voffB); PG8_STAGE(PG8_SB(1, 1), b3 + hstep, voffB); PG8_STAGE_A(1, 0, a3, true);
;             PG8_WAIT_V(8); PG8_WAIT_L(0); PG8_BAR; PG8_MMA(1, 0, At, B0); PG8_MMA(1, 1, At, B1); PG8_BAR; PG8_SCHED;
;     ...
;         if constexpr (ALIGN_EPI) { if (wr == 0) PG8_BAR; }
	s_add_i32 s38, s70, s51
	s_add_i32 m0, s38, 0xffffff80
	ds_read_b128 v[192:195], v159 offset:49152
	ds_read_b128 v[196:199], v159 offset:50176
	ds_read_b128 v[200:203], v159 offset:51200
	ds_read_b128 v[204:207], v159 offset:52224
	ds_read_b128 v[208:211], v159 offset:53248
	ds_read_b128 v[212:215], v159 offset:54272
	ds_read_b128 v[216:219], v159 offset:55296
	ds_read_b128 v[220:223], v159 offset:56320
	global_load_lds_dwordx4 v[152:153], off offset:128
	s_add_i32 m0, s38, 0x1f80
	s_add_u32 s38, s42, 0xe0080
	s_addc_u32 s39, s43, 0
	s_add_i32 s42, s71, s51
	global_load_lds_dwordx4 v[224:225], off offset:128
	s_mov_b32 m0, s42
	s_nop 0
	global_load_lds_dwordx4 v134, s[38:39]
	s_add_i32 m0, s42, 0x2000
	s_nop 0
	global_load_lds_dwordx4 v138, s[38:39]
	s_add_i32 m0, s57, 0xffffff80
	s_nop 0
	global_load_lds_dwordx4 v[226:227], off offset:128
	s_add_i32 m0, s58, 0xffffff80
	s_nop 0
	global_load_lds_dwordx4 v[230:231], off offset:128
	s_waitcnt vmcnt(8)
	s_waitcnt lgkmcnt(0)
	s_barrier
	s_setprio 3
	s_waitcnt lgkmcnt(0)
	v_mfma_f32_16x16x32_bf16 v[62:65], v[160:163], v[192:195], v[62:65]
	v_mfma_f32_16x16x32_bf16 v[58:61], v[168:171], v[192:195], v[58:61]
	v_mfma_f32_16x16x32_bf16 v[50:53], v[160:163], v[200:203], v[50:53]
	v_mfma_f32_16x16x32_bf16 v[42:45], v[168:171], v[200:203], v[42:45]
	v_mfma_f32_16x16x32_bf16 v[34:37], v[160:163], v[208:211], v[34:37]
	v_mfma_f32_16x16x32_bf16 v[26:29], v[168:171], v[208:211], v[26:29]
	v_mfma_f32_16x16x32_bf16 v[18:21], v[160:163], v[216:219], v[18:21]
	v_mfma_f32_16x16x32_bf16 v[10:13], v[168:171], v[216:219], v[10:13]
	v_mfma_f32_16x16x32_bf16 v[62:65], v[164:167], v[196:199], v[62:65]
	v_mfma_f32_16x16x32_bf16 v[58:61], v[172:175], v[196:199], v[58:61]
	v_mfma_f32_16x16x32_bf16 v[50:53], v[164:167], v[204:207], v[50:53]
	v_mfma_f32_16x16x32_bf16 v[42:45], v[172:175], v[204:207], v[42:45]
	v_mfma_f32_16x16x32_bf16 v[34:37], v[164:167], v[212:215], v[34:37]
	v_mfma_f32_16x16x32_bf16 v[26:29], v[172:175], v[212:215], v[26:29]
	v_mfma_f32_16x16x32_bf16 v[18:21], v[164:167], v[220:223], v[18:21]
	v_mfma_f32_16x16x32_bf16 v[10:13], v[172:175], v[220:223], v[10:13]
	v_mfma_f32_16x16x32_bf16 v[54:57], v[176:179], v[192:195], v[54:57]
	v_mfma_f32_16x16x32_bf16 v[46:49], v[184:187], v[192:195], v[46:49]
	v_mfma_f32_16x16x32_bf16 v[38:41], v[176:179], v[200:203], v[38:41]
	v_mfma_f32_16x16x32_bf16 v[30:33], v[184:187], v[200:203], v[30:33]
	v_mfma_f32_16x16x32_bf16 v[22:25], v[176:179], v[208:211], v[22:25]
	v_mfma_f32_16x16x32_bf16 v[14:17], v[184:187], v[208:211], v[14:17]
	v_mfma_f32_16x16x32_bf16 v[6:9], v[176:179], v[216:219], v[6:9]
	v_mfma_f32_16x16x32_bf16 v[2:5], v[184:187], v[216:219], v[2:5]
	v_mfma_f32_16x16x32_bf16 v[54:57], v[180:183], v[196:199], v[54:57]
	v_mfma_f32_16x16x32_bf16 v[46:49], v[188:191], v[196:199], v[46:49]
	v_mfma_f32_16x16x32_bf16 v[38:41], v[180:183], v[204:207], v[38:41]
	v_mfma_f32_16x16x32_bf16 v[30:33], v[188:191], v[204:207], v[30:33]
	v_mfma_f32_16x16x32_bf16 v[22:25], v[180:183], v[212:215], v[22:25]
	v_mfma_f32_16x16x32_bf16 v[14:17], v[188:191], v[212:215], v[14:17]
	v_mfma_f32_16x16x32_bf16 v[6:9], v[180:183], v[220:223], v[6:9]
	v_mfma_f32_16x16x32_bf16 v[2:5], v[188:191], v[220:223], v[2:5]
	s_setprio 0
	s_barrier
	s_add_i32 s69, s69, 2
	s_add_u32 s67, s67, 0x100
	s_addc_u32 s68, s68, 0
	s_cmp_gt_u32 s69, 53
	s_mov_b64 s[38:39], s[40:41]
	s_cbranch_scc0 .LBB0_1823
	s_and_b64 vcc, exec, s[20:21]
	s_cbranch_vccz .LBB0_1826
	s_barrier

; #define PG8_STAGE_A(b, h, ptr, NX) do { if constexpr (Sched::GATHER) { unsigned gs_[2]; gs_[0] = ((NX) && last_) ? gN[h][0] : gA[h][0]; gs_[1] = ((NX) && last_) ? gN[h][1] : gA[h][1]; PG8_STAGE(PG8_SA(b, h), ptr, gs_); } \
;         else PG8_STAGE(PG8_SA(b, h), (ptr) + ((h) ? hstep : (size_t)0), voffA); } while (0)
; #define PG8_STAGE(bufoff, gbase, voff) do { _Pragma("unroll") for (int _i = 0; _i < 2; ++_i) \
;         __builtin_amdgcn_global_load_lds((const unsigned*)((const char*)(gbase) + (voff)[_i]), (PG8_LAS unsigned*)(lds + (bufoff) + ldsw + _i * 8192), 16, 0, 0); } while (0)
; #define PG8_LDA(dst, b, h) do { _Pragma("unroll") for (int m = 0; m < 4; ++m) _Pragma("unroll") for (int k = 0; k < 2; ++k) dst[m][k] = *(const PG8_LAS bf16x8*)(lds + PG8_SA(b, h) + aoff + m * 2048 + k * 1024); } while (0)
; #define PG8_LDB(dst, b, h) do { _Pragma("unroll") for (int n = 0; n < 2; ++n) _Pragma("unroll") for (int k = 0; k < 2; ++k) dst[n][k] = *(const PG8_LAS bf16x8*)(lds + PG8_SB(b, h) + boff + n * 2048 + k * 1024); } while (0)
; #define PG8_MMA(ai, bj, At, Bt) do { __builtin_amdgcn_s_setprio(1); _Pragma("unroll") for (int m = 0; m < 4; ++m) _Pragma("unroll") for (int n = 0; n < 2; ++n) _Pragma("unroll") for (int k = 0; k < 2; ++k) \
;         acc[ai][bj][m][n] = __builtin_amdgcn_mfma_f32_16x16x32_bf16(Bt[n][k], At[m][k], acc[ai][bj][m][n], 0, 0, 0); __builtin_amdgcn_s_setprio(0); } while (0)
; #define PG8_WAIT_V(n) asm volatile("s_waitcnt vmcnt(" #n ")" ::: "memory")
; #define PG8_WAIT_L(n) asm volatile("s_waitcnt lgkmcnt(" #n ")" ::: "memory")
; #define PG8_BAR __builtin_amdgcn_s_barrier()
; #define PG8_SCHED __builtin_amdgcn_sched_barrier(0)
; template <class Epi, class Sched, bool ALIGN_EPI = false, bool SP2 = false>
; __device__ __forceinline__ void gemm_phase(PG8_LAS unsigned char* lds, const Gemm g, const Sched& S, const Epi& E, const bool skip_epi = false) {
;     ...
;             PG8_LDB(B0, 0, 0); PG8_LDB(B1, 0, 1); PG8_SCHED; PG8_LDA(At, 0, 0); PG8_STAGE_A(1, 1, a1, false);
;             PG8_WAIT_V(8); PG8_WAIT_L(0); PG8_BAR; PG8_MMA(0, 0, At, B0); PG8_MMA(0, 1, At, B1); PG8_BAR; PG8_SCHED;
;             PG8_LDA(At, 0, 1); PG8_STAGE(PG8_SB(0, 0), b2, voffB); PG8_STAGE(PG8_SB(0, 1), b2 + hstep, voffB); PG8_STAGE_A(0, 0, a2, true);
;             PG8_WAIT_V(8); PG8_WAIT_L(0); PG8_BAR; PG8_MMA(1, 0, At, B0); PG8_MMA(1, 1, At, B1); PG8_BAR; PG8_SCHED;
.LBB0_1843:
	s_add_u32 s54, s30, 0x100
	s_addc_u32 s55, s31, 0
	s_mov_b32 s56, -2
	ds_read_b128 v[142:145], v150
	ds_read_b128 v[154:157], v150 offset:1024
	ds_read_b128 v[158:161], v150 offset:2048
	ds_read_b128 v[162:165], v150 offset:3072
	ds_read_b128 v[166:169], v151
	ds_read_b128 v[170:173], v151 offset:1024
	ds_read_b128 v[174:177], v151 offset:2048
	ds_read_b128 v[178:181], v151 offset:3072
	s_add_u32 s30, s28, 0x100
	s_addc_u32 s31, s29, 0
	s_cmp_eq_u32 s56, 10
	s_cselect_b32 s37, s7, s31
	s_cselect_b32 s36, s6, s30
	s_cselect_b32 s35, s25, s55
	s_cselect_b32 s34, s24, s54
	v_lshl_add_u64 v[214:215], s[28:29], 0, v[136:137]
	s_add_i32 m0, s38, 0xc000
	ds_read_b128 v[182:185], v152
	ds_read_b128 v[186:189], v152 offset:1024
	ds_read_b128 v[190:193], v152 offset:2048
	ds_read_b128 v[194:197], v152 offset:3072
	ds_read_b128 v[198:201], v152 offset:4096
	ds_read_b128 v[202:205], v152 offset:5120
	ds_read_b128 v[206:209], v152 offset:6144
	ds_read_b128 v[210:213], v152 offset:7168
	global_load_lds_dwordx4 v[214:215], off
	v_lshl_add_u64 v[214:215], s[28:29], 0, v[138:139]
	s_add_i32 m0, s38, 0xe000
	s_nop 0
	global_load_lds_dwordx4 v[214:215], off
	s_waitcnt vmcnt(8)
	s_waitcnt lgkmcnt(0)
	s_barrier
	s_setprio 3
	s_waitcnt lgkmcnt(0)
	v_mfma_f32_16x16x32_bf16 v[126:129], v[142:145], v[182:185], 0
	v_mfma_f32_16x16x32_bf16 v[122:125], v[158:161], v[182:185], 0
	v_mfma_f32_16x16x32_bf16 v[110:113], v[142:145], v[190:193], 0
	v_mfma_f32_16x16x32_bf16 v[106:109], v[158:161], v[190:193], 0
	v_mfma_f32_16x16x32_bf16 v[94:97], v[142:145], v[198:201], 0
	v_mfma_f32_16x16x32_bf16 v[90:93], v[158:161], v[198:201], 0
	v_mfma_f32_16x16x32_bf16 v[78:81], v[142:145], v[206:209], 0
	v_mfma_f32_16x16x32_bf16 v[74:77], v[158:161], v[206:209], 0
	v_mfma_f32_16x16x32_bf16 v[126:129], v[154:157], v[186:189], v[126:129]
	v_mfma_f32_16x16x32_bf16 v[122:125], v[162:165], v[186:189], v[122:125]
	v_mfma_f32_16x16x32_bf16 v[110:113], v[154:157], v[194:197], v[110:113]
	v_mfma_f32_16x16x32_bf16 v[106:109], v[162:165], v[194:197], v[106:109]
	v_mfma_f32_16x16x32_bf16 v[94:97], v[154:157], v[202:205], v[94:97]
	v_mfma_f32_16x16x32_bf16 v[90:93], v[162:165], v[202:205], v[90:93]
	v_mfma_f32_16x16x32_bf16 v[78:81], v[154:157], v[210:213], v[78:81]
	v_mfma_f32_16x16x32_bf16 v[74:77], v[162:165], v[210:213], v[74:77]
	v_mfma_f32_16x16x32_bf16 v[118:121], v[166:169], v[182:185], 0
	v_mfma_f32_16x16x32_bf16 v[114:117], v[174:177], v[182:185], 0
	v_mfma_f32_16x16x32_bf16 v[102:105], v[166:169], v[190:193], 0
	v_mfma_f32_16x16x32_bf16 v[98:101], v[174:177], v[190:193], 0
	v_mfma_f32_16x16x32_bf16 v[86:89], v[166:169], v[198:201], 0
	v_mfma_f32_16x16x32_bf16 v[82:85], v[174:177], v[198:201], 0
	v_mfma_f32_16x16x32_bf16 v[70:73], v[166:169], v[206:209], 0
	v_mfma_f32_16x16x32_bf16 v[66:69], v[174:177], v[206:209], 0
	v_mfma_f32_16x16x32_bf16 v[118:121], v[170:173], v[186:189], v[118:121]
	v_mfma_f32_16x16x32_bf16 v[114:117], v[178:181], v[186:189], v[114:117]
	v_mfma_f32_16x16x32_bf16 v[102:105], v[170:173], v[194:197], v[102:105]
	v_mfma_f32_16x16x32_bf16 v[98:101], v[178:181], v[194:197], v[98:101]
	v_mfma_f32_16x16x32_bf16 v[86:89], v[170:173], v[202:205], v[86:89]
	v_mfma_f32_16x16x32_bf16 v[82:85], v[178:181], v[202:205], v[82:85]
	v_mfma_f32_16x16x32_bf16 v[70:73], v[170:173], v[210:213], v[70:73]
	v_mfma_f32_16x16x32_bf16 v[66:69], v[178:181], v[210:213], v[66:69]
	s_setprio 0
	s_barrier
	s_add_i32 s28, s50, s3
	v_lshl_add_u64 v[214:215], s[34:35], 0, v[132:133]
	s_mov_b32 m0, s28
	ds_read_b128 v[182:185], v152 offset:16384
	ds_read_b128 v[186:189], v152 offset:17408
	ds_read_b128 v[190:193], v152 offset:18432
	ds_read_b128 v[194:197], v152 offset:19456
	ds_read_b128 v[198:201], v152 offset:20480
	ds_read_b128 v[202:205], v152 offset:21504
	ds_read_b128 v[206:209], v152 offset:22528
	ds_read_b128 v[210:213], v152 offset:23552
	global_load_lds_dwordx4 v[214:215], off
	s_add_i32 m0, s28, 0x2000
	s_add_u32 s28, s34, 0xe0000
	v_lshl_add_u64 v[216:217], s[34:35], 0, v[134:135]
	s_addc_u32 s29, s35, 0
	s_add_i32 s57, s51, s3
	global_load_lds_dwordx4 v[216:217], off
	s_mov_b32 m0, s57
	v_lshl_add_u64 v[220:221], s[36:37], 0, v[134:135]
	global_load_lds_dwordx4 v132, s[28:29]
	s_add_i32 m0, s57, 0x2000
	s_nop 0
	global_load_lds_dwordx4 v134, s[28:29]
	v_lshl_add_u64 v[218:219], s[36:37], 0, v[132:133]
	s_mov_b32 m0, s38
	s_nop 0
	global_load_lds_dwordx4 v[218:219], off
	s_mov_b32 m0, s39
	s_nop 0
	global_load_lds_dwordx4 v[220:221], off
	s_waitcnt vmcnt(8)
	s_waitcnt lgkmcnt(0)
	s_barrier
	s_setprio 3
	s_waitcnt lgkmcnt(0)
	v_mfma_f32_16x16x32_bf16 v[62:65], v[142:145], v[182:185], 0
	v_mfma_f32_16x16x32_bf16 v[58:61], v[158:161], v[182:185], 0
	v_mfma_f32_16x16x32_bf16 v[46:49], v[142:145], v[190:193], 0
	v_mfma_f32_16x16x32_bf16 v[42:45], v[158:161], v[190:193], 0
	v_mfma_f32_16x16x32_bf16 v[30:33], v[142:145], v[198:201], 0
	v_mfma_f32_16x16x32_bf16 v[26:29], v[158:161], v[198:201], 0
	v_mfma_f32_16x16x32_bf16 v[14:17], v[142:145], v[206:209], 0
	v_mfma_f32_16x16x32_bf16 v[10:13], v[158:161], v[206:209], 0
	v_mfma_f32_16x16x32_bf16 v[62:65], v[154:157], v[186:189], v[62:65]
	v_mfma_f32_16x16x32_bf16 v[58:61], v[162:165], v[186:189], v[58:61]
	v_mfma_f32_16x16x32_bf16 v[46:49], v[154:157], v[194:197], v[46:49]
	v_mfma_f32_16x16x32_bf16 v[42:45], v[162:165], v[194:197], v[42:45]
	v_mfma_f32_16x16x32_bf16 v[30:33], v[154:157], v[202:205], v[30:33]
	v_mfma_f32_16x16x32_bf16 v[26:29], v[162:165], v[202:205], v[26:29]
	v_mfma_f32_16x16x32_bf16 v[14:17], v[154:157], v[210:213], v[14:17]
	v_mfma_f32_16x16x32_bf16 v[10:13], v[162:165], v[210:213], v[10:13]
	v_mfma_f32_16x16x32_bf16 v[54:57], v[166:169], v[182:185], 0
	v_mfma_f32_16x16x32_bf16 v[50:53], v[174:177], v[182:185], 0
	v_mfma_f32_16x16x32_bf16 v[38:41], v[166:169], v[190:193], 0
	v_mfma_f32_16x16x32_bf16 v[34:37], v[174:177], v[190:193], 0
	v_mfma_f32_16x16x32_bf16 v[22:25], v[166:169], v[198:201], 0
	v_mfma_f32_16x16x32_bf16 v[18:21], v[174:177], v[198:201], 0
	v_mfma_f32_16x16x32_bf16 v[6:9], v[166:169], v[206:209], 0
	v_mfma_f32_16x16x32_bf16 v[2:5], v[174:177], v[206:209], 0
	v_mfma_f32_16x16x32_bf16 v[54:57], v[170:173], v[186:189], v[54:57]
	v_mfma_f32_16x16x32_bf16 v[50:53], v[178:181], v[186:189], v[50:53]
	v_mfma_f32_16x16x32_bf16 v[38:41], v[170:173], v[194:197], v[38:41]
	v_mfma_f32_16x16x32_bf16 v[34:37], v[178:181], v[194:197], v[34:37]
	v_mfma_f32_16x16x32_bf16 v[22:25], v[170:173], v[202:205], v[22:25]
	v_mfma_f32_16x16x32_bf16 v[18:21], v[178:181], v[202:205], v[18:21]
	v_mfma_f32_16x16x32_bf16 v[6:9], v[170:173], v[210:213], v[6:9]
	v_mfma_f32_16x16x32_bf16 v[2:5], v[178:181], v[210:213], v[2:5]
	s_setprio 0
	s_barrier
; #define PG8_STAGE_A(b, h, ptr, NX) do { if constexpr (Sched::GATHER) { unsigned gs_[2]; gs_[0] = ((NX) && last_) ? gN[h][0] : gA[h][0]; gs_[1] = ((NX) && last_) ? gN[h][1] : gA[h][1]; PG8_STAGE(PG8_SA(b, h), ptr, gs_); } \
;         else PG8_STAGE(PG8_SA(b, h), (ptr) + ((h) ? hstep : (size_t)0), voffA); } while (0)
; #define PG8_STAGE(bufoff, gbase, voff) do { _Pragma("unroll") for (int _i = 0; _i < 2; ++_i) \
;         __builtin_amdgcn_global_load_lds((const unsigned*)((const char*)(gbase) + (voff)[_i]), (PG8_LAS unsigned*)(lds + (bufoff) + ldsw + _i * 8192), 16, 0, 0); } while (0)
; #define PG8_LDA(dst, b, h) do { _Pragma("unroll") for (int m = 0; m < 4; ++m) _Pragma("unroll") for (int k = 0; k < 2; ++k) dst[m][k] = *(const PG8_LAS bf16x8*)(lds + PG8_SA(b, h) + aoff + m * 2048 + k * 1024); } while (0)
; #define PG8_LDB(dst, b, h) do { _Pragma("unroll") for (int n = 0; n < 2; ++n) _Pragma("unroll") for (int k = 0; k < 2; ++k) dst[n][k] = *(const PG8_LAS bf16x8*)(lds + PG8_SB(b, h) + boff + n * 2048 + k * 1024); } while (0)
; #define PG8_MMA(ai, bj, At, Bt) do { __builtin_amdgcn_s_setprio(1); _Pragma("unroll") for (int m = 0; m < 4; ++m) _Pragma("unroll") for (int n = 0; n < 2; ++n) _Pragma("unroll") for (int k = 0; k < 2; ++k) \
;         acc[ai][bj][m][n] = __builtin_amdgcn_mfma_f32_16x16x32_bf16(Bt[n][k], At[m][k], acc[ai][bj][m][n], 0, 0, 0); __builtin_amdgcn_s_setprio(0); } while (0)
; #define PG8_WAIT_V(n) asm volatile("s_waitcnt vmcnt(" #n ")" ::: "memory")
; #define PG8_WAIT_L(n) asm volatile("s_waitcnt lgkmcnt(" #n ")" ::: "memory")
; #define PG8_BAR __builtin_amdgcn_s_barrier()
; #define PG8_SCHED __builtin_amdgcn_sched_barrier(0)
; template <class Epi, class Sched, bool ALIGN_EPI = false, bool SP2 = false>
; __device__ __forceinline__ void gemm_phase(PG8_LAS unsigned char* lds, const Gemm g, const Sched& S, const Epi& E, const bool skip_epi = false) {
;     ...
;             PG8_LDB(B0, 1, 0); PG8_LDB(B1, 1, 1); PG8_SCHED; PG8_LDA(At, 1, 0); PG8_STAGE_A(0, 1, a2, true);
;             PG8_WAIT_V(8); PG8_WAIT_L(0); PG8_BAR; PG8_MMA(0, 0, At, B0); PG8_MMA(0, 1, At, B1); PG8_BAR; PG8_SCHED;
;             PG8_LDA(At, 1, 1); PG8_STAGE(PG8_SB(1, 0), b3, voffB); PG8_STAGE(PG8_SB(1, 1), b3 + hstep, voffB); PG8_STAGE_A(1, 0, a3, true);
;             PG8_WAIT_V(8); PG8_WAIT_L(0); PG8_BAR; PG8_MMA(1, 0, At, B0); PG8_MMA(1, 1, At, B1); PG8_BAR; PG8_SCHED;
	s_add_i32 s57, 0, 0x18000
	v_add_u32_e32 v130, s57, v146
	s_add_i32 s58, 0, 0x1c000
	ds_read_b128 v[142:145], v130
	ds_read_b128 v[154:157], v130 offset:1024
	ds_read_b128 v[158:161], v130 offset:2048
	ds_read_b128 v[162:165], v130 offset:3072
	v_add_u32_e32 v130, s58, v146
	ds_read_b128 v[166:169], v130
	ds_read_b128 v[170:173], v130 offset:1024
	ds_read_b128 v[174:177], v130 offset:2048
	ds_read_b128 v[178:181], v130 offset:3072
	s_add_u32 s28, s36, 0xe0000
	s_addc_u32 s29, s37, 0
	s_mov_b32 m0, s40
	ds_read_b128 v[182:185], v152 offset:32768
	ds_read_b128 v[186:189], v152 offset:33792
	ds_read_b128 v[190:193], v152 offset:34816
	ds_read_b128 v[194:197], v152 offset:35840
	ds_read_b128 v[198:201], v152 offset:36864
	ds_read_b128 v[202:205], v152 offset:37888
	ds_read_b128 v[206:209], v152 offset:38912
	ds_read_b128 v[210:213], v152 offset:39936
	global_load_lds_dwordx4 v132, s[28:29]
	s_mov_b32 m0, s41
	s_nop 0
	global_load_lds_dwordx4 v134, s[28:29]
	s_waitcnt vmcnt(8)
	s_waitcnt lgkmcnt(0)
	s_barrier
	s_setprio 3
	s_waitcnt lgkmcnt(0)
	v_mfma_f32_16x16x32_bf16 v[126:129], v[142:145], v[182:185], v[126:129]
	v_mfma_f32_16x16x32_bf16 v[122:125], v[158:161], v[182:185], v[122:125]
	v_mfma_f32_16x16x32_bf16 v[110:113], v[142:145], v[190:193], v[110:113]
	v_mfma_f32_16x16x32_bf16 v[106:109], v[158:161], v[190:193], v[106:109]
	v_mfma_f32_16x16x32_bf16 v[94:97], v[142:145], v[198:201], v[94:97]
	v_mfma_f32_16x16x32_bf16 v[90:93], v[158:161], v[198:201], v[90:93]
	v_mfma_f32_16x16x32_bf16 v[78:81], v[142:145], v[206:209], v[78:81]
	v_mfma_f32_16x16x32_bf16 v[74:77], v[158:161], v[206:209], v[74:77]
	v_mfma_f32_16x16x32_bf16 v[126:129], v[154:157], v[186:189], v[126:129]
	v_mfma_f32_16x16x32_bf16 v[122:125], v[162:165], v[186:189], v[122:125]
	v_mfma_f32_16x16x32_bf16 v[110:113], v[154:157], v[194:197], v[110:113]
	v_mfma_f32_16x16x32_bf16 v[106:109], v[162:165], v[194:197], v[106:109]
	v_mfma_f32_16x16x32_bf16 v[94:97], v[154:157], v[202:205], v[94:97]
	v_mfma_f32_16x16x32_bf16 v[90:93], v[162:165], v[202:205], v[90:93]
	v_mfma_f32_16x16x32_bf16 v[78:81], v[154:157], v[210:213], v[78:81]
	v_mfma_f32_16x16x32_bf16 v[74:77], v[162:165], v[210:213], v[74:77]
	v_mfma_f32_16x16x32_bf16 v[118:121], v[166:169], v[182:185], v[118:121]
	v_mfma_f32_16x16x32_bf16 v[114:117], v[174:177], v[182:185], v[114:117]
	v_mfma_f32_16x16x32_bf16 v[102:105], v[166:169], v[190:193], v[102:105]
	v_mfma_f32_16x16x32_bf16 v[98:101], v[174:177], v[190:193], v[98:101]
	v_mfma_f32_16x16x32_bf16 v[86:89], v[166:169], v[198:201], v[86:89]
	v_mfma_f32_16x16x32_bf16 v[82:85], v[174:177], v[198:201], v[82:85]
	v_mfma_f32_16x16x32_bf16 v[70:73], v[166:169], v[206:209], v[70:73]
	v_mfma_f32_16x16x32_bf16 v[66:69], v[174:177], v[206:209], v[66:69]
	v_mfma_f32_16x16x32_bf16 v[118:121], v[170:173], v[186:189], v[118:121]
	v_mfma_f32_16x16x32_bf16 v[114:117], v[178:181], v[186:189], v[114:117]
	v_mfma_f32_16x16x32_bf16 v[102:105], v[170:173], v[194:197], v[102:105]
	v_mfma_f32_16x16x32_bf16 v[98:101], v[178:181], v[194:197], v[98:101]
	v_mfma_f32_16x16x32_bf16 v[86:89], v[170:173], v[202:205], v[86:89]
	v_mfma_f32_16x16x32_bf16 v[82:85], v[178:181], v[202:205], v[82:85]
	v_mfma_f32_16x16x32_bf16 v[70:73], v[170:173], v[210:213], v[70:73]
	v_mfma_f32_16x16x32_bf16 v[66:69], v[178:181], v[210:213], v[66:69]
	s_setprio 0
	s_barrier
	s_add_i32 s28, s57, s3
	s_add_i32 m0, s28, 0xffffff80
	ds_read_b128 v[182:185], v152 offset:49152
	ds_read_b128 v[186:189], v152 offset:50176
	ds_read_b128 v[190:193], v152 offset:51200
	ds_read_b128 v[194:197], v152 offset:52224
	ds_read_b128 v[198:201], v152 offset:53248
	ds_read_b128 v[202:205], v152 offset:54272
	ds_read_b128 v[206:209], v152 offset:55296
	ds_read_b128 v[210:213], v152 offset:56320
	global_load_lds_dwordx4 v[214:215], off offset:128
	s_add_i32 m0, s28, 0x1f80
	s_add_u32 s28, s34, 0xe0080
	s_addc_u32 s29, s35, 0
	s_add_i32 s34, s58, s3
	global_load_lds_dwordx4 v[216:217], off offset:128
	s_mov_b32 m0, s34
	s_nop 0
	global_load_lds_dwordx4 v132, s[28:29]
	s_add_i32 m0, s34, 0x2000
	s_nop 0
	global_load_lds_dwordx4 v134, s[28:29]
	s_add_i32 m0, s46, 0xffffff80
	s_nop 0
	global_load_lds_dwordx4 v[218:219], off offset:128
	s_add_i32 m0, s47, 0xffffff80
	s_nop 0
	global_load_lds_dwordx4 v[220:221], off offset:128
	s_waitcnt vmcnt(8)
	s_waitcnt lgkmcnt(0)
	s_barrier
	s_setprio 3
	s_waitcnt lgkmcnt(0)
	v_mfma_f32_16x16x32_bf16 v[62:65], v[142:145], v[182:185], v[62:65]
	v_mfma_f32_16x16x32_bf16 v[58:61], v[158:161], v[182:185], v[58:61]
	v_mfma_f32_16x16x32_bf16 v[46:49], v[142:145], v[190:193], v[46:49]
	v_mfma_f32_16x16x32_bf16 v[42:45], v[158:161], v[190:193], v[42:45]
	v_mfma_f32_16x16x32_bf16 v[30:33], v[142:145], v[198:201], v[30:33]
	v_mfma_f32_16x16x32_bf16 v[26:29], v[158:161], v[198:201], v[26:29]
	v_mfma_f32_16x16x32_bf16 v[14:17], v[142:145], v[206:209], v[14:17]
	v_mfma_f32_16x16x32_bf16 v[10:13], v[158:161], v[206:209], v[10:13]
	v_mfma_f32_16x16x32_bf16 v[62:65], v[154:157], v[186:189], v[62:65]
	v_mfma_f32_16x16x32_bf16 v[58:61], v[162:165], v[186:189], v[58:61]
	v_mfma_f32_16x16x32_bf16 v[46:49], v[154:157], v[194:197], v[46:49]
	v_mfma_f32_16x16x32_bf16 v[42:45], v[162:165], v[194:197], v[42:45]
	v_mfma_f32_16x16x32_bf16 v[30:33], v[154:157], v[202:205], v[30:33]
	v_mfma_f32_16x16x32_bf16 v[26:29], v[162:165], v[202:205], v[26:29]
	v_mfma_f32_16x16x32_bf16 v[14:17], v[154:157], v[210:213], v[14:17]
	v_mfma_f32_16x16x32_bf16 v[10:13], v[162:165], v[210:213], v[10:13]
	v_mfma_f32_16x16x32_bf16 v[54:57], v[166:169], v[182:185], v[54:57]
	v_mfma_f32_16x16x32_bf16 v[50:53], v[174:177], v[182:185], v[50:53]
	v_mfma_f32_16x16x32_bf16 v[38:41], v[166:169], v[190:193], v[38:41]
	v_mfma_f32_16x16x32_bf16 v[34:37], v[174:177], v[190:193], v[34:37]
	v_mfma_f32_16x16x32_bf16 v[22:25], v[166:169], v[198:201], v[22:25]
	v_mfma_f32_16x16x32_bf16 v[18:21], v[174:177], v[198:201], v[18:21]
	v_mfma_f32_16x16x32_bf16 v[6:9], v[166:169], v[206:209], v[6:9]
	v_mfma_f32_16x16x32_bf16 v[2:5], v[174:177], v[206:209], v[2:5]
	v_mfma_f32_16x16x32_bf16 v[54:57], v[170:173], v[186:189], v[54:57]
	v_mfma_f32_16x16x32_bf16 v[50:53], v[178:181], v[186:189], v[50:53]
	v_mfma_f32_16x16x32_bf16 v[38:41], v[170:173], v[194:197], v[38:41]
	v_mfma_f32_16x16x32_bf16 v[34:37], v[178:181], v[194:197], v[34:37]
	v_mfma_f32_16x16x32_bf16 v[22:25], v[170:173], v[202:205], v[22:25]
	v_mfma_f32_16x16x32_bf16 v[18:21], v[178:181], v[202:205], v[18:21]
	v_mfma_f32_16x16x32_bf16 v[6:9], v[170:173], v[210:213], v[6:9]
	v_mfma_f32_16x16x32_bf16 v[2:5], v[178:181], v[210:213], v[2:5]
	s_setprio 0
	s_barrier
	s_add_i32 s56, s56, 2
	s_add_u32 s54, s54, 0x100
	s_addc_u32 s55, s55, 0
	s_cmp_gt_u32 s56, 11
	s_mov_b64 s[28:29], s[30:31]
; #define PG8_STAGE_A(b, h, ptr, NX) do { if constexpr (Sched::GATHER) { unsigned gs_[2]; gs_[0] = ((NX) && last_) ? gN[h][0] : gA[h][0]; gs_[1] = ((NX) && last_) ? gN[h][1] : gA[h][1]; PG8_STAGE(PG8_SA(b, h), ptr, gs_); } \
;         else PG8_STAGE(PG8_SA(b, h), (ptr) + ((h) ? hstep : (size_t)0), voffA); } while (0)
; #define PG8_STAGE(bufoff, gbase, voff) do { _Pragma("unroll") for (int _i = 0; _i < 2; ++_i) \
;         __builtin_amdgcn_global_load_lds((const unsigned*)((const char*)(gbase) + (voff)[_i]), (PG8_LAS unsigned*)(lds + (bufoff) + ldsw + _i * 8192), 16, 0, 0); } while (0)
; #define PG8_LDA(dst, b, h) do { _Pragma("unroll") for (int m = 0; m < 4; ++m) _Pragma("unroll") for (int k = 0; k < 2; ++k) dst[m][k] = *(const PG8_LAS bf16x8*)(lds + PG8_SA(b, h) + aoff + m * 2048 + k * 1024); } while (0)
; #define PG8_LDB(dst, b, h) do { _Pragma("unroll") for (int n = 0; n < 2; ++n) _Pragma("unroll") for (int k = 0; k < 2; ++k) dst[n][k] = *(const PG8_LAS bf16x8*)(lds + PG8_SB(b, h) + boff + n * 2048 + k * 1024); } while (0)
; #define PG8_MMA(ai, bj, At, Bt) do { __builtin_amdgcn_s_setprio(1); _Pragma("unroll") for (int m = 0; m < 4; ++m) _Pragma("unroll") for (int n = 0; n < 2; ++n) _Pragma("unroll") for (int k = 0; k < 2; ++k) \
;         acc[ai][bj][m][n] = __builtin_amdgcn_mfma_f32_16x16x32_bf16(Bt[n][k], At[m][k], acc[ai][bj][m][n], 0, 0, 0); __builtin_amdgcn_s_setprio(0); } while (0)
; #define PG8_WAIT_V(n) asm volatile("s_waitcnt vmcnt(" #n ")" ::: "memory")
; #define PG8_WAIT_L(n) asm volatile("s_waitcnt lgkmcnt(" #n ")" ::: "memory")
; #define PG8_BAR __builtin_amdgcn_s_barrier()
; #define PG8_SCHED __builtin_amdgcn_sched_barrier(0)
; template <class Epi, class Sched, bool ALIGN_EPI = false, bool SP2 = false>
; __device__ __forceinline__ void gemm_phase(PG8_LAS unsigned char* lds, const Gemm g, const Sched& S, const Epi& E, const bool skip_epi = false) {
;     ...
;             PG8_LDB(B0, 0, 0); PG8_LDB(B1, 0, 1); PG8_SCHED; PG8_LDA(At, 0, 0); PG8_STAGE_A(1, 1, a1, false);
;             PG8_WAIT_V(8); PG8_WAIT_L(0); PG8_BAR; PG8_MMA(0, 0, At, B0); PG8_MMA(0, 1, At, B1); PG8_BAR; PG8_SCHED;
;             PG8_LDA(At, 0, 1); PG8_STAGE(PG8_SB(0, 0), b2, voffB); PG8_STAGE(PG8_SB(0, 1), b2 + hstep, voffB); PG8_STAGE_A(0, 0, a2, true);
.LBB0_1844:
	ds_read_b128 v[142:145], v150
	ds_read_b128 v[154:157], v150 offset:1024
	ds_read_b128 v[158:161], v150 offset:2048
	ds_read_b128 v[162:165], v150 offset:3072
	ds_read_b128 v[166:169], v151
	ds_read_b128 v[170:173], v151 offset:1024
	ds_read_b128 v[174:177], v151 offset:2048
	ds_read_b128 v[178:181], v151 offset:3072
	s_add_u32 s30, s28, 0x100
	s_addc_u32 s31, s29, 0
	s_cmp_eq_u32 s56, 10
	s_cselect_b32 s37, s7, s31
	s_cselect_b32 s36, s6, s30
	s_cselect_b32 s35, s25, s55
	s_cselect_b32 s34, s24, s54
	v_lshl_add_u64 v[214:215], s[28:29], 0, v[136:137]
	s_add_i32 m0, s38, 0xc000
	ds_read_b128 v[182:185], v152
	ds_read_b128 v[186:189], v152 offset:1024
	ds_read_b128 v[190:193], v152 offset:2048
	ds_read_b128 v[194:197], v152 offset:3072
	ds_read_b128 v[198:201], v152 offset:4096
	ds_read_b128 v[202:205], v152 offset:5120
	ds_read_b128 v[206:209], v152 offset:6144
	ds_read_b128 v[210:213], v152 offset:7168
	global_load_lds_dwordx4 v[214:215], off
	v_lshl_add_u64 v[214:215], s[28:29], 0, v[138:139]
	s_add_i32 m0, s38, 0xe000
	s_nop 0
	global_load_lds_dwordx4 v[214:215], off
	s_waitcnt vmcnt(8)
	s_waitcnt lgkmcnt(0)
	s_barrier
	s_setprio 3
	s_waitcnt lgkmcnt(0)
	v_mfma_f32_16x16x32_bf16 v[126:129], v[142:145], v[182:185], v[126:129]
	v_mfma_f32_16x16x32_bf16 v[122:125], v[158:161], v[182:185], v[122:125]
	v_mfma_f32_16x16x32_bf16 v[110:113], v[142:145], v[190:193], v[110:113]
	v_mfma_f32_16x16x32_bf16 v[106:109], v[158:161], v[190:193], v[106:109]
	v_mfma_f32_16x16x32_bf16 v[94:97], v[142:145], v[198:201], v[94:97]
	v_mfma_f32_16x16x32_bf16 v[90:93], v[158:161], v[198:201], v[90:93]
	v_mfma_f32_16x16x32_bf16 v[78:81], v[142:145], v[206:209], v[78:81]
	v_mfma_f32_16x16x32_bf16 v[74:77], v[158:161], v[206:209], v[74:77]
	v_mfma_f32_16x16x32_bf16 v[126:129], v[154:157], v[186:189], v[126:129]
	v_mfma_f32_16x16x32_bf16 v[122:125], v[162:165], v[186:189], v[122:125]
	v_mfma_f32_16x16x32_bf16 v[110:113], v[154:157], v[194:197], v[110:113]
	v_mfma_f32_16x16x32_bf16 v[106:109], v[162:165], v[194:197], v[106:109]
	v_mfma_f32_16x16x32_bf16 v[94:97], v[154:157], v[202:205], v[94:97]
	v_mfma_f32_16x16x32_bf16 v[90:93], v[162:165], v[202:205], v[90:93]
	v_mfma_f32_16x16x32_bf16 v[78:81], v[154:157], v[210:213], v[78:81]
	v_mfma_f32_16x16x32_bf16 v[74:77], v[162:165], v[210:213], v[74:77]
	v_mfma_f32_16x16x32_bf16 v[118:121], v[166:169], v[182:185], v[118:121]
	v_mfma_f32_16x16x32_bf16 v[114:117], v[174:177], v[182:185], v[114:117]
	v_mfma_f32_16x16x32_bf16 v[102:105], v[166:169], v[190:193], v[102:105]
	v_mfma_f32_16x16x32_bf16 v[98:101], v[174:177], v[190:193], v[98:101]
	v_mfma_f32_16x16x32_bf16 v[86:89], v[166:169], v[198:201], v[86:89]
	v_mfma_f32_16x16x32_bf16 v[82:85], v[174:177], v[198:201], v[82:85]
	v_mfma_f32_16x16x32_bf16 v[70:73], v[166:169], v[206:209], v[70:73]
	v_mfma_f32_16x16x32_bf16 v[66:69], v[174:177], v[206:209], v[66:69]
	v_mfma_f32_16x16x32_bf16 v[118:121], v[170:173], v[186:189], v[118:121]
	v_mfma_f32_16x16x32_bf16 v[114:117], v[178:181], v[186:189], v[114:117]
	v_mfma_f32_16x16x32_bf16 v[102:105], v[170:173], v[194:197], v[102:105]
	v_mfma_f32_16x16x32_bf16 v[98:101], v[178:181], v[194:197], v[98:101]
	v_mfma_f32_16x16x32_bf16 v[86:89], v[170:173], v[202:205], v[86:89]
	v_mfma_f32_16x16x32_bf16 v[82:85], v[178:181], v[202:205], v[82:85]
	v_mfma_f32_16x16x32_bf16 v[70:73], v[170:173], v[210:213], v[70:73]
	v_mfma_f32_16x16x32_bf16 v[66:69], v[178:181], v[210:213], v[66:69]
	s_setprio 0
	s_barrier
	s_add_i32 s28, s50, s3
	v_lshl_add_u64 v[214:215], s[34:35], 0, v[132:133]
	s_mov_b32 m0, s28
	ds_read_b128 v[182:185], v152 offset:16384
	ds_read_b128 v[186:189], v152 offset:17408
	ds_read_b128 v[190:193], v152 offset:18432
	ds_read_b128 v[194:197], v152 offset:19456
	ds_read_b128 v[198:201], v152 offset:20480
	ds_read_b128 v[202:205], v152 offset:21504
	ds_read_b128 v[206:209], v152 offset:22528
	ds_read_b128 v[210:213], v152 offset:23552
	global_load_lds_dwordx4 v[214:215], off
	s_add_i32 m0, s28, 0x2000
	s_add_u32 s28, s34, 0xe0000
	v_lshl_add_u64 v[216:217], s[34:35], 0, v[134:135]
	s_addc_u32 s29, s35, 0
	s_add_i32 s57, s51, s3
	global_load_lds_dwordx4 v[216:217], off
	s_mov_b32 m0, s57
	v_lshl_add_u64 v[220:221], s[36:37], 0, v[134:135]
	global_load_lds_dwordx4 v132, s[28:29]
	s_add_i32 m0, s57, 0x2000
	s_nop 0
	global_load_lds_dwordx4 v134, s[28:29]
	v_lshl_add_u64 v[218:219], s[36:37], 0, v[132:133]
	s_mov_b32 m0, s38
	s_nop 0
	global_load_lds_dwordx4 v[218:219], off
	s_mov_b32 m0, s39
	s_nop 0
	global_load_lds_dwordx4 v[220:221], off
	s_waitcnt vmcnt(8)
	s_waitcnt lgkmcnt(0)
	s_barrier
; #define PG8_STAGE_A(b, h, ptr, NX) do { if constexpr (Sched::GATHER) { unsigned gs_[2]; gs_[0] = ((NX) && last_) ? gN[h][0] : gA[h][0]; gs_[1] = ((NX) && last_) ? gN[h][1] : gA[h][1]; PG8_STAGE(PG8_SA(b, h), ptr, gs_); } \
;         else PG8_STAGE(PG8_SA(b, h), (ptr) + ((h) ? hstep : (size_t)0), voffA); } while (0)
; #define PG8_STAGE(bufoff, gbase, voff) do { _Pragma("unroll") for (int _i = 0; _i < 2; ++_i) \
;         __builtin_amdgcn_global_load_lds((const unsigned*)((const char*)(gbase) + (voff)[_i]), (PG8_LAS unsigned*)(lds + (bufoff) + ldsw + _i * 8192), 16, 0, 0); } while (0)
; #define PG8_LDA(dst, b, h) do { _Pragma("unroll") for (int m = 0; m < 4; ++m) _Pragma("unroll") for (int k = 0; k < 2; ++k) dst[m][k] = *(const PG8_LAS bf16x8*)(lds + PG8_SA(b, h) + aoff + m * 2048 + k * 1024); } while (0)
; #define PG8_LDB(dst, b, h) do { _Pragma("unroll") for (int n = 0; n < 2; ++n) _Pragma("unroll") for (int k = 0; k < 2; ++k) dst[n][k] = *(const PG8_LAS bf16x8*)(lds + PG8_SB(b, h) + boff + n * 2048 + k * 1024); } while (0)
; #define PG8_MMA(ai, bj, At, Bt) do { __builtin_amdgcn_s_setprio(1); _Pragma("unroll") for (int m = 0; m < 4; ++m) _Pragma("unroll") for (int n = 0; n < 2; ++n) _Pragma("unroll") for (int k = 0; k < 2; ++k) \
;         acc[ai][bj][m][n] = __builtin_amdgcn_mfma_f32_16x16x32_bf16(Bt[n][k], At[m][k], acc[ai][bj][m][n], 0, 0, 0); __builtin_amdgcn_s_setprio(0); } while (0)
; #define PG8_WAIT_V(n) asm volatile("s_waitcnt vmcnt(" #n ")" ::: "memory")
; #define PG8_WAIT_L(n) asm volatile("s_waitcnt lgkmcnt(" #n ")" ::: "memory")
; #define PG8_BAR __builtin_amdgcn_s_barrier()
; #define PG8_SCHED __builtin_amdgcn_sched_barrier(0)
; template <class Epi, class Sched, bool ALIGN_EPI = false, bool SP2 = false>
; __device__ __forceinline__ void gemm_phase(PG8_LAS unsigned char* lds, const Gemm g, const Sched& S, const Epi& E, const bool skip_epi = false) {
;     ...
;             PG8_LDA(At, 0, 1); PG8_STAGE(PG8_SB(0, 0), b2, voffB); PG8_STAGE(PG8_SB(0, 1), b2 + hstep, voffB); PG8_STAGE_A(0, 0, a2, true);
;             PG8_WAIT_V(8); PG8_WAIT_L(0); PG8_BAR; PG8_MMA(1, 0, At, B0); PG8_MMA(1, 1, At, B1); PG8_BAR; PG8_SCHED;
;             PG8_LDB(B0, 1, 0); PG8_LDB(B1, 1, 1); PG8_SCHED; PG8_LDA(At, 1, 0); PG8_STAGE_A(0, 1, a2, true);
;             PG8_WAIT_V(8); PG8_WAIT_L(0); PG8_BAR; PG8_MMA(0, 0, At, B0); PG8_MMA(0, 1, At, B1); PG8_BAR; PG8_SCHED;
	s_setprio 3
	s_waitcnt lgkmcnt(0)
	v_mfma_f32_16x16x32_bf16 v[62:65], v[142:145], v[182:185], v[62:65]
	v_mfma_f32_16x16x32_bf16 v[58:61], v[158:161], v[182:185], v[58:61]
	v_mfma_f32_16x16x32_bf16 v[46:49], v[142:145], v[190:193], v[46:49]
	v_mfma_f32_16x16x32_bf16 v[42:45], v[158:161], v[190:193], v[42:45]
	v_mfma_f32_16x16x32_bf16 v[30:33], v[142:145], v[198:201], v[30:33]
	v_mfma_f32_16x16x32_bf16 v[26:29], v[158:161], v[198:201], v[26:29]
	v_mfma_f32_16x16x32_bf16 v[14:17], v[142:145], v[206:209], v[14:17]
	v_mfma_f32_16x16x32_bf16 v[10:13], v[158:161], v[206:209], v[10:13]
	v_mfma_f32_16x16x32_bf16 v[62:65], v[154:157], v[186:189], v[62:65]
	v_mfma_f32_16x16x32_bf16 v[58:61], v[162:165], v[186:189], v[58:61]
	v_mfma_f32_16x16x32_bf16 v[46:49], v[154:157], v[194:197], v[46:49]
	v_mfma_f32_16x16x32_bf16 v[42:45], v[162:165], v[194:197], v[42:45]
	v_mfma_f32_16x16x32_bf16 v[30:33], v[154:157], v[202:205], v[30:33]
	v_mfma_f32_16x16x32_bf16 v[26:29], v[162:165], v[202:205], v[26:29]
	v_mfma_f32_16x16x32_bf16 v[14:17], v[154:157], v[210:213], v[14:17]
	v_mfma_f32_16x16x32_bf16 v[10:13], v[162:165], v[210:213], v[10:13]
	v_mfma_f32_16x16x32_bf16 v[54:57], v[166:169], v[182:185], v[54:57]
	v_mfma_f32_16x16x32_bf16 v[50:53], v[174:177], v[182:185], v[50:53]
	v_mfma_f32_16x16x32_bf16 v[38:41], v[166:169], v[190:193], v[38:41]
	v_mfma_f32_16x16x32_bf16 v[34:37], v[174:177], v[190:193], v[34:37]
	v_mfma_f32_16x16x32_bf16 v[22:25], v[166:169], v[198:201], v[22:25]
	v_mfma_f32_16x16x32_bf16 v[18:21], v[174:177], v[198:201], v[18:21]
	v_mfma_f32_16x16x32_bf16 v[6:9], v[166:169], v[206:209], v[6:9]
	v_mfma_f32_16x16x32_bf16 v[2:5], v[174:177], v[206:209], v[2:5]
	v_mfma_f32_16x16x32_bf16 v[54:57], v[170:173], v[186:189], v[54:57]
	v_mfma_f32_16x16x32_bf16 v[50:53], v[178:181], v[186:189], v[50:53]
	v_mfma_f32_16x16x32_bf16 v[38:41], v[170:173], v[194:197], v[38:41]
	v_mfma_f32_16x16x32_bf16 v[34:37], v[178:181], v[194:197], v[34:37]
	v_mfma_f32_16x16x32_bf16 v[22:25], v[170:173], v[202:205], v[22:25]
	v_mfma_f32_16x16x32_bf16 v[18:21], v[178:181], v[202:205], v[18:21]
	v_mfma_f32_16x16x32_bf16 v[6:9], v[170:173], v[210:213], v[6:9]
	v_mfma_f32_16x16x32_bf16 v[2:5], v[178:181], v[210:213], v[2:5]
	s_setprio 0
	s_barrier
	s_add_i32 s57, 0, 0x18000
	v_add_u32_e32 v130, s57, v146
	s_add_i32 s58, 0, 0x1c000
	ds_read_b128 v[142:145], v130
	ds_read_b128 v[154:157], v130 offset:1024
	ds_read_b128 v[158:161], v130 offset:2048
	ds_read_b128 v[162:165], v130 offset:3072
	v_add_u32_e32 v130, s58, v146
	ds_read_b128 v[166:169], v130
	ds_read_b128 v[170:173], v130 offset:1024
	ds_read_b128 v[174:177], v130 offset:2048
	ds_read_b128 v[178:181], v130 offset:3072
	s_add_u32 s28, s36, 0xe0000
	s_addc_u32 s29, s37, 0
	s_mov_b32 m0, s40
	ds_read_b128 v[182:185], v152 offset:32768
	ds_read_b128 v[186:189], v152 offset:33792
	ds_read_b128 v[190:193], v152 offset:34816
	ds_read_b128 v[194:197], v152 offset:35840
	ds_read_b128 v[198:201], v152 offset:36864
	ds_read_b128 v[202:205], v152 offset:37888
	ds_read_b128 v[206:209], v152 offset:38912
	ds_read_b128 v[210:213], v152 offset:39936
	global_load_lds_dwordx4 v132, s[28:29]
	s_mov_b32 m0, s41
	s_nop 0
	global_load_lds_dwordx4 v134, s[28:29]
	s_waitcnt vmcnt(8)
	s_waitcnt lgkmcnt(0)
	s_barrier
	s_setprio 3
	s_waitcnt lgkmcnt(0)
	v_mfma_f32_16x16x32_bf16 v[126:129], v[142:145], v[182:185], v[126:129]
	v_mfma_f32_16x16x32_bf16 v[122:125], v[158:161], v[182:185], v[122:125]
	v_mfma_f32_16x16x32_bf16 v[110:113], v[142:145], v[190:193], v[110:113]
	v_mfma_f32_16x16x32_bf16 v[106:109], v[158:161], v[190:193], v[106:109]
	v_mfma_f32_16x16x32_bf16 v[94:97], v[142:145], v[198:201], v[94:97]
	v_mfma_f32_16x16x32_bf16 v[90:93], v[158:161], v[198:201], v[90:93]
	v_mfma_f32_16x16x32_bf16 v[78:81], v[142:145], v[206:209], v[78:81]
	v_mfma_f32_16x16x32_bf16 v[74:77], v[158:161], v[206:209], v[74:77]
	v_mfma_f32_16x16x32_bf16 v[126:129], v[154:157], v[186:189], v[126:129]
	v_mfma_f32_16x16x32_bf16 v[122:125], v[162:165], v[186:189], v[122:125]
	v_mfma_f32_16x16x32_bf16 v[110:113], v[154:157], v[194:197], v[110:113]
	v_mfma_f32_16x16x32_bf16 v[106:109], v[162:165], v[194:197], v[106:109]
	v_mfma_f32_16x16x32_bf16 v[94:97], v[154:157], v[202:205], v[94:97]
	v_mfma_f32_16x16x32_bf16 v[90:93], v[162:165], v[202:205], v[90:93]
	v_mfma_f32_16x16x32_bf16 v[78:81], v[154:157], v[210:213], v[78:81]
	v_mfma_f32_16x16x32_bf16 v[74:77], v[162:165], v[210:213], v[74:77]
	v_mfma_f32_16x16x32_bf16 v[118:121], v[166:169], v[182:185], v[118:121]
	v_mfma_f32_16x16x32_bf16 v[114:117], v[174:177], v[182:185], v[114:117]
	v_mfma_f32_16x16x32_bf16 v[102:105], v[166:169], v[190:193], v[102:105]
	v_mfma_f32_16x16x32_bf16 v[98:101], v[174:177], v[190:193], v[98:101]
	v_mfma_f32_16x16x32_bf16 v[86:89], v[166:169], v[198:201], v[86:89]
	v_mfma_f32_16x16x32_bf16 v[82:85], v[174:177], v[198:201], v[82:85]
	v_mfma_f32_16x16x32_bf16 v[70:73], v[166:169], v[206:209], v[70:73]
	v_mfma_f32_16x16x32_bf16 v[66:69], v[174:177], v[206:209], v[66:69]
	v_mfma_f32_16x16x32_bf16 v[118:121], v[170:173], v[186:189], v[118:121]
	v_mfma_f32_16x16x32_bf16 v[114:117], v[178:181], v[186:189], v[114:117]
	v_mfma_f32_16x16x32_bf16 v[102:105], v[170:173], v[194:197], v[102:105]
	v_mfma_f32_16x16x32_bf16 v[98:101], v[178:181], v[194:197], v[98:101]
	v_mfma_f32_16x16x32_bf16 v[86:89], v[170:173], v[202:205], v[86:89]
	v_mfma_f32_16x16x32_bf16 v[82:85], v[178:181], v[202:205], v[82:85]
	v_mfma_f32_16x16x32_bf16 v[70:73], v[170:173], v[210:213], v[70:73]
	v_mfma_f32_16x16x32_bf16 v[66:69], v[178:181], v[210:213], v[66:69]
	s_setprio 0
	s_barrier
; #define PG8_STAGE_A(b, h, ptr, NX) do { if constexpr (Sched::GATHER) { unsigned gs_[2]; gs_[0] = ((NX) && last_) ? gN[h][0] : gA[h][0]; gs_[1] = ((NX) && last_) ? gN[h][1] : gA[h][1]; PG8_STAGE(PG8_SA(b, h), ptr, gs_); } \
;         else PG8_STAGE(PG8_SA(b, h), (ptr) + ((h) ? hstep : (size_t)0), voffA); } while (0)
; #define PG8_STAGE(bufoff, gbase, voff) do { _Pragma("unroll") for (int _i = 0; _i < 2; ++_i) \
;         __builtin_amdgcn_global_load_lds((const unsigned*)((const char*)(gbase) + (voff)[_i]), (PG8_LAS unsigned*)(lds + (bufoff) + ldsw + _i * 8192), 16, 0, 0); } while (0)
; #define PG8_LDA(dst, b, h) do { _Pragma("unroll") for (int m = 0; m < 4; ++m) _Pragma("unroll") for (int k = 0; k < 2; ++k) dst[m][k] = *(const PG8_LAS bf16x8*)(lds + PG8_SA(b, h) + aoff + m * 2048 + k * 1024); } while (0)
; #define PG8_MMA(ai, bj, At, Bt) do { __builtin_amdgcn_s_setprio(1); _Pragma("unroll") for (int m = 0; m < 4; ++m) _Pragma("unroll") for (int n = 0; n < 2; ++n) _Pragma("unroll") for (int k = 0; k < 2; ++k) \
;         acc[ai][bj][m][n] = __builtin_amdgcn_mfma_f32_16x16x32_bf16(Bt[n][k], At[m][k], acc[ai][bj][m][n], 0, 0, 0); __builtin_amdgcn_s_setprio(0); } while (0)
; #define PG8_WAIT_V(n) asm volatile("s_waitcnt vmcnt(" #n ")" ::: "memory")
; #define PG8_WAIT_L(n) asm volatile("s_waitcnt lgkmcnt(" #n ")" ::: "memory")
; #define PG8_BAR __builtin_amdgcn_s_barrier()
; #define PG8_SCHED __builtin_amdgcn_sched_barrier(0)
; template <class Epi, class Sched, bool ALIGN_EPI = false, bool SP2 = false>
; __device__ __forceinline__ void gemm_phase(PG8_LAS unsigned char* lds, const Gemm g, const Sched& S, const Epi& E, const bool skip_epi = false) {
;     ...
;             PG8_LDA(At, 1, 1); PG8_STAGE(PG8_SB(1, 0), b3, voffB); PG8_STAGE(PG8_SB(1, 1), b3 + hstep, voffB); PG8_STAGE_A(1, 0, a3, true);
;             PG8_WAIT_V(8); PG8_WAIT_L(0); PG8_BAR; PG8_MMA(1, 0, At, B0); PG8_MMA(1, 1, At, B1); PG8_BAR; PG8_SCHED;
;     ...
;         if constexpr (ALIGN_EPI) { if (wr == 0) PG8_BAR; }
	s_add_i32 s28, s57, s3
	s_add_i32 m0, s28, 0xffffff80
	ds_read_b128 v[182:185], v152 offset:49152
	ds_read_b128 v[186:189], v152 offset:50176
	ds_read_b128 v[190:193], v152 offset:51200
	ds_read_b128 v[194:197], v152 offset:52224
	ds_read_b128 v[198:201], v152 offset:53248
	ds_read_b128 v[202:205], v152 offset:54272
	ds_read_b128 v[206:209], v152 offset:55296
	ds_read_b128 v[210:213], v152 offset:56320
	global_load_lds_dwordx4 v[214:215], off offset:128
	s_add_i32 m0, s28, 0x1f80
	s_add_u32 s28, s34, 0xe0080
	s_addc_u32 s29, s35, 0
	s_add_i32 s34, s58, s3
	global_load_lds_dwordx4 v[216:217], off offset:128
	s_mov_b32 m0, s34
	s_nop 0
	global_load_lds_dwordx4 v132, s[28:29]
	s_add_i32 m0, s34, 0x2000
	s_nop 0
	global_load_lds_dwordx4 v134, s[28:29]
	s_add_i32 m0, s46, 0xffffff80
	s_nop 0
	global_load_lds_dwordx4 v[218:219], off offset:128
	s_add_i32 m0, s47, 0xffffff80
	s_nop 0
	global_load_lds_dwordx4 v[220:221], off offset:128
	s_waitcnt vmcnt(8)
	s_waitcnt lgkmcnt(0)
	s_barrier
	s_setprio 3
	s_waitcnt lgkmcnt(0)
	v_mfma_f32_16x16x32_bf16 v[62:65], v[142:145], v[182:185], v[62:65]
	v_mfma_f32_16x16x32_bf16 v[58:61], v[158:161], v[182:185], v[58:61]
	v_mfma_f32_16x16x32_bf16 v[46:49], v[142:145], v[190:193], v[46:49]
	v_mfma_f32_16x16x32_bf16 v[42:45], v[158:161], v[190:193], v[42:45]
	v_mfma_f32_16x16x32_bf16 v[30:33], v[142:145], v[198:201], v[30:33]
	v_mfma_f32_16x16x32_bf16 v[26:29], v[158:161], v[198:201], v[26:29]
	v_mfma_f32_16x16x32_bf16 v[14:17], v[142:145], v[206:209], v[14:17]
	v_mfma_f32_16x16x32_bf16 v[10:13], v[158:161], v[206:209], v[10:13]
	v_mfma_f32_16x16x32_bf16 v[62:65], v[154:157], v[186:189], v[62:65]
	v_mfma_f32_16x16x32_bf16 v[58:61], v[162:165], v[186:189], v[58:61]
	v_mfma_f32_16x16x32_bf16 v[46:49], v[154:157], v[194:197], v[46:49]
	v_mfma_f32_16x16x32_bf16 v[42:45], v[162:165], v[194:197], v[42:45]
	v_mfma_f32_16x16x32_bf16 v[30:33], v[154:157], v[202:205], v[30:33]
	v_mfma_f32_16x16x32_bf16 v[26:29], v[162:165], v[202:205], v[26:29]
	v_mfma_f32_16x16x32_bf16 v[14:17], v[154:157], v[210:213], v[14:17]
	v_mfma_f32_16x16x32_bf16 v[10:13], v[162:165], v[210:213], v[10:13]
	v_mfma_f32_16x16x32_bf16 v[54:57], v[166:169], v[182:185], v[54:57]
	v_mfma_f32_16x16x32_bf16 v[50:53], v[174:177], v[182:185], v[50:53]
	v_mfma_f32_16x16x32_bf16 v[38:41], v[166:169], v[190:193], v[38:41]
	v_mfma_f32_16x16x32_bf16 v[34:37], v[174:177], v[190:193], v[34:37]
	v_mfma_f32_16x16x32_bf16 v[22:25], v[166:169], v[198:201], v[22:25]
	v_mfma_f32_16x16x32_bf16 v[18:21], v[174:177], v[198:201], v[18:21]
	v_mfma_f32_16x16x32_bf16 v[6:9], v[166:169], v[206:209], v[6:9]
	v_mfma_f32_16x16x32_bf16 v[2:5], v[174:177], v[206:209], v[2:5]
	v_mfma_f32_16x16x32_bf16 v[54:57], v[170:173], v[186:189], v[54:57]
	v_mfma_f32_16x16x32_bf16 v[50:53], v[178:181], v[186:189], v[50:53]
	v_mfma_f32_16x16x32_bf16 v[38:41], v[170:173], v[194:197], v[38:41]
	v_mfma_f32_16x16x32_bf16 v[34:37], v[178:181], v[194:197], v[34:37]
	v_mfma_f32_16x16x32_bf16 v[22:25], v[170:173], v[202:205], v[22:25]
	v_mfma_f32_16x16x32_bf16 v[18:21], v[178:181], v[202:205], v[18:21]
	v_mfma_f32_16x16x32_bf16 v[6:9], v[170:173], v[210:213], v[6:9]
	v_mfma_f32_16x16x32_bf16 v[2:5], v[178:181], v[210:213], v[2:5]
	s_setprio 0
	s_barrier
	s_add_i32 s56, s56, 2
	s_add_u32 s54, s54, 0x100
	s_addc_u32 s55, s55, 0
	s_cmp_gt_u32 s56, 11
	s_mov_b64 s[28:29], s[30:31]
	s_cbranch_scc0 .LBB0_1844
	s_and_b64 vcc, exec, s[20:21]
	s_cbranch_vccz .LBB0_1847
	s_barrier
